# v71 with static priorities in the fused fp8 loops (older half 1, younger half 2 for the whole K-loop, no per-segment s_setprio toggling)
# baseline (speedup 1.0000x reference)
; #define PG8_STAGE(bufoff, gbase, voff) do { _Pragma("unroll") for (int _i = 0; _i < 2; ++_i) \
;         __builtin_amdgcn_global_load_lds((const unsigned*)((const char*)(gbase) + (voff)[_i]), (PG8_LAS unsigned*)(lds + (bufoff) + ldsw + _i * 8192), 16, 0, 0); } while (0)
; #define PG8_WAIT_V(n) asm volatile("s_waitcnt vmcnt(" #n ")" ::: "memory")
; #define PG8_WAIT_L(n) asm volatile("s_waitcnt lgkmcnt(" #n ")" ::: "memory")
; #define PG8_BAR __builtin_amdgcn_s_barrier()
; #define PG8_SCHED __builtin_amdgcn_sched_barrier(0)
; template <class Epi, class Sched, bool ALIGN_EPI = true, bool F8 = false>
; __device__ __forceinline__ void gemm_phase(PG8_LAS unsigned char* lds, const Sched& S, const Epi& E) {
;     ...
;             PG8_LDB(B0, 0, 0); PG8_LDB(B1, 0, 1); PG8_SCHED; PG8_LDA(At, 0, 0); PG8_STAGE(PG8_SA(1, 1), a1, voffA[1]);
;             PG8_WAIT_V(8); PG8_WAIT_L(0); PG8_BAR; PG8_MMA(0, 0, At, B0); PG8_MMA(0, 1, At, B1); PG8_BAR; PG8_SCHED;
;             PG8_LDA(At, 0, 1); PG8_STAGE(PG8_SB(0, 0), b2, voffB[0]); PG8_STAGE(PG8_SB(0, 1), b2, voffB[1]); PG8_STAGE(PG8_SA(0, 0), a2, vA2[0]);
;             PG8_WAIT_V(8); PG8_WAIT_L(0); PG8_BAR; PG8_MMA(1, 0, At, B0); PG8_MMA(1, 1, At, B1); PG8_BAR; PG8_SCHED;
;             PG8_LDB(B0, 1, 0); PG8_LDB(B1, 1, 1); PG8_SCHED; PG8_LDA(At, 1, 0); PG8_STAGE(PG8_SA(0, 1), a2, vA2[1]);
;             PG8_WAIT_V(8); PG8_WAIT_L(0); PG8_BAR; PG8_MMA(0, 0, At, B0); PG8_MMA(0, 1, At, B1); PG8_BAR; PG8_SCHED;
;             PG8_LDA(At, 1, 1); PG8_STAGE(PG8_SB(1, 0), b3, voffB[0]); PG8_STAGE(PG8_SB(1, 1), b3, voffB[1]); PG8_STAGE(PG8_SA(1, 0), a3, vA2[0]);
;             PG8_WAIT_V(8); PG8_WAIT_L(0); PG8_BAR; PG8_MMA(1, 0, At, B0); PG8_MMA(1, 1, At, B1); PG8_BAR; PG8_SCHED;
.LBB0_371:
	s_add_u32 s5, s28, 0x10000
	s_addc_u32 s19, s29, 0
	s_add_u32 s26, s26, 0x8000
	s_addc_u32 s27, s27, 0
	s_mov_b32 s21, -2
	s_bitcmp1_b32 s3, 2
	s_cbranch_scc1 .Lh1e_9967
	s_setprio 1
.Lpk0_372:
	ds_read_b128 v[18:21], v207
	ds_read_b128 v[22:25], v207 offset:1024
	ds_read_b128 v[26:29], v207 offset:2048
	ds_read_b128 v[30:33], v207 offset:3072
	ds_read_b128 v[2:5], v208
	ds_read_b128 v[6:9], v208 offset:1024
	ds_read_b128 v[10:13], v208 offset:2048
	ds_read_b128 v[14:17], v208 offset:3072
	s_add_u32 s28, s26, 0x8000
	s_addc_u32 s29, s27, 0
	s_cmp_eq_u32 s21, 12
	s_cselect_b32 s40, s22, s28
	s_cselect_b32 s41, s23, s29
	s_cselect_b32 s30, s24, s5
	s_cselect_b32 s31, s25, s19
	s_add_u32 s28, s40, 0x8000
	s_addc_u32 s29, s41, 0
	v_lshl_add_u64 v[244:245], s[26:27], 0, v[190:191]
	s_add_i32 m0, s46, 0xc000
	ds_read_b128 v[212:215], v209
	ds_read_b128 v[216:219], v209 offset:1024
	ds_read_b128 v[220:223], v209 offset:2048
	ds_read_b128 v[224:227], v209 offset:3072
	ds_read_b128 v[228:231], v209 offset:4096
	ds_read_b128 v[232:235], v209 offset:5120
	ds_read_b128 v[236:239], v209 offset:6144
	ds_read_b128 v[240:243], v209 offset:7168
	global_load_lds_dwordx4 v[244:245], off
	v_lshl_add_u64 v[244:245], s[26:27], 0, v[188:189]
	s_add_i32 m0, s46, 0xe000
	s_nop 0
	global_load_lds_dwordx4 v[244:245], off
	s_waitcnt vmcnt(8)
	s_waitcnt lgkmcnt(0)
	v_mfma_scale_f32_16x16x128_f8f6f4 v[158:161], v[18:25], v[212:219], 0, v210, v210 op_sel_hi:[0,0,0]
	v_mfma_scale_f32_16x16x128_f8f6f4 v[154:157], v[26:33], v[212:219], 0, v210, v210 op_sel_hi:[0,0,0]
	v_mfma_scale_f32_16x16x128_f8f6f4 v[142:145], v[18:25], v[220:227], 0, v210, v210 op_sel_hi:[0,0,0]
	v_mfma_scale_f32_16x16x128_f8f6f4 v[138:141], v[26:33], v[220:227], 0, v210, v210 op_sel_hi:[0,0,0]
	v_mfma_scale_f32_16x16x128_f8f6f4 v[126:129], v[18:25], v[228:235], 0, v210, v210 op_sel_hi:[0,0,0]
	v_mfma_scale_f32_16x16x128_f8f6f4 v[122:125], v[26:33], v[228:235], 0, v210, v210 op_sel_hi:[0,0,0]
	v_mfma_scale_f32_16x16x128_f8f6f4 v[110:113], v[18:25], v[236:243], 0, v210, v210 op_sel_hi:[0,0,0]
	v_mfma_scale_f32_16x16x128_f8f6f4 v[106:109], v[26:33], v[236:243], 0, v210, v210 op_sel_hi:[0,0,0]
	s_nop 3
	v_mfma_scale_f32_16x16x128_f8f6f4 v[150:153], v[2:9], v[212:219], 0, v210, v210 op_sel_hi:[0,0,0]
	v_mfma_scale_f32_16x16x128_f8f6f4 v[146:149], v[10:17], v[212:219], 0, v210, v210 op_sel_hi:[0,0,0]
	v_mfma_scale_f32_16x16x128_f8f6f4 v[134:137], v[2:9], v[220:227], 0, v210, v210 op_sel_hi:[0,0,0]
	v_mfma_scale_f32_16x16x128_f8f6f4 v[130:133], v[10:17], v[220:227], 0, v210, v210 op_sel_hi:[0,0,0]
	v_mfma_scale_f32_16x16x128_f8f6f4 v[118:121], v[2:9], v[228:235], 0, v210, v210 op_sel_hi:[0,0,0]
	v_mfma_scale_f32_16x16x128_f8f6f4 v[114:117], v[10:17], v[228:235], 0, v210, v210 op_sel_hi:[0,0,0]
	v_mfma_scale_f32_16x16x128_f8f6f4 v[102:105], v[2:9], v[236:243], 0, v210, v210 op_sel_hi:[0,0,0]
	v_mfma_scale_f32_16x16x128_f8f6f4 v[98:101], v[10:17], v[236:243], 0, v210, v210 op_sel_hi:[0,0,0]
	s_barrier
	s_add_i32 s67, s62, s45
	v_lshl_add_u64 v[244:245], s[30:31], 0, v[164:165]
	s_mov_b32 m0, s67
	ds_read_b128 v[212:215], v209 offset:16384
	ds_read_b128 v[216:219], v209 offset:17408
	ds_read_b128 v[220:223], v209 offset:18432
	ds_read_b128 v[224:227], v209 offset:19456
	ds_read_b128 v[228:231], v209 offset:20480
	ds_read_b128 v[232:235], v209 offset:21504
	ds_read_b128 v[236:239], v209 offset:22528
	ds_read_b128 v[240:243], v209 offset:23552
	global_load_lds_dwordx4 v[244:245], off
	v_lshl_add_u64 v[246:247], s[30:31], 0, v[166:167]
	s_add_i32 m0, s67, 0x2000
	s_add_i32 s67, s63, s45
	global_load_lds_dwordx4 v[246:247], off
	v_lshl_add_u64 v[244:245], v[244:245], 0, s[8:9]
	s_mov_b32 m0, s67
	s_nop 0
	global_load_lds_dwordx4 v[244:245], off
	v_lshl_add_u64 v[244:245], v[246:247], 0, s[8:9]
	s_add_i32 m0, s67, 0x2000
	s_nop 0
	global_load_lds_dwordx4 v[244:245], off
	v_lshl_add_u64 v[244:245], s[40:41], 0, v[174:175]
	s_mov_b32 m0, s46
	s_nop 0
	global_load_lds_dwordx4 v[244:245], off
	v_lshl_add_u64 v[244:245], s[40:41], 0, v[176:177]
	s_mov_b32 m0, s47
	s_nop 0
	global_load_lds_dwordx4 v[244:245], off
	s_waitcnt vmcnt(8)
	s_waitcnt lgkmcnt(0)
	v_mfma_scale_f32_16x16x128_f8f6f4 v[94:97], v[18:25], v[212:219], 0, v210, v210 op_sel_hi:[0,0,0]
	v_mfma_scale_f32_16x16x128_f8f6f4 v[90:93], v[26:33], v[212:219], 0, v210, v210 op_sel_hi:[0,0,0]
	v_mfma_scale_f32_16x16x128_f8f6f4 v[78:81], v[18:25], v[220:227], 0, v210, v210 op_sel_hi:[0,0,0]
	v_mfma_scale_f32_16x16x128_f8f6f4 v[74:77], v[26:33], v[220:227], 0, v210, v210 op_sel_hi:[0,0,0]
	v_mfma_scale_f32_16x16x128_f8f6f4 v[62:65], v[18:25], v[228:235], 0, v210, v210 op_sel_hi:[0,0,0]
	v_mfma_scale_f32_16x16x128_f8f6f4 v[58:61], v[26:33], v[228:235], 0, v210, v210 op_sel_hi:[0,0,0]
	v_mfma_scale_f32_16x16x128_f8f6f4 v[46:49], v[18:25], v[236:243], 0, v210, v210 op_sel_hi:[0,0,0]
	v_mfma_scale_f32_16x16x128_f8f6f4 v[42:45], v[26:33], v[236:243], 0, v210, v210 op_sel_hi:[0,0,0]
	s_nop 3
	v_mfma_scale_f32_16x16x128_f8f6f4 v[86:89], v[2:9], v[212:219], 0, v210, v210 op_sel_hi:[0,0,0]
	v_mfma_scale_f32_16x16x128_f8f6f4 v[82:85], v[10:17], v[212:219], 0, v210, v210 op_sel_hi:[0,0,0]
	v_mfma_scale_f32_16x16x128_f8f6f4 v[70:73], v[2:9], v[220:227], 0, v210, v210 op_sel_hi:[0,0,0]
	v_mfma_scale_f32_16x16x128_f8f6f4 v[66:69], v[10:17], v[220:227], 0, v210, v210 op_sel_hi:[0,0,0]
	v_mfma_scale_f32_16x16x128_f8f6f4 v[54:57], v[2:9], v[228:235], 0, v210, v210 op_sel_hi:[0,0,0]
	v_mfma_scale_f32_16x16x128_f8f6f4 v[50:53], v[10:17], v[228:235], 0, v210, v210 op_sel_hi:[0,0,0]
	v_mfma_scale_f32_16x16x128_f8f6f4 v[38:41], v[2:9], v[236:243], 0, v210, v210 op_sel_hi:[0,0,0]
	v_mfma_scale_f32_16x16x128_f8f6f4 v[34:37], v[10:17], v[236:243], 0, v210, v210 op_sel_hi:[0,0,0]
	s_barrier
; #define PG8_STAGE(bufoff, gbase, voff) do { _Pragma("unroll") for (int _i = 0; _i < 2; ++_i) \
;         __builtin_amdgcn_global_load_lds((const unsigned*)((const char*)(gbase) + (voff)[_i]), (PG8_LAS unsigned*)(lds + (bufoff) + ldsw + _i * 8192), 16, 0, 0); } while (0)
; #define PG8_WAIT_V(n) asm volatile("s_waitcnt vmcnt(" #n ")" ::: "memory")
; #define PG8_WAIT_L(n) asm volatile("s_waitcnt lgkmcnt(" #n ")" ::: "memory")
; #define PG8_BAR __builtin_amdgcn_s_barrier()
; #define PG8_SCHED __builtin_amdgcn_sched_barrier(0)
; template <class Epi, class Sched, bool ALIGN_EPI = true, bool F8 = false>
; __device__ __forceinline__ void gemm_phase(PG8_LAS unsigned char* lds, const Sched& S, const Epi& E) {
;     ...
;             PG8_LDB(B0, 0, 0); PG8_LDB(B1, 0, 1); PG8_SCHED; PG8_LDA(At, 0, 0); PG8_STAGE(PG8_SA(1, 1), a1, voffA[1]);
;             PG8_WAIT_V(8); PG8_WAIT_L(0); PG8_BAR; PG8_MMA(0, 0, At, B0); PG8_MMA(0, 1, At, B1); PG8_BAR; PG8_SCHED;
;             PG8_LDA(At, 0, 1); PG8_STAGE(PG8_SB(0, 0), b2, voffB[0]); PG8_STAGE(PG8_SB(0, 1), b2, voffB[1]); PG8_STAGE(PG8_SA(0, 0), a2, vA2[0]);
;             PG8_WAIT_V(8); PG8_WAIT_L(0); PG8_BAR; PG8_MMA(1, 0, At, B0); PG8_MMA(1, 1, At, B1); PG8_BAR; PG8_SCHED;
;             PG8_LDB(B0, 1, 0); PG8_LDB(B1, 1, 1); PG8_SCHED; PG8_LDA(At, 1, 0); PG8_STAGE(PG8_SA(0, 1), a2, vA2[1]);
;             PG8_WAIT_V(8); PG8_WAIT_L(0); PG8_BAR; PG8_MMA(0, 0, At, B0); PG8_MMA(0, 1, At, B1); PG8_BAR; PG8_SCHED;
;             PG8_LDA(At, 1, 1); PG8_STAGE(PG8_SB(1, 0), b3, voffB[0]); PG8_STAGE(PG8_SB(1, 1), b3, voffB[1]); PG8_STAGE(PG8_SA(1, 0), a3, vA2[0]);
;             PG8_WAIT_V(8); PG8_WAIT_L(0); PG8_BAR; PG8_MMA(1, 0, At, B0); PG8_MMA(1, 1, At, B1); PG8_BAR; PG8_SCHED;
	s_add_i32 s67, 0, 0x18000
	s_add_i32 s68, 0, 0x1c000
	v_add_u32_e32 v14, s67, v202
	v_add_u32_e32 v30, s68, v202
	ds_read_b128 v[2:5], v14
	ds_read_b128 v[6:9], v14 offset:1024
	ds_read_b128 v[10:13], v14 offset:2048
	ds_read_b128 v[14:17], v14 offset:3072
	ds_read_b128 v[18:21], v30
	ds_read_b128 v[22:25], v30 offset:1024
	ds_read_b128 v[26:29], v30 offset:2048
	ds_read_b128 v[30:33], v30 offset:3072
	s_mov_b32 m0, s48
	v_lshl_add_u64 v[244:245], s[40:41], 0, v[178:179]
	ds_read_b128 v[212:215], v209 offset:32768
	ds_read_b128 v[216:219], v209 offset:33792
	ds_read_b128 v[220:223], v209 offset:34816
	ds_read_b128 v[224:227], v209 offset:35840
	ds_read_b128 v[228:231], v209 offset:36864
	ds_read_b128 v[232:235], v209 offset:37888
	ds_read_b128 v[236:239], v209 offset:38912
	ds_read_b128 v[240:243], v209 offset:39936
	global_load_lds_dwordx4 v[244:245], off
	v_lshl_add_u64 v[244:245], s[40:41], 0, v[180:181]
	s_mov_b32 m0, s49
	s_nop 0
	global_load_lds_dwordx4 v[244:245], off
	s_waitcnt vmcnt(8)
	s_waitcnt lgkmcnt(0)
	v_mfma_scale_f32_16x16x128_f8f6f4 v[158:161], v[2:9], v[212:219], v[158:161], v210, v210 op_sel_hi:[0,0,0]
	v_mfma_scale_f32_16x16x128_f8f6f4 v[154:157], v[10:17], v[212:219], v[154:157], v210, v210 op_sel_hi:[0,0,0]
	v_mfma_scale_f32_16x16x128_f8f6f4 v[142:145], v[2:9], v[220:227], v[142:145], v210, v210 op_sel_hi:[0,0,0]
	v_mfma_scale_f32_16x16x128_f8f6f4 v[138:141], v[10:17], v[220:227], v[138:141], v210, v210 op_sel_hi:[0,0,0]
	v_mfma_scale_f32_16x16x128_f8f6f4 v[126:129], v[2:9], v[228:235], v[126:129], v210, v210 op_sel_hi:[0,0,0]
	v_mfma_scale_f32_16x16x128_f8f6f4 v[122:125], v[10:17], v[228:235], v[122:125], v210, v210 op_sel_hi:[0,0,0]
	v_mfma_scale_f32_16x16x128_f8f6f4 v[110:113], v[2:9], v[236:243], v[110:113], v210, v210 op_sel_hi:[0,0,0]
	v_mfma_scale_f32_16x16x128_f8f6f4 v[106:109], v[10:17], v[236:243], v[106:109], v210, v210 op_sel_hi:[0,0,0]
	s_nop 3
	v_mfma_scale_f32_16x16x128_f8f6f4 v[150:153], v[18:25], v[212:219], v[150:153], v210, v210 op_sel_hi:[0,0,0]
	v_mfma_scale_f32_16x16x128_f8f6f4 v[146:149], v[26:33], v[212:219], v[146:149], v210, v210 op_sel_hi:[0,0,0]
	v_mfma_scale_f32_16x16x128_f8f6f4 v[134:137], v[18:25], v[220:227], v[134:137], v210, v210 op_sel_hi:[0,0,0]
	v_mfma_scale_f32_16x16x128_f8f6f4 v[130:133], v[26:33], v[220:227], v[130:133], v210, v210 op_sel_hi:[0,0,0]
	v_mfma_scale_f32_16x16x128_f8f6f4 v[118:121], v[18:25], v[228:235], v[118:121], v210, v210 op_sel_hi:[0,0,0]
	v_mfma_scale_f32_16x16x128_f8f6f4 v[114:117], v[26:33], v[228:235], v[114:117], v210, v210 op_sel_hi:[0,0,0]
	v_mfma_scale_f32_16x16x128_f8f6f4 v[102:105], v[18:25], v[236:243], v[102:105], v210, v210 op_sel_hi:[0,0,0]
	v_mfma_scale_f32_16x16x128_f8f6f4 v[98:101], v[26:33], v[236:243], v[98:101], v210, v210 op_sel_hi:[0,0,0]
	s_barrier
	s_add_u32 s30, s30, 0x8000
	s_addc_u32 s31, s31, 0
	s_add_i32 s40, s67, s45
	v_lshl_add_u64 v[244:245], s[30:31], 0, v[164:165]
	s_mov_b32 m0, s40
	ds_read_b128 v[212:215], v209 offset:49152
	ds_read_b128 v[216:219], v209 offset:50176
	ds_read_b128 v[220:223], v209 offset:51200
	ds_read_b128 v[224:227], v209 offset:52224
	ds_read_b128 v[228:231], v209 offset:53248
	ds_read_b128 v[232:235], v209 offset:54272
	ds_read_b128 v[236:239], v209 offset:55296
	ds_read_b128 v[240:243], v209 offset:56320
	global_load_lds_dwordx4 v[244:245], off
	v_lshl_add_u64 v[244:245], s[30:31], 0, v[166:167]
	s_add_i32 m0, s40, 0x2000
	s_add_i32 s40, s68, s45
	global_load_lds_dwordx4 v[244:245], off
	v_lshl_add_u64 v[244:245], s[30:31], 0, v[168:169]
	s_mov_b32 m0, s40
	s_nop 0
	global_load_lds_dwordx4 v[244:245], off
	v_lshl_add_u64 v[244:245], s[30:31], 0, v[172:173]
	s_add_i32 m0, s40, 0x2000
	s_nop 0
	global_load_lds_dwordx4 v[244:245], off
	v_lshl_add_u64 v[244:245], s[28:29], 0, v[174:175]
	s_mov_b32 m0, s52
	s_nop 0
	global_load_lds_dwordx4 v[244:245], off
	v_lshl_add_u64 v[244:245], s[28:29], 0, v[176:177]
	s_mov_b32 m0, s53
	s_nop 0
	global_load_lds_dwordx4 v[244:245], off
	s_waitcnt vmcnt(8)
	s_waitcnt lgkmcnt(0)
	v_mfma_scale_f32_16x16x128_f8f6f4 v[94:97], v[2:9], v[212:219], v[94:97], v210, v210 op_sel_hi:[0,0,0]
	v_mfma_scale_f32_16x16x128_f8f6f4 v[90:93], v[10:17], v[212:219], v[90:93], v210, v210 op_sel_hi:[0,0,0]
	v_mfma_scale_f32_16x16x128_f8f6f4 v[78:81], v[2:9], v[220:227], v[78:81], v210, v210 op_sel_hi:[0,0,0]
	v_mfma_scale_f32_16x16x128_f8f6f4 v[74:77], v[10:17], v[220:227], v[74:77], v210, v210 op_sel_hi:[0,0,0]
	v_mfma_scale_f32_16x16x128_f8f6f4 v[62:65], v[2:9], v[228:235], v[62:65], v210, v210 op_sel_hi:[0,0,0]
	v_mfma_scale_f32_16x16x128_f8f6f4 v[58:61], v[10:17], v[228:235], v[58:61], v210, v210 op_sel_hi:[0,0,0]
	v_mfma_scale_f32_16x16x128_f8f6f4 v[46:49], v[2:9], v[236:243], v[46:49], v210, v210 op_sel_hi:[0,0,0]
	v_mfma_scale_f32_16x16x128_f8f6f4 v[42:45], v[10:17], v[236:243], v[42:45], v210, v210 op_sel_hi:[0,0,0]
	s_nop 3
	v_mfma_scale_f32_16x16x128_f8f6f4 v[86:89], v[18:25], v[212:219], v[86:89], v210, v210 op_sel_hi:[0,0,0]
	v_mfma_scale_f32_16x16x128_f8f6f4 v[82:85], v[26:33], v[212:219], v[82:85], v210, v210 op_sel_hi:[0,0,0]
	v_mfma_scale_f32_16x16x128_f8f6f4 v[70:73], v[18:25], v[220:227], v[70:73], v210, v210 op_sel_hi:[0,0,0]
	v_mfma_scale_f32_16x16x128_f8f6f4 v[66:69], v[26:33], v[220:227], v[66:69], v210, v210 op_sel_hi:[0,0,0]
	v_mfma_scale_f32_16x16x128_f8f6f4 v[54:57], v[18:25], v[228:235], v[54:57], v210, v210 op_sel_hi:[0,0,0]
	v_mfma_scale_f32_16x16x128_f8f6f4 v[50:53], v[26:33], v[228:235], v[50:53], v210, v210 op_sel_hi:[0,0,0]
	v_mfma_scale_f32_16x16x128_f8f6f4 v[38:41], v[18:25], v[236:243], v[38:41], v210, v210 op_sel_hi:[0,0,0]
	v_mfma_scale_f32_16x16x128_f8f6f4 v[34:37], v[26:33], v[236:243], v[34:37], v210, v210 op_sel_hi:[0,0,0]
	s_barrier
	s_add_i32 s21, s21, 2
	s_add_u32 s5, s5, 0x10000
	s_addc_u32 s19, s19, 0
	s_add_u32 s26, s26, 0x10000
	s_addc_u32 s27, s27, 0
	s_cmp_gt_u32 s21, 13
	s_cbranch_scc0 .LBB0_372
	s_branch .Lfx_9967
; #define PG8_STAGE(bufoff, gbase, voff) do { _Pragma("unroll") for (int _i = 0; _i < 2; ++_i) \
;         __builtin_amdgcn_global_load_lds((const unsigned*)((const char*)(gbase) + (voff)[_i]), (PG8_LAS unsigned*)(lds + (bufoff) + ldsw + _i * 8192), 16, 0, 0); } while (0)
; #define PG8_WAIT_V(n) asm volatile("s_waitcnt vmcnt(" #n ")" ::: "memory")
; #define PG8_WAIT_L(n) asm volatile("s_waitcnt lgkmcnt(" #n ")" ::: "memory")
; #define PG8_BAR __builtin_amdgcn_s_barrier()
; #define PG8_SCHED __builtin_amdgcn_sched_barrier(0)
; template <class Epi, class Sched, bool ALIGN_EPI = true, bool F8 = false>
; __device__ __forceinline__ void gemm_phase(PG8_LAS unsigned char* lds, const Sched& S, const Epi& E) {
;     ...
;             PG8_LDB(B0, 0, 0); PG8_LDB(B1, 0, 1); PG8_SCHED; PG8_LDA(At, 0, 0); PG8_STAGE(PG8_SA(1, 1), a1, voffA[1]);
;             PG8_WAIT_V(8); PG8_WAIT_L(0); PG8_BAR; PG8_MMA(0, 0, At, B0); PG8_MMA(0, 1, At, B1); PG8_BAR; PG8_SCHED;
;             PG8_LDA(At, 0, 1); PG8_STAGE(PG8_SB(0, 0), b2, voffB[0]); PG8_STAGE(PG8_SB(0, 1), b2, voffB[1]); PG8_STAGE(PG8_SA(0, 0), a2, vA2[0]);
;             PG8_WAIT_V(8); PG8_WAIT_L(0); PG8_BAR; PG8_MMA(1, 0, At, B0); PG8_MMA(1, 1, At, B1); PG8_BAR; PG8_SCHED;
;             PG8_LDB(B0, 1, 0); PG8_LDB(B1, 1, 1); PG8_SCHED; PG8_LDA(At, 1, 0); PG8_STAGE(PG8_SA(0, 1), a2, vA2[1]);
;             PG8_WAIT_V(8); PG8_WAIT_L(0); PG8_BAR; PG8_MMA(0, 0, At, B0); PG8_MMA(0, 1, At, B1); PG8_BAR; PG8_SCHED;
;             PG8_LDA(At, 1, 1); PG8_STAGE(PG8_SB(1, 0), b3, voffB[0]); PG8_STAGE(PG8_SB(1, 1), b3, voffB[1]); PG8_STAGE(PG8_SA(1, 0), a3, vA2[0]);
;             PG8_WAIT_V(8); PG8_WAIT_L(0); PG8_BAR; PG8_MMA(1, 0, At, B0); PG8_MMA(1, 1, At, B1); PG8_BAR; PG8_SCHED;
.LBB0_372:
	ds_read_b128 v[18:21], v207
	ds_read_b128 v[22:25], v207 offset:1024
	ds_read_b128 v[26:29], v207 offset:2048
	ds_read_b128 v[30:33], v207 offset:3072
	ds_read_b128 v[2:5], v208
	ds_read_b128 v[6:9], v208 offset:1024
	ds_read_b128 v[10:13], v208 offset:2048
	ds_read_b128 v[14:17], v208 offset:3072
	s_add_u32 s28, s26, 0x8000
	s_addc_u32 s29, s27, 0
	s_cmp_eq_u32 s21, 12
	s_cselect_b32 s40, s22, s28
	s_cselect_b32 s41, s23, s29
	s_cselect_b32 s30, s24, s5
	s_cselect_b32 s31, s25, s19
	s_add_u32 s28, s40, 0x8000
	s_addc_u32 s29, s41, 0
	v_lshl_add_u64 v[244:245], s[26:27], 0, v[190:191]
	s_add_i32 m0, s46, 0xc000
	ds_read_b128 v[212:215], v209
	ds_read_b128 v[216:219], v209 offset:1024
	ds_read_b128 v[220:223], v209 offset:2048
	ds_read_b128 v[224:227], v209 offset:3072
	ds_read_b128 v[228:231], v209 offset:4096
	ds_read_b128 v[232:235], v209 offset:5120
	ds_read_b128 v[236:239], v209 offset:6144
	ds_read_b128 v[240:243], v209 offset:7168
	global_load_lds_dwordx4 v[244:245], off
	v_lshl_add_u64 v[244:245], s[26:27], 0, v[188:189]
	s_add_i32 m0, s46, 0xe000
	s_nop 0
	global_load_lds_dwordx4 v[244:245], off
	s_waitcnt vmcnt(8)
	s_waitcnt lgkmcnt(0)
	v_mfma_scale_f32_16x16x128_f8f6f4 v[158:161], v[18:25], v[212:219], v[158:161], v210, v210 op_sel_hi:[0,0,0]
	v_mfma_scale_f32_16x16x128_f8f6f4 v[154:157], v[26:33], v[212:219], v[154:157], v210, v210 op_sel_hi:[0,0,0]
	v_mfma_scale_f32_16x16x128_f8f6f4 v[142:145], v[18:25], v[220:227], v[142:145], v210, v210 op_sel_hi:[0,0,0]
	v_mfma_scale_f32_16x16x128_f8f6f4 v[138:141], v[26:33], v[220:227], v[138:141], v210, v210 op_sel_hi:[0,0,0]
	v_mfma_scale_f32_16x16x128_f8f6f4 v[126:129], v[18:25], v[228:235], v[126:129], v210, v210 op_sel_hi:[0,0,0]
	v_mfma_scale_f32_16x16x128_f8f6f4 v[122:125], v[26:33], v[228:235], v[122:125], v210, v210 op_sel_hi:[0,0,0]
	v_mfma_scale_f32_16x16x128_f8f6f4 v[110:113], v[18:25], v[236:243], v[110:113], v210, v210 op_sel_hi:[0,0,0]
	v_mfma_scale_f32_16x16x128_f8f6f4 v[106:109], v[26:33], v[236:243], v[106:109], v210, v210 op_sel_hi:[0,0,0]
	s_nop 3
	v_mfma_scale_f32_16x16x128_f8f6f4 v[150:153], v[2:9], v[212:219], v[150:153], v210, v210 op_sel_hi:[0,0,0]
	v_mfma_scale_f32_16x16x128_f8f6f4 v[146:149], v[10:17], v[212:219], v[146:149], v210, v210 op_sel_hi:[0,0,0]
	v_mfma_scale_f32_16x16x128_f8f6f4 v[134:137], v[2:9], v[220:227], v[134:137], v210, v210 op_sel_hi:[0,0,0]
	v_mfma_scale_f32_16x16x128_f8f6f4 v[130:133], v[10:17], v[220:227], v[130:133], v210, v210 op_sel_hi:[0,0,0]
	v_mfma_scale_f32_16x16x128_f8f6f4 v[118:121], v[2:9], v[228:235], v[118:121], v210, v210 op_sel_hi:[0,0,0]
	v_mfma_scale_f32_16x16x128_f8f6f4 v[114:117], v[10:17], v[228:235], v[114:117], v210, v210 op_sel_hi:[0,0,0]
	v_mfma_scale_f32_16x16x128_f8f6f4 v[102:105], v[2:9], v[236:243], v[102:105], v210, v210 op_sel_hi:[0,0,0]
	v_mfma_scale_f32_16x16x128_f8f6f4 v[98:101], v[10:17], v[236:243], v[98:101], v210, v210 op_sel_hi:[0,0,0]
	s_barrier
	s_add_i32 s67, s62, s45
	v_lshl_add_u64 v[244:245], s[30:31], 0, v[164:165]
	s_mov_b32 m0, s67
	ds_read_b128 v[212:215], v209 offset:16384
	ds_read_b128 v[216:219], v209 offset:17408
	ds_read_b128 v[220:223], v209 offset:18432
	ds_read_b128 v[224:227], v209 offset:19456
	ds_read_b128 v[228:231], v209 offset:20480
	ds_read_b128 v[232:235], v209 offset:21504
	ds_read_b128 v[236:239], v209 offset:22528
	ds_read_b128 v[240:243], v209 offset:23552
	global_load_lds_dwordx4 v[244:245], off
	v_lshl_add_u64 v[246:247], s[30:31], 0, v[166:167]
	s_add_i32 m0, s67, 0x2000
	s_add_i32 s67, s63, s45
	global_load_lds_dwordx4 v[246:247], off
	v_lshl_add_u64 v[244:245], v[244:245], 0, s[8:9]
	s_mov_b32 m0, s67
	s_nop 0
	global_load_lds_dwordx4 v[244:245], off
	v_lshl_add_u64 v[244:245], v[246:247], 0, s[8:9]
	s_add_i32 m0, s67, 0x2000
	s_nop 0
	global_load_lds_dwordx4 v[244:245], off
	v_lshl_add_u64 v[244:245], s[40:41], 0, v[174:175]
	s_mov_b32 m0, s46
	s_nop 0
	global_load_lds_dwordx4 v[244:245], off
	v_lshl_add_u64 v[244:245], s[40:41], 0, v[176:177]
	s_mov_b32 m0, s47
	s_nop 0
	global_load_lds_dwordx4 v[244:245], off
	s_waitcnt vmcnt(8)
	s_waitcnt lgkmcnt(0)
	v_mfma_scale_f32_16x16x128_f8f6f4 v[94:97], v[18:25], v[212:219], v[94:97], v210, v210 op_sel_hi:[0,0,0]
	v_mfma_scale_f32_16x16x128_f8f6f4 v[90:93], v[26:33], v[212:219], v[90:93], v210, v210 op_sel_hi:[0,0,0]
	v_mfma_scale_f32_16x16x128_f8f6f4 v[78:81], v[18:25], v[220:227], v[78:81], v210, v210 op_sel_hi:[0,0,0]
	v_mfma_scale_f32_16x16x128_f8f6f4 v[74:77], v[26:33], v[220:227], v[74:77], v210, v210 op_sel_hi:[0,0,0]
	v_mfma_scale_f32_16x16x128_f8f6f4 v[62:65], v[18:25], v[228:235], v[62:65], v210, v210 op_sel_hi:[0,0,0]
	v_mfma_scale_f32_16x16x128_f8f6f4 v[58:61], v[26:33], v[228:235], v[58:61], v210, v210 op_sel_hi:[0,0,0]
	v_mfma_scale_f32_16x16x128_f8f6f4 v[46:49], v[18:25], v[236:243], v[46:49], v210, v210 op_sel_hi:[0,0,0]
	v_mfma_scale_f32_16x16x128_f8f6f4 v[42:45], v[26:33], v[236:243], v[42:45], v210, v210 op_sel_hi:[0,0,0]
	s_nop 3
	v_mfma_scale_f32_16x16x128_f8f6f4 v[86:89], v[2:9], v[212:219], v[86:89], v210, v210 op_sel_hi:[0,0,0]
	v_mfma_scale_f32_16x16x128_f8f6f4 v[82:85], v[10:17], v[212:219], v[82:85], v210, v210 op_sel_hi:[0,0,0]
	v_mfma_scale_f32_16x16x128_f8f6f4 v[70:73], v[2:9], v[220:227], v[70:73], v210, v210 op_sel_hi:[0,0,0]
	v_mfma_scale_f32_16x16x128_f8f6f4 v[66:69], v[10:17], v[220:227], v[66:69], v210, v210 op_sel_hi:[0,0,0]
	v_mfma_scale_f32_16x16x128_f8f6f4 v[54:57], v[2:9], v[228:235], v[54:57], v210, v210 op_sel_hi:[0,0,0]
	v_mfma_scale_f32_16x16x128_f8f6f4 v[50:53], v[10:17], v[228:235], v[50:53], v210, v210 op_sel_hi:[0,0,0]
	v_mfma_scale_f32_16x16x128_f8f6f4 v[38:41], v[2:9], v[236:243], v[38:41], v210, v210 op_sel_hi:[0,0,0]
	v_mfma_scale_f32_16x16x128_f8f6f4 v[34:37], v[10:17], v[236:243], v[34:37], v210, v210 op_sel_hi:[0,0,0]
	s_barrier
; #define PG8_STAGE(bufoff, gbase, voff) do { _Pragma("unroll") for (int _i = 0; _i < 2; ++_i) \
;         __builtin_amdgcn_global_load_lds((const unsigned*)((const char*)(gbase) + (voff)[_i]), (PG8_LAS unsigned*)(lds + (bufoff) + ldsw + _i * 8192), 16, 0, 0); } while (0)
; #define PG8_WAIT_V(n) asm volatile("s_waitcnt vmcnt(" #n ")" ::: "memory")
; #define PG8_WAIT_L(n) asm volatile("s_waitcnt lgkmcnt(" #n ")" ::: "memory")
; #define PG8_BAR __builtin_amdgcn_s_barrier()
; #define PG8_SCHED __builtin_amdgcn_sched_barrier(0)
; template <class Epi, class Sched, bool ALIGN_EPI = true, bool F8 = false>
; __device__ __forceinline__ void gemm_phase(PG8_LAS unsigned char* lds, const Sched& S, const Epi& E) {
;     ...
;             PG8_LDB(B0, 0, 0); PG8_LDB(B1, 0, 1); PG8_SCHED; PG8_LDA(At, 0, 0); PG8_STAGE(PG8_SA(1, 1), a1, voffA[1]);
;             PG8_WAIT_V(8); PG8_WAIT_L(0); PG8_BAR; PG8_MMA(0, 0, At, B0); PG8_MMA(0, 1, At, B1); PG8_BAR; PG8_SCHED;
;             PG8_LDA(At, 0, 1); PG8_STAGE(PG8_SB(0, 0), b2, voffB[0]); PG8_STAGE(PG8_SB(0, 1), b2, voffB[1]); PG8_STAGE(PG8_SA(0, 0), a2, vA2[0]);
;             PG8_WAIT_V(8); PG8_WAIT_L(0); PG8_BAR; PG8_MMA(1, 0, At, B0); PG8_MMA(1, 1, At, B1); PG8_BAR; PG8_SCHED;
;             PG8_LDB(B0, 1, 0); PG8_LDB(B1, 1, 1); PG8_SCHED; PG8_LDA(At, 1, 0); PG8_STAGE(PG8_SA(0, 1), a2, vA2[1]);
;             PG8_WAIT_V(8); PG8_WAIT_L(0); PG8_BAR; PG8_MMA(0, 0, At, B0); PG8_MMA(0, 1, At, B1); PG8_BAR; PG8_SCHED;
;             PG8_LDA(At, 1, 1); PG8_STAGE(PG8_SB(1, 0), b3, voffB[0]); PG8_STAGE(PG8_SB(1, 1), b3, voffB[1]); PG8_STAGE(PG8_SA(1, 0), a3, vA2[0]);
;             PG8_WAIT_V(8); PG8_WAIT_L(0); PG8_BAR; PG8_MMA(1, 0, At, B0); PG8_MMA(1, 1, At, B1); PG8_BAR; PG8_SCHED;
	s_add_i32 s67, 0, 0x18000
	s_add_i32 s68, 0, 0x1c000
	v_add_u32_e32 v14, s67, v202
	v_add_u32_e32 v30, s68, v202
	ds_read_b128 v[2:5], v14
	ds_read_b128 v[6:9], v14 offset:1024
	ds_read_b128 v[10:13], v14 offset:2048
	ds_read_b128 v[14:17], v14 offset:3072
	ds_read_b128 v[18:21], v30
	ds_read_b128 v[22:25], v30 offset:1024
	ds_read_b128 v[26:29], v30 offset:2048
	ds_read_b128 v[30:33], v30 offset:3072
	s_mov_b32 m0, s48
	v_lshl_add_u64 v[244:245], s[40:41], 0, v[178:179]
	ds_read_b128 v[212:215], v209 offset:32768
	ds_read_b128 v[216:219], v209 offset:33792
	ds_read_b128 v[220:223], v209 offset:34816
	ds_read_b128 v[224:227], v209 offset:35840
	ds_read_b128 v[228:231], v209 offset:36864
	ds_read_b128 v[232:235], v209 offset:37888
	ds_read_b128 v[236:239], v209 offset:38912
	ds_read_b128 v[240:243], v209 offset:39936
	global_load_lds_dwordx4 v[244:245], off
	v_lshl_add_u64 v[244:245], s[40:41], 0, v[180:181]
	s_mov_b32 m0, s49
	s_nop 0
	global_load_lds_dwordx4 v[244:245], off
	s_waitcnt vmcnt(8)
	s_waitcnt lgkmcnt(0)
	v_mfma_scale_f32_16x16x128_f8f6f4 v[158:161], v[2:9], v[212:219], v[158:161], v210, v210 op_sel_hi:[0,0,0]
	v_mfma_scale_f32_16x16x128_f8f6f4 v[154:157], v[10:17], v[212:219], v[154:157], v210, v210 op_sel_hi:[0,0,0]
	v_mfma_scale_f32_16x16x128_f8f6f4 v[142:145], v[2:9], v[220:227], v[142:145], v210, v210 op_sel_hi:[0,0,0]
	v_mfma_scale_f32_16x16x128_f8f6f4 v[138:141], v[10:17], v[220:227], v[138:141], v210, v210 op_sel_hi:[0,0,0]
	v_mfma_scale_f32_16x16x128_f8f6f4 v[126:129], v[2:9], v[228:235], v[126:129], v210, v210 op_sel_hi:[0,0,0]
	v_mfma_scale_f32_16x16x128_f8f6f4 v[122:125], v[10:17], v[228:235], v[122:125], v210, v210 op_sel_hi:[0,0,0]
	v_mfma_scale_f32_16x16x128_f8f6f4 v[110:113], v[2:9], v[236:243], v[110:113], v210, v210 op_sel_hi:[0,0,0]
	v_mfma_scale_f32_16x16x128_f8f6f4 v[106:109], v[10:17], v[236:243], v[106:109], v210, v210 op_sel_hi:[0,0,0]
	s_nop 3
	v_mfma_scale_f32_16x16x128_f8f6f4 v[150:153], v[18:25], v[212:219], v[150:153], v210, v210 op_sel_hi:[0,0,0]
	v_mfma_scale_f32_16x16x128_f8f6f4 v[146:149], v[26:33], v[212:219], v[146:149], v210, v210 op_sel_hi:[0,0,0]
	v_mfma_scale_f32_16x16x128_f8f6f4 v[134:137], v[18:25], v[220:227], v[134:137], v210, v210 op_sel_hi:[0,0,0]
	v_mfma_scale_f32_16x16x128_f8f6f4 v[130:133], v[26:33], v[220:227], v[130:133], v210, v210 op_sel_hi:[0,0,0]
	v_mfma_scale_f32_16x16x128_f8f6f4 v[118:121], v[18:25], v[228:235], v[118:121], v210, v210 op_sel_hi:[0,0,0]
	v_mfma_scale_f32_16x16x128_f8f6f4 v[114:117], v[26:33], v[228:235], v[114:117], v210, v210 op_sel_hi:[0,0,0]
	v_mfma_scale_f32_16x16x128_f8f6f4 v[102:105], v[18:25], v[236:243], v[102:105], v210, v210 op_sel_hi:[0,0,0]
	v_mfma_scale_f32_16x16x128_f8f6f4 v[98:101], v[26:33], v[236:243], v[98:101], v210, v210 op_sel_hi:[0,0,0]
	s_barrier
	s_add_u32 s30, s30, 0x8000
	s_addc_u32 s31, s31, 0
	s_add_i32 s40, s67, s45
	v_lshl_add_u64 v[244:245], s[30:31], 0, v[164:165]
	s_mov_b32 m0, s40
	ds_read_b128 v[212:215], v209 offset:49152
	ds_read_b128 v[216:219], v209 offset:50176
	ds_read_b128 v[220:223], v209 offset:51200
	ds_read_b128 v[224:227], v209 offset:52224
	ds_read_b128 v[228:231], v209 offset:53248
	ds_read_b128 v[232:235], v209 offset:54272
	ds_read_b128 v[236:239], v209 offset:55296
	ds_read_b128 v[240:243], v209 offset:56320
	global_load_lds_dwordx4 v[244:245], off
	v_lshl_add_u64 v[244:245], s[30:31], 0, v[166:167]
	s_add_i32 m0, s40, 0x2000
	s_add_i32 s40, s68, s45
	global_load_lds_dwordx4 v[244:245], off
	v_lshl_add_u64 v[244:245], s[30:31], 0, v[168:169]
	s_mov_b32 m0, s40
	s_nop 0
	global_load_lds_dwordx4 v[244:245], off
	v_lshl_add_u64 v[244:245], s[30:31], 0, v[172:173]
	s_add_i32 m0, s40, 0x2000
	s_nop 0
	global_load_lds_dwordx4 v[244:245], off
	v_lshl_add_u64 v[244:245], s[28:29], 0, v[174:175]
	s_mov_b32 m0, s52
	s_nop 0
	global_load_lds_dwordx4 v[244:245], off
	v_lshl_add_u64 v[244:245], s[28:29], 0, v[176:177]
	s_mov_b32 m0, s53
	s_nop 0
	global_load_lds_dwordx4 v[244:245], off
	s_waitcnt vmcnt(8)
	s_waitcnt lgkmcnt(0)
	v_mfma_scale_f32_16x16x128_f8f6f4 v[94:97], v[2:9], v[212:219], v[94:97], v210, v210 op_sel_hi:[0,0,0]
	v_mfma_scale_f32_16x16x128_f8f6f4 v[90:93], v[10:17], v[212:219], v[90:93], v210, v210 op_sel_hi:[0,0,0]
	v_mfma_scale_f32_16x16x128_f8f6f4 v[78:81], v[2:9], v[220:227], v[78:81], v210, v210 op_sel_hi:[0,0,0]
	v_mfma_scale_f32_16x16x128_f8f6f4 v[74:77], v[10:17], v[220:227], v[74:77], v210, v210 op_sel_hi:[0,0,0]
	v_mfma_scale_f32_16x16x128_f8f6f4 v[62:65], v[2:9], v[228:235], v[62:65], v210, v210 op_sel_hi:[0,0,0]
	v_mfma_scale_f32_16x16x128_f8f6f4 v[58:61], v[10:17], v[228:235], v[58:61], v210, v210 op_sel_hi:[0,0,0]
	v_mfma_scale_f32_16x16x128_f8f6f4 v[46:49], v[2:9], v[236:243], v[46:49], v210, v210 op_sel_hi:[0,0,0]
	v_mfma_scale_f32_16x16x128_f8f6f4 v[42:45], v[10:17], v[236:243], v[42:45], v210, v210 op_sel_hi:[0,0,0]
	s_nop 3
	v_mfma_scale_f32_16x16x128_f8f6f4 v[86:89], v[18:25], v[212:219], v[86:89], v210, v210 op_sel_hi:[0,0,0]
	v_mfma_scale_f32_16x16x128_f8f6f4 v[82:85], v[26:33], v[212:219], v[82:85], v210, v210 op_sel_hi:[0,0,0]
	v_mfma_scale_f32_16x16x128_f8f6f4 v[70:73], v[18:25], v[220:227], v[70:73], v210, v210 op_sel_hi:[0,0,0]
	v_mfma_scale_f32_16x16x128_f8f6f4 v[66:69], v[26:33], v[220:227], v[66:69], v210, v210 op_sel_hi:[0,0,0]
	v_mfma_scale_f32_16x16x128_f8f6f4 v[54:57], v[18:25], v[228:235], v[54:57], v210, v210 op_sel_hi:[0,0,0]
	v_mfma_scale_f32_16x16x128_f8f6f4 v[50:53], v[26:33], v[228:235], v[50:53], v210, v210 op_sel_hi:[0,0,0]
	v_mfma_scale_f32_16x16x128_f8f6f4 v[38:41], v[18:25], v[236:243], v[38:41], v210, v210 op_sel_hi:[0,0,0]
	v_mfma_scale_f32_16x16x128_f8f6f4 v[34:37], v[26:33], v[236:243], v[34:37], v210, v210 op_sel_hi:[0,0,0]
	s_barrier
	s_add_i32 s21, s21, 2
	s_add_u32 s5, s5, 0x10000
	s_addc_u32 s19, s19, 0
	s_add_u32 s26, s26, 0x10000
	s_addc_u32 s27, s27, 0
	s_cmp_gt_u32 s21, 13
	s_cbranch_scc0 .LBB0_372
	s_branch .Lfx_9967
; #define PG8_STAGE(bufoff, gbase, voff) do { _Pragma("unroll") for (int _i = 0; _i < 2; ++_i) \
;         __builtin_amdgcn_global_load_lds((const unsigned*)((const char*)(gbase) + (voff)[_i]), (PG8_LAS unsigned*)(lds + (bufoff) + ldsw + _i * 8192), 16, 0, 0); } while (0)
; #define PG8_WAIT_V(n) asm volatile("s_waitcnt vmcnt(" #n ")" ::: "memory")
; #define PG8_WAIT_L(n) asm volatile("s_waitcnt lgkmcnt(" #n ")" ::: "memory")
; #define PG8_BAR __builtin_amdgcn_s_barrier()
; #define PG8_SCHED __builtin_amdgcn_sched_barrier(0)
; template <class Epi, class Sched, bool ALIGN_EPI = true, bool F8 = false>
; __device__ __forceinline__ void gemm_phase(PG8_LAS unsigned char* lds, const Sched& S, const Epi& E) {
;     ...
;             PG8_LDB(B0, 0, 0); PG8_LDB(B1, 0, 1); PG8_SCHED; PG8_LDA(At, 0, 0); PG8_STAGE(PG8_SA(1, 1), a1, voffA[1]);
;             PG8_WAIT_V(8); PG8_WAIT_L(0); PG8_BAR; PG8_MMA(0, 0, At, B0); PG8_MMA(0, 1, At, B1); PG8_BAR; PG8_SCHED;
;             PG8_LDA(At, 0, 1); PG8_STAGE(PG8_SB(0, 0), b2, voffB[0]); PG8_STAGE(PG8_SB(0, 1), b2, voffB[1]); PG8_STAGE(PG8_SA(0, 0), a2, vA2[0]);
;             PG8_WAIT_V(8); PG8_WAIT_L(0); PG8_BAR; PG8_MMA(1, 0, At, B0); PG8_MMA(1, 1, At, B1); PG8_BAR; PG8_SCHED;
;             PG8_LDB(B0, 1, 0); PG8_LDB(B1, 1, 1); PG8_SCHED; PG8_LDA(At, 1, 0); PG8_STAGE(PG8_SA(0, 1), a2, vA2[1]);
;             PG8_WAIT_V(8); PG8_WAIT_L(0); PG8_BAR; PG8_MMA(0, 0, At, B0); PG8_MMA(0, 1, At, B1); PG8_BAR; PG8_SCHED;
;             PG8_LDA(At, 1, 1); PG8_STAGE(PG8_SB(1, 0), b3, voffB[0]); PG8_STAGE(PG8_SB(1, 1), b3, voffB[1]); PG8_STAGE(PG8_SA(1, 0), a3, vA2[0]);
;             PG8_WAIT_V(8); PG8_WAIT_L(0); PG8_BAR; PG8_MMA(1, 0, At, B0); PG8_MMA(1, 1, At, B1); PG8_BAR; PG8_SCHED;
.Lh1e_9967:
	s_setprio 2
.Lpk1_372:
	ds_read_b128 v[18:21], v207
	ds_read_b128 v[22:25], v207 offset:1024
	ds_read_b128 v[26:29], v207 offset:2048
	ds_read_b128 v[30:33], v207 offset:3072
	ds_read_b128 v[2:5], v208
	ds_read_b128 v[6:9], v208 offset:1024
	ds_read_b128 v[10:13], v208 offset:2048
	ds_read_b128 v[14:17], v208 offset:3072
	s_add_u32 s28, s26, 0x8000
	s_addc_u32 s29, s27, 0
	s_cmp_eq_u32 s21, 12
	s_cselect_b32 s40, s22, s28
	s_cselect_b32 s41, s23, s29
	s_cselect_b32 s30, s24, s5
	s_cselect_b32 s31, s25, s19
	s_add_u32 s28, s40, 0x8000
	s_addc_u32 s29, s41, 0
	v_lshl_add_u64 v[244:245], s[26:27], 0, v[190:191]
	s_add_i32 m0, s46, 0xc000
	ds_read_b128 v[212:215], v209
	ds_read_b128 v[216:219], v209 offset:1024
	ds_read_b128 v[220:223], v209 offset:2048
	ds_read_b128 v[224:227], v209 offset:3072
	ds_read_b128 v[228:231], v209 offset:4096
	ds_read_b128 v[232:235], v209 offset:5120
	ds_read_b128 v[236:239], v209 offset:6144
	ds_read_b128 v[240:243], v209 offset:7168
	global_load_lds_dwordx4 v[244:245], off
	v_lshl_add_u64 v[244:245], s[26:27], 0, v[188:189]
	s_add_i32 m0, s46, 0xe000
	s_nop 0
	global_load_lds_dwordx4 v[244:245], off
	s_waitcnt vmcnt(8)
	s_waitcnt lgkmcnt(0)
	s_barrier
	v_mfma_scale_f32_16x16x128_f8f6f4 v[158:161], v[18:25], v[212:219], 0, v210, v210 op_sel_hi:[0,0,0]
	v_mfma_scale_f32_16x16x128_f8f6f4 v[154:157], v[26:33], v[212:219], 0, v210, v210 op_sel_hi:[0,0,0]
	v_mfma_scale_f32_16x16x128_f8f6f4 v[142:145], v[18:25], v[220:227], 0, v210, v210 op_sel_hi:[0,0,0]
	v_mfma_scale_f32_16x16x128_f8f6f4 v[138:141], v[26:33], v[220:227], 0, v210, v210 op_sel_hi:[0,0,0]
	v_mfma_scale_f32_16x16x128_f8f6f4 v[126:129], v[18:25], v[228:235], 0, v210, v210 op_sel_hi:[0,0,0]
	v_mfma_scale_f32_16x16x128_f8f6f4 v[122:125], v[26:33], v[228:235], 0, v210, v210 op_sel_hi:[0,0,0]
	v_mfma_scale_f32_16x16x128_f8f6f4 v[110:113], v[18:25], v[236:243], 0, v210, v210 op_sel_hi:[0,0,0]
	v_mfma_scale_f32_16x16x128_f8f6f4 v[106:109], v[26:33], v[236:243], 0, v210, v210 op_sel_hi:[0,0,0]
	s_nop 3
	v_mfma_scale_f32_16x16x128_f8f6f4 v[150:153], v[2:9], v[212:219], 0, v210, v210 op_sel_hi:[0,0,0]
	v_mfma_scale_f32_16x16x128_f8f6f4 v[146:149], v[10:17], v[212:219], 0, v210, v210 op_sel_hi:[0,0,0]
	v_mfma_scale_f32_16x16x128_f8f6f4 v[134:137], v[2:9], v[220:227], 0, v210, v210 op_sel_hi:[0,0,0]
	v_mfma_scale_f32_16x16x128_f8f6f4 v[130:133], v[10:17], v[220:227], 0, v210, v210 op_sel_hi:[0,0,0]
	v_mfma_scale_f32_16x16x128_f8f6f4 v[118:121], v[2:9], v[228:235], 0, v210, v210 op_sel_hi:[0,0,0]
	v_mfma_scale_f32_16x16x128_f8f6f4 v[114:117], v[10:17], v[228:235], 0, v210, v210 op_sel_hi:[0,0,0]
	v_mfma_scale_f32_16x16x128_f8f6f4 v[102:105], v[2:9], v[236:243], 0, v210, v210 op_sel_hi:[0,0,0]
	v_mfma_scale_f32_16x16x128_f8f6f4 v[98:101], v[10:17], v[236:243], 0, v210, v210 op_sel_hi:[0,0,0]
	s_add_i32 s67, s62, s45
	v_lshl_add_u64 v[244:245], s[30:31], 0, v[164:165]
	s_mov_b32 m0, s67
	ds_read_b128 v[212:215], v209 offset:16384
	ds_read_b128 v[216:219], v209 offset:17408
	ds_read_b128 v[220:223], v209 offset:18432
	ds_read_b128 v[224:227], v209 offset:19456
	ds_read_b128 v[228:231], v209 offset:20480
	ds_read_b128 v[232:235], v209 offset:21504
	ds_read_b128 v[236:239], v209 offset:22528
	ds_read_b128 v[240:243], v209 offset:23552
	global_load_lds_dwordx4 v[244:245], off
	v_lshl_add_u64 v[246:247], s[30:31], 0, v[166:167]
	s_add_i32 m0, s67, 0x2000
	s_add_i32 s67, s63, s45
	global_load_lds_dwordx4 v[246:247], off
	v_lshl_add_u64 v[244:245], v[244:245], 0, s[8:9]
	s_mov_b32 m0, s67
	s_nop 0
	global_load_lds_dwordx4 v[244:245], off
	v_lshl_add_u64 v[244:245], v[246:247], 0, s[8:9]
	s_add_i32 m0, s67, 0x2000
	s_nop 0
	global_load_lds_dwordx4 v[244:245], off
	v_lshl_add_u64 v[244:245], s[40:41], 0, v[174:175]
	s_mov_b32 m0, s46
	s_nop 0
	global_load_lds_dwordx4 v[244:245], off
	v_lshl_add_u64 v[244:245], s[40:41], 0, v[176:177]
	s_mov_b32 m0, s47
	s_nop 0
	global_load_lds_dwordx4 v[244:245], off
	s_waitcnt vmcnt(8)
	s_waitcnt lgkmcnt(0)
	s_barrier
	v_mfma_scale_f32_16x16x128_f8f6f4 v[94:97], v[18:25], v[212:219], 0, v210, v210 op_sel_hi:[0,0,0]
	v_mfma_scale_f32_16x16x128_f8f6f4 v[90:93], v[26:33], v[212:219], 0, v210, v210 op_sel_hi:[0,0,0]
	v_mfma_scale_f32_16x16x128_f8f6f4 v[78:81], v[18:25], v[220:227], 0, v210, v210 op_sel_hi:[0,0,0]
	v_mfma_scale_f32_16x16x128_f8f6f4 v[74:77], v[26:33], v[220:227], 0, v210, v210 op_sel_hi:[0,0,0]
	v_mfma_scale_f32_16x16x128_f8f6f4 v[62:65], v[18:25], v[228:235], 0, v210, v210 op_sel_hi:[0,0,0]
	v_mfma_scale_f32_16x16x128_f8f6f4 v[58:61], v[26:33], v[228:235], 0, v210, v210 op_sel_hi:[0,0,0]
	v_mfma_scale_f32_16x16x128_f8f6f4 v[46:49], v[18:25], v[236:243], 0, v210, v210 op_sel_hi:[0,0,0]
	v_mfma_scale_f32_16x16x128_f8f6f4 v[42:45], v[26:33], v[236:243], 0, v210, v210 op_sel_hi:[0,0,0]
	s_nop 3
	v_mfma_scale_f32_16x16x128_f8f6f4 v[86:89], v[2:9], v[212:219], 0, v210, v210 op_sel_hi:[0,0,0]
	v_mfma_scale_f32_16x16x128_f8f6f4 v[82:85], v[10:17], v[212:219], 0, v210, v210 op_sel_hi:[0,0,0]
	v_mfma_scale_f32_16x16x128_f8f6f4 v[70:73], v[2:9], v[220:227], 0, v210, v210 op_sel_hi:[0,0,0]
	v_mfma_scale_f32_16x16x128_f8f6f4 v[66:69], v[10:17], v[220:227], 0, v210, v210 op_sel_hi:[0,0,0]
	v_mfma_scale_f32_16x16x128_f8f6f4 v[54:57], v[2:9], v[228:235], 0, v210, v210 op_sel_hi:[0,0,0]
	v_mfma_scale_f32_16x16x128_f8f6f4 v[50:53], v[10:17], v[228:235], 0, v210, v210 op_sel_hi:[0,0,0]
	v_mfma_scale_f32_16x16x128_f8f6f4 v[38:41], v[2:9], v[236:243], 0, v210, v210 op_sel_hi:[0,0,0]
	v_mfma_scale_f32_16x16x128_f8f6f4 v[34:37], v[10:17], v[236:243], 0, v210, v210 op_sel_hi:[0,0,0]
	s_add_i32 s67, 0, 0x18000
	s_add_i32 s68, 0, 0x1c000
	v_add_u32_e32 v14, s67, v202
	v_add_u32_e32 v30, s68, v202
	ds_read_b128 v[2:5], v14
	ds_read_b128 v[6:9], v14 offset:1024
	ds_read_b128 v[10:13], v14 offset:2048
	ds_read_b128 v[14:17], v14 offset:3072
	ds_read_b128 v[18:21], v30
	ds_read_b128 v[22:25], v30 offset:1024
	ds_read_b128 v[26:29], v30 offset:2048
	ds_read_b128 v[30:33], v30 offset:3072
	s_mov_b32 m0, s48
	v_lshl_add_u64 v[244:245], s[40:41], 0, v[178:179]
	ds_read_b128 v[212:215], v209 offset:32768
	ds_read_b128 v[216:219], v209 offset:33792
	ds_read_b128 v[220:223], v209 offset:34816
	ds_read_b128 v[224:227], v209 offset:35840
	ds_read_b128 v[228:231], v209 offset:36864
	ds_read_b128 v[232:235], v209 offset:37888
	ds_read_b128 v[236:239], v209 offset:38912
	ds_read_b128 v[240:243], v209 offset:39936
	global_load_lds_dwordx4 v[244:245], off
	v_lshl_add_u64 v[244:245], s[40:41], 0, v[180:181]
	s_mov_b32 m0, s49
	s_nop 0
	global_load_lds_dwordx4 v[244:245], off
	s_waitcnt vmcnt(8)
	s_waitcnt lgkmcnt(0)
	s_barrier
; #define PG8_STAGE(bufoff, gbase, voff) do { _Pragma("unroll") for (int _i = 0; _i < 2; ++_i) \
;         __builtin_amdgcn_global_load_lds((const unsigned*)((const char*)(gbase) + (voff)[_i]), (PG8_LAS unsigned*)(lds + (bufoff) + ldsw + _i * 8192), 16, 0, 0); } while (0)
; #define PG8_WAIT_V(n) asm volatile("s_waitcnt vmcnt(" #n ")" ::: "memory")
; #define PG8_WAIT_L(n) asm volatile("s_waitcnt lgkmcnt(" #n ")" ::: "memory")
; #define PG8_BAR __builtin_amdgcn_s_barrier()
; #define PG8_SCHED __builtin_amdgcn_sched_barrier(0)
; template <class Epi, class Sched, bool ALIGN_EPI = true, bool F8 = false>
; __device__ __forceinline__ void gemm_phase(PG8_LAS unsigned char* lds, const Sched& S, const Epi& E) {
;     ...
;             PG8_LDB(B0, 0, 0); PG8_LDB(B1, 0, 1); PG8_SCHED; PG8_LDA(At, 0, 0); PG8_STAGE(PG8_SA(1, 1), a1, voffA[1]);
;             PG8_WAIT_V(8); PG8_WAIT_L(0); PG8_BAR; PG8_MMA(0, 0, At, B0); PG8_MMA(0, 1, At, B1); PG8_BAR; PG8_SCHED;
;             PG8_LDA(At, 0, 1); PG8_STAGE(PG8_SB(0, 0), b2, voffB[0]); PG8_STAGE(PG8_SB(0, 1), b2, voffB[1]); PG8_STAGE(PG8_SA(0, 0), a2, vA2[0]);
;             PG8_WAIT_V(8); PG8_WAIT_L(0); PG8_BAR; PG8_MMA(1, 0, At, B0); PG8_MMA(1, 1, At, B1); PG8_BAR; PG8_SCHED;
;             PG8_LDB(B0, 1, 0); PG8_LDB(B1, 1, 1); PG8_SCHED; PG8_LDA(At, 1, 0); PG8_STAGE(PG8_SA(0, 1), a2, vA2[1]);
;             PG8_WAIT_V(8); PG8_WAIT_L(0); PG8_BAR; PG8_MMA(0, 0, At, B0); PG8_MMA(0, 1, At, B1); PG8_BAR; PG8_SCHED;
;             PG8_LDA(At, 1, 1); PG8_STAGE(PG8_SB(1, 0), b3, voffB[0]); PG8_STAGE(PG8_SB(1, 1), b3, voffB[1]); PG8_STAGE(PG8_SA(1, 0), a3, vA2[0]);
;             PG8_WAIT_V(8); PG8_WAIT_L(0); PG8_BAR; PG8_MMA(1, 0, At, B0); PG8_MMA(1, 1, At, B1); PG8_BAR; PG8_SCHED;
	v_mfma_scale_f32_16x16x128_f8f6f4 v[158:161], v[2:9], v[212:219], v[158:161], v210, v210 op_sel_hi:[0,0,0]
	v_mfma_scale_f32_16x16x128_f8f6f4 v[154:157], v[10:17], v[212:219], v[154:157], v210, v210 op_sel_hi:[0,0,0]
	v_mfma_scale_f32_16x16x128_f8f6f4 v[142:145], v[2:9], v[220:227], v[142:145], v210, v210 op_sel_hi:[0,0,0]
	v_mfma_scale_f32_16x16x128_f8f6f4 v[138:141], v[10:17], v[220:227], v[138:141], v210, v210 op_sel_hi:[0,0,0]
	v_mfma_scale_f32_16x16x128_f8f6f4 v[126:129], v[2:9], v[228:235], v[126:129], v210, v210 op_sel_hi:[0,0,0]
	v_mfma_scale_f32_16x16x128_f8f6f4 v[122:125], v[10:17], v[228:235], v[122:125], v210, v210 op_sel_hi:[0,0,0]
	v_mfma_scale_f32_16x16x128_f8f6f4 v[110:113], v[2:9], v[236:243], v[110:113], v210, v210 op_sel_hi:[0,0,0]
	v_mfma_scale_f32_16x16x128_f8f6f4 v[106:109], v[10:17], v[236:243], v[106:109], v210, v210 op_sel_hi:[0,0,0]
	s_nop 3
	v_mfma_scale_f32_16x16x128_f8f6f4 v[150:153], v[18:25], v[212:219], v[150:153], v210, v210 op_sel_hi:[0,0,0]
	v_mfma_scale_f32_16x16x128_f8f6f4 v[146:149], v[26:33], v[212:219], v[146:149], v210, v210 op_sel_hi:[0,0,0]
	v_mfma_scale_f32_16x16x128_f8f6f4 v[134:137], v[18:25], v[220:227], v[134:137], v210, v210 op_sel_hi:[0,0,0]
	v_mfma_scale_f32_16x16x128_f8f6f4 v[130:133], v[26:33], v[220:227], v[130:133], v210, v210 op_sel_hi:[0,0,0]
	v_mfma_scale_f32_16x16x128_f8f6f4 v[118:121], v[18:25], v[228:235], v[118:121], v210, v210 op_sel_hi:[0,0,0]
	v_mfma_scale_f32_16x16x128_f8f6f4 v[114:117], v[26:33], v[228:235], v[114:117], v210, v210 op_sel_hi:[0,0,0]
	v_mfma_scale_f32_16x16x128_f8f6f4 v[102:105], v[18:25], v[236:243], v[102:105], v210, v210 op_sel_hi:[0,0,0]
	v_mfma_scale_f32_16x16x128_f8f6f4 v[98:101], v[26:33], v[236:243], v[98:101], v210, v210 op_sel_hi:[0,0,0]
	s_add_u32 s30, s30, 0x8000
	s_addc_u32 s31, s31, 0
	s_add_i32 s40, s67, s45
	v_lshl_add_u64 v[244:245], s[30:31], 0, v[164:165]
	s_mov_b32 m0, s40
	ds_read_b128 v[212:215], v209 offset:49152
	ds_read_b128 v[216:219], v209 offset:50176
	ds_read_b128 v[220:223], v209 offset:51200
	ds_read_b128 v[224:227], v209 offset:52224
	ds_read_b128 v[228:231], v209 offset:53248
	ds_read_b128 v[232:235], v209 offset:54272
	ds_read_b128 v[236:239], v209 offset:55296
	ds_read_b128 v[240:243], v209 offset:56320
	global_load_lds_dwordx4 v[244:245], off
	v_lshl_add_u64 v[244:245], s[30:31], 0, v[166:167]
	s_add_i32 m0, s40, 0x2000
	s_add_i32 s40, s68, s45
	global_load_lds_dwordx4 v[244:245], off
	v_lshl_add_u64 v[244:245], s[30:31], 0, v[168:169]
	s_mov_b32 m0, s40
	s_nop 0
	global_load_lds_dwordx4 v[244:245], off
	v_lshl_add_u64 v[244:245], s[30:31], 0, v[172:173]
	s_add_i32 m0, s40, 0x2000
	s_nop 0
	global_load_lds_dwordx4 v[244:245], off
	v_lshl_add_u64 v[244:245], s[28:29], 0, v[174:175]
	s_mov_b32 m0, s52
	s_nop 0
	global_load_lds_dwordx4 v[244:245], off
	v_lshl_add_u64 v[244:245], s[28:29], 0, v[176:177]
	s_mov_b32 m0, s53
	s_nop 0
	global_load_lds_dwordx4 v[244:245], off
	s_waitcnt vmcnt(8)
	s_waitcnt lgkmcnt(0)
	s_barrier
	v_mfma_scale_f32_16x16x128_f8f6f4 v[94:97], v[2:9], v[212:219], v[94:97], v210, v210 op_sel_hi:[0,0,0]
	v_mfma_scale_f32_16x16x128_f8f6f4 v[90:93], v[10:17], v[212:219], v[90:93], v210, v210 op_sel_hi:[0,0,0]
	v_mfma_scale_f32_16x16x128_f8f6f4 v[78:81], v[2:9], v[220:227], v[78:81], v210, v210 op_sel_hi:[0,0,0]
	v_mfma_scale_f32_16x16x128_f8f6f4 v[74:77], v[10:17], v[220:227], v[74:77], v210, v210 op_sel_hi:[0,0,0]
	v_mfma_scale_f32_16x16x128_f8f6f4 v[62:65], v[2:9], v[228:235], v[62:65], v210, v210 op_sel_hi:[0,0,0]
	v_mfma_scale_f32_16x16x128_f8f6f4 v[58:61], v[10:17], v[228:235], v[58:61], v210, v210 op_sel_hi:[0,0,0]
	v_mfma_scale_f32_16x16x128_f8f6f4 v[46:49], v[2:9], v[236:243], v[46:49], v210, v210 op_sel_hi:[0,0,0]
	v_mfma_scale_f32_16x16x128_f8f6f4 v[42:45], v[10:17], v[236:243], v[42:45], v210, v210 op_sel_hi:[0,0,0]
	s_nop 3
	v_mfma_scale_f32_16x16x128_f8f6f4 v[86:89], v[18:25], v[212:219], v[86:89], v210, v210 op_sel_hi:[0,0,0]
	v_mfma_scale_f32_16x16x128_f8f6f4 v[82:85], v[26:33], v[212:219], v[82:85], v210, v210 op_sel_hi:[0,0,0]
	v_mfma_scale_f32_16x16x128_f8f6f4 v[70:73], v[18:25], v[220:227], v[70:73], v210, v210 op_sel_hi:[0,0,0]
	v_mfma_scale_f32_16x16x128_f8f6f4 v[66:69], v[26:33], v[220:227], v[66:69], v210, v210 op_sel_hi:[0,0,0]
	v_mfma_scale_f32_16x16x128_f8f6f4 v[54:57], v[18:25], v[228:235], v[54:57], v210, v210 op_sel_hi:[0,0,0]
	v_mfma_scale_f32_16x16x128_f8f6f4 v[50:53], v[26:33], v[228:235], v[50:53], v210, v210 op_sel_hi:[0,0,0]
	v_mfma_scale_f32_16x16x128_f8f6f4 v[38:41], v[18:25], v[236:243], v[38:41], v210, v210 op_sel_hi:[0,0,0]
	v_mfma_scale_f32_16x16x128_f8f6f4 v[34:37], v[26:33], v[236:243], v[34:37], v210, v210 op_sel_hi:[0,0,0]
	s_add_i32 s21, s21, 2
	s_add_u32 s5, s5, 0x10000
	s_addc_u32 s19, s19, 0
	s_add_u32 s26, s26, 0x10000
	s_addc_u32 s27, s27, 0
	s_cmp_gt_u32 s21, 13
	s_cbranch_scc0 .Lh1_372
	s_branch .Lfx_9967
; #define PG8_STAGE(bufoff, gbase, voff) do { _Pragma("unroll") for (int _i = 0; _i < 2; ++_i) \
;         __builtin_amdgcn_global_load_lds((const unsigned*)((const char*)(gbase) + (voff)[_i]), (PG8_LAS unsigned*)(lds + (bufoff) + ldsw + _i * 8192), 16, 0, 0); } while (0)
; #define PG8_WAIT_V(n) asm volatile("s_waitcnt vmcnt(" #n ")" ::: "memory")
; #define PG8_WAIT_L(n) asm volatile("s_waitcnt lgkmcnt(" #n ")" ::: "memory")
; #define PG8_BAR __builtin_amdgcn_s_barrier()
; #define PG8_SCHED __builtin_amdgcn_sched_barrier(0)
; template <class Epi, class Sched, bool ALIGN_EPI = true, bool F8 = false>
; __device__ __forceinline__ void gemm_phase(PG8_LAS unsigned char* lds, const Sched& S, const Epi& E) {
;     ...
;             PG8_LDB(B0, 0, 0); PG8_LDB(B1, 0, 1); PG8_SCHED; PG8_LDA(At, 0, 0); PG8_STAGE(PG8_SA(1, 1), a1, voffA[1]);
;             PG8_WAIT_V(8); PG8_WAIT_L(0); PG8_BAR; PG8_MMA(0, 0, At, B0); PG8_MMA(0, 1, At, B1); PG8_BAR; PG8_SCHED;
;             PG8_LDA(At, 0, 1); PG8_STAGE(PG8_SB(0, 0), b2, voffB[0]); PG8_STAGE(PG8_SB(0, 1), b2, voffB[1]); PG8_STAGE(PG8_SA(0, 0), a2, vA2[0]);
;             PG8_WAIT_V(8); PG8_WAIT_L(0); PG8_BAR; PG8_MMA(1, 0, At, B0); PG8_MMA(1, 1, At, B1); PG8_BAR; PG8_SCHED;
;             PG8_LDB(B0, 1, 0); PG8_LDB(B1, 1, 1); PG8_SCHED; PG8_LDA(At, 1, 0); PG8_STAGE(PG8_SA(0, 1), a2, vA2[1]);
;             PG8_WAIT_V(8); PG8_WAIT_L(0); PG8_BAR; PG8_MMA(0, 0, At, B0); PG8_MMA(0, 1, At, B1); PG8_BAR; PG8_SCHED;
;             PG8_LDA(At, 1, 1); PG8_STAGE(PG8_SB(1, 0), b3, voffB[0]); PG8_STAGE(PG8_SB(1, 1), b3, voffB[1]); PG8_STAGE(PG8_SA(1, 0), a3, vA2[0]);
;             PG8_WAIT_V(8); PG8_WAIT_L(0); PG8_BAR; PG8_MMA(1, 0, At, B0); PG8_MMA(1, 1, At, B1); PG8_BAR; PG8_SCHED;
.Lh1_372:
	ds_read_b128 v[18:21], v207
	ds_read_b128 v[22:25], v207 offset:1024
	ds_read_b128 v[26:29], v207 offset:2048
	ds_read_b128 v[30:33], v207 offset:3072
	ds_read_b128 v[2:5], v208
	ds_read_b128 v[6:9], v208 offset:1024
	ds_read_b128 v[10:13], v208 offset:2048
	ds_read_b128 v[14:17], v208 offset:3072
	s_add_u32 s28, s26, 0x8000
	s_addc_u32 s29, s27, 0
	s_cmp_eq_u32 s21, 12
	s_cselect_b32 s40, s22, s28
	s_cselect_b32 s41, s23, s29
	s_cselect_b32 s30, s24, s5
	s_cselect_b32 s31, s25, s19
	s_add_u32 s28, s40, 0x8000
	s_addc_u32 s29, s41, 0
	v_lshl_add_u64 v[244:245], s[26:27], 0, v[190:191]
	s_add_i32 m0, s46, 0xc000
	ds_read_b128 v[212:215], v209
	ds_read_b128 v[216:219], v209 offset:1024
	ds_read_b128 v[220:223], v209 offset:2048
	ds_read_b128 v[224:227], v209 offset:3072
	ds_read_b128 v[228:231], v209 offset:4096
	ds_read_b128 v[232:235], v209 offset:5120
	ds_read_b128 v[236:239], v209 offset:6144
	ds_read_b128 v[240:243], v209 offset:7168
	global_load_lds_dwordx4 v[244:245], off
	v_lshl_add_u64 v[244:245], s[26:27], 0, v[188:189]
	s_add_i32 m0, s46, 0xe000
	s_nop 0
	global_load_lds_dwordx4 v[244:245], off
	s_waitcnt vmcnt(8)
	s_waitcnt lgkmcnt(0)
	s_barrier
	v_mfma_scale_f32_16x16x128_f8f6f4 v[158:161], v[18:25], v[212:219], v[158:161], v210, v210 op_sel_hi:[0,0,0]
	v_mfma_scale_f32_16x16x128_f8f6f4 v[154:157], v[26:33], v[212:219], v[154:157], v210, v210 op_sel_hi:[0,0,0]
	v_mfma_scale_f32_16x16x128_f8f6f4 v[142:145], v[18:25], v[220:227], v[142:145], v210, v210 op_sel_hi:[0,0,0]
	v_mfma_scale_f32_16x16x128_f8f6f4 v[138:141], v[26:33], v[220:227], v[138:141], v210, v210 op_sel_hi:[0,0,0]
	v_mfma_scale_f32_16x16x128_f8f6f4 v[126:129], v[18:25], v[228:235], v[126:129], v210, v210 op_sel_hi:[0,0,0]
	v_mfma_scale_f32_16x16x128_f8f6f4 v[122:125], v[26:33], v[228:235], v[122:125], v210, v210 op_sel_hi:[0,0,0]
	v_mfma_scale_f32_16x16x128_f8f6f4 v[110:113], v[18:25], v[236:243], v[110:113], v210, v210 op_sel_hi:[0,0,0]
	v_mfma_scale_f32_16x16x128_f8f6f4 v[106:109], v[26:33], v[236:243], v[106:109], v210, v210 op_sel_hi:[0,0,0]
	s_nop 3
	v_mfma_scale_f32_16x16x128_f8f6f4 v[150:153], v[2:9], v[212:219], v[150:153], v210, v210 op_sel_hi:[0,0,0]
	v_mfma_scale_f32_16x16x128_f8f6f4 v[146:149], v[10:17], v[212:219], v[146:149], v210, v210 op_sel_hi:[0,0,0]
	v_mfma_scale_f32_16x16x128_f8f6f4 v[134:137], v[2:9], v[220:227], v[134:137], v210, v210 op_sel_hi:[0,0,0]
	v_mfma_scale_f32_16x16x128_f8f6f4 v[130:133], v[10:17], v[220:227], v[130:133], v210, v210 op_sel_hi:[0,0,0]
	v_mfma_scale_f32_16x16x128_f8f6f4 v[118:121], v[2:9], v[228:235], v[118:121], v210, v210 op_sel_hi:[0,0,0]
	v_mfma_scale_f32_16x16x128_f8f6f4 v[114:117], v[10:17], v[228:235], v[114:117], v210, v210 op_sel_hi:[0,0,0]
	v_mfma_scale_f32_16x16x128_f8f6f4 v[102:105], v[2:9], v[236:243], v[102:105], v210, v210 op_sel_hi:[0,0,0]
	v_mfma_scale_f32_16x16x128_f8f6f4 v[98:101], v[10:17], v[236:243], v[98:101], v210, v210 op_sel_hi:[0,0,0]
	s_add_i32 s67, s62, s45
	v_lshl_add_u64 v[244:245], s[30:31], 0, v[164:165]
	s_mov_b32 m0, s67
	ds_read_b128 v[212:215], v209 offset:16384
	ds_read_b128 v[216:219], v209 offset:17408
	ds_read_b128 v[220:223], v209 offset:18432
	ds_read_b128 v[224:227], v209 offset:19456
	ds_read_b128 v[228:231], v209 offset:20480
	ds_read_b128 v[232:235], v209 offset:21504
	ds_read_b128 v[236:239], v209 offset:22528
	ds_read_b128 v[240:243], v209 offset:23552
	global_load_lds_dwordx4 v[244:245], off
	v_lshl_add_u64 v[246:247], s[30:31], 0, v[166:167]
	s_add_i32 m0, s67, 0x2000
	s_add_i32 s67, s63, s45
	global_load_lds_dwordx4 v[246:247], off
	v_lshl_add_u64 v[244:245], v[244:245], 0, s[8:9]
	s_mov_b32 m0, s67
	s_nop 0
	global_load_lds_dwordx4 v[244:245], off
	v_lshl_add_u64 v[244:245], v[246:247], 0, s[8:9]
	s_add_i32 m0, s67, 0x2000
	s_nop 0
	global_load_lds_dwordx4 v[244:245], off
	v_lshl_add_u64 v[244:245], s[40:41], 0, v[174:175]
	s_mov_b32 m0, s46
	s_nop 0
	global_load_lds_dwordx4 v[244:245], off
	v_lshl_add_u64 v[244:245], s[40:41], 0, v[176:177]
	s_mov_b32 m0, s47
	s_nop 0
	global_load_lds_dwordx4 v[244:245], off
	s_waitcnt vmcnt(8)
	s_waitcnt lgkmcnt(0)
	s_barrier
	v_mfma_scale_f32_16x16x128_f8f6f4 v[94:97], v[18:25], v[212:219], v[94:97], v210, v210 op_sel_hi:[0,0,0]
	v_mfma_scale_f32_16x16x128_f8f6f4 v[90:93], v[26:33], v[212:219], v[90:93], v210, v210 op_sel_hi:[0,0,0]
	v_mfma_scale_f32_16x16x128_f8f6f4 v[78:81], v[18:25], v[220:227], v[78:81], v210, v210 op_sel_hi:[0,0,0]
	v_mfma_scale_f32_16x16x128_f8f6f4 v[74:77], v[26:33], v[220:227], v[74:77], v210, v210 op_sel_hi:[0,0,0]
	v_mfma_scale_f32_16x16x128_f8f6f4 v[62:65], v[18:25], v[228:235], v[62:65], v210, v210 op_sel_hi:[0,0,0]
	v_mfma_scale_f32_16x16x128_f8f6f4 v[58:61], v[26:33], v[228:235], v[58:61], v210, v210 op_sel_hi:[0,0,0]
	v_mfma_scale_f32_16x16x128_f8f6f4 v[46:49], v[18:25], v[236:243], v[46:49], v210, v210 op_sel_hi:[0,0,0]
	v_mfma_scale_f32_16x16x128_f8f6f4 v[42:45], v[26:33], v[236:243], v[42:45], v210, v210 op_sel_hi:[0,0,0]
	s_nop 3
	v_mfma_scale_f32_16x16x128_f8f6f4 v[86:89], v[2:9], v[212:219], v[86:89], v210, v210 op_sel_hi:[0,0,0]
	v_mfma_scale_f32_16x16x128_f8f6f4 v[82:85], v[10:17], v[212:219], v[82:85], v210, v210 op_sel_hi:[0,0,0]
	v_mfma_scale_f32_16x16x128_f8f6f4 v[70:73], v[2:9], v[220:227], v[70:73], v210, v210 op_sel_hi:[0,0,0]
	v_mfma_scale_f32_16x16x128_f8f6f4 v[66:69], v[10:17], v[220:227], v[66:69], v210, v210 op_sel_hi:[0,0,0]
	v_mfma_scale_f32_16x16x128_f8f6f4 v[54:57], v[2:9], v[228:235], v[54:57], v210, v210 op_sel_hi:[0,0,0]
	v_mfma_scale_f32_16x16x128_f8f6f4 v[50:53], v[10:17], v[228:235], v[50:53], v210, v210 op_sel_hi:[0,0,0]
	v_mfma_scale_f32_16x16x128_f8f6f4 v[38:41], v[2:9], v[236:243], v[38:41], v210, v210 op_sel_hi:[0,0,0]
	v_mfma_scale_f32_16x16x128_f8f6f4 v[34:37], v[10:17], v[236:243], v[34:37], v210, v210 op_sel_hi:[0,0,0]
	s_add_i32 s67, 0, 0x18000
	s_add_i32 s68, 0, 0x1c000
	v_add_u32_e32 v14, s67, v202
	v_add_u32_e32 v30, s68, v202
	ds_read_b128 v[2:5], v14
	ds_read_b128 v[6:9], v14 offset:1024
	ds_read_b128 v[10:13], v14 offset:2048
	ds_read_b128 v[14:17], v14 offset:3072
	ds_read_b128 v[18:21], v30
	ds_read_b128 v[22:25], v30 offset:1024
	ds_read_b128 v[26:29], v30 offset:2048
	ds_read_b128 v[30:33], v30 offset:3072
	s_mov_b32 m0, s48
	v_lshl_add_u64 v[244:245], s[40:41], 0, v[178:179]
	ds_read_b128 v[212:215], v209 offset:32768
	ds_read_b128 v[216:219], v209 offset:33792
	ds_read_b128 v[220:223], v209 offset:34816
	ds_read_b128 v[224:227], v209 offset:35840
	ds_read_b128 v[228:231], v209 offset:36864
	ds_read_b128 v[232:235], v209 offset:37888
	ds_read_b128 v[236:239], v209 offset:38912
	ds_read_b128 v[240:243], v209 offset:39936
	global_load_lds_dwordx4 v[244:245], off
	v_lshl_add_u64 v[244:245], s[40:41], 0, v[180:181]
	s_mov_b32 m0, s49
	s_nop 0
	global_load_lds_dwordx4 v[244:245], off
	s_waitcnt vmcnt(8)
	s_waitcnt lgkmcnt(0)
	s_barrier
; #define PG8_STAGE(bufoff, gbase, voff) do { _Pragma("unroll") for (int _i = 0; _i < 2; ++_i) \
;         __builtin_amdgcn_global_load_lds((const unsigned*)((const char*)(gbase) + (voff)[_i]), (PG8_LAS unsigned*)(lds + (bufoff) + ldsw + _i * 8192), 16, 0, 0); } while (0)
; #define PG8_WAIT_V(n) asm volatile("s_waitcnt vmcnt(" #n ")" ::: "memory")
; #define PG8_WAIT_L(n) asm volatile("s_waitcnt lgkmcnt(" #n ")" ::: "memory")
; #define PG8_BAR __builtin_amdgcn_s_barrier()
; #define PG8_SCHED __builtin_amdgcn_sched_barrier(0)
; template <class Epi, class Sched, bool ALIGN_EPI = true, bool F8 = false>
; __device__ __forceinline__ void gemm_phase(PG8_LAS unsigned char* lds, const Sched& S, const Epi& E) {
;     ...
;             PG8_LDB(B0, 0, 0); PG8_LDB(B1, 0, 1); PG8_SCHED; PG8_LDA(At, 0, 0); PG8_STAGE(PG8_SA(1, 1), a1, voffA[1]);
;             PG8_WAIT_V(8); PG8_WAIT_L(0); PG8_BAR; PG8_MMA(0, 0, At, B0); PG8_MMA(0, 1, At, B1); PG8_BAR; PG8_SCHED;
;             PG8_LDA(At, 0, 1); PG8_STAGE(PG8_SB(0, 0), b2, voffB[0]); PG8_STAGE(PG8_SB(0, 1), b2, voffB[1]); PG8_STAGE(PG8_SA(0, 0), a2, vA2[0]);
;             PG8_WAIT_V(8); PG8_WAIT_L(0); PG8_BAR; PG8_MMA(1, 0, At, B0); PG8_MMA(1, 1, At, B1); PG8_BAR; PG8_SCHED;
;             PG8_LDB(B0, 1, 0); PG8_LDB(B1, 1, 1); PG8_SCHED; PG8_LDA(At, 1, 0); PG8_STAGE(PG8_SA(0, 1), a2, vA2[1]);
;             PG8_WAIT_V(8); PG8_WAIT_L(0); PG8_BAR; PG8_MMA(0, 0, At, B0); PG8_MMA(0, 1, At, B1); PG8_BAR; PG8_SCHED;
;             PG8_LDA(At, 1, 1); PG8_STAGE(PG8_SB(1, 0), b3, voffB[0]); PG8_STAGE(PG8_SB(1, 1), b3, voffB[1]); PG8_STAGE(PG8_SA(1, 0), a3, vA2[0]);
;             PG8_WAIT_V(8); PG8_WAIT_L(0); PG8_BAR; PG8_MMA(1, 0, At, B0); PG8_MMA(1, 1, At, B1); PG8_BAR; PG8_SCHED;
	v_mfma_scale_f32_16x16x128_f8f6f4 v[158:161], v[2:9], v[212:219], v[158:161], v210, v210 op_sel_hi:[0,0,0]
	v_mfma_scale_f32_16x16x128_f8f6f4 v[154:157], v[10:17], v[212:219], v[154:157], v210, v210 op_sel_hi:[0,0,0]
	v_mfma_scale_f32_16x16x128_f8f6f4 v[142:145], v[2:9], v[220:227], v[142:145], v210, v210 op_sel_hi:[0,0,0]
	v_mfma_scale_f32_16x16x128_f8f6f4 v[138:141], v[10:17], v[220:227], v[138:141], v210, v210 op_sel_hi:[0,0,0]
	v_mfma_scale_f32_16x16x128_f8f6f4 v[126:129], v[2:9], v[228:235], v[126:129], v210, v210 op_sel_hi:[0,0,0]
	v_mfma_scale_f32_16x16x128_f8f6f4 v[122:125], v[10:17], v[228:235], v[122:125], v210, v210 op_sel_hi:[0,0,0]
	v_mfma_scale_f32_16x16x128_f8f6f4 v[110:113], v[2:9], v[236:243], v[110:113], v210, v210 op_sel_hi:[0,0,0]
	v_mfma_scale_f32_16x16x128_f8f6f4 v[106:109], v[10:17], v[236:243], v[106:109], v210, v210 op_sel_hi:[0,0,0]
	s_nop 3
	v_mfma_scale_f32_16x16x128_f8f6f4 v[150:153], v[18:25], v[212:219], v[150:153], v210, v210 op_sel_hi:[0,0,0]
	v_mfma_scale_f32_16x16x128_f8f6f4 v[146:149], v[26:33], v[212:219], v[146:149], v210, v210 op_sel_hi:[0,0,0]
	v_mfma_scale_f32_16x16x128_f8f6f4 v[134:137], v[18:25], v[220:227], v[134:137], v210, v210 op_sel_hi:[0,0,0]
	v_mfma_scale_f32_16x16x128_f8f6f4 v[130:133], v[26:33], v[220:227], v[130:133], v210, v210 op_sel_hi:[0,0,0]
	v_mfma_scale_f32_16x16x128_f8f6f4 v[118:121], v[18:25], v[228:235], v[118:121], v210, v210 op_sel_hi:[0,0,0]
	v_mfma_scale_f32_16x16x128_f8f6f4 v[114:117], v[26:33], v[228:235], v[114:117], v210, v210 op_sel_hi:[0,0,0]
	v_mfma_scale_f32_16x16x128_f8f6f4 v[102:105], v[18:25], v[236:243], v[102:105], v210, v210 op_sel_hi:[0,0,0]
	v_mfma_scale_f32_16x16x128_f8f6f4 v[98:101], v[26:33], v[236:243], v[98:101], v210, v210 op_sel_hi:[0,0,0]
	s_add_u32 s30, s30, 0x8000
	s_addc_u32 s31, s31, 0
	s_add_i32 s40, s67, s45
	v_lshl_add_u64 v[244:245], s[30:31], 0, v[164:165]
	s_mov_b32 m0, s40
	ds_read_b128 v[212:215], v209 offset:49152
	ds_read_b128 v[216:219], v209 offset:50176
	ds_read_b128 v[220:223], v209 offset:51200
	ds_read_b128 v[224:227], v209 offset:52224
	ds_read_b128 v[228:231], v209 offset:53248
	ds_read_b128 v[232:235], v209 offset:54272
	ds_read_b128 v[236:239], v209 offset:55296
	ds_read_b128 v[240:243], v209 offset:56320
	global_load_lds_dwordx4 v[244:245], off
	v_lshl_add_u64 v[244:245], s[30:31], 0, v[166:167]
	s_add_i32 m0, s40, 0x2000
	s_add_i32 s40, s68, s45
	global_load_lds_dwordx4 v[244:245], off
	v_lshl_add_u64 v[244:245], s[30:31], 0, v[168:169]
	s_mov_b32 m0, s40
	s_nop 0
	global_load_lds_dwordx4 v[244:245], off
	v_lshl_add_u64 v[244:245], s[30:31], 0, v[172:173]
	s_add_i32 m0, s40, 0x2000
	s_nop 0
	global_load_lds_dwordx4 v[244:245], off
	v_lshl_add_u64 v[244:245], s[28:29], 0, v[174:175]
	s_mov_b32 m0, s52
	s_nop 0
	global_load_lds_dwordx4 v[244:245], off
	v_lshl_add_u64 v[244:245], s[28:29], 0, v[176:177]
	s_mov_b32 m0, s53
	s_nop 0
	global_load_lds_dwordx4 v[244:245], off
	s_waitcnt vmcnt(8)
	s_waitcnt lgkmcnt(0)
	s_barrier
	v_mfma_scale_f32_16x16x128_f8f6f4 v[94:97], v[2:9], v[212:219], v[94:97], v210, v210 op_sel_hi:[0,0,0]
	v_mfma_scale_f32_16x16x128_f8f6f4 v[90:93], v[10:17], v[212:219], v[90:93], v210, v210 op_sel_hi:[0,0,0]
	v_mfma_scale_f32_16x16x128_f8f6f4 v[78:81], v[2:9], v[220:227], v[78:81], v210, v210 op_sel_hi:[0,0,0]
	v_mfma_scale_f32_16x16x128_f8f6f4 v[74:77], v[10:17], v[220:227], v[74:77], v210, v210 op_sel_hi:[0,0,0]
	v_mfma_scale_f32_16x16x128_f8f6f4 v[62:65], v[2:9], v[228:235], v[62:65], v210, v210 op_sel_hi:[0,0,0]
	v_mfma_scale_f32_16x16x128_f8f6f4 v[58:61], v[10:17], v[228:235], v[58:61], v210, v210 op_sel_hi:[0,0,0]
	v_mfma_scale_f32_16x16x128_f8f6f4 v[46:49], v[2:9], v[236:243], v[46:49], v210, v210 op_sel_hi:[0,0,0]
	v_mfma_scale_f32_16x16x128_f8f6f4 v[42:45], v[10:17], v[236:243], v[42:45], v210, v210 op_sel_hi:[0,0,0]
	s_nop 3
	v_mfma_scale_f32_16x16x128_f8f6f4 v[86:89], v[18:25], v[212:219], v[86:89], v210, v210 op_sel_hi:[0,0,0]
	v_mfma_scale_f32_16x16x128_f8f6f4 v[82:85], v[26:33], v[212:219], v[82:85], v210, v210 op_sel_hi:[0,0,0]
	v_mfma_scale_f32_16x16x128_f8f6f4 v[70:73], v[18:25], v[220:227], v[70:73], v210, v210 op_sel_hi:[0,0,0]
	v_mfma_scale_f32_16x16x128_f8f6f4 v[66:69], v[26:33], v[220:227], v[66:69], v210, v210 op_sel_hi:[0,0,0]
	v_mfma_scale_f32_16x16x128_f8f6f4 v[54:57], v[18:25], v[228:235], v[54:57], v210, v210 op_sel_hi:[0,0,0]
	v_mfma_scale_f32_16x16x128_f8f6f4 v[50:53], v[26:33], v[228:235], v[50:53], v210, v210 op_sel_hi:[0,0,0]
	v_mfma_scale_f32_16x16x128_f8f6f4 v[38:41], v[18:25], v[236:243], v[38:41], v210, v210 op_sel_hi:[0,0,0]
	v_mfma_scale_f32_16x16x128_f8f6f4 v[34:37], v[26:33], v[236:243], v[34:37], v210, v210 op_sel_hi:[0,0,0]
	s_add_i32 s21, s21, 2
	s_add_u32 s5, s5, 0x10000
	s_addc_u32 s19, s19, 0
	s_add_u32 s26, s26, 0x10000
	s_addc_u32 s27, s27, 0
	s_cmp_gt_u32 s21, 13
	s_cbranch_scc0 .Lh1_372
.Lfx_9967:
	s_setprio 0
	s_and_b64 vcc, exec, s[14:15]
	s_cbranch_vccz .LBB0_375

; #define PG8_STAGE(bufoff, gbase, voff) do { _Pragma("unroll") for (int _i = 0; _i < 2; ++_i) \
;         __builtin_amdgcn_global_load_lds((const unsigned*)((const char*)(gbase) + (voff)[_i]), (PG8_LAS unsigned*)(lds + (bufoff) + ldsw + _i * 8192), 16, 0, 0); } while (0)
; #define PG8_WAIT_V(n) asm volatile("s_waitcnt vmcnt(" #n ")" ::: "memory")
; #define PG8_WAIT_L(n) asm volatile("s_waitcnt lgkmcnt(" #n ")" ::: "memory")
; #define PG8_BAR __builtin_amdgcn_s_barrier()
; #define PG8_SCHED __builtin_amdgcn_sched_barrier(0)
; template <class Epi, class Sched, bool ALIGN_EPI = true, bool F8 = false>
; __device__ __forceinline__ void gemm_phase(PG8_LAS unsigned char* lds, const Sched& S, const Epi& E) {
;     ...
;             PG8_LDB(B0, 0, 0); PG8_LDB(B1, 0, 1); PG8_SCHED; PG8_LDA(At, 0, 0); PG8_STAGE(PG8_SA(1, 1), a1, voffA[1]);
;             PG8_WAIT_V(8); PG8_WAIT_L(0); PG8_BAR; PG8_MMA(0, 0, At, B0); PG8_MMA(0, 1, At, B1); PG8_BAR; PG8_SCHED;
;             PG8_LDA(At, 0, 1); PG8_STAGE(PG8_SB(0, 0), b2, voffB[0]); PG8_STAGE(PG8_SB(0, 1), b2, voffB[1]); PG8_STAGE(PG8_SA(0, 0), a2, vA2[0]);
;             PG8_WAIT_V(8); PG8_WAIT_L(0); PG8_BAR; PG8_MMA(1, 0, At, B0); PG8_MMA(1, 1, At, B1); PG8_BAR; PG8_SCHED;
;             PG8_LDB(B0, 1, 0); PG8_LDB(B1, 1, 1); PG8_SCHED; PG8_LDA(At, 1, 0); PG8_STAGE(PG8_SA(0, 1), a2, vA2[1]);
;             PG8_WAIT_V(8); PG8_WAIT_L(0); PG8_BAR; PG8_MMA(0, 0, At, B0); PG8_MMA(0, 1, At, B1); PG8_BAR; PG8_SCHED;
;             PG8_LDA(At, 1, 1); PG8_STAGE(PG8_SB(1, 0), b3, voffB[0]); PG8_STAGE(PG8_SB(1, 1), b3, voffB[1]); PG8_STAGE(PG8_SA(1, 0), a3, vA2[0]);
;             PG8_WAIT_V(8); PG8_WAIT_L(0); PG8_BAR; PG8_MMA(1, 0, At, B0); PG8_MMA(1, 1, At, B1); PG8_BAR; PG8_SCHED;
.LBB0_427:
	s_add_u32 s17, s26, 0x10000
	s_addc_u32 s19, s27, 0
	s_add_u32 s24, s24, 0x8000
	s_addc_u32 s25, s25, 0
	s_mov_b32 s74, -2
	s_bitcmp1_b32 s3, 2
	s_cbranch_scc1 .Lh1e_11141
	s_setprio 1
.Lpk0_428:
	ds_read_b128 v[18:21], v192
	ds_read_b128 v[22:25], v192 offset:1024
	ds_read_b128 v[26:29], v192 offset:2048
	ds_read_b128 v[30:33], v192 offset:3072
	ds_read_b128 v[2:5], v193
	ds_read_b128 v[6:9], v193 offset:1024
	ds_read_b128 v[10:13], v193 offset:2048
	ds_read_b128 v[14:17], v193 offset:3072
	s_add_u32 s26, s24, 0x8000
	s_addc_u32 s27, s25, 0
	s_cmp_eq_u32 s74, 12
	s_cselect_b32 s30, s20, s26
	s_cselect_b32 s31, s21, s27
	s_cselect_b32 s28, s22, s17
	s_cselect_b32 s29, s23, s19
	s_add_u32 s26, s30, 0x8000
	s_addc_u32 s27, s31, 0
	v_lshl_add_u64 v[230:231], s[24:25], 0, v[184:185]
	s_add_i32 m0, s48, 0xc000
	ds_read_b128 v[198:201], v194
	ds_read_b128 v[202:205], v194 offset:1024
	ds_read_b128 v[206:209], v194 offset:2048
	ds_read_b128 v[210:213], v194 offset:3072
	ds_read_b128 v[214:217], v194 offset:4096
	ds_read_b128 v[218:221], v194 offset:5120
	ds_read_b128 v[222:225], v194 offset:6144
	ds_read_b128 v[226:229], v194 offset:7168
	global_load_lds_dwordx4 v[230:231], off
	v_lshl_add_u64 v[230:231], s[24:25], 0, v[182:183]
	s_add_i32 m0, s48, 0xe000
	s_nop 0
	global_load_lds_dwordx4 v[230:231], off
	s_waitcnt vmcnt(8)
	s_waitcnt lgkmcnt(0)
	v_mfma_scale_f32_16x16x128_f8f6f4 v[158:161], v[18:25], v[198:205], 0, v195, v195 op_sel_hi:[0,0,0]
	v_mfma_scale_f32_16x16x128_f8f6f4 v[154:157], v[26:33], v[198:205], 0, v195, v195 op_sel_hi:[0,0,0]
	v_mfma_scale_f32_16x16x128_f8f6f4 v[142:145], v[18:25], v[206:213], 0, v195, v195 op_sel_hi:[0,0,0]
	v_mfma_scale_f32_16x16x128_f8f6f4 v[138:141], v[26:33], v[206:213], 0, v195, v195 op_sel_hi:[0,0,0]
	v_mfma_scale_f32_16x16x128_f8f6f4 v[126:129], v[18:25], v[214:221], 0, v195, v195 op_sel_hi:[0,0,0]
	v_mfma_scale_f32_16x16x128_f8f6f4 v[122:125], v[26:33], v[214:221], 0, v195, v195 op_sel_hi:[0,0,0]
	v_mfma_scale_f32_16x16x128_f8f6f4 v[110:113], v[18:25], v[222:229], 0, v195, v195 op_sel_hi:[0,0,0]
	v_mfma_scale_f32_16x16x128_f8f6f4 v[106:109], v[26:33], v[222:229], 0, v195, v195 op_sel_hi:[0,0,0]
	s_nop 3
	v_mfma_scale_f32_16x16x128_f8f6f4 v[150:153], v[2:9], v[198:205], 0, v195, v195 op_sel_hi:[0,0,0]
	v_mfma_scale_f32_16x16x128_f8f6f4 v[146:149], v[10:17], v[198:205], 0, v195, v195 op_sel_hi:[0,0,0]
	v_mfma_scale_f32_16x16x128_f8f6f4 v[134:137], v[2:9], v[206:213], 0, v195, v195 op_sel_hi:[0,0,0]
	v_mfma_scale_f32_16x16x128_f8f6f4 v[130:133], v[10:17], v[206:213], 0, v195, v195 op_sel_hi:[0,0,0]
	v_mfma_scale_f32_16x16x128_f8f6f4 v[118:121], v[2:9], v[214:221], 0, v195, v195 op_sel_hi:[0,0,0]
	v_mfma_scale_f32_16x16x128_f8f6f4 v[114:117], v[10:17], v[214:221], 0, v195, v195 op_sel_hi:[0,0,0]
	v_mfma_scale_f32_16x16x128_f8f6f4 v[102:105], v[2:9], v[222:229], 0, v195, v195 op_sel_hi:[0,0,0]
	v_mfma_scale_f32_16x16x128_f8f6f4 v[98:101], v[10:17], v[222:229], 0, v195, v195 op_sel_hi:[0,0,0]
	s_barrier
	s_add_i32 s75, s65, s47
	v_lshl_add_u64 v[230:231], s[28:29], 0, v[164:165]
	s_mov_b32 m0, s75
	ds_read_b128 v[198:201], v194 offset:16384
	ds_read_b128 v[202:205], v194 offset:17408
	ds_read_b128 v[206:209], v194 offset:18432
	ds_read_b128 v[210:213], v194 offset:19456
	ds_read_b128 v[214:217], v194 offset:20480
	ds_read_b128 v[218:221], v194 offset:21504
	ds_read_b128 v[222:225], v194 offset:22528
	ds_read_b128 v[226:229], v194 offset:23552
	global_load_lds_dwordx4 v[230:231], off
	v_lshl_add_u64 v[232:233], s[28:29], 0, v[166:167]
	s_add_i32 m0, s75, 0x2000
	s_add_i32 s75, s66, s47
	global_load_lds_dwordx4 v[232:233], off
	v_lshl_add_u64 v[230:231], v[230:231], 0, s[4:5]
	s_mov_b32 m0, s75
	s_nop 0
	global_load_lds_dwordx4 v[230:231], off
	v_lshl_add_u64 v[230:231], v[232:233], 0, s[4:5]
	s_add_i32 m0, s75, 0x2000
	s_nop 0
	global_load_lds_dwordx4 v[230:231], off
	v_lshl_add_u64 v[230:231], s[30:31], 0, v[174:175]
	s_mov_b32 m0, s48
	s_nop 0
	global_load_lds_dwordx4 v[230:231], off
	v_lshl_add_u64 v[230:231], s[30:31], 0, v[176:177]
	s_mov_b32 m0, s49
	s_nop 0
	global_load_lds_dwordx4 v[230:231], off
	s_waitcnt vmcnt(8)
	s_waitcnt lgkmcnt(0)
	v_mfma_scale_f32_16x16x128_f8f6f4 v[94:97], v[18:25], v[198:205], 0, v195, v195 op_sel_hi:[0,0,0]
	v_mfma_scale_f32_16x16x128_f8f6f4 v[90:93], v[26:33], v[198:205], 0, v195, v195 op_sel_hi:[0,0,0]
	v_mfma_scale_f32_16x16x128_f8f6f4 v[78:81], v[18:25], v[206:213], 0, v195, v195 op_sel_hi:[0,0,0]
	v_mfma_scale_f32_16x16x128_f8f6f4 v[74:77], v[26:33], v[206:213], 0, v195, v195 op_sel_hi:[0,0,0]
	v_mfma_scale_f32_16x16x128_f8f6f4 v[62:65], v[18:25], v[214:221], 0, v195, v195 op_sel_hi:[0,0,0]
	v_mfma_scale_f32_16x16x128_f8f6f4 v[58:61], v[26:33], v[214:221], 0, v195, v195 op_sel_hi:[0,0,0]
	v_mfma_scale_f32_16x16x128_f8f6f4 v[46:49], v[18:25], v[222:229], 0, v195, v195 op_sel_hi:[0,0,0]
	v_mfma_scale_f32_16x16x128_f8f6f4 v[42:45], v[26:33], v[222:229], 0, v195, v195 op_sel_hi:[0,0,0]
	s_nop 3
	v_mfma_scale_f32_16x16x128_f8f6f4 v[86:89], v[2:9], v[198:205], 0, v195, v195 op_sel_hi:[0,0,0]
	v_mfma_scale_f32_16x16x128_f8f6f4 v[82:85], v[10:17], v[198:205], 0, v195, v195 op_sel_hi:[0,0,0]
	v_mfma_scale_f32_16x16x128_f8f6f4 v[70:73], v[2:9], v[206:213], 0, v195, v195 op_sel_hi:[0,0,0]
	v_mfma_scale_f32_16x16x128_f8f6f4 v[66:69], v[10:17], v[206:213], 0, v195, v195 op_sel_hi:[0,0,0]
	v_mfma_scale_f32_16x16x128_f8f6f4 v[54:57], v[2:9], v[214:221], 0, v195, v195 op_sel_hi:[0,0,0]
	v_mfma_scale_f32_16x16x128_f8f6f4 v[50:53], v[10:17], v[214:221], 0, v195, v195 op_sel_hi:[0,0,0]
	v_mfma_scale_f32_16x16x128_f8f6f4 v[38:41], v[2:9], v[222:229], 0, v195, v195 op_sel_hi:[0,0,0]
	v_mfma_scale_f32_16x16x128_f8f6f4 v[34:37], v[10:17], v[222:229], 0, v195, v195 op_sel_hi:[0,0,0]
	s_barrier
; #define PG8_STAGE(bufoff, gbase, voff) do { _Pragma("unroll") for (int _i = 0; _i < 2; ++_i) \
;         __builtin_amdgcn_global_load_lds((const unsigned*)((const char*)(gbase) + (voff)[_i]), (PG8_LAS unsigned*)(lds + (bufoff) + ldsw + _i * 8192), 16, 0, 0); } while (0)
; #define PG8_WAIT_V(n) asm volatile("s_waitcnt vmcnt(" #n ")" ::: "memory")
; #define PG8_WAIT_L(n) asm volatile("s_waitcnt lgkmcnt(" #n ")" ::: "memory")
; #define PG8_BAR __builtin_amdgcn_s_barrier()
; #define PG8_SCHED __builtin_amdgcn_sched_barrier(0)
; template <class Epi, class Sched, bool ALIGN_EPI = true, bool F8 = false>
; __device__ __forceinline__ void gemm_phase(PG8_LAS unsigned char* lds, const Sched& S, const Epi& E) {
;     ...
;             PG8_LDB(B0, 0, 0); PG8_LDB(B1, 0, 1); PG8_SCHED; PG8_LDA(At, 0, 0); PG8_STAGE(PG8_SA(1, 1), a1, voffA[1]);
;             PG8_WAIT_V(8); PG8_WAIT_L(0); PG8_BAR; PG8_MMA(0, 0, At, B0); PG8_MMA(0, 1, At, B1); PG8_BAR; PG8_SCHED;
;             PG8_LDA(At, 0, 1); PG8_STAGE(PG8_SB(0, 0), b2, voffB[0]); PG8_STAGE(PG8_SB(0, 1), b2, voffB[1]); PG8_STAGE(PG8_SA(0, 0), a2, vA2[0]);
;             PG8_WAIT_V(8); PG8_WAIT_L(0); PG8_BAR; PG8_MMA(1, 0, At, B0); PG8_MMA(1, 1, At, B1); PG8_BAR; PG8_SCHED;
;             PG8_LDB(B0, 1, 0); PG8_LDB(B1, 1, 1); PG8_SCHED; PG8_LDA(At, 1, 0); PG8_STAGE(PG8_SA(0, 1), a2, vA2[1]);
;             PG8_WAIT_V(8); PG8_WAIT_L(0); PG8_BAR; PG8_MMA(0, 0, At, B0); PG8_MMA(0, 1, At, B1); PG8_BAR; PG8_SCHED;
;             PG8_LDA(At, 1, 1); PG8_STAGE(PG8_SB(1, 0), b3, voffB[0]); PG8_STAGE(PG8_SB(1, 1), b3, voffB[1]); PG8_STAGE(PG8_SA(1, 0), a3, vA2[0]);
;             PG8_WAIT_V(8); PG8_WAIT_L(0); PG8_BAR; PG8_MMA(1, 0, At, B0); PG8_MMA(1, 1, At, B1); PG8_BAR; PG8_SCHED;
	s_add_i32 s75, 0, 0x18000
	s_add_i32 s76, 0, 0x1c000
	v_add_u32_e32 v14, s75, v191
	v_add_u32_e32 v30, s76, v191
	ds_read_b128 v[2:5], v14
	ds_read_b128 v[6:9], v14 offset:1024
	ds_read_b128 v[10:13], v14 offset:2048
	ds_read_b128 v[14:17], v14 offset:3072
	ds_read_b128 v[18:21], v30
	ds_read_b128 v[22:25], v30 offset:1024
	ds_read_b128 v[26:29], v30 offset:2048
	ds_read_b128 v[30:33], v30 offset:3072
	s_mov_b32 m0, s50
	v_lshl_add_u64 v[230:231], s[30:31], 0, v[178:179]
	ds_read_b128 v[198:201], v194 offset:32768
	ds_read_b128 v[202:205], v194 offset:33792
	ds_read_b128 v[206:209], v194 offset:34816
	ds_read_b128 v[210:213], v194 offset:35840
	ds_read_b128 v[214:217], v194 offset:36864
	ds_read_b128 v[218:221], v194 offset:37888
	ds_read_b128 v[222:225], v194 offset:38912
	ds_read_b128 v[226:229], v194 offset:39936
	global_load_lds_dwordx4 v[230:231], off
	v_lshl_add_u64 v[230:231], s[30:31], 0, v[180:181]
	s_mov_b32 m0, s51
	s_nop 0
	global_load_lds_dwordx4 v[230:231], off
	s_waitcnt vmcnt(8)
	s_waitcnt lgkmcnt(0)
	v_mfma_scale_f32_16x16x128_f8f6f4 v[158:161], v[2:9], v[198:205], v[158:161], v195, v195 op_sel_hi:[0,0,0]
	v_mfma_scale_f32_16x16x128_f8f6f4 v[154:157], v[10:17], v[198:205], v[154:157], v195, v195 op_sel_hi:[0,0,0]
	v_mfma_scale_f32_16x16x128_f8f6f4 v[142:145], v[2:9], v[206:213], v[142:145], v195, v195 op_sel_hi:[0,0,0]
	v_mfma_scale_f32_16x16x128_f8f6f4 v[138:141], v[10:17], v[206:213], v[138:141], v195, v195 op_sel_hi:[0,0,0]
	v_mfma_scale_f32_16x16x128_f8f6f4 v[126:129], v[2:9], v[214:221], v[126:129], v195, v195 op_sel_hi:[0,0,0]
	v_mfma_scale_f32_16x16x128_f8f6f4 v[122:125], v[10:17], v[214:221], v[122:125], v195, v195 op_sel_hi:[0,0,0]
	v_mfma_scale_f32_16x16x128_f8f6f4 v[110:113], v[2:9], v[222:229], v[110:113], v195, v195 op_sel_hi:[0,0,0]
	v_mfma_scale_f32_16x16x128_f8f6f4 v[106:109], v[10:17], v[222:229], v[106:109], v195, v195 op_sel_hi:[0,0,0]
	s_nop 3
	v_mfma_scale_f32_16x16x128_f8f6f4 v[150:153], v[18:25], v[198:205], v[150:153], v195, v195 op_sel_hi:[0,0,0]
	v_mfma_scale_f32_16x16x128_f8f6f4 v[146:149], v[26:33], v[198:205], v[146:149], v195, v195 op_sel_hi:[0,0,0]
	v_mfma_scale_f32_16x16x128_f8f6f4 v[134:137], v[18:25], v[206:213], v[134:137], v195, v195 op_sel_hi:[0,0,0]
	v_mfma_scale_f32_16x16x128_f8f6f4 v[130:133], v[26:33], v[206:213], v[130:133], v195, v195 op_sel_hi:[0,0,0]
	v_mfma_scale_f32_16x16x128_f8f6f4 v[118:121], v[18:25], v[214:221], v[118:121], v195, v195 op_sel_hi:[0,0,0]
	v_mfma_scale_f32_16x16x128_f8f6f4 v[114:117], v[26:33], v[214:221], v[114:117], v195, v195 op_sel_hi:[0,0,0]
	v_mfma_scale_f32_16x16x128_f8f6f4 v[102:105], v[18:25], v[222:229], v[102:105], v195, v195 op_sel_hi:[0,0,0]
	v_mfma_scale_f32_16x16x128_f8f6f4 v[98:101], v[26:33], v[222:229], v[98:101], v195, v195 op_sel_hi:[0,0,0]
	s_barrier
	s_add_u32 s28, s28, 0x8000
	s_addc_u32 s29, s29, 0
	s_add_i32 s30, s75, s47
	v_lshl_add_u64 v[230:231], s[28:29], 0, v[164:165]
	s_mov_b32 m0, s30
	ds_read_b128 v[198:201], v194 offset:49152
	ds_read_b128 v[202:205], v194 offset:50176
	ds_read_b128 v[206:209], v194 offset:51200
	ds_read_b128 v[210:213], v194 offset:52224
	ds_read_b128 v[214:217], v194 offset:53248
	ds_read_b128 v[218:221], v194 offset:54272
	ds_read_b128 v[222:225], v194 offset:55296
	ds_read_b128 v[226:229], v194 offset:56320
	global_load_lds_dwordx4 v[230:231], off
	v_lshl_add_u64 v[230:231], s[28:29], 0, v[166:167]
	s_add_i32 m0, s30, 0x2000
	s_add_i32 s30, s76, s47
	global_load_lds_dwordx4 v[230:231], off
	v_lshl_add_u64 v[230:231], s[28:29], 0, v[168:169]
	s_mov_b32 m0, s30
	s_nop 0
	global_load_lds_dwordx4 v[230:231], off
	v_lshl_add_u64 v[230:231], s[28:29], 0, v[172:173]
	s_add_i32 m0, s30, 0x2000
	s_nop 0
	global_load_lds_dwordx4 v[230:231], off
	v_lshl_add_u64 v[230:231], s[26:27], 0, v[174:175]
	s_mov_b32 m0, s60
	s_nop 0
	global_load_lds_dwordx4 v[230:231], off
	v_lshl_add_u64 v[230:231], s[26:27], 0, v[176:177]
	s_mov_b32 m0, s61
	s_nop 0
	global_load_lds_dwordx4 v[230:231], off
	s_waitcnt vmcnt(8)
	s_waitcnt lgkmcnt(0)
	v_mfma_scale_f32_16x16x128_f8f6f4 v[94:97], v[2:9], v[198:205], v[94:97], v195, v195 op_sel_hi:[0,0,0]
	v_mfma_scale_f32_16x16x128_f8f6f4 v[90:93], v[10:17], v[198:205], v[90:93], v195, v195 op_sel_hi:[0,0,0]
	v_mfma_scale_f32_16x16x128_f8f6f4 v[78:81], v[2:9], v[206:213], v[78:81], v195, v195 op_sel_hi:[0,0,0]
	v_mfma_scale_f32_16x16x128_f8f6f4 v[74:77], v[10:17], v[206:213], v[74:77], v195, v195 op_sel_hi:[0,0,0]
	v_mfma_scale_f32_16x16x128_f8f6f4 v[62:65], v[2:9], v[214:221], v[62:65], v195, v195 op_sel_hi:[0,0,0]
	v_mfma_scale_f32_16x16x128_f8f6f4 v[58:61], v[10:17], v[214:221], v[58:61], v195, v195 op_sel_hi:[0,0,0]
	v_mfma_scale_f32_16x16x128_f8f6f4 v[46:49], v[2:9], v[222:229], v[46:49], v195, v195 op_sel_hi:[0,0,0]
	v_mfma_scale_f32_16x16x128_f8f6f4 v[42:45], v[10:17], v[222:229], v[42:45], v195, v195 op_sel_hi:[0,0,0]
	s_nop 3
	v_mfma_scale_f32_16x16x128_f8f6f4 v[86:89], v[18:25], v[198:205], v[86:89], v195, v195 op_sel_hi:[0,0,0]
	v_mfma_scale_f32_16x16x128_f8f6f4 v[82:85], v[26:33], v[198:205], v[82:85], v195, v195 op_sel_hi:[0,0,0]
	v_mfma_scale_f32_16x16x128_f8f6f4 v[70:73], v[18:25], v[206:213], v[70:73], v195, v195 op_sel_hi:[0,0,0]
	v_mfma_scale_f32_16x16x128_f8f6f4 v[66:69], v[26:33], v[206:213], v[66:69], v195, v195 op_sel_hi:[0,0,0]
	v_mfma_scale_f32_16x16x128_f8f6f4 v[54:57], v[18:25], v[214:221], v[54:57], v195, v195 op_sel_hi:[0,0,0]
	v_mfma_scale_f32_16x16x128_f8f6f4 v[50:53], v[26:33], v[214:221], v[50:53], v195, v195 op_sel_hi:[0,0,0]
	v_mfma_scale_f32_16x16x128_f8f6f4 v[38:41], v[18:25], v[222:229], v[38:41], v195, v195 op_sel_hi:[0,0,0]
	v_mfma_scale_f32_16x16x128_f8f6f4 v[34:37], v[26:33], v[222:229], v[34:37], v195, v195 op_sel_hi:[0,0,0]
	s_barrier
	s_add_i32 s74, s74, 2
	s_add_u32 s17, s17, 0x10000
	s_addc_u32 s19, s19, 0
	s_add_u32 s24, s24, 0x10000
	s_addc_u32 s25, s25, 0
	s_cmp_gt_u32 s74, 13
	s_cbranch_scc0 .LBB0_428
	s_branch .Lfx_11141
; #define PG8_STAGE(bufoff, gbase, voff) do { _Pragma("unroll") for (int _i = 0; _i < 2; ++_i) \
;         __builtin_amdgcn_global_load_lds((const unsigned*)((const char*)(gbase) + (voff)[_i]), (PG8_LAS unsigned*)(lds + (bufoff) + ldsw + _i * 8192), 16, 0, 0); } while (0)
; #define PG8_WAIT_V(n) asm volatile("s_waitcnt vmcnt(" #n ")" ::: "memory")
; #define PG8_WAIT_L(n) asm volatile("s_waitcnt lgkmcnt(" #n ")" ::: "memory")
; #define PG8_BAR __builtin_amdgcn_s_barrier()
; #define PG8_SCHED __builtin_amdgcn_sched_barrier(0)
; template <class Epi, class Sched, bool ALIGN_EPI = true, bool F8 = false>
; __device__ __forceinline__ void gemm_phase(PG8_LAS unsigned char* lds, const Sched& S, const Epi& E) {
;     ...
;             PG8_LDB(B0, 0, 0); PG8_LDB(B1, 0, 1); PG8_SCHED; PG8_LDA(At, 0, 0); PG8_STAGE(PG8_SA(1, 1), a1, voffA[1]);
;             PG8_WAIT_V(8); PG8_WAIT_L(0); PG8_BAR; PG8_MMA(0, 0, At, B0); PG8_MMA(0, 1, At, B1); PG8_BAR; PG8_SCHED;
;             PG8_LDA(At, 0, 1); PG8_STAGE(PG8_SB(0, 0), b2, voffB[0]); PG8_STAGE(PG8_SB(0, 1), b2, voffB[1]); PG8_STAGE(PG8_SA(0, 0), a2, vA2[0]);
;             PG8_WAIT_V(8); PG8_WAIT_L(0); PG8_BAR; PG8_MMA(1, 0, At, B0); PG8_MMA(1, 1, At, B1); PG8_BAR; PG8_SCHED;
;             PG8_LDB(B0, 1, 0); PG8_LDB(B1, 1, 1); PG8_SCHED; PG8_LDA(At, 1, 0); PG8_STAGE(PG8_SA(0, 1), a2, vA2[1]);
;             PG8_WAIT_V(8); PG8_WAIT_L(0); PG8_BAR; PG8_MMA(0, 0, At, B0); PG8_MMA(0, 1, At, B1); PG8_BAR; PG8_SCHED;
;             PG8_LDA(At, 1, 1); PG8_STAGE(PG8_SB(1, 0), b3, voffB[0]); PG8_STAGE(PG8_SB(1, 1), b3, voffB[1]); PG8_STAGE(PG8_SA(1, 0), a3, vA2[0]);
;             PG8_WAIT_V(8); PG8_WAIT_L(0); PG8_BAR; PG8_MMA(1, 0, At, B0); PG8_MMA(1, 1, At, B1); PG8_BAR; PG8_SCHED;
.LBB0_428:
	ds_read_b128 v[18:21], v192
	ds_read_b128 v[22:25], v192 offset:1024
	ds_read_b128 v[26:29], v192 offset:2048
	ds_read_b128 v[30:33], v192 offset:3072
	ds_read_b128 v[2:5], v193
	ds_read_b128 v[6:9], v193 offset:1024
	ds_read_b128 v[10:13], v193 offset:2048
	ds_read_b128 v[14:17], v193 offset:3072
	s_add_u32 s26, s24, 0x8000
	s_addc_u32 s27, s25, 0
	s_cmp_eq_u32 s74, 12
	s_cselect_b32 s30, s20, s26
	s_cselect_b32 s31, s21, s27
	s_cselect_b32 s28, s22, s17
	s_cselect_b32 s29, s23, s19
	s_add_u32 s26, s30, 0x8000
	s_addc_u32 s27, s31, 0
	v_lshl_add_u64 v[230:231], s[24:25], 0, v[184:185]
	s_add_i32 m0, s48, 0xc000
	ds_read_b128 v[198:201], v194
	ds_read_b128 v[202:205], v194 offset:1024
	ds_read_b128 v[206:209], v194 offset:2048
	ds_read_b128 v[210:213], v194 offset:3072
	ds_read_b128 v[214:217], v194 offset:4096
	ds_read_b128 v[218:221], v194 offset:5120
	ds_read_b128 v[222:225], v194 offset:6144
	ds_read_b128 v[226:229], v194 offset:7168
	global_load_lds_dwordx4 v[230:231], off
	v_lshl_add_u64 v[230:231], s[24:25], 0, v[182:183]
	s_add_i32 m0, s48, 0xe000
	s_nop 0
	global_load_lds_dwordx4 v[230:231], off
	s_waitcnt vmcnt(8)
	s_waitcnt lgkmcnt(0)
	v_mfma_scale_f32_16x16x128_f8f6f4 v[158:161], v[18:25], v[198:205], v[158:161], v195, v195 op_sel_hi:[0,0,0]
	v_mfma_scale_f32_16x16x128_f8f6f4 v[154:157], v[26:33], v[198:205], v[154:157], v195, v195 op_sel_hi:[0,0,0]
	v_mfma_scale_f32_16x16x128_f8f6f4 v[142:145], v[18:25], v[206:213], v[142:145], v195, v195 op_sel_hi:[0,0,0]
	v_mfma_scale_f32_16x16x128_f8f6f4 v[138:141], v[26:33], v[206:213], v[138:141], v195, v195 op_sel_hi:[0,0,0]
	v_mfma_scale_f32_16x16x128_f8f6f4 v[126:129], v[18:25], v[214:221], v[126:129], v195, v195 op_sel_hi:[0,0,0]
	v_mfma_scale_f32_16x16x128_f8f6f4 v[122:125], v[26:33], v[214:221], v[122:125], v195, v195 op_sel_hi:[0,0,0]
	v_mfma_scale_f32_16x16x128_f8f6f4 v[110:113], v[18:25], v[222:229], v[110:113], v195, v195 op_sel_hi:[0,0,0]
	v_mfma_scale_f32_16x16x128_f8f6f4 v[106:109], v[26:33], v[222:229], v[106:109], v195, v195 op_sel_hi:[0,0,0]
	s_nop 3
	v_mfma_scale_f32_16x16x128_f8f6f4 v[150:153], v[2:9], v[198:205], v[150:153], v195, v195 op_sel_hi:[0,0,0]
	v_mfma_scale_f32_16x16x128_f8f6f4 v[146:149], v[10:17], v[198:205], v[146:149], v195, v195 op_sel_hi:[0,0,0]
	v_mfma_scale_f32_16x16x128_f8f6f4 v[134:137], v[2:9], v[206:213], v[134:137], v195, v195 op_sel_hi:[0,0,0]
	v_mfma_scale_f32_16x16x128_f8f6f4 v[130:133], v[10:17], v[206:213], v[130:133], v195, v195 op_sel_hi:[0,0,0]
	v_mfma_scale_f32_16x16x128_f8f6f4 v[118:121], v[2:9], v[214:221], v[118:121], v195, v195 op_sel_hi:[0,0,0]
	v_mfma_scale_f32_16x16x128_f8f6f4 v[114:117], v[10:17], v[214:221], v[114:117], v195, v195 op_sel_hi:[0,0,0]
	v_mfma_scale_f32_16x16x128_f8f6f4 v[102:105], v[2:9], v[222:229], v[102:105], v195, v195 op_sel_hi:[0,0,0]
	v_mfma_scale_f32_16x16x128_f8f6f4 v[98:101], v[10:17], v[222:229], v[98:101], v195, v195 op_sel_hi:[0,0,0]
	s_barrier
	s_add_i32 s75, s65, s47
	v_lshl_add_u64 v[230:231], s[28:29], 0, v[164:165]
	s_mov_b32 m0, s75
	ds_read_b128 v[198:201], v194 offset:16384
	ds_read_b128 v[202:205], v194 offset:17408
	ds_read_b128 v[206:209], v194 offset:18432
	ds_read_b128 v[210:213], v194 offset:19456
	ds_read_b128 v[214:217], v194 offset:20480
	ds_read_b128 v[218:221], v194 offset:21504
	ds_read_b128 v[222:225], v194 offset:22528
	ds_read_b128 v[226:229], v194 offset:23552
	global_load_lds_dwordx4 v[230:231], off
	v_lshl_add_u64 v[232:233], s[28:29], 0, v[166:167]
	s_add_i32 m0, s75, 0x2000
	s_add_i32 s75, s66, s47
	global_load_lds_dwordx4 v[232:233], off
	v_lshl_add_u64 v[230:231], v[230:231], 0, s[4:5]
	s_mov_b32 m0, s75
	s_nop 0
	global_load_lds_dwordx4 v[230:231], off
	v_lshl_add_u64 v[230:231], v[232:233], 0, s[4:5]
	s_add_i32 m0, s75, 0x2000
	s_nop 0
	global_load_lds_dwordx4 v[230:231], off
	v_lshl_add_u64 v[230:231], s[30:31], 0, v[174:175]
	s_mov_b32 m0, s48
	s_nop 0
	global_load_lds_dwordx4 v[230:231], off
	v_lshl_add_u64 v[230:231], s[30:31], 0, v[176:177]
	s_mov_b32 m0, s49
	s_nop 0
	global_load_lds_dwordx4 v[230:231], off
	s_waitcnt vmcnt(8)
	s_waitcnt lgkmcnt(0)
	v_mfma_scale_f32_16x16x128_f8f6f4 v[94:97], v[18:25], v[198:205], v[94:97], v195, v195 op_sel_hi:[0,0,0]
	v_mfma_scale_f32_16x16x128_f8f6f4 v[90:93], v[26:33], v[198:205], v[90:93], v195, v195 op_sel_hi:[0,0,0]
	v_mfma_scale_f32_16x16x128_f8f6f4 v[78:81], v[18:25], v[206:213], v[78:81], v195, v195 op_sel_hi:[0,0,0]
	v_mfma_scale_f32_16x16x128_f8f6f4 v[74:77], v[26:33], v[206:213], v[74:77], v195, v195 op_sel_hi:[0,0,0]
	v_mfma_scale_f32_16x16x128_f8f6f4 v[62:65], v[18:25], v[214:221], v[62:65], v195, v195 op_sel_hi:[0,0,0]
	v_mfma_scale_f32_16x16x128_f8f6f4 v[58:61], v[26:33], v[214:221], v[58:61], v195, v195 op_sel_hi:[0,0,0]
	v_mfma_scale_f32_16x16x128_f8f6f4 v[46:49], v[18:25], v[222:229], v[46:49], v195, v195 op_sel_hi:[0,0,0]
	v_mfma_scale_f32_16x16x128_f8f6f4 v[42:45], v[26:33], v[222:229], v[42:45], v195, v195 op_sel_hi:[0,0,0]
	s_nop 3
	v_mfma_scale_f32_16x16x128_f8f6f4 v[86:89], v[2:9], v[198:205], v[86:89], v195, v195 op_sel_hi:[0,0,0]
	v_mfma_scale_f32_16x16x128_f8f6f4 v[82:85], v[10:17], v[198:205], v[82:85], v195, v195 op_sel_hi:[0,0,0]
	v_mfma_scale_f32_16x16x128_f8f6f4 v[70:73], v[2:9], v[206:213], v[70:73], v195, v195 op_sel_hi:[0,0,0]
	v_mfma_scale_f32_16x16x128_f8f6f4 v[66:69], v[10:17], v[206:213], v[66:69], v195, v195 op_sel_hi:[0,0,0]
	v_mfma_scale_f32_16x16x128_f8f6f4 v[54:57], v[2:9], v[214:221], v[54:57], v195, v195 op_sel_hi:[0,0,0]
	v_mfma_scale_f32_16x16x128_f8f6f4 v[50:53], v[10:17], v[214:221], v[50:53], v195, v195 op_sel_hi:[0,0,0]
	v_mfma_scale_f32_16x16x128_f8f6f4 v[38:41], v[2:9], v[222:229], v[38:41], v195, v195 op_sel_hi:[0,0,0]
	v_mfma_scale_f32_16x16x128_f8f6f4 v[34:37], v[10:17], v[222:229], v[34:37], v195, v195 op_sel_hi:[0,0,0]
	s_barrier
; #define PG8_STAGE(bufoff, gbase, voff) do { _Pragma("unroll") for (int _i = 0; _i < 2; ++_i) \
;         __builtin_amdgcn_global_load_lds((const unsigned*)((const char*)(gbase) + (voff)[_i]), (PG8_LAS unsigned*)(lds + (bufoff) + ldsw + _i * 8192), 16, 0, 0); } while (0)
; #define PG8_WAIT_V(n) asm volatile("s_waitcnt vmcnt(" #n ")" ::: "memory")
; #define PG8_WAIT_L(n) asm volatile("s_waitcnt lgkmcnt(" #n ")" ::: "memory")
; #define PG8_BAR __builtin_amdgcn_s_barrier()
; #define PG8_SCHED __builtin_amdgcn_sched_barrier(0)
; template <class Epi, class Sched, bool ALIGN_EPI = true, bool F8 = false>
; __device__ __forceinline__ void gemm_phase(PG8_LAS unsigned char* lds, const Sched& S, const Epi& E) {
;     ...
;             PG8_LDB(B0, 0, 0); PG8_LDB(B1, 0, 1); PG8_SCHED; PG8_LDA(At, 0, 0); PG8_STAGE(PG8_SA(1, 1), a1, voffA[1]);
;             PG8_WAIT_V(8); PG8_WAIT_L(0); PG8_BAR; PG8_MMA(0, 0, At, B0); PG8_MMA(0, 1, At, B1); PG8_BAR; PG8_SCHED;
;             PG8_LDA(At, 0, 1); PG8_STAGE(PG8_SB(0, 0), b2, voffB[0]); PG8_STAGE(PG8_SB(0, 1), b2, voffB[1]); PG8_STAGE(PG8_SA(0, 0), a2, vA2[0]);
;             PG8_WAIT_V(8); PG8_WAIT_L(0); PG8_BAR; PG8_MMA(1, 0, At, B0); PG8_MMA(1, 1, At, B1); PG8_BAR; PG8_SCHED;
;             PG8_LDB(B0, 1, 0); PG8_LDB(B1, 1, 1); PG8_SCHED; PG8_LDA(At, 1, 0); PG8_STAGE(PG8_SA(0, 1), a2, vA2[1]);
;             PG8_WAIT_V(8); PG8_WAIT_L(0); PG8_BAR; PG8_MMA(0, 0, At, B0); PG8_MMA(0, 1, At, B1); PG8_BAR; PG8_SCHED;
;             PG8_LDA(At, 1, 1); PG8_STAGE(PG8_SB(1, 0), b3, voffB[0]); PG8_STAGE(PG8_SB(1, 1), b3, voffB[1]); PG8_STAGE(PG8_SA(1, 0), a3, vA2[0]);
;             PG8_WAIT_V(8); PG8_WAIT_L(0); PG8_BAR; PG8_MMA(1, 0, At, B0); PG8_MMA(1, 1, At, B1); PG8_BAR; PG8_SCHED;
	s_add_i32 s75, 0, 0x18000
	s_add_i32 s76, 0, 0x1c000
	v_add_u32_e32 v14, s75, v191
	v_add_u32_e32 v30, s76, v191
	ds_read_b128 v[2:5], v14
	ds_read_b128 v[6:9], v14 offset:1024
	ds_read_b128 v[10:13], v14 offset:2048
	ds_read_b128 v[14:17], v14 offset:3072
	ds_read_b128 v[18:21], v30
	ds_read_b128 v[22:25], v30 offset:1024
	ds_read_b128 v[26:29], v30 offset:2048
	ds_read_b128 v[30:33], v30 offset:3072
	s_mov_b32 m0, s50
	v_lshl_add_u64 v[230:231], s[30:31], 0, v[178:179]
	ds_read_b128 v[198:201], v194 offset:32768
	ds_read_b128 v[202:205], v194 offset:33792
	ds_read_b128 v[206:209], v194 offset:34816
	ds_read_b128 v[210:213], v194 offset:35840
	ds_read_b128 v[214:217], v194 offset:36864
	ds_read_b128 v[218:221], v194 offset:37888
	ds_read_b128 v[222:225], v194 offset:38912
	ds_read_b128 v[226:229], v194 offset:39936
	global_load_lds_dwordx4 v[230:231], off
	v_lshl_add_u64 v[230:231], s[30:31], 0, v[180:181]
	s_mov_b32 m0, s51
	s_nop 0
	global_load_lds_dwordx4 v[230:231], off
	s_waitcnt vmcnt(8)
	s_waitcnt lgkmcnt(0)
	v_mfma_scale_f32_16x16x128_f8f6f4 v[158:161], v[2:9], v[198:205], v[158:161], v195, v195 op_sel_hi:[0,0,0]
	v_mfma_scale_f32_16x16x128_f8f6f4 v[154:157], v[10:17], v[198:205], v[154:157], v195, v195 op_sel_hi:[0,0,0]
	v_mfma_scale_f32_16x16x128_f8f6f4 v[142:145], v[2:9], v[206:213], v[142:145], v195, v195 op_sel_hi:[0,0,0]
	v_mfma_scale_f32_16x16x128_f8f6f4 v[138:141], v[10:17], v[206:213], v[138:141], v195, v195 op_sel_hi:[0,0,0]
	v_mfma_scale_f32_16x16x128_f8f6f4 v[126:129], v[2:9], v[214:221], v[126:129], v195, v195 op_sel_hi:[0,0,0]
	v_mfma_scale_f32_16x16x128_f8f6f4 v[122:125], v[10:17], v[214:221], v[122:125], v195, v195 op_sel_hi:[0,0,0]
	v_mfma_scale_f32_16x16x128_f8f6f4 v[110:113], v[2:9], v[222:229], v[110:113], v195, v195 op_sel_hi:[0,0,0]
	v_mfma_scale_f32_16x16x128_f8f6f4 v[106:109], v[10:17], v[222:229], v[106:109], v195, v195 op_sel_hi:[0,0,0]
	s_nop 3
	v_mfma_scale_f32_16x16x128_f8f6f4 v[150:153], v[18:25], v[198:205], v[150:153], v195, v195 op_sel_hi:[0,0,0]
	v_mfma_scale_f32_16x16x128_f8f6f4 v[146:149], v[26:33], v[198:205], v[146:149], v195, v195 op_sel_hi:[0,0,0]
	v_mfma_scale_f32_16x16x128_f8f6f4 v[134:137], v[18:25], v[206:213], v[134:137], v195, v195 op_sel_hi:[0,0,0]
	v_mfma_scale_f32_16x16x128_f8f6f4 v[130:133], v[26:33], v[206:213], v[130:133], v195, v195 op_sel_hi:[0,0,0]
	v_mfma_scale_f32_16x16x128_f8f6f4 v[118:121], v[18:25], v[214:221], v[118:121], v195, v195 op_sel_hi:[0,0,0]
	v_mfma_scale_f32_16x16x128_f8f6f4 v[114:117], v[26:33], v[214:221], v[114:117], v195, v195 op_sel_hi:[0,0,0]
	v_mfma_scale_f32_16x16x128_f8f6f4 v[102:105], v[18:25], v[222:229], v[102:105], v195, v195 op_sel_hi:[0,0,0]
	v_mfma_scale_f32_16x16x128_f8f6f4 v[98:101], v[26:33], v[222:229], v[98:101], v195, v195 op_sel_hi:[0,0,0]
	s_barrier
	s_add_u32 s28, s28, 0x8000
	s_addc_u32 s29, s29, 0
	s_add_i32 s30, s75, s47
	v_lshl_add_u64 v[230:231], s[28:29], 0, v[164:165]
	s_mov_b32 m0, s30
	ds_read_b128 v[198:201], v194 offset:49152
	ds_read_b128 v[202:205], v194 offset:50176
	ds_read_b128 v[206:209], v194 offset:51200
	ds_read_b128 v[210:213], v194 offset:52224
	ds_read_b128 v[214:217], v194 offset:53248
	ds_read_b128 v[218:221], v194 offset:54272
	ds_read_b128 v[222:225], v194 offset:55296
	ds_read_b128 v[226:229], v194 offset:56320
	global_load_lds_dwordx4 v[230:231], off
	v_lshl_add_u64 v[230:231], s[28:29], 0, v[166:167]
	s_add_i32 m0, s30, 0x2000
	s_add_i32 s30, s76, s47
	global_load_lds_dwordx4 v[230:231], off
	v_lshl_add_u64 v[230:231], s[28:29], 0, v[168:169]
	s_mov_b32 m0, s30
	s_nop 0
	global_load_lds_dwordx4 v[230:231], off
	v_lshl_add_u64 v[230:231], s[28:29], 0, v[172:173]
	s_add_i32 m0, s30, 0x2000
	s_nop 0
	global_load_lds_dwordx4 v[230:231], off
	v_lshl_add_u64 v[230:231], s[26:27], 0, v[174:175]
	s_mov_b32 m0, s60
	s_nop 0
	global_load_lds_dwordx4 v[230:231], off
	v_lshl_add_u64 v[230:231], s[26:27], 0, v[176:177]
	s_mov_b32 m0, s61
	s_nop 0
	global_load_lds_dwordx4 v[230:231], off
	s_waitcnt vmcnt(8)
	s_waitcnt lgkmcnt(0)
	v_mfma_scale_f32_16x16x128_f8f6f4 v[94:97], v[2:9], v[198:205], v[94:97], v195, v195 op_sel_hi:[0,0,0]
	v_mfma_scale_f32_16x16x128_f8f6f4 v[90:93], v[10:17], v[198:205], v[90:93], v195, v195 op_sel_hi:[0,0,0]
	v_mfma_scale_f32_16x16x128_f8f6f4 v[78:81], v[2:9], v[206:213], v[78:81], v195, v195 op_sel_hi:[0,0,0]
	v_mfma_scale_f32_16x16x128_f8f6f4 v[74:77], v[10:17], v[206:213], v[74:77], v195, v195 op_sel_hi:[0,0,0]
	v_mfma_scale_f32_16x16x128_f8f6f4 v[62:65], v[2:9], v[214:221], v[62:65], v195, v195 op_sel_hi:[0,0,0]
	v_mfma_scale_f32_16x16x128_f8f6f4 v[58:61], v[10:17], v[214:221], v[58:61], v195, v195 op_sel_hi:[0,0,0]
	v_mfma_scale_f32_16x16x128_f8f6f4 v[46:49], v[2:9], v[222:229], v[46:49], v195, v195 op_sel_hi:[0,0,0]
	v_mfma_scale_f32_16x16x128_f8f6f4 v[42:45], v[10:17], v[222:229], v[42:45], v195, v195 op_sel_hi:[0,0,0]
	s_nop 3
	v_mfma_scale_f32_16x16x128_f8f6f4 v[86:89], v[18:25], v[198:205], v[86:89], v195, v195 op_sel_hi:[0,0,0]
	v_mfma_scale_f32_16x16x128_f8f6f4 v[82:85], v[26:33], v[198:205], v[82:85], v195, v195 op_sel_hi:[0,0,0]
	v_mfma_scale_f32_16x16x128_f8f6f4 v[70:73], v[18:25], v[206:213], v[70:73], v195, v195 op_sel_hi:[0,0,0]
	v_mfma_scale_f32_16x16x128_f8f6f4 v[66:69], v[26:33], v[206:213], v[66:69], v195, v195 op_sel_hi:[0,0,0]
	v_mfma_scale_f32_16x16x128_f8f6f4 v[54:57], v[18:25], v[214:221], v[54:57], v195, v195 op_sel_hi:[0,0,0]
	v_mfma_scale_f32_16x16x128_f8f6f4 v[50:53], v[26:33], v[214:221], v[50:53], v195, v195 op_sel_hi:[0,0,0]
	v_mfma_scale_f32_16x16x128_f8f6f4 v[38:41], v[18:25], v[222:229], v[38:41], v195, v195 op_sel_hi:[0,0,0]
	v_mfma_scale_f32_16x16x128_f8f6f4 v[34:37], v[26:33], v[222:229], v[34:37], v195, v195 op_sel_hi:[0,0,0]
	s_barrier
	s_add_i32 s74, s74, 2
	s_add_u32 s17, s17, 0x10000
	s_addc_u32 s19, s19, 0
	s_add_u32 s24, s24, 0x10000
	s_addc_u32 s25, s25, 0
	s_cmp_gt_u32 s74, 13
	s_cbranch_scc0 .LBB0_428
	s_branch .Lfx_11141

; #define PG8_STAGE(bufoff, gbase, voff) do { _Pragma("unroll") for (int _i = 0; _i < 2; ++_i) \
;         __builtin_amdgcn_global_load_lds((const unsigned*)((const char*)(gbase) + (voff)[_i]), (PG8_LAS unsigned*)(lds + (bufoff) + ldsw + _i * 8192), 16, 0, 0); } while (0)
; #define PG8_WAIT_V(n) asm volatile("s_waitcnt vmcnt(" #n ")" ::: "memory")
; #define PG8_WAIT_L(n) asm volatile("s_waitcnt lgkmcnt(" #n ")" ::: "memory")
; #define PG8_BAR __builtin_amdgcn_s_barrier()
; #define PG8_SCHED __builtin_amdgcn_sched_barrier(0)
; template <class Epi, class Sched, bool ALIGN_EPI = true, bool F8 = false>
; __device__ __forceinline__ void gemm_phase(PG8_LAS unsigned char* lds, const Sched& S, const Epi& E) {
;     ...
;             PG8_LDB(B0, 0, 0); PG8_LDB(B1, 0, 1); PG8_SCHED; PG8_LDA(At, 0, 0); PG8_STAGE(PG8_SA(1, 1), a1, voffA[1]);
;             PG8_WAIT_V(8); PG8_WAIT_L(0); PG8_BAR; PG8_MMA(0, 0, At, B0); PG8_MMA(0, 1, At, B1); PG8_BAR; PG8_SCHED;
;             PG8_LDA(At, 0, 1); PG8_STAGE(PG8_SB(0, 0), b2, voffB[0]); PG8_STAGE(PG8_SB(0, 1), b2, voffB[1]); PG8_STAGE(PG8_SA(0, 0), a2, vA2[0]);
;             PG8_WAIT_V(8); PG8_WAIT_L(0); PG8_BAR; PG8_MMA(1, 0, At, B0); PG8_MMA(1, 1, At, B1); PG8_BAR; PG8_SCHED;
;             PG8_LDB(B0, 1, 0); PG8_LDB(B1, 1, 1); PG8_SCHED; PG8_LDA(At, 1, 0); PG8_STAGE(PG8_SA(0, 1), a2, vA2[1]);
;             PG8_WAIT_V(8); PG8_WAIT_L(0); PG8_BAR; PG8_MMA(0, 0, At, B0); PG8_MMA(0, 1, At, B1); PG8_BAR; PG8_SCHED;
;             PG8_LDA(At, 1, 1); PG8_STAGE(PG8_SB(1, 0), b3, voffB[0]); PG8_STAGE(PG8_SB(1, 1), b3, voffB[1]); PG8_STAGE(PG8_SA(1, 0), a3, vA2[0]);
;             PG8_WAIT_V(8); PG8_WAIT_L(0); PG8_BAR; PG8_MMA(1, 0, At, B0); PG8_MMA(1, 1, At, B1); PG8_BAR; PG8_SCHED;
.Lpk1_428:
	ds_read_b128 v[18:21], v192
	ds_read_b128 v[22:25], v192 offset:1024
	ds_read_b128 v[26:29], v192 offset:2048
	ds_read_b128 v[30:33], v192 offset:3072
	ds_read_b128 v[2:5], v193
	ds_read_b128 v[6:9], v193 offset:1024
	ds_read_b128 v[10:13], v193 offset:2048
	ds_read_b128 v[14:17], v193 offset:3072
	s_add_u32 s26, s24, 0x8000
	s_addc_u32 s27, s25, 0
	s_cmp_eq_u32 s74, 12
	s_cselect_b32 s30, s20, s26
	s_cselect_b32 s31, s21, s27
	s_cselect_b32 s28, s22, s17
	s_cselect_b32 s29, s23, s19
	s_add_u32 s26, s30, 0x8000
	s_addc_u32 s27, s31, 0
	v_lshl_add_u64 v[230:231], s[24:25], 0, v[184:185]
	s_add_i32 m0, s48, 0xc000
	ds_read_b128 v[198:201], v194
	ds_read_b128 v[202:205], v194 offset:1024
	ds_read_b128 v[206:209], v194 offset:2048
	ds_read_b128 v[210:213], v194 offset:3072
	ds_read_b128 v[214:217], v194 offset:4096
	ds_read_b128 v[218:221], v194 offset:5120
	ds_read_b128 v[222:225], v194 offset:6144
	ds_read_b128 v[226:229], v194 offset:7168
	global_load_lds_dwordx4 v[230:231], off
	v_lshl_add_u64 v[230:231], s[24:25], 0, v[182:183]
	s_add_i32 m0, s48, 0xe000
	s_nop 0
	global_load_lds_dwordx4 v[230:231], off
	s_waitcnt vmcnt(8)
	s_waitcnt lgkmcnt(0)
	s_barrier
	v_mfma_scale_f32_16x16x128_f8f6f4 v[158:161], v[18:25], v[198:205], 0, v195, v195 op_sel_hi:[0,0,0]
	v_mfma_scale_f32_16x16x128_f8f6f4 v[154:157], v[26:33], v[198:205], 0, v195, v195 op_sel_hi:[0,0,0]
	v_mfma_scale_f32_16x16x128_f8f6f4 v[142:145], v[18:25], v[206:213], 0, v195, v195 op_sel_hi:[0,0,0]
	v_mfma_scale_f32_16x16x128_f8f6f4 v[138:141], v[26:33], v[206:213], 0, v195, v195 op_sel_hi:[0,0,0]
	v_mfma_scale_f32_16x16x128_f8f6f4 v[126:129], v[18:25], v[214:221], 0, v195, v195 op_sel_hi:[0,0,0]
	v_mfma_scale_f32_16x16x128_f8f6f4 v[122:125], v[26:33], v[214:221], 0, v195, v195 op_sel_hi:[0,0,0]
	v_mfma_scale_f32_16x16x128_f8f6f4 v[110:113], v[18:25], v[222:229], 0, v195, v195 op_sel_hi:[0,0,0]
	v_mfma_scale_f32_16x16x128_f8f6f4 v[106:109], v[26:33], v[222:229], 0, v195, v195 op_sel_hi:[0,0,0]
	s_nop 3
	v_mfma_scale_f32_16x16x128_f8f6f4 v[150:153], v[2:9], v[198:205], 0, v195, v195 op_sel_hi:[0,0,0]
	v_mfma_scale_f32_16x16x128_f8f6f4 v[146:149], v[10:17], v[198:205], 0, v195, v195 op_sel_hi:[0,0,0]
	v_mfma_scale_f32_16x16x128_f8f6f4 v[134:137], v[2:9], v[206:213], 0, v195, v195 op_sel_hi:[0,0,0]
	v_mfma_scale_f32_16x16x128_f8f6f4 v[130:133], v[10:17], v[206:213], 0, v195, v195 op_sel_hi:[0,0,0]
	v_mfma_scale_f32_16x16x128_f8f6f4 v[118:121], v[2:9], v[214:221], 0, v195, v195 op_sel_hi:[0,0,0]
	v_mfma_scale_f32_16x16x128_f8f6f4 v[114:117], v[10:17], v[214:221], 0, v195, v195 op_sel_hi:[0,0,0]
	v_mfma_scale_f32_16x16x128_f8f6f4 v[102:105], v[2:9], v[222:229], 0, v195, v195 op_sel_hi:[0,0,0]
	v_mfma_scale_f32_16x16x128_f8f6f4 v[98:101], v[10:17], v[222:229], 0, v195, v195 op_sel_hi:[0,0,0]
	s_add_i32 s75, s65, s47
	v_lshl_add_u64 v[230:231], s[28:29], 0, v[164:165]
	s_mov_b32 m0, s75
	ds_read_b128 v[198:201], v194 offset:16384
	ds_read_b128 v[202:205], v194 offset:17408
	ds_read_b128 v[206:209], v194 offset:18432
	ds_read_b128 v[210:213], v194 offset:19456
	ds_read_b128 v[214:217], v194 offset:20480
	ds_read_b128 v[218:221], v194 offset:21504
	ds_read_b128 v[222:225], v194 offset:22528
	ds_read_b128 v[226:229], v194 offset:23552
	global_load_lds_dwordx4 v[230:231], off
	v_lshl_add_u64 v[232:233], s[28:29], 0, v[166:167]
	s_add_i32 m0, s75, 0x2000
	s_add_i32 s75, s66, s47
	global_load_lds_dwordx4 v[232:233], off
	v_lshl_add_u64 v[230:231], v[230:231], 0, s[4:5]
	s_mov_b32 m0, s75
	s_nop 0
	global_load_lds_dwordx4 v[230:231], off
	v_lshl_add_u64 v[230:231], v[232:233], 0, s[4:5]
	s_add_i32 m0, s75, 0x2000
	s_nop 0
	global_load_lds_dwordx4 v[230:231], off
	v_lshl_add_u64 v[230:231], s[30:31], 0, v[174:175]
	s_mov_b32 m0, s48
	s_nop 0
	global_load_lds_dwordx4 v[230:231], off
	v_lshl_add_u64 v[230:231], s[30:31], 0, v[176:177]
	s_mov_b32 m0, s49
	s_nop 0
	global_load_lds_dwordx4 v[230:231], off
	s_waitcnt vmcnt(8)
	s_waitcnt lgkmcnt(0)
	s_barrier
	v_mfma_scale_f32_16x16x128_f8f6f4 v[94:97], v[18:25], v[198:205], 0, v195, v195 op_sel_hi:[0,0,0]
	v_mfma_scale_f32_16x16x128_f8f6f4 v[90:93], v[26:33], v[198:205], 0, v195, v195 op_sel_hi:[0,0,0]
	v_mfma_scale_f32_16x16x128_f8f6f4 v[78:81], v[18:25], v[206:213], 0, v195, v195 op_sel_hi:[0,0,0]
	v_mfma_scale_f32_16x16x128_f8f6f4 v[74:77], v[26:33], v[206:213], 0, v195, v195 op_sel_hi:[0,0,0]
	v_mfma_scale_f32_16x16x128_f8f6f4 v[62:65], v[18:25], v[214:221], 0, v195, v195 op_sel_hi:[0,0,0]
	v_mfma_scale_f32_16x16x128_f8f6f4 v[58:61], v[26:33], v[214:221], 0, v195, v195 op_sel_hi:[0,0,0]
	v_mfma_scale_f32_16x16x128_f8f6f4 v[46:49], v[18:25], v[222:229], 0, v195, v195 op_sel_hi:[0,0,0]
	v_mfma_scale_f32_16x16x128_f8f6f4 v[42:45], v[26:33], v[222:229], 0, v195, v195 op_sel_hi:[0,0,0]
	s_nop 3
	v_mfma_scale_f32_16x16x128_f8f6f4 v[86:89], v[2:9], v[198:205], 0, v195, v195 op_sel_hi:[0,0,0]
	v_mfma_scale_f32_16x16x128_f8f6f4 v[82:85], v[10:17], v[198:205], 0, v195, v195 op_sel_hi:[0,0,0]
	v_mfma_scale_f32_16x16x128_f8f6f4 v[70:73], v[2:9], v[206:213], 0, v195, v195 op_sel_hi:[0,0,0]
	v_mfma_scale_f32_16x16x128_f8f6f4 v[66:69], v[10:17], v[206:213], 0, v195, v195 op_sel_hi:[0,0,0]
	v_mfma_scale_f32_16x16x128_f8f6f4 v[54:57], v[2:9], v[214:221], 0, v195, v195 op_sel_hi:[0,0,0]
	v_mfma_scale_f32_16x16x128_f8f6f4 v[50:53], v[10:17], v[214:221], 0, v195, v195 op_sel_hi:[0,0,0]
	v_mfma_scale_f32_16x16x128_f8f6f4 v[38:41], v[2:9], v[222:229], 0, v195, v195 op_sel_hi:[0,0,0]
	v_mfma_scale_f32_16x16x128_f8f6f4 v[34:37], v[10:17], v[222:229], 0, v195, v195 op_sel_hi:[0,0,0]
	s_add_i32 s75, 0, 0x18000
	s_add_i32 s76, 0, 0x1c000
	v_add_u32_e32 v14, s75, v191
	v_add_u32_e32 v30, s76, v191
	ds_read_b128 v[2:5], v14
	ds_read_b128 v[6:9], v14 offset:1024
	ds_read_b128 v[10:13], v14 offset:2048
	ds_read_b128 v[14:17], v14 offset:3072
	ds_read_b128 v[18:21], v30
	ds_read_b128 v[22:25], v30 offset:1024
	ds_read_b128 v[26:29], v30 offset:2048
	ds_read_b128 v[30:33], v30 offset:3072
	s_mov_b32 m0, s50
	v_lshl_add_u64 v[230:231], s[30:31], 0, v[178:179]
	ds_read_b128 v[198:201], v194 offset:32768
	ds_read_b128 v[202:205], v194 offset:33792
	ds_read_b128 v[206:209], v194 offset:34816
	ds_read_b128 v[210:213], v194 offset:35840
	ds_read_b128 v[214:217], v194 offset:36864
	ds_read_b128 v[218:221], v194 offset:37888
	ds_read_b128 v[222:225], v194 offset:38912
	ds_read_b128 v[226:229], v194 offset:39936
	global_load_lds_dwordx4 v[230:231], off
	v_lshl_add_u64 v[230:231], s[30:31], 0, v[180:181]
	s_mov_b32 m0, s51
	s_nop 0
	global_load_lds_dwordx4 v[230:231], off
	s_waitcnt vmcnt(8)
	s_waitcnt lgkmcnt(0)
	s_barrier
; #define PG8_STAGE(bufoff, gbase, voff) do { _Pragma("unroll") for (int _i = 0; _i < 2; ++_i) \
;         __builtin_amdgcn_global_load_lds((const unsigned*)((const char*)(gbase) + (voff)[_i]), (PG8_LAS unsigned*)(lds + (bufoff) + ldsw + _i * 8192), 16, 0, 0); } while (0)
; #define PG8_WAIT_V(n) asm volatile("s_waitcnt vmcnt(" #n ")" ::: "memory")
; #define PG8_WAIT_L(n) asm volatile("s_waitcnt lgkmcnt(" #n ")" ::: "memory")
; #define PG8_BAR __builtin_amdgcn_s_barrier()
; #define PG8_SCHED __builtin_amdgcn_sched_barrier(0)
; template <class Epi, class Sched, bool ALIGN_EPI = true, bool F8 = false>
; __device__ __forceinline__ void gemm_phase(PG8_LAS unsigned char* lds, const Sched& S, const Epi& E) {
;     ...
;             PG8_LDB(B0, 0, 0); PG8_LDB(B1, 0, 1); PG8_SCHED; PG8_LDA(At, 0, 0); PG8_STAGE(PG8_SA(1, 1), a1, voffA[1]);
;             PG8_WAIT_V(8); PG8_WAIT_L(0); PG8_BAR; PG8_MMA(0, 0, At, B0); PG8_MMA(0, 1, At, B1); PG8_BAR; PG8_SCHED;
;             PG8_LDA(At, 0, 1); PG8_STAGE(PG8_SB(0, 0), b2, voffB[0]); PG8_STAGE(PG8_SB(0, 1), b2, voffB[1]); PG8_STAGE(PG8_SA(0, 0), a2, vA2[0]);
;             PG8_WAIT_V(8); PG8_WAIT_L(0); PG8_BAR; PG8_MMA(1, 0, At, B0); PG8_MMA(1, 1, At, B1); PG8_BAR; PG8_SCHED;
;             PG8_LDB(B0, 1, 0); PG8_LDB(B1, 1, 1); PG8_SCHED; PG8_LDA(At, 1, 0); PG8_STAGE(PG8_SA(0, 1), a2, vA2[1]);
;             PG8_WAIT_V(8); PG8_WAIT_L(0); PG8_BAR; PG8_MMA(0, 0, At, B0); PG8_MMA(0, 1, At, B1); PG8_BAR; PG8_SCHED;
;             PG8_LDA(At, 1, 1); PG8_STAGE(PG8_SB(1, 0), b3, voffB[0]); PG8_STAGE(PG8_SB(1, 1), b3, voffB[1]); PG8_STAGE(PG8_SA(1, 0), a3, vA2[0]);
;             PG8_WAIT_V(8); PG8_WAIT_L(0); PG8_BAR; PG8_MMA(1, 0, At, B0); PG8_MMA(1, 1, At, B1); PG8_BAR; PG8_SCHED;
	v_mfma_scale_f32_16x16x128_f8f6f4 v[158:161], v[2:9], v[198:205], v[158:161], v195, v195 op_sel_hi:[0,0,0]
	v_mfma_scale_f32_16x16x128_f8f6f4 v[154:157], v[10:17], v[198:205], v[154:157], v195, v195 op_sel_hi:[0,0,0]
	v_mfma_scale_f32_16x16x128_f8f6f4 v[142:145], v[2:9], v[206:213], v[142:145], v195, v195 op_sel_hi:[0,0,0]
	v_mfma_scale_f32_16x16x128_f8f6f4 v[138:141], v[10:17], v[206:213], v[138:141], v195, v195 op_sel_hi:[0,0,0]
	v_mfma_scale_f32_16x16x128_f8f6f4 v[126:129], v[2:9], v[214:221], v[126:129], v195, v195 op_sel_hi:[0,0,0]
	v_mfma_scale_f32_16x16x128_f8f6f4 v[122:125], v[10:17], v[214:221], v[122:125], v195, v195 op_sel_hi:[0,0,0]
	v_mfma_scale_f32_16x16x128_f8f6f4 v[110:113], v[2:9], v[222:229], v[110:113], v195, v195 op_sel_hi:[0,0,0]
	v_mfma_scale_f32_16x16x128_f8f6f4 v[106:109], v[10:17], v[222:229], v[106:109], v195, v195 op_sel_hi:[0,0,0]
	s_nop 3
	v_mfma_scale_f32_16x16x128_f8f6f4 v[150:153], v[18:25], v[198:205], v[150:153], v195, v195 op_sel_hi:[0,0,0]
	v_mfma_scale_f32_16x16x128_f8f6f4 v[146:149], v[26:33], v[198:205], v[146:149], v195, v195 op_sel_hi:[0,0,0]
	v_mfma_scale_f32_16x16x128_f8f6f4 v[134:137], v[18:25], v[206:213], v[134:137], v195, v195 op_sel_hi:[0,0,0]
	v_mfma_scale_f32_16x16x128_f8f6f4 v[130:133], v[26:33], v[206:213], v[130:133], v195, v195 op_sel_hi:[0,0,0]
	v_mfma_scale_f32_16x16x128_f8f6f4 v[118:121], v[18:25], v[214:221], v[118:121], v195, v195 op_sel_hi:[0,0,0]
	v_mfma_scale_f32_16x16x128_f8f6f4 v[114:117], v[26:33], v[214:221], v[114:117], v195, v195 op_sel_hi:[0,0,0]
	v_mfma_scale_f32_16x16x128_f8f6f4 v[102:105], v[18:25], v[222:229], v[102:105], v195, v195 op_sel_hi:[0,0,0]
	v_mfma_scale_f32_16x16x128_f8f6f4 v[98:101], v[26:33], v[222:229], v[98:101], v195, v195 op_sel_hi:[0,0,0]
	s_add_u32 s28, s28, 0x8000
	s_addc_u32 s29, s29, 0
	s_add_i32 s30, s75, s47
	v_lshl_add_u64 v[230:231], s[28:29], 0, v[164:165]
	s_mov_b32 m0, s30
	ds_read_b128 v[198:201], v194 offset:49152
	ds_read_b128 v[202:205], v194 offset:50176
	ds_read_b128 v[206:209], v194 offset:51200
	ds_read_b128 v[210:213], v194 offset:52224
	ds_read_b128 v[214:217], v194 offset:53248
	ds_read_b128 v[218:221], v194 offset:54272
	ds_read_b128 v[222:225], v194 offset:55296
	ds_read_b128 v[226:229], v194 offset:56320
	global_load_lds_dwordx4 v[230:231], off
	v_lshl_add_u64 v[230:231], s[28:29], 0, v[166:167]
	s_add_i32 m0, s30, 0x2000
	s_add_i32 s30, s76, s47
	global_load_lds_dwordx4 v[230:231], off
	v_lshl_add_u64 v[230:231], s[28:29], 0, v[168:169]
	s_mov_b32 m0, s30
	s_nop 0
	global_load_lds_dwordx4 v[230:231], off
	v_lshl_add_u64 v[230:231], s[28:29], 0, v[172:173]
	s_add_i32 m0, s30, 0x2000
	s_nop 0
	global_load_lds_dwordx4 v[230:231], off
	v_lshl_add_u64 v[230:231], s[26:27], 0, v[174:175]
	s_mov_b32 m0, s60
	s_nop 0
	global_load_lds_dwordx4 v[230:231], off
	v_lshl_add_u64 v[230:231], s[26:27], 0, v[176:177]
	s_mov_b32 m0, s61
	s_nop 0
	global_load_lds_dwordx4 v[230:231], off
	s_waitcnt vmcnt(8)
	s_waitcnt lgkmcnt(0)
	s_barrier
	v_mfma_scale_f32_16x16x128_f8f6f4 v[94:97], v[2:9], v[198:205], v[94:97], v195, v195 op_sel_hi:[0,0,0]
	v_mfma_scale_f32_16x16x128_f8f6f4 v[90:93], v[10:17], v[198:205], v[90:93], v195, v195 op_sel_hi:[0,0,0]
	v_mfma_scale_f32_16x16x128_f8f6f4 v[78:81], v[2:9], v[206:213], v[78:81], v195, v195 op_sel_hi:[0,0,0]
	v_mfma_scale_f32_16x16x128_f8f6f4 v[74:77], v[10:17], v[206:213], v[74:77], v195, v195 op_sel_hi:[0,0,0]
	v_mfma_scale_f32_16x16x128_f8f6f4 v[62:65], v[2:9], v[214:221], v[62:65], v195, v195 op_sel_hi:[0,0,0]
	v_mfma_scale_f32_16x16x128_f8f6f4 v[58:61], v[10:17], v[214:221], v[58:61], v195, v195 op_sel_hi:[0,0,0]
	v_mfma_scale_f32_16x16x128_f8f6f4 v[46:49], v[2:9], v[222:229], v[46:49], v195, v195 op_sel_hi:[0,0,0]
	v_mfma_scale_f32_16x16x128_f8f6f4 v[42:45], v[10:17], v[222:229], v[42:45], v195, v195 op_sel_hi:[0,0,0]
	s_nop 3
	v_mfma_scale_f32_16x16x128_f8f6f4 v[86:89], v[18:25], v[198:205], v[86:89], v195, v195 op_sel_hi:[0,0,0]
	v_mfma_scale_f32_16x16x128_f8f6f4 v[82:85], v[26:33], v[198:205], v[82:85], v195, v195 op_sel_hi:[0,0,0]
	v_mfma_scale_f32_16x16x128_f8f6f4 v[70:73], v[18:25], v[206:213], v[70:73], v195, v195 op_sel_hi:[0,0,0]
	v_mfma_scale_f32_16x16x128_f8f6f4 v[66:69], v[26:33], v[206:213], v[66:69], v195, v195 op_sel_hi:[0,0,0]
	v_mfma_scale_f32_16x16x128_f8f6f4 v[54:57], v[18:25], v[214:221], v[54:57], v195, v195 op_sel_hi:[0,0,0]
	v_mfma_scale_f32_16x16x128_f8f6f4 v[50:53], v[26:33], v[214:221], v[50:53], v195, v195 op_sel_hi:[0,0,0]
	v_mfma_scale_f32_16x16x128_f8f6f4 v[38:41], v[18:25], v[222:229], v[38:41], v195, v195 op_sel_hi:[0,0,0]
	v_mfma_scale_f32_16x16x128_f8f6f4 v[34:37], v[26:33], v[222:229], v[34:37], v195, v195 op_sel_hi:[0,0,0]
	s_add_i32 s74, s74, 2
	s_add_u32 s17, s17, 0x10000
	s_addc_u32 s19, s19, 0
	s_add_u32 s24, s24, 0x10000
	s_addc_u32 s25, s25, 0
	s_cmp_gt_u32 s74, 13
	s_cbranch_scc0 .Lh1_428
	s_branch .Lfx_11141
; #define PG8_STAGE(bufoff, gbase, voff) do { _Pragma("unroll") for (int _i = 0; _i < 2; ++_i) \
;         __builtin_amdgcn_global_load_lds((const unsigned*)((const char*)(gbase) + (voff)[_i]), (PG8_LAS unsigned*)(lds + (bufoff) + ldsw + _i * 8192), 16, 0, 0); } while (0)
; #define PG8_WAIT_V(n) asm volatile("s_waitcnt vmcnt(" #n ")" ::: "memory")
; #define PG8_WAIT_L(n) asm volatile("s_waitcnt lgkmcnt(" #n ")" ::: "memory")
; #define PG8_BAR __builtin_amdgcn_s_barrier()
; #define PG8_SCHED __builtin_amdgcn_sched_barrier(0)
; template <class Epi, class Sched, bool ALIGN_EPI = true, bool F8 = false>
; __device__ __forceinline__ void gemm_phase(PG8_LAS unsigned char* lds, const Sched& S, const Epi& E) {
;     ...
;             PG8_LDB(B0, 0, 0); PG8_LDB(B1, 0, 1); PG8_SCHED; PG8_LDA(At, 0, 0); PG8_STAGE(PG8_SA(1, 1), a1, voffA[1]);
;             PG8_WAIT_V(8); PG8_WAIT_L(0); PG8_BAR; PG8_MMA(0, 0, At, B0); PG8_MMA(0, 1, At, B1); PG8_BAR; PG8_SCHED;
;             PG8_LDA(At, 0, 1); PG8_STAGE(PG8_SB(0, 0), b2, voffB[0]); PG8_STAGE(PG8_SB(0, 1), b2, voffB[1]); PG8_STAGE(PG8_SA(0, 0), a2, vA2[0]);
;             PG8_WAIT_V(8); PG8_WAIT_L(0); PG8_BAR; PG8_MMA(1, 0, At, B0); PG8_MMA(1, 1, At, B1); PG8_BAR; PG8_SCHED;
;             PG8_LDB(B0, 1, 0); PG8_LDB(B1, 1, 1); PG8_SCHED; PG8_LDA(At, 1, 0); PG8_STAGE(PG8_SA(0, 1), a2, vA2[1]);
;             PG8_WAIT_V(8); PG8_WAIT_L(0); PG8_BAR; PG8_MMA(0, 0, At, B0); PG8_MMA(0, 1, At, B1); PG8_BAR; PG8_SCHED;
;             PG8_LDA(At, 1, 1); PG8_STAGE(PG8_SB(1, 0), b3, voffB[0]); PG8_STAGE(PG8_SB(1, 1), b3, voffB[1]); PG8_STAGE(PG8_SA(1, 0), a3, vA2[0]);
;             PG8_WAIT_V(8); PG8_WAIT_L(0); PG8_BAR; PG8_MMA(1, 0, At, B0); PG8_MMA(1, 1, At, B1); PG8_BAR; PG8_SCHED;
.Lh1_428:
	ds_read_b128 v[18:21], v192
	ds_read_b128 v[22:25], v192 offset:1024
	ds_read_b128 v[26:29], v192 offset:2048
	ds_read_b128 v[30:33], v192 offset:3072
	ds_read_b128 v[2:5], v193
	ds_read_b128 v[6:9], v193 offset:1024
	ds_read_b128 v[10:13], v193 offset:2048
	ds_read_b128 v[14:17], v193 offset:3072
	s_add_u32 s26, s24, 0x8000
	s_addc_u32 s27, s25, 0
	s_cmp_eq_u32 s74, 12
	s_cselect_b32 s30, s20, s26
	s_cselect_b32 s31, s21, s27
	s_cselect_b32 s28, s22, s17
	s_cselect_b32 s29, s23, s19
	s_add_u32 s26, s30, 0x8000
	s_addc_u32 s27, s31, 0
	v_lshl_add_u64 v[230:231], s[24:25], 0, v[184:185]
	s_add_i32 m0, s48, 0xc000
	ds_read_b128 v[198:201], v194
	ds_read_b128 v[202:205], v194 offset:1024
	ds_read_b128 v[206:209], v194 offset:2048
	ds_read_b128 v[210:213], v194 offset:3072
	ds_read_b128 v[214:217], v194 offset:4096
	ds_read_b128 v[218:221], v194 offset:5120
	ds_read_b128 v[222:225], v194 offset:6144
	ds_read_b128 v[226:229], v194 offset:7168
	global_load_lds_dwordx4 v[230:231], off
	v_lshl_add_u64 v[230:231], s[24:25], 0, v[182:183]
	s_add_i32 m0, s48, 0xe000
	s_nop 0
	global_load_lds_dwordx4 v[230:231], off
	s_waitcnt vmcnt(8)
	s_waitcnt lgkmcnt(0)
	s_barrier
	v_mfma_scale_f32_16x16x128_f8f6f4 v[158:161], v[18:25], v[198:205], v[158:161], v195, v195 op_sel_hi:[0,0,0]
	v_mfma_scale_f32_16x16x128_f8f6f4 v[154:157], v[26:33], v[198:205], v[154:157], v195, v195 op_sel_hi:[0,0,0]
	v_mfma_scale_f32_16x16x128_f8f6f4 v[142:145], v[18:25], v[206:213], v[142:145], v195, v195 op_sel_hi:[0,0,0]
	v_mfma_scale_f32_16x16x128_f8f6f4 v[138:141], v[26:33], v[206:213], v[138:141], v195, v195 op_sel_hi:[0,0,0]
	v_mfma_scale_f32_16x16x128_f8f6f4 v[126:129], v[18:25], v[214:221], v[126:129], v195, v195 op_sel_hi:[0,0,0]
	v_mfma_scale_f32_16x16x128_f8f6f4 v[122:125], v[26:33], v[214:221], v[122:125], v195, v195 op_sel_hi:[0,0,0]
	v_mfma_scale_f32_16x16x128_f8f6f4 v[110:113], v[18:25], v[222:229], v[110:113], v195, v195 op_sel_hi:[0,0,0]
	v_mfma_scale_f32_16x16x128_f8f6f4 v[106:109], v[26:33], v[222:229], v[106:109], v195, v195 op_sel_hi:[0,0,0]
	s_nop 3
	v_mfma_scale_f32_16x16x128_f8f6f4 v[150:153], v[2:9], v[198:205], v[150:153], v195, v195 op_sel_hi:[0,0,0]
	v_mfma_scale_f32_16x16x128_f8f6f4 v[146:149], v[10:17], v[198:205], v[146:149], v195, v195 op_sel_hi:[0,0,0]
	v_mfma_scale_f32_16x16x128_f8f6f4 v[134:137], v[2:9], v[206:213], v[134:137], v195, v195 op_sel_hi:[0,0,0]
	v_mfma_scale_f32_16x16x128_f8f6f4 v[130:133], v[10:17], v[206:213], v[130:133], v195, v195 op_sel_hi:[0,0,0]
	v_mfma_scale_f32_16x16x128_f8f6f4 v[118:121], v[2:9], v[214:221], v[118:121], v195, v195 op_sel_hi:[0,0,0]
	v_mfma_scale_f32_16x16x128_f8f6f4 v[114:117], v[10:17], v[214:221], v[114:117], v195, v195 op_sel_hi:[0,0,0]
	v_mfma_scale_f32_16x16x128_f8f6f4 v[102:105], v[2:9], v[222:229], v[102:105], v195, v195 op_sel_hi:[0,0,0]
	v_mfma_scale_f32_16x16x128_f8f6f4 v[98:101], v[10:17], v[222:229], v[98:101], v195, v195 op_sel_hi:[0,0,0]
	s_add_i32 s75, s65, s47
	v_lshl_add_u64 v[230:231], s[28:29], 0, v[164:165]
	s_mov_b32 m0, s75
	ds_read_b128 v[198:201], v194 offset:16384
	ds_read_b128 v[202:205], v194 offset:17408
	ds_read_b128 v[206:209], v194 offset:18432
	ds_read_b128 v[210:213], v194 offset:19456
	ds_read_b128 v[214:217], v194 offset:20480
	ds_read_b128 v[218:221], v194 offset:21504
	ds_read_b128 v[222:225], v194 offset:22528
	ds_read_b128 v[226:229], v194 offset:23552
	global_load_lds_dwordx4 v[230:231], off
	v_lshl_add_u64 v[232:233], s[28:29], 0, v[166:167]
	s_add_i32 m0, s75, 0x2000
	s_add_i32 s75, s66, s47
	global_load_lds_dwordx4 v[232:233], off
	v_lshl_add_u64 v[230:231], v[230:231], 0, s[4:5]
	s_mov_b32 m0, s75
	s_nop 0
	global_load_lds_dwordx4 v[230:231], off
	v_lshl_add_u64 v[230:231], v[232:233], 0, s[4:5]
	s_add_i32 m0, s75, 0x2000
	s_nop 0
	global_load_lds_dwordx4 v[230:231], off
	v_lshl_add_u64 v[230:231], s[30:31], 0, v[174:175]
	s_mov_b32 m0, s48
	s_nop 0
	global_load_lds_dwordx4 v[230:231], off
	v_lshl_add_u64 v[230:231], s[30:31], 0, v[176:177]
	s_mov_b32 m0, s49
	s_nop 0
	global_load_lds_dwordx4 v[230:231], off
	s_waitcnt vmcnt(8)
	s_waitcnt lgkmcnt(0)
	s_barrier
	v_mfma_scale_f32_16x16x128_f8f6f4 v[94:97], v[18:25], v[198:205], v[94:97], v195, v195 op_sel_hi:[0,0,0]
	v_mfma_scale_f32_16x16x128_f8f6f4 v[90:93], v[26:33], v[198:205], v[90:93], v195, v195 op_sel_hi:[0,0,0]
	v_mfma_scale_f32_16x16x128_f8f6f4 v[78:81], v[18:25], v[206:213], v[78:81], v195, v195 op_sel_hi:[0,0,0]
	v_mfma_scale_f32_16x16x128_f8f6f4 v[74:77], v[26:33], v[206:213], v[74:77], v195, v195 op_sel_hi:[0,0,0]
	v_mfma_scale_f32_16x16x128_f8f6f4 v[62:65], v[18:25], v[214:221], v[62:65], v195, v195 op_sel_hi:[0,0,0]
	v_mfma_scale_f32_16x16x128_f8f6f4 v[58:61], v[26:33], v[214:221], v[58:61], v195, v195 op_sel_hi:[0,0,0]
	v_mfma_scale_f32_16x16x128_f8f6f4 v[46:49], v[18:25], v[222:229], v[46:49], v195, v195 op_sel_hi:[0,0,0]
	v_mfma_scale_f32_16x16x128_f8f6f4 v[42:45], v[26:33], v[222:229], v[42:45], v195, v195 op_sel_hi:[0,0,0]
	s_nop 3
	v_mfma_scale_f32_16x16x128_f8f6f4 v[86:89], v[2:9], v[198:205], v[86:89], v195, v195 op_sel_hi:[0,0,0]
	v_mfma_scale_f32_16x16x128_f8f6f4 v[82:85], v[10:17], v[198:205], v[82:85], v195, v195 op_sel_hi:[0,0,0]
	v_mfma_scale_f32_16x16x128_f8f6f4 v[70:73], v[2:9], v[206:213], v[70:73], v195, v195 op_sel_hi:[0,0,0]
	v_mfma_scale_f32_16x16x128_f8f6f4 v[66:69], v[10:17], v[206:213], v[66:69], v195, v195 op_sel_hi:[0,0,0]
	v_mfma_scale_f32_16x16x128_f8f6f4 v[54:57], v[2:9], v[214:221], v[54:57], v195, v195 op_sel_hi:[0,0,0]
	v_mfma_scale_f32_16x16x128_f8f6f4 v[50:53], v[10:17], v[214:221], v[50:53], v195, v195 op_sel_hi:[0,0,0]
	v_mfma_scale_f32_16x16x128_f8f6f4 v[38:41], v[2:9], v[222:229], v[38:41], v195, v195 op_sel_hi:[0,0,0]
	v_mfma_scale_f32_16x16x128_f8f6f4 v[34:37], v[10:17], v[222:229], v[34:37], v195, v195 op_sel_hi:[0,0,0]
	s_add_i32 s75, 0, 0x18000
	s_add_i32 s76, 0, 0x1c000
	v_add_u32_e32 v14, s75, v191
	v_add_u32_e32 v30, s76, v191
	ds_read_b128 v[2:5], v14
	ds_read_b128 v[6:9], v14 offset:1024
	ds_read_b128 v[10:13], v14 offset:2048
	ds_read_b128 v[14:17], v14 offset:3072
	ds_read_b128 v[18:21], v30
	ds_read_b128 v[22:25], v30 offset:1024
	ds_read_b128 v[26:29], v30 offset:2048
	ds_read_b128 v[30:33], v30 offset:3072
	s_mov_b32 m0, s50
	v_lshl_add_u64 v[230:231], s[30:31], 0, v[178:179]
	ds_read_b128 v[198:201], v194 offset:32768
	ds_read_b128 v[202:205], v194 offset:33792
	ds_read_b128 v[206:209], v194 offset:34816
	ds_read_b128 v[210:213], v194 offset:35840
	ds_read_b128 v[214:217], v194 offset:36864
	ds_read_b128 v[218:221], v194 offset:37888
	ds_read_b128 v[222:225], v194 offset:38912
	ds_read_b128 v[226:229], v194 offset:39936
	global_load_lds_dwordx4 v[230:231], off
	v_lshl_add_u64 v[230:231], s[30:31], 0, v[180:181]
	s_mov_b32 m0, s51
	s_nop 0
	global_load_lds_dwordx4 v[230:231], off
	s_waitcnt vmcnt(8)
	s_waitcnt lgkmcnt(0)
	s_barrier
; #define PG8_STAGE(bufoff, gbase, voff) do { _Pragma("unroll") for (int _i = 0; _i < 2; ++_i) \
;         __builtin_amdgcn_global_load_lds((const unsigned*)((const char*)(gbase) + (voff)[_i]), (PG8_LAS unsigned*)(lds + (bufoff) + ldsw + _i * 8192), 16, 0, 0); } while (0)
; #define PG8_WAIT_V(n) asm volatile("s_waitcnt vmcnt(" #n ")" ::: "memory")
; #define PG8_WAIT_L(n) asm volatile("s_waitcnt lgkmcnt(" #n ")" ::: "memory")
; #define PG8_BAR __builtin_amdgcn_s_barrier()
; #define PG8_SCHED __builtin_amdgcn_sched_barrier(0)
; template <class Epi, class Sched, bool ALIGN_EPI = true, bool F8 = false>
; __device__ __forceinline__ void gemm_phase(PG8_LAS unsigned char* lds, const Sched& S, const Epi& E) {
;     ...
;             PG8_LDB(B0, 0, 0); PG8_LDB(B1, 0, 1); PG8_SCHED; PG8_LDA(At, 0, 0); PG8_STAGE(PG8_SA(1, 1), a1, voffA[1]);
;             PG8_WAIT_V(8); PG8_WAIT_L(0); PG8_BAR; PG8_MMA(0, 0, At, B0); PG8_MMA(0, 1, At, B1); PG8_BAR; PG8_SCHED;
;             PG8_LDA(At, 0, 1); PG8_STAGE(PG8_SB(0, 0), b2, voffB[0]); PG8_STAGE(PG8_SB(0, 1), b2, voffB[1]); PG8_STAGE(PG8_SA(0, 0), a2, vA2[0]);
;             PG8_WAIT_V(8); PG8_WAIT_L(0); PG8_BAR; PG8_MMA(1, 0, At, B0); PG8_MMA(1, 1, At, B1); PG8_BAR; PG8_SCHED;
;             PG8_LDB(B0, 1, 0); PG8_LDB(B1, 1, 1); PG8_SCHED; PG8_LDA(At, 1, 0); PG8_STAGE(PG8_SA(0, 1), a2, vA2[1]);
;             PG8_WAIT_V(8); PG8_WAIT_L(0); PG8_BAR; PG8_MMA(0, 0, At, B0); PG8_MMA(0, 1, At, B1); PG8_BAR; PG8_SCHED;
;             PG8_LDA(At, 1, 1); PG8_STAGE(PG8_SB(1, 0), b3, voffB[0]); PG8_STAGE(PG8_SB(1, 1), b3, voffB[1]); PG8_STAGE(PG8_SA(1, 0), a3, vA2[0]);
;             PG8_WAIT_V(8); PG8_WAIT_L(0); PG8_BAR; PG8_MMA(1, 0, At, B0); PG8_MMA(1, 1, At, B1); PG8_BAR; PG8_SCHED;
	v_mfma_scale_f32_16x16x128_f8f6f4 v[158:161], v[2:9], v[198:205], v[158:161], v195, v195 op_sel_hi:[0,0,0]
	v_mfma_scale_f32_16x16x128_f8f6f4 v[154:157], v[10:17], v[198:205], v[154:157], v195, v195 op_sel_hi:[0,0,0]
	v_mfma_scale_f32_16x16x128_f8f6f4 v[142:145], v[2:9], v[206:213], v[142:145], v195, v195 op_sel_hi:[0,0,0]
	v_mfma_scale_f32_16x16x128_f8f6f4 v[138:141], v[10:17], v[206:213], v[138:141], v195, v195 op_sel_hi:[0,0,0]
	v_mfma_scale_f32_16x16x128_f8f6f4 v[126:129], v[2:9], v[214:221], v[126:129], v195, v195 op_sel_hi:[0,0,0]
	v_mfma_scale_f32_16x16x128_f8f6f4 v[122:125], v[10:17], v[214:221], v[122:125], v195, v195 op_sel_hi:[0,0,0]
	v_mfma_scale_f32_16x16x128_f8f6f4 v[110:113], v[2:9], v[222:229], v[110:113], v195, v195 op_sel_hi:[0,0,0]
	v_mfma_scale_f32_16x16x128_f8f6f4 v[106:109], v[10:17], v[222:229], v[106:109], v195, v195 op_sel_hi:[0,0,0]
	s_nop 3
	v_mfma_scale_f32_16x16x128_f8f6f4 v[150:153], v[18:25], v[198:205], v[150:153], v195, v195 op_sel_hi:[0,0,0]
	v_mfma_scale_f32_16x16x128_f8f6f4 v[146:149], v[26:33], v[198:205], v[146:149], v195, v195 op_sel_hi:[0,0,0]
	v_mfma_scale_f32_16x16x128_f8f6f4 v[134:137], v[18:25], v[206:213], v[134:137], v195, v195 op_sel_hi:[0,0,0]
	v_mfma_scale_f32_16x16x128_f8f6f4 v[130:133], v[26:33], v[206:213], v[130:133], v195, v195 op_sel_hi:[0,0,0]
	v_mfma_scale_f32_16x16x128_f8f6f4 v[118:121], v[18:25], v[214:221], v[118:121], v195, v195 op_sel_hi:[0,0,0]
	v_mfma_scale_f32_16x16x128_f8f6f4 v[114:117], v[26:33], v[214:221], v[114:117], v195, v195 op_sel_hi:[0,0,0]
	v_mfma_scale_f32_16x16x128_f8f6f4 v[102:105], v[18:25], v[222:229], v[102:105], v195, v195 op_sel_hi:[0,0,0]
	v_mfma_scale_f32_16x16x128_f8f6f4 v[98:101], v[26:33], v[222:229], v[98:101], v195, v195 op_sel_hi:[0,0,0]
	s_add_u32 s28, s28, 0x8000
	s_addc_u32 s29, s29, 0
	s_add_i32 s30, s75, s47
	v_lshl_add_u64 v[230:231], s[28:29], 0, v[164:165]
	s_mov_b32 m0, s30
	ds_read_b128 v[198:201], v194 offset:49152
	ds_read_b128 v[202:205], v194 offset:50176
	ds_read_b128 v[206:209], v194 offset:51200
	ds_read_b128 v[210:213], v194 offset:52224
	ds_read_b128 v[214:217], v194 offset:53248
	ds_read_b128 v[218:221], v194 offset:54272
	ds_read_b128 v[222:225], v194 offset:55296
	ds_read_b128 v[226:229], v194 offset:56320
	global_load_lds_dwordx4 v[230:231], off
	v_lshl_add_u64 v[230:231], s[28:29], 0, v[166:167]
	s_add_i32 m0, s30, 0x2000
	s_add_i32 s30, s76, s47
	global_load_lds_dwordx4 v[230:231], off
	v_lshl_add_u64 v[230:231], s[28:29], 0, v[168:169]
	s_mov_b32 m0, s30
	s_nop 0
	global_load_lds_dwordx4 v[230:231], off
	v_lshl_add_u64 v[230:231], s[28:29], 0, v[172:173]
	s_add_i32 m0, s30, 0x2000
	s_nop 0
	global_load_lds_dwordx4 v[230:231], off
	v_lshl_add_u64 v[230:231], s[26:27], 0, v[174:175]
	s_mov_b32 m0, s60
	s_nop 0
	global_load_lds_dwordx4 v[230:231], off
	v_lshl_add_u64 v[230:231], s[26:27], 0, v[176:177]
	s_mov_b32 m0, s61
	s_nop 0
	global_load_lds_dwordx4 v[230:231], off
	s_waitcnt vmcnt(8)
	s_waitcnt lgkmcnt(0)
	s_barrier
	v_mfma_scale_f32_16x16x128_f8f6f4 v[94:97], v[2:9], v[198:205], v[94:97], v195, v195 op_sel_hi:[0,0,0]
	v_mfma_scale_f32_16x16x128_f8f6f4 v[90:93], v[10:17], v[198:205], v[90:93], v195, v195 op_sel_hi:[0,0,0]
	v_mfma_scale_f32_16x16x128_f8f6f4 v[78:81], v[2:9], v[206:213], v[78:81], v195, v195 op_sel_hi:[0,0,0]
	v_mfma_scale_f32_16x16x128_f8f6f4 v[74:77], v[10:17], v[206:213], v[74:77], v195, v195 op_sel_hi:[0,0,0]
	v_mfma_scale_f32_16x16x128_f8f6f4 v[62:65], v[2:9], v[214:221], v[62:65], v195, v195 op_sel_hi:[0,0,0]
	v_mfma_scale_f32_16x16x128_f8f6f4 v[58:61], v[10:17], v[214:221], v[58:61], v195, v195 op_sel_hi:[0,0,0]
	v_mfma_scale_f32_16x16x128_f8f6f4 v[46:49], v[2:9], v[222:229], v[46:49], v195, v195 op_sel_hi:[0,0,0]
	v_mfma_scale_f32_16x16x128_f8f6f4 v[42:45], v[10:17], v[222:229], v[42:45], v195, v195 op_sel_hi:[0,0,0]
	s_nop 3
	v_mfma_scale_f32_16x16x128_f8f6f4 v[86:89], v[18:25], v[198:205], v[86:89], v195, v195 op_sel_hi:[0,0,0]
	v_mfma_scale_f32_16x16x128_f8f6f4 v[82:85], v[26:33], v[198:205], v[82:85], v195, v195 op_sel_hi:[0,0,0]
	v_mfma_scale_f32_16x16x128_f8f6f4 v[70:73], v[18:25], v[206:213], v[70:73], v195, v195 op_sel_hi:[0,0,0]
	v_mfma_scale_f32_16x16x128_f8f6f4 v[66:69], v[26:33], v[206:213], v[66:69], v195, v195 op_sel_hi:[0,0,0]
	v_mfma_scale_f32_16x16x128_f8f6f4 v[54:57], v[18:25], v[214:221], v[54:57], v195, v195 op_sel_hi:[0,0,0]
	v_mfma_scale_f32_16x16x128_f8f6f4 v[50:53], v[26:33], v[214:221], v[50:53], v195, v195 op_sel_hi:[0,0,0]
	v_mfma_scale_f32_16x16x128_f8f6f4 v[38:41], v[18:25], v[222:229], v[38:41], v195, v195 op_sel_hi:[0,0,0]
	v_mfma_scale_f32_16x16x128_f8f6f4 v[34:37], v[26:33], v[222:229], v[34:37], v195, v195 op_sel_hi:[0,0,0]
	s_add_i32 s74, s74, 2
	s_add_u32 s17, s17, 0x10000
	s_addc_u32 s19, s19, 0
	s_add_u32 s24, s24, 0x10000
	s_addc_u32 s25, s25, 0
	s_cmp_gt_u32 s74, 13
	s_cbranch_scc0 .Lh1_428
.Lfx_11141:
	s_setprio 0
	s_and_b64 vcc, exec, s[12:13]
	s_cbranch_vccz .LBB0_431

; #define PG8_WAIT_V(n) asm volatile("s_waitcnt vmcnt(" #n ")" ::: "memory")
; #define PG8_WAIT_L(n) asm volatile("s_waitcnt lgkmcnt(" #n ")" ::: "memory")
; #define PG8_BAR __builtin_amdgcn_s_barrier()
; #define PG8_SCHED __builtin_amdgcn_sched_barrier(0)
; template <class Epi, class Sched, bool ALIGN_EPI = true, bool F8 = false>
; __device__ __forceinline__ void gemm_phase(PG8_LAS unsigned char* lds, const Sched& S, const Epi& E) {
;     ...
;     for (;;) {
;         const bool has_next = S.next(ui + 1, nxt);
;         const char* nA = has_next ? nxt.A : cA; const char* nB = has_next ? nxt.B : cB;
;         const int nt = cur.nt;
; #pragma unroll 1
;         for (int t = 0; t < nt; t += 2) {
;             const bool last = (t == nt - 2);
;             if constexpr (Sched::GATHER) { if (last && has_next) S.a_off(nxt, Rs, Cs, voffAn); }
;             const char* a1 = cA + (size_t)(t + 1) * kstep;
;             const char* a2 = last ? nA : cA + (size_t)(t + 2) * kstep; const char* b2 = last ? nB : cB + (size_t)(t + 2) * kstepB;
;             const char* a3 = a2 + kstep; const char* b3 = b2 + kstepB;
;             unsigned vA2[2][2];
; #pragma unroll
;             for (int h = 0; h < 2; ++h)
; #pragma unroll
;                 for (int i = 0; i < 2; ++i) { if constexpr (Sched::GATHER) vA2[h][i] = (last && has_next) ? voffAn[h][i] : voffA[h][i]; else vA2[h][i] = voffA[h][i]; }
;             PG8_LDB(B0, 0, 0); PG8_LDB(B1, 0, 1); PG8_SCHED; PG8_LDA(At, 0, 0); PG8_STAGE(PG8_SA(1, 1), a1, voffA[1]);
;             PG8_WAIT_V(8); PG8_WAIT_L(0); PG8_BAR; PG8_MMA(0, 0, At, B0); PG8_MMA(0, 1, At, B1); PG8_BAR; PG8_SCHED;
;             PG8_LDA(At, 0, 1); PG8_STAGE(PG8_SB(0, 0), b2, voffB[0]); PG8_STAGE(PG8_SB(0, 1), b2, voffB[1]); PG8_STAGE(PG8_SA(0, 0), a2, vA2[0]);
;             PG8_WAIT_V(8); PG8_WAIT_L(0); PG8_BAR; PG8_MMA(1, 0, At, B0); PG8_MMA(1, 1, At, B1); PG8_BAR; PG8_SCHED;
;             PG8_LDB(B0, 1, 0); PG8_LDB(B1, 1, 1); PG8_SCHED; PG8_LDA(At, 1, 0); PG8_STAGE(PG8_SA(0, 1), a2, vA2[1]);
;             PG8_WAIT_V(8); PG8_WAIT_L(0); PG8_BAR; PG8_MMA(0, 0, At, B0); PG8_MMA(0, 1, At, B1); PG8_BAR; PG8_SCHED;
;             PG8_LDA(At, 1, 1); PG8_STAGE(PG8_SB(1, 0), b3, voffB[0]); PG8_STAGE(PG8_SB(1, 1), b3, voffB[1]); PG8_STAGE(PG8_SA(1, 0), a3, vA2[0]);
;             PG8_WAIT_V(8); PG8_WAIT_L(0); PG8_BAR; PG8_MMA(1, 0, At, B0); PG8_MMA(1, 1, At, B1); PG8_BAR; PG8_SCHED;
.LBB0_833:
	s_add_i32 s74, s72, -2
	s_add_u32 s75, s26, 0x10000
	s_addc_u32 s76, s27, 0
	s_add_u32 s24, s24, 0x8000
	s_addc_u32 s25, s25, 0
	s_mov_b32 s26, 0
	s_bitcmp1_b32 s3, 2
	s_cbranch_scc1 .Lh1e_23459
	s_setprio 1
.LBB0_834:
	v_add_u32_e32 v10, s58, v190
	ds_read_b128 v[2:5], v10
	ds_read_b128 v[6:9], v10 offset:1024
	ds_read_b128 v[142:145], v10 offset:2048
	ds_read_b128 v[146:149], v10 offset:3072
	v_add_u32_e32 v10, s59, v190
	ds_read_b128 v[150:153], v10
	ds_read_b128 v[154:157], v10 offset:1024
	ds_read_b128 v[202:205], v10 offset:2048
	ds_read_b128 v[206:209], v10 offset:3072
	s_add_i32 s77, s26, 2
	s_add_u32 s27, s24, 0x8000
	s_addc_u32 s28, s25, 0
	s_cmp_eq_u32 s74, s26
	s_cselect_b32 s30, s20, s27
	s_cselect_b32 s31, s21, s28
	s_cselect_b32 s28, s22, s75
	s_cselect_b32 s29, s23, s76
	s_add_u32 s26, s30, 0x8000
	s_addc_u32 s27, s31, 0
	v_lshl_add_u64 v[12:13], s[24:25], 0, v[182:183]
	s_add_i32 m0, s45, 0xc000
	ds_read_b128 v[210:213], v198
	ds_read_b128 v[214:217], v198 offset:1024
	ds_read_b128 v[218:221], v198 offset:2048
	ds_read_b128 v[222:225], v198 offset:3072
	ds_read_b128 v[226:229], v198 offset:4096
	ds_read_b128 v[230:233], v198 offset:5120
	ds_read_b128 v[234:237], v198 offset:6144
	ds_read_b128 v[238:241], v198 offset:7168
	global_load_lds_dwordx4 v[12:13], off
	v_lshl_add_u64 v[12:13], s[24:25], 0, v[180:181]
	s_add_i32 m0, s45, 0xe000
	s_nop 0
	global_load_lds_dwordx4 v[12:13], off
	s_waitcnt vmcnt(8)
	s_waitcnt lgkmcnt(0)
	v_mfma_scale_f32_16x16x128_f8f6f4 v[138:141], v[2:9], v[210:217], v[138:141], v199, v199 op_sel_hi:[0,0,0]
	v_mfma_scale_f32_16x16x128_f8f6f4 v[134:137], v[142:149], v[210:217], v[134:137], v199, v199 op_sel_hi:[0,0,0]
	v_mfma_scale_f32_16x16x128_f8f6f4 v[130:133], v[2:9], v[218:225], v[130:133], v199, v199 op_sel_hi:[0,0,0]
	v_mfma_scale_f32_16x16x128_f8f6f4 v[126:129], v[142:149], v[218:225], v[126:129], v199, v199 op_sel_hi:[0,0,0]
	v_mfma_scale_f32_16x16x128_f8f6f4 v[122:125], v[2:9], v[226:233], v[122:125], v199, v199 op_sel_hi:[0,0,0]
	v_mfma_scale_f32_16x16x128_f8f6f4 v[118:121], v[142:149], v[226:233], v[118:121], v199, v199 op_sel_hi:[0,0,0]
	v_mfma_scale_f32_16x16x128_f8f6f4 v[114:117], v[2:9], v[234:241], v[114:117], v199, v199 op_sel_hi:[0,0,0]
	v_mfma_scale_f32_16x16x128_f8f6f4 v[110:113], v[142:149], v[234:241], v[110:113], v199, v199 op_sel_hi:[0,0,0]
	s_nop 3
	v_mfma_scale_f32_16x16x128_f8f6f4 v[106:109], v[150:157], v[210:217], v[106:109], v199, v199 op_sel_hi:[0,0,0]
	v_mfma_scale_f32_16x16x128_f8f6f4 v[102:105], v[202:209], v[210:217], v[102:105], v199, v199 op_sel_hi:[0,0,0]
	v_mfma_scale_f32_16x16x128_f8f6f4 v[98:101], v[150:157], v[218:225], v[98:101], v199, v199 op_sel_hi:[0,0,0]
	v_mfma_scale_f32_16x16x128_f8f6f4 v[94:97], v[202:209], v[218:225], v[94:97], v199, v199 op_sel_hi:[0,0,0]
	v_mfma_scale_f32_16x16x128_f8f6f4 v[90:93], v[150:157], v[226:233], v[90:93], v199, v199 op_sel_hi:[0,0,0]
	v_mfma_scale_f32_16x16x128_f8f6f4 v[86:89], v[202:209], v[226:233], v[86:89], v199, v199 op_sel_hi:[0,0,0]
	v_mfma_scale_f32_16x16x128_f8f6f4 v[82:85], v[150:157], v[234:241], v[82:85], v199, v199 op_sel_hi:[0,0,0]
	v_mfma_scale_f32_16x16x128_f8f6f4 v[78:81], v[202:209], v[234:241], v[78:81], v199, v199 op_sel_hi:[0,0,0]
	s_barrier
	s_add_i32 s78, s58, s44
	v_lshl_add_u64 v[12:13], s[28:29], 0, v[158:159]
	s_mov_b32 m0, s78
	ds_read_b128 v[210:213], v198 offset:16384
	ds_read_b128 v[214:217], v198 offset:17408
	ds_read_b128 v[218:221], v198 offset:18432
	ds_read_b128 v[222:225], v198 offset:19456
	ds_read_b128 v[226:229], v198 offset:20480
	ds_read_b128 v[230:233], v198 offset:21504
	ds_read_b128 v[234:237], v198 offset:22528
	ds_read_b128 v[238:241], v198 offset:23552
	global_load_lds_dwordx4 v[12:13], off
	v_lshl_add_u64 v[188:189], s[28:29], 0, v[160:161]
	s_add_i32 m0, s78, 0x2000
	s_add_i32 s78, s59, s44
	global_load_lds_dwordx4 v[188:189], off
	v_lshl_add_u64 v[12:13], v[12:13], 0, s[8:9]
	s_mov_b32 m0, s78
	s_nop 0
	global_load_lds_dwordx4 v[12:13], off
	v_lshl_add_u64 v[12:13], v[188:189], 0, s[8:9]
	s_add_i32 m0, s78, 0x2000
	s_nop 0
	global_load_lds_dwordx4 v[12:13], off
	v_lshl_add_u64 v[12:13], s[30:31], 0, v[162:163]
	s_mov_b32 m0, s45
	s_nop 0
	global_load_lds_dwordx4 v[12:13], off
	v_lshl_add_u64 v[12:13], s[30:31], 0, v[164:165]
	s_mov_b32 m0, s46
	s_nop 0
	global_load_lds_dwordx4 v[12:13], off
	s_waitcnt vmcnt(8)
	s_waitcnt lgkmcnt(0)
	v_mfma_scale_f32_16x16x128_f8f6f4 v[74:77], v[2:9], v[210:217], v[74:77], v199, v199 op_sel_hi:[0,0,0]
	v_mfma_scale_f32_16x16x128_f8f6f4 v[70:73], v[142:149], v[210:217], v[70:73], v199, v199 op_sel_hi:[0,0,0]
	v_mfma_scale_f32_16x16x128_f8f6f4 v[66:69], v[2:9], v[218:225], v[66:69], v199, v199 op_sel_hi:[0,0,0]
	v_mfma_scale_f32_16x16x128_f8f6f4 v[62:65], v[142:149], v[218:225], v[62:65], v199, v199 op_sel_hi:[0,0,0]
	v_mfma_scale_f32_16x16x128_f8f6f4 v[58:61], v[2:9], v[226:233], v[58:61], v199, v199 op_sel_hi:[0,0,0]
	v_mfma_scale_f32_16x16x128_f8f6f4 v[54:57], v[142:149], v[226:233], v[54:57], v199, v199 op_sel_hi:[0,0,0]
	v_mfma_scale_f32_16x16x128_f8f6f4 v[50:53], v[2:9], v[234:241], v[50:53], v199, v199 op_sel_hi:[0,0,0]
	v_mfma_scale_f32_16x16x128_f8f6f4 v[46:49], v[142:149], v[234:241], v[46:49], v199, v199 op_sel_hi:[0,0,0]
	s_nop 3
	v_mfma_scale_f32_16x16x128_f8f6f4 v[42:45], v[150:157], v[210:217], v[42:45], v199, v199 op_sel_hi:[0,0,0]
	v_mfma_scale_f32_16x16x128_f8f6f4 v[38:41], v[202:209], v[210:217], v[38:41], v199, v199 op_sel_hi:[0,0,0]
	v_mfma_scale_f32_16x16x128_f8f6f4 v[34:37], v[150:157], v[218:225], v[34:37], v199, v199 op_sel_hi:[0,0,0]
	v_mfma_scale_f32_16x16x128_f8f6f4 v[30:33], v[202:209], v[218:225], v[30:33], v199, v199 op_sel_hi:[0,0,0]
	v_mfma_scale_f32_16x16x128_f8f6f4 v[26:29], v[150:157], v[226:233], v[26:29], v199, v199 op_sel_hi:[0,0,0]
	v_mfma_scale_f32_16x16x128_f8f6f4 v[22:25], v[202:209], v[226:233], v[22:25], v199, v199 op_sel_hi:[0,0,0]
	v_mfma_scale_f32_16x16x128_f8f6f4 v[18:21], v[150:157], v[234:241], v[18:21], v199, v199 op_sel_hi:[0,0,0]
	v_mfma_scale_f32_16x16x128_f8f6f4 v[14:17], v[202:209], v[234:241], v[14:17], v199, v199 op_sel_hi:[0,0,0]
	s_barrier
; #define PG8_STAGE(bufoff, gbase, voff) do { _Pragma("unroll") for (int _i = 0; _i < 2; ++_i) \
;         __builtin_amdgcn_global_load_lds((const unsigned*)((const char*)(gbase) + (voff)[_i]), (PG8_LAS unsigned*)(lds + (bufoff) + ldsw + _i * 8192), 16, 0, 0); } while (0)
; #define PG8_WAIT_V(n) asm volatile("s_waitcnt vmcnt(" #n ")" ::: "memory")
; #define PG8_WAIT_L(n) asm volatile("s_waitcnt lgkmcnt(" #n ")" ::: "memory")
; #define PG8_BAR __builtin_amdgcn_s_barrier()
; #define PG8_SCHED __builtin_amdgcn_sched_barrier(0)
; template <class Epi, class Sched, bool ALIGN_EPI = true, bool F8 = false>
; __device__ __forceinline__ void gemm_phase(PG8_LAS unsigned char* lds, const Sched& S, const Epi& E) {
;     ...
;             PG8_LDB(B0, 0, 0); PG8_LDB(B1, 0, 1); PG8_SCHED; PG8_LDA(At, 0, 0); PG8_STAGE(PG8_SA(1, 1), a1, voffA[1]);
;             PG8_WAIT_V(8); PG8_WAIT_L(0); PG8_BAR; PG8_MMA(0, 0, At, B0); PG8_MMA(0, 1, At, B1); PG8_BAR; PG8_SCHED;
;             PG8_LDA(At, 0, 1); PG8_STAGE(PG8_SB(0, 0), b2, voffB[0]); PG8_STAGE(PG8_SB(0, 1), b2, voffB[1]); PG8_STAGE(PG8_SA(0, 0), a2, vA2[0]);
;             PG8_WAIT_V(8); PG8_WAIT_L(0); PG8_BAR; PG8_MMA(1, 0, At, B0); PG8_MMA(1, 1, At, B1); PG8_BAR; PG8_SCHED;
;             PG8_LDB(B0, 1, 0); PG8_LDB(B1, 1, 1); PG8_SCHED; PG8_LDA(At, 1, 0); PG8_STAGE(PG8_SA(0, 1), a2, vA2[1]);
;             PG8_WAIT_V(8); PG8_WAIT_L(0); PG8_BAR; PG8_MMA(0, 0, At, B0); PG8_MMA(0, 1, At, B1); PG8_BAR; PG8_SCHED;
;             PG8_LDA(At, 1, 1); PG8_STAGE(PG8_SB(1, 0), b3, voffB[0]); PG8_STAGE(PG8_SB(1, 1), b3, voffB[1]); PG8_STAGE(PG8_SA(1, 0), a3, vA2[0]);
;             PG8_WAIT_V(8); PG8_WAIT_L(0); PG8_BAR; PG8_MMA(1, 0, At, B0); PG8_MMA(1, 1, At, B1); PG8_BAR; PG8_SCHED;
	s_add_i32 s78, 0, 0x18000
	s_add_i32 s79, 0, 0x1c000
	v_add_u32_e32 v2, s78, v190
	v_add_u32_e32 v10, s79, v190
	ds_read_b128 v[142:145], v2
	ds_read_b128 v[146:149], v2 offset:1024
	ds_read_b128 v[150:153], v2 offset:2048
	ds_read_b128 v[154:157], v2 offset:3072
	ds_read_b128 v[2:5], v10
	ds_read_b128 v[6:9], v10 offset:1024
	ds_read_b128 v[202:205], v10 offset:2048
	ds_read_b128 v[206:209], v10 offset:3072
	s_mov_b32 m0, s47
	v_lshl_add_u64 v[12:13], s[30:31], 0, v[166:167]
	ds_read_b128 v[210:213], v198 offset:32768
	ds_read_b128 v[214:217], v198 offset:33792
	ds_read_b128 v[218:221], v198 offset:34816
	ds_read_b128 v[222:225], v198 offset:35840
	ds_read_b128 v[226:229], v198 offset:36864
	ds_read_b128 v[230:233], v198 offset:37888
	ds_read_b128 v[234:237], v198 offset:38912
	ds_read_b128 v[238:241], v198 offset:39936
	global_load_lds_dwordx4 v[12:13], off
	v_lshl_add_u64 v[12:13], s[30:31], 0, v[168:169]
	s_mov_b32 m0, s48
	s_nop 0
	global_load_lds_dwordx4 v[12:13], off
	s_waitcnt vmcnt(8)
	s_waitcnt lgkmcnt(0)
	v_mfma_scale_f32_16x16x128_f8f6f4 v[138:141], v[142:149], v[210:217], v[138:141], v199, v199 op_sel_hi:[0,0,0]
	v_mfma_scale_f32_16x16x128_f8f6f4 v[134:137], v[150:157], v[210:217], v[134:137], v199, v199 op_sel_hi:[0,0,0]
	v_mfma_scale_f32_16x16x128_f8f6f4 v[130:133], v[142:149], v[218:225], v[130:133], v199, v199 op_sel_hi:[0,0,0]
	v_mfma_scale_f32_16x16x128_f8f6f4 v[126:129], v[150:157], v[218:225], v[126:129], v199, v199 op_sel_hi:[0,0,0]
	v_mfma_scale_f32_16x16x128_f8f6f4 v[122:125], v[142:149], v[226:233], v[122:125], v199, v199 op_sel_hi:[0,0,0]
	v_mfma_scale_f32_16x16x128_f8f6f4 v[118:121], v[150:157], v[226:233], v[118:121], v199, v199 op_sel_hi:[0,0,0]
	v_mfma_scale_f32_16x16x128_f8f6f4 v[114:117], v[142:149], v[234:241], v[114:117], v199, v199 op_sel_hi:[0,0,0]
	v_mfma_scale_f32_16x16x128_f8f6f4 v[110:113], v[150:157], v[234:241], v[110:113], v199, v199 op_sel_hi:[0,0,0]
	s_nop 3
	v_mfma_scale_f32_16x16x128_f8f6f4 v[106:109], v[2:9], v[210:217], v[106:109], v199, v199 op_sel_hi:[0,0,0]
	v_mfma_scale_f32_16x16x128_f8f6f4 v[102:105], v[202:209], v[210:217], v[102:105], v199, v199 op_sel_hi:[0,0,0]
	v_mfma_scale_f32_16x16x128_f8f6f4 v[98:101], v[2:9], v[218:225], v[98:101], v199, v199 op_sel_hi:[0,0,0]
	v_mfma_scale_f32_16x16x128_f8f6f4 v[94:97], v[202:209], v[218:225], v[94:97], v199, v199 op_sel_hi:[0,0,0]
	v_mfma_scale_f32_16x16x128_f8f6f4 v[90:93], v[2:9], v[226:233], v[90:93], v199, v199 op_sel_hi:[0,0,0]
	v_mfma_scale_f32_16x16x128_f8f6f4 v[86:89], v[202:209], v[226:233], v[86:89], v199, v199 op_sel_hi:[0,0,0]
	v_mfma_scale_f32_16x16x128_f8f6f4 v[82:85], v[2:9], v[234:241], v[82:85], v199, v199 op_sel_hi:[0,0,0]
	v_mfma_scale_f32_16x16x128_f8f6f4 v[78:81], v[202:209], v[234:241], v[78:81], v199, v199 op_sel_hi:[0,0,0]
	s_barrier
	s_add_u32 s28, s28, 0x8000
	s_addc_u32 s29, s29, 0
	s_add_i32 s30, s78, s44
	v_lshl_add_u64 v[12:13], s[28:29], 0, v[158:159]
	s_mov_b32 m0, s30
	ds_read_b128 v[210:213], v198 offset:49152
	ds_read_b128 v[214:217], v198 offset:50176
	ds_read_b128 v[218:221], v198 offset:51200
	ds_read_b128 v[222:225], v198 offset:52224
	ds_read_b128 v[226:229], v198 offset:53248
	ds_read_b128 v[230:233], v198 offset:54272
	ds_read_b128 v[234:237], v198 offset:55296
	ds_read_b128 v[238:241], v198 offset:56320
	global_load_lds_dwordx4 v[12:13], off
	v_lshl_add_u64 v[12:13], s[28:29], 0, v[160:161]
	s_add_i32 m0, s30, 0x2000
	s_add_i32 s30, s79, s44
	global_load_lds_dwordx4 v[12:13], off
	v_lshl_add_u64 v[12:13], s[28:29], 0, v[172:173]
	s_mov_b32 m0, s30
	s_nop 0
	global_load_lds_dwordx4 v[12:13], off
	v_lshl_add_u64 v[12:13], s[28:29], 0, v[174:175]
	s_add_i32 m0, s30, 0x2000
	s_nop 0
	global_load_lds_dwordx4 v[12:13], off
	v_lshl_add_u64 v[12:13], s[26:27], 0, v[162:163]
	s_mov_b32 m0, s50
	s_nop 0
	global_load_lds_dwordx4 v[12:13], off
	v_lshl_add_u64 v[12:13], s[26:27], 0, v[164:165]
	s_mov_b32 m0, s51
	s_nop 0
	global_load_lds_dwordx4 v[12:13], off
	s_waitcnt vmcnt(8)
	s_waitcnt lgkmcnt(0)
	v_mfma_scale_f32_16x16x128_f8f6f4 v[74:77], v[142:149], v[210:217], v[74:77], v199, v199 op_sel_hi:[0,0,0]
	v_mfma_scale_f32_16x16x128_f8f6f4 v[70:73], v[150:157], v[210:217], v[70:73], v199, v199 op_sel_hi:[0,0,0]
	v_mfma_scale_f32_16x16x128_f8f6f4 v[66:69], v[142:149], v[218:225], v[66:69], v199, v199 op_sel_hi:[0,0,0]
	v_mfma_scale_f32_16x16x128_f8f6f4 v[62:65], v[150:157], v[218:225], v[62:65], v199, v199 op_sel_hi:[0,0,0]
	v_mfma_scale_f32_16x16x128_f8f6f4 v[58:61], v[142:149], v[226:233], v[58:61], v199, v199 op_sel_hi:[0,0,0]
	v_mfma_scale_f32_16x16x128_f8f6f4 v[54:57], v[150:157], v[226:233], v[54:57], v199, v199 op_sel_hi:[0,0,0]
	v_mfma_scale_f32_16x16x128_f8f6f4 v[50:53], v[142:149], v[234:241], v[50:53], v199, v199 op_sel_hi:[0,0,0]
	v_mfma_scale_f32_16x16x128_f8f6f4 v[46:49], v[150:157], v[234:241], v[46:49], v199, v199 op_sel_hi:[0,0,0]
	s_nop 3
	v_mfma_scale_f32_16x16x128_f8f6f4 v[42:45], v[2:9], v[210:217], v[42:45], v199, v199 op_sel_hi:[0,0,0]
	v_mfma_scale_f32_16x16x128_f8f6f4 v[38:41], v[202:209], v[210:217], v[38:41], v199, v199 op_sel_hi:[0,0,0]
	v_mfma_scale_f32_16x16x128_f8f6f4 v[34:37], v[2:9], v[218:225], v[34:37], v199, v199 op_sel_hi:[0,0,0]
	v_mfma_scale_f32_16x16x128_f8f6f4 v[30:33], v[202:209], v[218:225], v[30:33], v199, v199 op_sel_hi:[0,0,0]
	v_mfma_scale_f32_16x16x128_f8f6f4 v[26:29], v[2:9], v[226:233], v[26:29], v199, v199 op_sel_hi:[0,0,0]
	v_mfma_scale_f32_16x16x128_f8f6f4 v[22:25], v[202:209], v[226:233], v[22:25], v199, v199 op_sel_hi:[0,0,0]
	v_mfma_scale_f32_16x16x128_f8f6f4 v[18:21], v[2:9], v[234:241], v[18:21], v199, v199 op_sel_hi:[0,0,0]
	v_mfma_scale_f32_16x16x128_f8f6f4 v[14:17], v[202:209], v[234:241], v[14:17], v199, v199 op_sel_hi:[0,0,0]
	s_barrier
	s_add_u32 s75, s75, 0x10000
	s_addc_u32 s76, s76, 0
	s_add_u32 s24, s24, 0x10000
	s_addc_u32 s25, s25, 0
	s_cmp_ge_i32 s77, s72
	s_mov_b32 s26, s77
	s_cbranch_scc0 .LBB0_834
	s_branch .Lfx_23459

; #define PG8_STAGE(bufoff, gbase, voff) do { _Pragma("unroll") for (int _i = 0; _i < 2; ++_i) \
;         __builtin_amdgcn_global_load_lds((const unsigned*)((const char*)(gbase) + (voff)[_i]), (PG8_LAS unsigned*)(lds + (bufoff) + ldsw + _i * 8192), 16, 0, 0); } while (0)
; #define PG8_WAIT_V(n) asm volatile("s_waitcnt vmcnt(" #n ")" ::: "memory")
; #define PG8_WAIT_L(n) asm volatile("s_waitcnt lgkmcnt(" #n ")" ::: "memory")
; #define PG8_BAR __builtin_amdgcn_s_barrier()
; #define PG8_SCHED __builtin_amdgcn_sched_barrier(0)
; template <class Epi, class Sched, bool ALIGN_EPI = true, bool F8 = false>
; __device__ __forceinline__ void gemm_phase(PG8_LAS unsigned char* lds, const Sched& S, const Epi& E) {
;     ...
;             PG8_LDB(B0, 0, 0); PG8_LDB(B1, 0, 1); PG8_SCHED; PG8_LDA(At, 0, 0); PG8_STAGE(PG8_SA(1, 1), a1, voffA[1]);
;             PG8_WAIT_V(8); PG8_WAIT_L(0); PG8_BAR; PG8_MMA(0, 0, At, B0); PG8_MMA(0, 1, At, B1); PG8_BAR; PG8_SCHED;
;             PG8_LDA(At, 0, 1); PG8_STAGE(PG8_SB(0, 0), b2, voffB[0]); PG8_STAGE(PG8_SB(0, 1), b2, voffB[1]); PG8_STAGE(PG8_SA(0, 0), a2, vA2[0]);
;             PG8_WAIT_V(8); PG8_WAIT_L(0); PG8_BAR; PG8_MMA(1, 0, At, B0); PG8_MMA(1, 1, At, B1); PG8_BAR; PG8_SCHED;
;             PG8_LDB(B0, 1, 0); PG8_LDB(B1, 1, 1); PG8_SCHED; PG8_LDA(At, 1, 0); PG8_STAGE(PG8_SA(0, 1), a2, vA2[1]);
;             PG8_WAIT_V(8); PG8_WAIT_L(0); PG8_BAR; PG8_MMA(0, 0, At, B0); PG8_MMA(0, 1, At, B1); PG8_BAR; PG8_SCHED;
;             PG8_LDA(At, 1, 1); PG8_STAGE(PG8_SB(1, 0), b3, voffB[0]); PG8_STAGE(PG8_SB(1, 1), b3, voffB[1]); PG8_STAGE(PG8_SA(1, 0), a3, vA2[0]);
;             PG8_WAIT_V(8); PG8_WAIT_L(0); PG8_BAR; PG8_MMA(1, 0, At, B0); PG8_MMA(1, 1, At, B1); PG8_BAR; PG8_SCHED;
.Lh1_834:
	v_add_u32_e32 v10, s58, v190
	ds_read_b128 v[2:5], v10
	ds_read_b128 v[6:9], v10 offset:1024
	ds_read_b128 v[142:145], v10 offset:2048
	ds_read_b128 v[146:149], v10 offset:3072
	v_add_u32_e32 v10, s59, v190
	ds_read_b128 v[150:153], v10
	ds_read_b128 v[154:157], v10 offset:1024
	ds_read_b128 v[202:205], v10 offset:2048
	ds_read_b128 v[206:209], v10 offset:3072
	s_add_i32 s77, s26, 2
	s_add_u32 s27, s24, 0x8000
	s_addc_u32 s28, s25, 0
	s_cmp_eq_u32 s74, s26
	s_cselect_b32 s30, s20, s27
	s_cselect_b32 s31, s21, s28
	s_cselect_b32 s28, s22, s75
	s_cselect_b32 s29, s23, s76
	s_add_u32 s26, s30, 0x8000
	s_addc_u32 s27, s31, 0
	v_lshl_add_u64 v[12:13], s[24:25], 0, v[182:183]
	s_add_i32 m0, s45, 0xc000
	ds_read_b128 v[210:213], v198
	ds_read_b128 v[214:217], v198 offset:1024
	ds_read_b128 v[218:221], v198 offset:2048
	ds_read_b128 v[222:225], v198 offset:3072
	ds_read_b128 v[226:229], v198 offset:4096
	ds_read_b128 v[230:233], v198 offset:5120
	ds_read_b128 v[234:237], v198 offset:6144
	ds_read_b128 v[238:241], v198 offset:7168
	global_load_lds_dwordx4 v[12:13], off
	v_lshl_add_u64 v[12:13], s[24:25], 0, v[180:181]
	s_add_i32 m0, s45, 0xe000
	s_nop 0
	global_load_lds_dwordx4 v[12:13], off
	s_waitcnt vmcnt(8)
	s_waitcnt lgkmcnt(0)
	s_barrier
	v_mfma_scale_f32_16x16x128_f8f6f4 v[138:141], v[2:9], v[210:217], v[138:141], v199, v199 op_sel_hi:[0,0,0]
	v_mfma_scale_f32_16x16x128_f8f6f4 v[134:137], v[142:149], v[210:217], v[134:137], v199, v199 op_sel_hi:[0,0,0]
	v_mfma_scale_f32_16x16x128_f8f6f4 v[130:133], v[2:9], v[218:225], v[130:133], v199, v199 op_sel_hi:[0,0,0]
	v_mfma_scale_f32_16x16x128_f8f6f4 v[126:129], v[142:149], v[218:225], v[126:129], v199, v199 op_sel_hi:[0,0,0]
	v_mfma_scale_f32_16x16x128_f8f6f4 v[122:125], v[2:9], v[226:233], v[122:125], v199, v199 op_sel_hi:[0,0,0]
	v_mfma_scale_f32_16x16x128_f8f6f4 v[118:121], v[142:149], v[226:233], v[118:121], v199, v199 op_sel_hi:[0,0,0]
	v_mfma_scale_f32_16x16x128_f8f6f4 v[114:117], v[2:9], v[234:241], v[114:117], v199, v199 op_sel_hi:[0,0,0]
	v_mfma_scale_f32_16x16x128_f8f6f4 v[110:113], v[142:149], v[234:241], v[110:113], v199, v199 op_sel_hi:[0,0,0]
	s_nop 3
	v_mfma_scale_f32_16x16x128_f8f6f4 v[106:109], v[150:157], v[210:217], v[106:109], v199, v199 op_sel_hi:[0,0,0]
	v_mfma_scale_f32_16x16x128_f8f6f4 v[102:105], v[202:209], v[210:217], v[102:105], v199, v199 op_sel_hi:[0,0,0]
	v_mfma_scale_f32_16x16x128_f8f6f4 v[98:101], v[150:157], v[218:225], v[98:101], v199, v199 op_sel_hi:[0,0,0]
	v_mfma_scale_f32_16x16x128_f8f6f4 v[94:97], v[202:209], v[218:225], v[94:97], v199, v199 op_sel_hi:[0,0,0]
	v_mfma_scale_f32_16x16x128_f8f6f4 v[90:93], v[150:157], v[226:233], v[90:93], v199, v199 op_sel_hi:[0,0,0]
	v_mfma_scale_f32_16x16x128_f8f6f4 v[86:89], v[202:209], v[226:233], v[86:89], v199, v199 op_sel_hi:[0,0,0]
	v_mfma_scale_f32_16x16x128_f8f6f4 v[82:85], v[150:157], v[234:241], v[82:85], v199, v199 op_sel_hi:[0,0,0]
	v_mfma_scale_f32_16x16x128_f8f6f4 v[78:81], v[202:209], v[234:241], v[78:81], v199, v199 op_sel_hi:[0,0,0]
	s_add_i32 s78, s58, s44
	v_lshl_add_u64 v[12:13], s[28:29], 0, v[158:159]
	s_mov_b32 m0, s78
	ds_read_b128 v[210:213], v198 offset:16384
	ds_read_b128 v[214:217], v198 offset:17408
	ds_read_b128 v[218:221], v198 offset:18432
	ds_read_b128 v[222:225], v198 offset:19456
	ds_read_b128 v[226:229], v198 offset:20480
	ds_read_b128 v[230:233], v198 offset:21504
	ds_read_b128 v[234:237], v198 offset:22528
	ds_read_b128 v[238:241], v198 offset:23552
	global_load_lds_dwordx4 v[12:13], off
	v_lshl_add_u64 v[188:189], s[28:29], 0, v[160:161]
	s_add_i32 m0, s78, 0x2000
	s_add_i32 s78, s59, s44
	global_load_lds_dwordx4 v[188:189], off
	v_lshl_add_u64 v[12:13], v[12:13], 0, s[8:9]
	s_mov_b32 m0, s78
	s_nop 0
	global_load_lds_dwordx4 v[12:13], off
	v_lshl_add_u64 v[12:13], v[188:189], 0, s[8:9]
	s_add_i32 m0, s78, 0x2000
	s_nop 0
	global_load_lds_dwordx4 v[12:13], off
	v_lshl_add_u64 v[12:13], s[30:31], 0, v[162:163]
	s_mov_b32 m0, s45
	s_nop 0
	global_load_lds_dwordx4 v[12:13], off
	v_lshl_add_u64 v[12:13], s[30:31], 0, v[164:165]
	s_mov_b32 m0, s46
	s_nop 0
	global_load_lds_dwordx4 v[12:13], off
	s_waitcnt vmcnt(8)
	s_waitcnt lgkmcnt(0)
	s_barrier
	v_mfma_scale_f32_16x16x128_f8f6f4 v[74:77], v[2:9], v[210:217], v[74:77], v199, v199 op_sel_hi:[0,0,0]
	v_mfma_scale_f32_16x16x128_f8f6f4 v[70:73], v[142:149], v[210:217], v[70:73], v199, v199 op_sel_hi:[0,0,0]
	v_mfma_scale_f32_16x16x128_f8f6f4 v[66:69], v[2:9], v[218:225], v[66:69], v199, v199 op_sel_hi:[0,0,0]
	v_mfma_scale_f32_16x16x128_f8f6f4 v[62:65], v[142:149], v[218:225], v[62:65], v199, v199 op_sel_hi:[0,0,0]
	v_mfma_scale_f32_16x16x128_f8f6f4 v[58:61], v[2:9], v[226:233], v[58:61], v199, v199 op_sel_hi:[0,0,0]
	v_mfma_scale_f32_16x16x128_f8f6f4 v[54:57], v[142:149], v[226:233], v[54:57], v199, v199 op_sel_hi:[0,0,0]
	v_mfma_scale_f32_16x16x128_f8f6f4 v[50:53], v[2:9], v[234:241], v[50:53], v199, v199 op_sel_hi:[0,0,0]
	v_mfma_scale_f32_16x16x128_f8f6f4 v[46:49], v[142:149], v[234:241], v[46:49], v199, v199 op_sel_hi:[0,0,0]
	s_nop 3
	v_mfma_scale_f32_16x16x128_f8f6f4 v[42:45], v[150:157], v[210:217], v[42:45], v199, v199 op_sel_hi:[0,0,0]
	v_mfma_scale_f32_16x16x128_f8f6f4 v[38:41], v[202:209], v[210:217], v[38:41], v199, v199 op_sel_hi:[0,0,0]
	v_mfma_scale_f32_16x16x128_f8f6f4 v[34:37], v[150:157], v[218:225], v[34:37], v199, v199 op_sel_hi:[0,0,0]
	v_mfma_scale_f32_16x16x128_f8f6f4 v[30:33], v[202:209], v[218:225], v[30:33], v199, v199 op_sel_hi:[0,0,0]
	v_mfma_scale_f32_16x16x128_f8f6f4 v[26:29], v[150:157], v[226:233], v[26:29], v199, v199 op_sel_hi:[0,0,0]
	v_mfma_scale_f32_16x16x128_f8f6f4 v[22:25], v[202:209], v[226:233], v[22:25], v199, v199 op_sel_hi:[0,0,0]
	v_mfma_scale_f32_16x16x128_f8f6f4 v[18:21], v[150:157], v[234:241], v[18:21], v199, v199 op_sel_hi:[0,0,0]
	v_mfma_scale_f32_16x16x128_f8f6f4 v[14:17], v[202:209], v[234:241], v[14:17], v199, v199 op_sel_hi:[0,0,0]
	s_add_i32 s78, 0, 0x18000
	s_add_i32 s79, 0, 0x1c000
	v_add_u32_e32 v2, s78, v190
	v_add_u32_e32 v10, s79, v190
	ds_read_b128 v[142:145], v2
	ds_read_b128 v[146:149], v2 offset:1024
	ds_read_b128 v[150:153], v2 offset:2048
	ds_read_b128 v[154:157], v2 offset:3072
	ds_read_b128 v[2:5], v10
	ds_read_b128 v[6:9], v10 offset:1024
	ds_read_b128 v[202:205], v10 offset:2048
	ds_read_b128 v[206:209], v10 offset:3072
	s_mov_b32 m0, s47
	v_lshl_add_u64 v[12:13], s[30:31], 0, v[166:167]
	ds_read_b128 v[210:213], v198 offset:32768
	ds_read_b128 v[214:217], v198 offset:33792
	ds_read_b128 v[218:221], v198 offset:34816
	ds_read_b128 v[222:225], v198 offset:35840
	ds_read_b128 v[226:229], v198 offset:36864
	ds_read_b128 v[230:233], v198 offset:37888
	ds_read_b128 v[234:237], v198 offset:38912
	ds_read_b128 v[238:241], v198 offset:39936
	global_load_lds_dwordx4 v[12:13], off
	v_lshl_add_u64 v[12:13], s[30:31], 0, v[168:169]
	s_mov_b32 m0, s48
	s_nop 0
	global_load_lds_dwordx4 v[12:13], off
	s_waitcnt vmcnt(8)
	s_waitcnt lgkmcnt(0)
	s_barrier
; #define PG8_STAGE(bufoff, gbase, voff) do { _Pragma("unroll") for (int _i = 0; _i < 2; ++_i) \
;         __builtin_amdgcn_global_load_lds((const unsigned*)((const char*)(gbase) + (voff)[_i]), (PG8_LAS unsigned*)(lds + (bufoff) + ldsw + _i * 8192), 16, 0, 0); } while (0)
; #define PG8_WAIT_V(n) asm volatile("s_waitcnt vmcnt(" #n ")" ::: "memory")
; #define PG8_WAIT_L(n) asm volatile("s_waitcnt lgkmcnt(" #n ")" ::: "memory")
; #define PG8_BAR __builtin_amdgcn_s_barrier()
; #define PG8_SCHED __builtin_amdgcn_sched_barrier(0)
; template <class Epi, class Sched, bool ALIGN_EPI = true, bool F8 = false>
; __device__ __forceinline__ void gemm_phase(PG8_LAS unsigned char* lds, const Sched& S, const Epi& E) {
;     ...
;             PG8_LDB(B0, 0, 0); PG8_LDB(B1, 0, 1); PG8_SCHED; PG8_LDA(At, 0, 0); PG8_STAGE(PG8_SA(1, 1), a1, voffA[1]);
;             PG8_WAIT_V(8); PG8_WAIT_L(0); PG8_BAR; PG8_MMA(0, 0, At, B0); PG8_MMA(0, 1, At, B1); PG8_BAR; PG8_SCHED;
;             PG8_LDA(At, 0, 1); PG8_STAGE(PG8_SB(0, 0), b2, voffB[0]); PG8_STAGE(PG8_SB(0, 1), b2, voffB[1]); PG8_STAGE(PG8_SA(0, 0), a2, vA2[0]);
;             PG8_WAIT_V(8); PG8_WAIT_L(0); PG8_BAR; PG8_MMA(1, 0, At, B0); PG8_MMA(1, 1, At, B1); PG8_BAR; PG8_SCHED;
;             PG8_LDB(B0, 1, 0); PG8_LDB(B1, 1, 1); PG8_SCHED; PG8_LDA(At, 1, 0); PG8_STAGE(PG8_SA(0, 1), a2, vA2[1]);
;             PG8_WAIT_V(8); PG8_WAIT_L(0); PG8_BAR; PG8_MMA(0, 0, At, B0); PG8_MMA(0, 1, At, B1); PG8_BAR; PG8_SCHED;
;             PG8_LDA(At, 1, 1); PG8_STAGE(PG8_SB(1, 0), b3, voffB[0]); PG8_STAGE(PG8_SB(1, 1), b3, voffB[1]); PG8_STAGE(PG8_SA(1, 0), a3, vA2[0]);
;             PG8_WAIT_V(8); PG8_WAIT_L(0); PG8_BAR; PG8_MMA(1, 0, At, B0); PG8_MMA(1, 1, At, B1); PG8_BAR; PG8_SCHED;
	v_mfma_scale_f32_16x16x128_f8f6f4 v[138:141], v[142:149], v[210:217], v[138:141], v199, v199 op_sel_hi:[0,0,0]
	v_mfma_scale_f32_16x16x128_f8f6f4 v[134:137], v[150:157], v[210:217], v[134:137], v199, v199 op_sel_hi:[0,0,0]
	v_mfma_scale_f32_16x16x128_f8f6f4 v[130:133], v[142:149], v[218:225], v[130:133], v199, v199 op_sel_hi:[0,0,0]
	v_mfma_scale_f32_16x16x128_f8f6f4 v[126:129], v[150:157], v[218:225], v[126:129], v199, v199 op_sel_hi:[0,0,0]
	v_mfma_scale_f32_16x16x128_f8f6f4 v[122:125], v[142:149], v[226:233], v[122:125], v199, v199 op_sel_hi:[0,0,0]
	v_mfma_scale_f32_16x16x128_f8f6f4 v[118:121], v[150:157], v[226:233], v[118:121], v199, v199 op_sel_hi:[0,0,0]
	v_mfma_scale_f32_16x16x128_f8f6f4 v[114:117], v[142:149], v[234:241], v[114:117], v199, v199 op_sel_hi:[0,0,0]
	v_mfma_scale_f32_16x16x128_f8f6f4 v[110:113], v[150:157], v[234:241], v[110:113], v199, v199 op_sel_hi:[0,0,0]
	s_nop 3
	v_mfma_scale_f32_16x16x128_f8f6f4 v[106:109], v[2:9], v[210:217], v[106:109], v199, v199 op_sel_hi:[0,0,0]
	v_mfma_scale_f32_16x16x128_f8f6f4 v[102:105], v[202:209], v[210:217], v[102:105], v199, v199 op_sel_hi:[0,0,0]
	v_mfma_scale_f32_16x16x128_f8f6f4 v[98:101], v[2:9], v[218:225], v[98:101], v199, v199 op_sel_hi:[0,0,0]
	v_mfma_scale_f32_16x16x128_f8f6f4 v[94:97], v[202:209], v[218:225], v[94:97], v199, v199 op_sel_hi:[0,0,0]
	v_mfma_scale_f32_16x16x128_f8f6f4 v[90:93], v[2:9], v[226:233], v[90:93], v199, v199 op_sel_hi:[0,0,0]
	v_mfma_scale_f32_16x16x128_f8f6f4 v[86:89], v[202:209], v[226:233], v[86:89], v199, v199 op_sel_hi:[0,0,0]
	v_mfma_scale_f32_16x16x128_f8f6f4 v[82:85], v[2:9], v[234:241], v[82:85], v199, v199 op_sel_hi:[0,0,0]
	v_mfma_scale_f32_16x16x128_f8f6f4 v[78:81], v[202:209], v[234:241], v[78:81], v199, v199 op_sel_hi:[0,0,0]
	s_add_u32 s28, s28, 0x8000
	s_addc_u32 s29, s29, 0
	s_add_i32 s30, s78, s44
	v_lshl_add_u64 v[12:13], s[28:29], 0, v[158:159]
	s_mov_b32 m0, s30
	ds_read_b128 v[210:213], v198 offset:49152
	ds_read_b128 v[214:217], v198 offset:50176
	ds_read_b128 v[218:221], v198 offset:51200
	ds_read_b128 v[222:225], v198 offset:52224
	ds_read_b128 v[226:229], v198 offset:53248
	ds_read_b128 v[230:233], v198 offset:54272
	ds_read_b128 v[234:237], v198 offset:55296
	ds_read_b128 v[238:241], v198 offset:56320
	global_load_lds_dwordx4 v[12:13], off
	v_lshl_add_u64 v[12:13], s[28:29], 0, v[160:161]
	s_add_i32 m0, s30, 0x2000
	s_add_i32 s30, s79, s44
	global_load_lds_dwordx4 v[12:13], off
	v_lshl_add_u64 v[12:13], s[28:29], 0, v[172:173]
	s_mov_b32 m0, s30
	s_nop 0
	global_load_lds_dwordx4 v[12:13], off
	v_lshl_add_u64 v[12:13], s[28:29], 0, v[174:175]
	s_add_i32 m0, s30, 0x2000
	s_nop 0
	global_load_lds_dwordx4 v[12:13], off
	v_lshl_add_u64 v[12:13], s[26:27], 0, v[162:163]
	s_mov_b32 m0, s50
	s_nop 0
	global_load_lds_dwordx4 v[12:13], off
	v_lshl_add_u64 v[12:13], s[26:27], 0, v[164:165]
	s_mov_b32 m0, s51
	s_nop 0
	global_load_lds_dwordx4 v[12:13], off
	s_waitcnt vmcnt(8)
	s_waitcnt lgkmcnt(0)
	s_barrier
	v_mfma_scale_f32_16x16x128_f8f6f4 v[74:77], v[142:149], v[210:217], v[74:77], v199, v199 op_sel_hi:[0,0,0]
	v_mfma_scale_f32_16x16x128_f8f6f4 v[70:73], v[150:157], v[210:217], v[70:73], v199, v199 op_sel_hi:[0,0,0]
	v_mfma_scale_f32_16x16x128_f8f6f4 v[66:69], v[142:149], v[218:225], v[66:69], v199, v199 op_sel_hi:[0,0,0]
	v_mfma_scale_f32_16x16x128_f8f6f4 v[62:65], v[150:157], v[218:225], v[62:65], v199, v199 op_sel_hi:[0,0,0]
	v_mfma_scale_f32_16x16x128_f8f6f4 v[58:61], v[142:149], v[226:233], v[58:61], v199, v199 op_sel_hi:[0,0,0]
	v_mfma_scale_f32_16x16x128_f8f6f4 v[54:57], v[150:157], v[226:233], v[54:57], v199, v199 op_sel_hi:[0,0,0]
	v_mfma_scale_f32_16x16x128_f8f6f4 v[50:53], v[142:149], v[234:241], v[50:53], v199, v199 op_sel_hi:[0,0,0]
	v_mfma_scale_f32_16x16x128_f8f6f4 v[46:49], v[150:157], v[234:241], v[46:49], v199, v199 op_sel_hi:[0,0,0]
	s_nop 3
	v_mfma_scale_f32_16x16x128_f8f6f4 v[42:45], v[2:9], v[210:217], v[42:45], v199, v199 op_sel_hi:[0,0,0]
	v_mfma_scale_f32_16x16x128_f8f6f4 v[38:41], v[202:209], v[210:217], v[38:41], v199, v199 op_sel_hi:[0,0,0]
	v_mfma_scale_f32_16x16x128_f8f6f4 v[34:37], v[2:9], v[218:225], v[34:37], v199, v199 op_sel_hi:[0,0,0]
	v_mfma_scale_f32_16x16x128_f8f6f4 v[30:33], v[202:209], v[218:225], v[30:33], v199, v199 op_sel_hi:[0,0,0]
	v_mfma_scale_f32_16x16x128_f8f6f4 v[26:29], v[2:9], v[226:233], v[26:29], v199, v199 op_sel_hi:[0,0,0]
	v_mfma_scale_f32_16x16x128_f8f6f4 v[22:25], v[202:209], v[226:233], v[22:25], v199, v199 op_sel_hi:[0,0,0]
	v_mfma_scale_f32_16x16x128_f8f6f4 v[18:21], v[2:9], v[234:241], v[18:21], v199, v199 op_sel_hi:[0,0,0]
	v_mfma_scale_f32_16x16x128_f8f6f4 v[14:17], v[202:209], v[234:241], v[14:17], v199, v199 op_sel_hi:[0,0,0]
	s_add_u32 s75, s75, 0x10000
	s_addc_u32 s76, s76, 0
	s_add_u32 s24, s24, 0x10000
	s_addc_u32 s25, s25, 0
	s_cmp_ge_i32 s77, s72
	s_mov_b32 s26, s77
	s_cbranch_scc0 .Lh1_834
.Lfx_23459:
	s_setprio 0
	s_and_b64 vcc, exec, s[16:17]
	s_cbranch_vccz .LBB0_837

; #define PG8_WAIT_V(n) asm volatile("s_waitcnt vmcnt(" #n ")" ::: "memory")
; #define PG8_WAIT_L(n) asm volatile("s_waitcnt lgkmcnt(" #n ")" ::: "memory")
; #define PG8_BAR __builtin_amdgcn_s_barrier()
; #define PG8_SCHED __builtin_amdgcn_sched_barrier(0)
; template <class Epi, class Sched, bool ALIGN_EPI = true, bool F8 = false>
; __device__ __forceinline__ void gemm_phase(PG8_LAS unsigned char* lds, const Sched& S, const Epi& E) {
;     ...
;     for (;;) {
;         const bool has_next = S.next(ui + 1, nxt);
;         const char* nA = has_next ? nxt.A : cA; const char* nB = has_next ? nxt.B : cB;
;         const int nt = cur.nt;
; #pragma unroll 1
;         for (int t = 0; t < nt; t += 2) {
;             const bool last = (t == nt - 2);
;             if constexpr (Sched::GATHER) { if (last && has_next) S.a_off(nxt, Rs, Cs, voffAn); }
;             const char* a1 = cA + (size_t)(t + 1) * kstep;
;             const char* a2 = last ? nA : cA + (size_t)(t + 2) * kstep; const char* b2 = last ? nB : cB + (size_t)(t + 2) * kstepB;
;             const char* a3 = a2 + kstep; const char* b3 = b2 + kstepB;
;             unsigned vA2[2][2];
; #pragma unroll
;             for (int h = 0; h < 2; ++h)
; #pragma unroll
;                 for (int i = 0; i < 2; ++i) { if constexpr (Sched::GATHER) vA2[h][i] = (last && has_next) ? voffAn[h][i] : voffA[h][i]; else vA2[h][i] = voffA[h][i]; }
;             PG8_LDB(B0, 0, 0); PG8_LDB(B1, 0, 1); PG8_SCHED; PG8_LDA(At, 0, 0); PG8_STAGE(PG8_SA(1, 1), a1, voffA[1]);
;             PG8_WAIT_V(8); PG8_WAIT_L(0); PG8_BAR; PG8_MMA(0, 0, At, B0); PG8_MMA(0, 1, At, B1); PG8_BAR; PG8_SCHED;
;             PG8_LDA(At, 0, 1); PG8_STAGE(PG8_SB(0, 0), b2, voffB[0]); PG8_STAGE(PG8_SB(0, 1), b2, voffB[1]); PG8_STAGE(PG8_SA(0, 0), a2, vA2[0]);
;             PG8_WAIT_V(8); PG8_WAIT_L(0); PG8_BAR; PG8_MMA(1, 0, At, B0); PG8_MMA(1, 1, At, B1); PG8_BAR; PG8_SCHED;
;             PG8_LDB(B0, 1, 0); PG8_LDB(B1, 1, 1); PG8_SCHED; PG8_LDA(At, 1, 0); PG8_STAGE(PG8_SA(0, 1), a2, vA2[1]);
;             PG8_WAIT_V(8); PG8_WAIT_L(0); PG8_BAR; PG8_MMA(0, 0, At, B0); PG8_MMA(0, 1, At, B1); PG8_BAR; PG8_SCHED;
;             PG8_LDA(At, 1, 1); PG8_STAGE(PG8_SB(1, 0), b3, voffB[0]); PG8_STAGE(PG8_SB(1, 1), b3, voffB[1]); PG8_STAGE(PG8_SA(1, 0), a3, vA2[0]);
;             PG8_WAIT_V(8); PG8_WAIT_L(0); PG8_BAR; PG8_MMA(1, 0, At, B0); PG8_MMA(1, 1, At, B1); PG8_BAR; PG8_SCHED;
.LBB0_910:
	s_add_u32 s19, s30, 0x10000
	s_addc_u32 s21, s31, 0
	s_add_u32 s28, s28, 0x8000
	s_addc_u32 s29, s29, 0
	s_mov_b32 s65, -2
	s_bitcmp1_b32 s3, 2
	s_cbranch_scc1 .Lh1e_26630
	s_setprio 1
.Lpk0_911:
	ds_read_b128 v[18:21], v191
	ds_read_b128 v[22:25], v191 offset:1024
	ds_read_b128 v[26:29], v191 offset:2048
	ds_read_b128 v[30:33], v191 offset:3072
	ds_read_b128 v[2:5], v192
	ds_read_b128 v[6:9], v192 offset:1024
	ds_read_b128 v[10:13], v192 offset:2048
	ds_read_b128 v[14:17], v192 offset:3072
	s_add_u32 s30, s28, 0x8000
	s_addc_u32 s31, s29, 0
	s_cmp_eq_u32 s65, 12
	s_cselect_b32 s42, s22, s30
	s_cselect_b32 s43, s23, s31
	s_cselect_b32 s40, s24, s19
	s_cselect_b32 s41, s25, s21
	s_add_u32 s30, s42, 0x8000
	s_addc_u32 s31, s43, 0
	v_lshl_add_u64 v[228:229], s[28:29], 0, v[182:183]
	s_add_i32 m0, s27, 0xc000
	ds_read_b128 v[196:199], v193
	ds_read_b128 v[200:203], v193 offset:1024
	ds_read_b128 v[204:207], v193 offset:2048
	ds_read_b128 v[208:211], v193 offset:3072
	ds_read_b128 v[212:215], v193 offset:4096
	ds_read_b128 v[216:219], v193 offset:5120
	ds_read_b128 v[220:223], v193 offset:6144
	ds_read_b128 v[224:227], v193 offset:7168
	global_load_lds_dwordx4 v[228:229], off
	v_lshl_add_u64 v[228:229], s[28:29], 0, v[180:181]
	s_add_i32 m0, s27, 0xe000
	s_nop 0
	global_load_lds_dwordx4 v[228:229], off
	s_waitcnt vmcnt(8)
	s_waitcnt lgkmcnt(0)
	v_mfma_scale_f32_16x16x128_f8f6f4 v[158:161], v[18:25], v[196:203], 0, v194, v194 op_sel_hi:[0,0,0]
	v_mfma_scale_f32_16x16x128_f8f6f4 v[154:157], v[26:33], v[196:203], 0, v194, v194 op_sel_hi:[0,0,0]
	v_mfma_scale_f32_16x16x128_f8f6f4 v[150:153], v[18:25], v[204:211], 0, v194, v194 op_sel_hi:[0,0,0]
	v_mfma_scale_f32_16x16x128_f8f6f4 v[146:149], v[26:33], v[204:211], 0, v194, v194 op_sel_hi:[0,0,0]
	v_mfma_scale_f32_16x16x128_f8f6f4 v[130:133], v[18:25], v[212:219], 0, v194, v194 op_sel_hi:[0,0,0]
	v_mfma_scale_f32_16x16x128_f8f6f4 v[122:125], v[26:33], v[212:219], 0, v194, v194 op_sel_hi:[0,0,0]
	v_mfma_scale_f32_16x16x128_f8f6f4 v[114:117], v[18:25], v[220:227], 0, v194, v194 op_sel_hi:[0,0,0]
	v_mfma_scale_f32_16x16x128_f8f6f4 v[106:109], v[26:33], v[220:227], 0, v194, v194 op_sel_hi:[0,0,0]
	s_nop 3
	v_mfma_scale_f32_16x16x128_f8f6f4 v[142:145], v[2:9], v[196:203], 0, v194, v194 op_sel_hi:[0,0,0]
	v_mfma_scale_f32_16x16x128_f8f6f4 v[138:141], v[10:17], v[196:203], 0, v194, v194 op_sel_hi:[0,0,0]
	v_mfma_scale_f32_16x16x128_f8f6f4 v[134:137], v[2:9], v[204:211], 0, v194, v194 op_sel_hi:[0,0,0]
	v_mfma_scale_f32_16x16x128_f8f6f4 v[126:129], v[10:17], v[204:211], 0, v194, v194 op_sel_hi:[0,0,0]
	v_mfma_scale_f32_16x16x128_f8f6f4 v[118:121], v[2:9], v[212:219], 0, v194, v194 op_sel_hi:[0,0,0]
	v_mfma_scale_f32_16x16x128_f8f6f4 v[110:113], v[10:17], v[212:219], 0, v194, v194 op_sel_hi:[0,0,0]
	v_mfma_scale_f32_16x16x128_f8f6f4 v[102:105], v[2:9], v[220:227], 0, v194, v194 op_sel_hi:[0,0,0]
	v_mfma_scale_f32_16x16x128_f8f6f4 v[98:101], v[10:17], v[220:227], 0, v194, v194 op_sel_hi:[0,0,0]
	s_barrier
	s_add_i32 s66, s60, s48
	v_lshl_add_u64 v[228:229], s[40:41], 0, v[162:163]
	s_mov_b32 m0, s66
	ds_read_b128 v[196:199], v193 offset:16384
	ds_read_b128 v[200:203], v193 offset:17408
	ds_read_b128 v[204:207], v193 offset:18432
	ds_read_b128 v[208:211], v193 offset:19456
	ds_read_b128 v[212:215], v193 offset:20480
	ds_read_b128 v[216:219], v193 offset:21504
	ds_read_b128 v[220:223], v193 offset:22528
	ds_read_b128 v[224:227], v193 offset:23552
	global_load_lds_dwordx4 v[228:229], off
	v_lshl_add_u64 v[230:231], s[40:41], 0, v[164:165]
	s_add_i32 m0, s66, 0x2000
	s_add_i32 s66, s61, s48
	global_load_lds_dwordx4 v[230:231], off
	v_lshl_add_u64 v[228:229], v[228:229], 0, s[6:7]
	s_mov_b32 m0, s66
	s_nop 0
	global_load_lds_dwordx4 v[228:229], off
	v_lshl_add_u64 v[228:229], v[230:231], 0, s[6:7]
	s_add_i32 m0, s66, 0x2000
	s_nop 0
	global_load_lds_dwordx4 v[228:229], off
	v_lshl_add_u64 v[228:229], s[42:43], 0, v[166:167]
	s_mov_b32 m0, s27
	s_nop 0
	global_load_lds_dwordx4 v[228:229], off
	v_lshl_add_u64 v[228:229], s[42:43], 0, v[168:169]
	s_mov_b32 m0, s49
	s_nop 0
	global_load_lds_dwordx4 v[228:229], off
	s_waitcnt vmcnt(8)
	s_waitcnt lgkmcnt(0)
	v_mfma_scale_f32_16x16x128_f8f6f4 v[94:97], v[18:25], v[196:203], 0, v194, v194 op_sel_hi:[0,0,0]
	v_mfma_scale_f32_16x16x128_f8f6f4 v[90:93], v[26:33], v[196:203], 0, v194, v194 op_sel_hi:[0,0,0]
	v_mfma_scale_f32_16x16x128_f8f6f4 v[82:85], v[18:25], v[204:211], 0, v194, v194 op_sel_hi:[0,0,0]
	v_mfma_scale_f32_16x16x128_f8f6f4 v[74:77], v[26:33], v[204:211], 0, v194, v194 op_sel_hi:[0,0,0]
	v_mfma_scale_f32_16x16x128_f8f6f4 v[66:69], v[18:25], v[212:219], 0, v194, v194 op_sel_hi:[0,0,0]
	v_mfma_scale_f32_16x16x128_f8f6f4 v[58:61], v[26:33], v[212:219], 0, v194, v194 op_sel_hi:[0,0,0]
	v_mfma_scale_f32_16x16x128_f8f6f4 v[50:53], v[18:25], v[220:227], 0, v194, v194 op_sel_hi:[0,0,0]
	v_mfma_scale_f32_16x16x128_f8f6f4 v[42:45], v[26:33], v[220:227], 0, v194, v194 op_sel_hi:[0,0,0]
	s_nop 3
	v_mfma_scale_f32_16x16x128_f8f6f4 v[86:89], v[2:9], v[196:203], 0, v194, v194 op_sel_hi:[0,0,0]
	v_mfma_scale_f32_16x16x128_f8f6f4 v[78:81], v[10:17], v[196:203], 0, v194, v194 op_sel_hi:[0,0,0]
	v_mfma_scale_f32_16x16x128_f8f6f4 v[70:73], v[2:9], v[204:211], 0, v194, v194 op_sel_hi:[0,0,0]
	v_mfma_scale_f32_16x16x128_f8f6f4 v[62:65], v[10:17], v[204:211], 0, v194, v194 op_sel_hi:[0,0,0]
	v_mfma_scale_f32_16x16x128_f8f6f4 v[54:57], v[2:9], v[212:219], 0, v194, v194 op_sel_hi:[0,0,0]
	v_mfma_scale_f32_16x16x128_f8f6f4 v[46:49], v[10:17], v[212:219], 0, v194, v194 op_sel_hi:[0,0,0]
	v_mfma_scale_f32_16x16x128_f8f6f4 v[38:41], v[2:9], v[220:227], 0, v194, v194 op_sel_hi:[0,0,0]
	v_mfma_scale_f32_16x16x128_f8f6f4 v[34:37], v[10:17], v[220:227], 0, v194, v194 op_sel_hi:[0,0,0]
	s_barrier
; #define PG8_STAGE(bufoff, gbase, voff) do { _Pragma("unroll") for (int _i = 0; _i < 2; ++_i) \
;         __builtin_amdgcn_global_load_lds((const unsigned*)((const char*)(gbase) + (voff)[_i]), (PG8_LAS unsigned*)(lds + (bufoff) + ldsw + _i * 8192), 16, 0, 0); } while (0)
; #define PG8_WAIT_V(n) asm volatile("s_waitcnt vmcnt(" #n ")" ::: "memory")
; #define PG8_WAIT_L(n) asm volatile("s_waitcnt lgkmcnt(" #n ")" ::: "memory")
; #define PG8_BAR __builtin_amdgcn_s_barrier()
; #define PG8_SCHED __builtin_amdgcn_sched_barrier(0)
; template <class Epi, class Sched, bool ALIGN_EPI = true, bool F8 = false>
; __device__ __forceinline__ void gemm_phase(PG8_LAS unsigned char* lds, const Sched& S, const Epi& E) {
;     ...
;             PG8_LDB(B0, 0, 0); PG8_LDB(B1, 0, 1); PG8_SCHED; PG8_LDA(At, 0, 0); PG8_STAGE(PG8_SA(1, 1), a1, voffA[1]);
;             PG8_WAIT_V(8); PG8_WAIT_L(0); PG8_BAR; PG8_MMA(0, 0, At, B0); PG8_MMA(0, 1, At, B1); PG8_BAR; PG8_SCHED;
;             PG8_LDA(At, 0, 1); PG8_STAGE(PG8_SB(0, 0), b2, voffB[0]); PG8_STAGE(PG8_SB(0, 1), b2, voffB[1]); PG8_STAGE(PG8_SA(0, 0), a2, vA2[0]);
;             PG8_WAIT_V(8); PG8_WAIT_L(0); PG8_BAR; PG8_MMA(1, 0, At, B0); PG8_MMA(1, 1, At, B1); PG8_BAR; PG8_SCHED;
;             PG8_LDB(B0, 1, 0); PG8_LDB(B1, 1, 1); PG8_SCHED; PG8_LDA(At, 1, 0); PG8_STAGE(PG8_SA(0, 1), a2, vA2[1]);
;             PG8_WAIT_V(8); PG8_WAIT_L(0); PG8_BAR; PG8_MMA(0, 0, At, B0); PG8_MMA(0, 1, At, B1); PG8_BAR; PG8_SCHED;
;             PG8_LDA(At, 1, 1); PG8_STAGE(PG8_SB(1, 0), b3, voffB[0]); PG8_STAGE(PG8_SB(1, 1), b3, voffB[1]); PG8_STAGE(PG8_SA(1, 0), a3, vA2[0]);
;             PG8_WAIT_V(8); PG8_WAIT_L(0); PG8_BAR; PG8_MMA(1, 0, At, B0); PG8_MMA(1, 1, At, B1); PG8_BAR; PG8_SCHED;
	s_add_i32 s66, 0, 0x18000
	s_add_i32 s67, 0, 0x1c000
	v_add_u32_e32 v14, s66, v189
	v_add_u32_e32 v30, s67, v189
	ds_read_b128 v[2:5], v14
	ds_read_b128 v[6:9], v14 offset:1024
	ds_read_b128 v[10:13], v14 offset:2048
	ds_read_b128 v[14:17], v14 offset:3072
	ds_read_b128 v[18:21], v30
	ds_read_b128 v[22:25], v30 offset:1024
	ds_read_b128 v[26:29], v30 offset:2048
	ds_read_b128 v[30:33], v30 offset:3072
	s_mov_b32 m0, s50
	v_lshl_add_u64 v[228:229], s[42:43], 0, v[172:173]
	ds_read_b128 v[196:199], v193 offset:32768
	ds_read_b128 v[200:203], v193 offset:33792
	ds_read_b128 v[204:207], v193 offset:34816
	ds_read_b128 v[208:211], v193 offset:35840
	ds_read_b128 v[212:215], v193 offset:36864
	ds_read_b128 v[216:219], v193 offset:37888
	ds_read_b128 v[220:223], v193 offset:38912
	ds_read_b128 v[224:227], v193 offset:39936
	global_load_lds_dwordx4 v[228:229], off
	v_lshl_add_u64 v[228:229], s[42:43], 0, v[174:175]
	s_mov_b32 m0, s51
	s_nop 0
	global_load_lds_dwordx4 v[228:229], off
	s_waitcnt vmcnt(8)
	s_waitcnt lgkmcnt(0)
	v_mfma_scale_f32_16x16x128_f8f6f4 v[158:161], v[2:9], v[196:203], v[158:161], v194, v194 op_sel_hi:[0,0,0]
	v_mfma_scale_f32_16x16x128_f8f6f4 v[154:157], v[10:17], v[196:203], v[154:157], v194, v194 op_sel_hi:[0,0,0]
	v_mfma_scale_f32_16x16x128_f8f6f4 v[150:153], v[2:9], v[204:211], v[150:153], v194, v194 op_sel_hi:[0,0,0]
	v_mfma_scale_f32_16x16x128_f8f6f4 v[146:149], v[10:17], v[204:211], v[146:149], v194, v194 op_sel_hi:[0,0,0]
	v_mfma_scale_f32_16x16x128_f8f6f4 v[130:133], v[2:9], v[212:219], v[130:133], v194, v194 op_sel_hi:[0,0,0]
	v_mfma_scale_f32_16x16x128_f8f6f4 v[122:125], v[10:17], v[212:219], v[122:125], v194, v194 op_sel_hi:[0,0,0]
	v_mfma_scale_f32_16x16x128_f8f6f4 v[114:117], v[2:9], v[220:227], v[114:117], v194, v194 op_sel_hi:[0,0,0]
	v_mfma_scale_f32_16x16x128_f8f6f4 v[106:109], v[10:17], v[220:227], v[106:109], v194, v194 op_sel_hi:[0,0,0]
	s_nop 3
	v_mfma_scale_f32_16x16x128_f8f6f4 v[142:145], v[18:25], v[196:203], v[142:145], v194, v194 op_sel_hi:[0,0,0]
	v_mfma_scale_f32_16x16x128_f8f6f4 v[138:141], v[26:33], v[196:203], v[138:141], v194, v194 op_sel_hi:[0,0,0]
	v_mfma_scale_f32_16x16x128_f8f6f4 v[134:137], v[18:25], v[204:211], v[134:137], v194, v194 op_sel_hi:[0,0,0]
	v_mfma_scale_f32_16x16x128_f8f6f4 v[126:129], v[26:33], v[204:211], v[126:129], v194, v194 op_sel_hi:[0,0,0]
	v_mfma_scale_f32_16x16x128_f8f6f4 v[118:121], v[18:25], v[212:219], v[118:121], v194, v194 op_sel_hi:[0,0,0]
	v_mfma_scale_f32_16x16x128_f8f6f4 v[110:113], v[26:33], v[212:219], v[110:113], v194, v194 op_sel_hi:[0,0,0]
	v_mfma_scale_f32_16x16x128_f8f6f4 v[102:105], v[18:25], v[220:227], v[102:105], v194, v194 op_sel_hi:[0,0,0]
	v_mfma_scale_f32_16x16x128_f8f6f4 v[98:101], v[26:33], v[220:227], v[98:101], v194, v194 op_sel_hi:[0,0,0]
	s_barrier
	s_add_u32 s40, s40, 0x8000
	s_addc_u32 s41, s41, 0
	s_add_i32 s42, s66, s48
	v_lshl_add_u64 v[228:229], s[40:41], 0, v[162:163]
	s_mov_b32 m0, s42
	ds_read_b128 v[196:199], v193 offset:49152
	ds_read_b128 v[200:203], v193 offset:50176
	ds_read_b128 v[204:207], v193 offset:51200
	ds_read_b128 v[208:211], v193 offset:52224
	ds_read_b128 v[212:215], v193 offset:53248
	ds_read_b128 v[216:219], v193 offset:54272
	ds_read_b128 v[220:223], v193 offset:55296
	ds_read_b128 v[224:227], v193 offset:56320
	global_load_lds_dwordx4 v[228:229], off
	v_lshl_add_u64 v[228:229], s[40:41], 0, v[164:165]
	s_add_i32 m0, s42, 0x2000
	s_add_i32 s42, s67, s48
	global_load_lds_dwordx4 v[228:229], off
	v_lshl_add_u64 v[228:229], s[40:41], 0, v[176:177]
	s_mov_b32 m0, s42
	s_nop 0
	global_load_lds_dwordx4 v[228:229], off
	v_lshl_add_u64 v[228:229], s[40:41], 0, v[178:179]
	s_add_i32 m0, s42, 0x2000
	s_nop 0
	global_load_lds_dwordx4 v[228:229], off
	v_lshl_add_u64 v[228:229], s[30:31], 0, v[166:167]
	s_mov_b32 m0, s53
	s_nop 0
	global_load_lds_dwordx4 v[228:229], off
	v_lshl_add_u64 v[228:229], s[30:31], 0, v[168:169]
	s_mov_b32 m0, s58
	s_nop 0
	global_load_lds_dwordx4 v[228:229], off
	s_waitcnt vmcnt(8)
	s_waitcnt lgkmcnt(0)
	v_mfma_scale_f32_16x16x128_f8f6f4 v[94:97], v[2:9], v[196:203], v[94:97], v194, v194 op_sel_hi:[0,0,0]
	v_mfma_scale_f32_16x16x128_f8f6f4 v[90:93], v[10:17], v[196:203], v[90:93], v194, v194 op_sel_hi:[0,0,0]
	v_mfma_scale_f32_16x16x128_f8f6f4 v[82:85], v[2:9], v[204:211], v[82:85], v194, v194 op_sel_hi:[0,0,0]
	v_mfma_scale_f32_16x16x128_f8f6f4 v[74:77], v[10:17], v[204:211], v[74:77], v194, v194 op_sel_hi:[0,0,0]
	v_mfma_scale_f32_16x16x128_f8f6f4 v[66:69], v[2:9], v[212:219], v[66:69], v194, v194 op_sel_hi:[0,0,0]
	v_mfma_scale_f32_16x16x128_f8f6f4 v[58:61], v[10:17], v[212:219], v[58:61], v194, v194 op_sel_hi:[0,0,0]
	v_mfma_scale_f32_16x16x128_f8f6f4 v[50:53], v[2:9], v[220:227], v[50:53], v194, v194 op_sel_hi:[0,0,0]
	v_mfma_scale_f32_16x16x128_f8f6f4 v[42:45], v[10:17], v[220:227], v[42:45], v194, v194 op_sel_hi:[0,0,0]
	s_nop 3
	v_mfma_scale_f32_16x16x128_f8f6f4 v[86:89], v[18:25], v[196:203], v[86:89], v194, v194 op_sel_hi:[0,0,0]
	v_mfma_scale_f32_16x16x128_f8f6f4 v[78:81], v[26:33], v[196:203], v[78:81], v194, v194 op_sel_hi:[0,0,0]
	v_mfma_scale_f32_16x16x128_f8f6f4 v[70:73], v[18:25], v[204:211], v[70:73], v194, v194 op_sel_hi:[0,0,0]
	v_mfma_scale_f32_16x16x128_f8f6f4 v[62:65], v[26:33], v[204:211], v[62:65], v194, v194 op_sel_hi:[0,0,0]
	v_mfma_scale_f32_16x16x128_f8f6f4 v[54:57], v[18:25], v[212:219], v[54:57], v194, v194 op_sel_hi:[0,0,0]
	v_mfma_scale_f32_16x16x128_f8f6f4 v[46:49], v[26:33], v[212:219], v[46:49], v194, v194 op_sel_hi:[0,0,0]
	v_mfma_scale_f32_16x16x128_f8f6f4 v[38:41], v[18:25], v[220:227], v[38:41], v194, v194 op_sel_hi:[0,0,0]
	v_mfma_scale_f32_16x16x128_f8f6f4 v[34:37], v[26:33], v[220:227], v[34:37], v194, v194 op_sel_hi:[0,0,0]
	s_barrier
	s_add_i32 s65, s65, 2
	s_add_u32 s19, s19, 0x10000
	s_addc_u32 s21, s21, 0
	s_add_u32 s28, s28, 0x10000
	s_addc_u32 s29, s29, 0
	s_cmp_gt_u32 s65, 13
	s_cbranch_scc0 .LBB0_911
	s_branch .Lfx_26630
; #define PG8_STAGE(bufoff, gbase, voff) do { _Pragma("unroll") for (int _i = 0; _i < 2; ++_i) \
;         __builtin_amdgcn_global_load_lds((const unsigned*)((const char*)(gbase) + (voff)[_i]), (PG8_LAS unsigned*)(lds + (bufoff) + ldsw + _i * 8192), 16, 0, 0); } while (0)
; #define PG8_WAIT_V(n) asm volatile("s_waitcnt vmcnt(" #n ")" ::: "memory")
; #define PG8_WAIT_L(n) asm volatile("s_waitcnt lgkmcnt(" #n ")" ::: "memory")
; #define PG8_BAR __builtin_amdgcn_s_barrier()
; #define PG8_SCHED __builtin_amdgcn_sched_barrier(0)
; template <class Epi, class Sched, bool ALIGN_EPI = true, bool F8 = false>
; __device__ __forceinline__ void gemm_phase(PG8_LAS unsigned char* lds, const Sched& S, const Epi& E) {
;     ...
;             PG8_LDB(B0, 0, 0); PG8_LDB(B1, 0, 1); PG8_SCHED; PG8_LDA(At, 0, 0); PG8_STAGE(PG8_SA(1, 1), a1, voffA[1]);
;             PG8_WAIT_V(8); PG8_WAIT_L(0); PG8_BAR; PG8_MMA(0, 0, At, B0); PG8_MMA(0, 1, At, B1); PG8_BAR; PG8_SCHED;
;             PG8_LDA(At, 0, 1); PG8_STAGE(PG8_SB(0, 0), b2, voffB[0]); PG8_STAGE(PG8_SB(0, 1), b2, voffB[1]); PG8_STAGE(PG8_SA(0, 0), a2, vA2[0]);
;             PG8_WAIT_V(8); PG8_WAIT_L(0); PG8_BAR; PG8_MMA(1, 0, At, B0); PG8_MMA(1, 1, At, B1); PG8_BAR; PG8_SCHED;
;             PG8_LDB(B0, 1, 0); PG8_LDB(B1, 1, 1); PG8_SCHED; PG8_LDA(At, 1, 0); PG8_STAGE(PG8_SA(0, 1), a2, vA2[1]);
;             PG8_WAIT_V(8); PG8_WAIT_L(0); PG8_BAR; PG8_MMA(0, 0, At, B0); PG8_MMA(0, 1, At, B1); PG8_BAR; PG8_SCHED;
;             PG8_LDA(At, 1, 1); PG8_STAGE(PG8_SB(1, 0), b3, voffB[0]); PG8_STAGE(PG8_SB(1, 1), b3, voffB[1]); PG8_STAGE(PG8_SA(1, 0), a3, vA2[0]);
;             PG8_WAIT_V(8); PG8_WAIT_L(0); PG8_BAR; PG8_MMA(1, 0, At, B0); PG8_MMA(1, 1, At, B1); PG8_BAR; PG8_SCHED;
.LBB0_911:
	ds_read_b128 v[18:21], v191
	ds_read_b128 v[22:25], v191 offset:1024
	ds_read_b128 v[26:29], v191 offset:2048
	ds_read_b128 v[30:33], v191 offset:3072
	ds_read_b128 v[2:5], v192
	ds_read_b128 v[6:9], v192 offset:1024
	ds_read_b128 v[10:13], v192 offset:2048
	ds_read_b128 v[14:17], v192 offset:3072
	s_add_u32 s30, s28, 0x8000
	s_addc_u32 s31, s29, 0
	s_cmp_eq_u32 s65, 12
	s_cselect_b32 s42, s22, s30
	s_cselect_b32 s43, s23, s31
	s_cselect_b32 s40, s24, s19
	s_cselect_b32 s41, s25, s21
	s_add_u32 s30, s42, 0x8000
	s_addc_u32 s31, s43, 0
	v_lshl_add_u64 v[228:229], s[28:29], 0, v[182:183]
	s_add_i32 m0, s27, 0xc000
	ds_read_b128 v[196:199], v193
	ds_read_b128 v[200:203], v193 offset:1024
	ds_read_b128 v[204:207], v193 offset:2048
	ds_read_b128 v[208:211], v193 offset:3072
	ds_read_b128 v[212:215], v193 offset:4096
	ds_read_b128 v[216:219], v193 offset:5120
	ds_read_b128 v[220:223], v193 offset:6144
	ds_read_b128 v[224:227], v193 offset:7168
	global_load_lds_dwordx4 v[228:229], off
	v_lshl_add_u64 v[228:229], s[28:29], 0, v[180:181]
	s_add_i32 m0, s27, 0xe000
	s_nop 0
	global_load_lds_dwordx4 v[228:229], off
	s_waitcnt vmcnt(8)
	s_waitcnt lgkmcnt(0)
	v_mfma_scale_f32_16x16x128_f8f6f4 v[158:161], v[18:25], v[196:203], v[158:161], v194, v194 op_sel_hi:[0,0,0]
	v_mfma_scale_f32_16x16x128_f8f6f4 v[154:157], v[26:33], v[196:203], v[154:157], v194, v194 op_sel_hi:[0,0,0]
	v_mfma_scale_f32_16x16x128_f8f6f4 v[150:153], v[18:25], v[204:211], v[150:153], v194, v194 op_sel_hi:[0,0,0]
	v_mfma_scale_f32_16x16x128_f8f6f4 v[146:149], v[26:33], v[204:211], v[146:149], v194, v194 op_sel_hi:[0,0,0]
	v_mfma_scale_f32_16x16x128_f8f6f4 v[130:133], v[18:25], v[212:219], v[130:133], v194, v194 op_sel_hi:[0,0,0]
	v_mfma_scale_f32_16x16x128_f8f6f4 v[122:125], v[26:33], v[212:219], v[122:125], v194, v194 op_sel_hi:[0,0,0]
	v_mfma_scale_f32_16x16x128_f8f6f4 v[114:117], v[18:25], v[220:227], v[114:117], v194, v194 op_sel_hi:[0,0,0]
	v_mfma_scale_f32_16x16x128_f8f6f4 v[106:109], v[26:33], v[220:227], v[106:109], v194, v194 op_sel_hi:[0,0,0]
	s_nop 3
	v_mfma_scale_f32_16x16x128_f8f6f4 v[142:145], v[2:9], v[196:203], v[142:145], v194, v194 op_sel_hi:[0,0,0]
	v_mfma_scale_f32_16x16x128_f8f6f4 v[138:141], v[10:17], v[196:203], v[138:141], v194, v194 op_sel_hi:[0,0,0]
	v_mfma_scale_f32_16x16x128_f8f6f4 v[134:137], v[2:9], v[204:211], v[134:137], v194, v194 op_sel_hi:[0,0,0]
	v_mfma_scale_f32_16x16x128_f8f6f4 v[126:129], v[10:17], v[204:211], v[126:129], v194, v194 op_sel_hi:[0,0,0]
	v_mfma_scale_f32_16x16x128_f8f6f4 v[118:121], v[2:9], v[212:219], v[118:121], v194, v194 op_sel_hi:[0,0,0]
	v_mfma_scale_f32_16x16x128_f8f6f4 v[110:113], v[10:17], v[212:219], v[110:113], v194, v194 op_sel_hi:[0,0,0]
	v_mfma_scale_f32_16x16x128_f8f6f4 v[102:105], v[2:9], v[220:227], v[102:105], v194, v194 op_sel_hi:[0,0,0]
	v_mfma_scale_f32_16x16x128_f8f6f4 v[98:101], v[10:17], v[220:227], v[98:101], v194, v194 op_sel_hi:[0,0,0]
	s_barrier
	s_add_i32 s66, s60, s48
	v_lshl_add_u64 v[228:229], s[40:41], 0, v[162:163]
	s_mov_b32 m0, s66
	ds_read_b128 v[196:199], v193 offset:16384
	ds_read_b128 v[200:203], v193 offset:17408
	ds_read_b128 v[204:207], v193 offset:18432
	ds_read_b128 v[208:211], v193 offset:19456
	ds_read_b128 v[212:215], v193 offset:20480
	ds_read_b128 v[216:219], v193 offset:21504
	ds_read_b128 v[220:223], v193 offset:22528
	ds_read_b128 v[224:227], v193 offset:23552
	global_load_lds_dwordx4 v[228:229], off
	v_lshl_add_u64 v[230:231], s[40:41], 0, v[164:165]
	s_add_i32 m0, s66, 0x2000
	s_add_i32 s66, s61, s48
	global_load_lds_dwordx4 v[230:231], off
	v_lshl_add_u64 v[228:229], v[228:229], 0, s[6:7]
	s_mov_b32 m0, s66
	s_nop 0
	global_load_lds_dwordx4 v[228:229], off
	v_lshl_add_u64 v[228:229], v[230:231], 0, s[6:7]
	s_add_i32 m0, s66, 0x2000
	s_nop 0
	global_load_lds_dwordx4 v[228:229], off
	v_lshl_add_u64 v[228:229], s[42:43], 0, v[166:167]
	s_mov_b32 m0, s27
	s_nop 0
	global_load_lds_dwordx4 v[228:229], off
	v_lshl_add_u64 v[228:229], s[42:43], 0, v[168:169]
	s_mov_b32 m0, s49
	s_nop 0
	global_load_lds_dwordx4 v[228:229], off
	s_waitcnt vmcnt(8)
	s_waitcnt lgkmcnt(0)
	v_mfma_scale_f32_16x16x128_f8f6f4 v[94:97], v[18:25], v[196:203], v[94:97], v194, v194 op_sel_hi:[0,0,0]
	v_mfma_scale_f32_16x16x128_f8f6f4 v[90:93], v[26:33], v[196:203], v[90:93], v194, v194 op_sel_hi:[0,0,0]
	v_mfma_scale_f32_16x16x128_f8f6f4 v[82:85], v[18:25], v[204:211], v[82:85], v194, v194 op_sel_hi:[0,0,0]
	v_mfma_scale_f32_16x16x128_f8f6f4 v[74:77], v[26:33], v[204:211], v[74:77], v194, v194 op_sel_hi:[0,0,0]
	v_mfma_scale_f32_16x16x128_f8f6f4 v[66:69], v[18:25], v[212:219], v[66:69], v194, v194 op_sel_hi:[0,0,0]
	v_mfma_scale_f32_16x16x128_f8f6f4 v[58:61], v[26:33], v[212:219], v[58:61], v194, v194 op_sel_hi:[0,0,0]
	v_mfma_scale_f32_16x16x128_f8f6f4 v[50:53], v[18:25], v[220:227], v[50:53], v194, v194 op_sel_hi:[0,0,0]
	v_mfma_scale_f32_16x16x128_f8f6f4 v[42:45], v[26:33], v[220:227], v[42:45], v194, v194 op_sel_hi:[0,0,0]
	s_nop 3
	v_mfma_scale_f32_16x16x128_f8f6f4 v[86:89], v[2:9], v[196:203], v[86:89], v194, v194 op_sel_hi:[0,0,0]
	v_mfma_scale_f32_16x16x128_f8f6f4 v[78:81], v[10:17], v[196:203], v[78:81], v194, v194 op_sel_hi:[0,0,0]
	v_mfma_scale_f32_16x16x128_f8f6f4 v[70:73], v[2:9], v[204:211], v[70:73], v194, v194 op_sel_hi:[0,0,0]
	v_mfma_scale_f32_16x16x128_f8f6f4 v[62:65], v[10:17], v[204:211], v[62:65], v194, v194 op_sel_hi:[0,0,0]
	v_mfma_scale_f32_16x16x128_f8f6f4 v[54:57], v[2:9], v[212:219], v[54:57], v194, v194 op_sel_hi:[0,0,0]
	v_mfma_scale_f32_16x16x128_f8f6f4 v[46:49], v[10:17], v[212:219], v[46:49], v194, v194 op_sel_hi:[0,0,0]
	v_mfma_scale_f32_16x16x128_f8f6f4 v[38:41], v[2:9], v[220:227], v[38:41], v194, v194 op_sel_hi:[0,0,0]
	v_mfma_scale_f32_16x16x128_f8f6f4 v[34:37], v[10:17], v[220:227], v[34:37], v194, v194 op_sel_hi:[0,0,0]
	s_barrier
; #define PG8_STAGE(bufoff, gbase, voff) do { _Pragma("unroll") for (int _i = 0; _i < 2; ++_i) \
;         __builtin_amdgcn_global_load_lds((const unsigned*)((const char*)(gbase) + (voff)[_i]), (PG8_LAS unsigned*)(lds + (bufoff) + ldsw + _i * 8192), 16, 0, 0); } while (0)
; #define PG8_WAIT_V(n) asm volatile("s_waitcnt vmcnt(" #n ")" ::: "memory")
; #define PG8_WAIT_L(n) asm volatile("s_waitcnt lgkmcnt(" #n ")" ::: "memory")
; #define PG8_BAR __builtin_amdgcn_s_barrier()
; #define PG8_SCHED __builtin_amdgcn_sched_barrier(0)
; template <class Epi, class Sched, bool ALIGN_EPI = true, bool F8 = false>
; __device__ __forceinline__ void gemm_phase(PG8_LAS unsigned char* lds, const Sched& S, const Epi& E) {
;     ...
;             PG8_LDB(B0, 0, 0); PG8_LDB(B1, 0, 1); PG8_SCHED; PG8_LDA(At, 0, 0); PG8_STAGE(PG8_SA(1, 1), a1, voffA[1]);
;             PG8_WAIT_V(8); PG8_WAIT_L(0); PG8_BAR; PG8_MMA(0, 0, At, B0); PG8_MMA(0, 1, At, B1); PG8_BAR; PG8_SCHED;
;             PG8_LDA(At, 0, 1); PG8_STAGE(PG8_SB(0, 0), b2, voffB[0]); PG8_STAGE(PG8_SB(0, 1), b2, voffB[1]); PG8_STAGE(PG8_SA(0, 0), a2, vA2[0]);
;             PG8_WAIT_V(8); PG8_WAIT_L(0); PG8_BAR; PG8_MMA(1, 0, At, B0); PG8_MMA(1, 1, At, B1); PG8_BAR; PG8_SCHED;
;             PG8_LDB(B0, 1, 0); PG8_LDB(B1, 1, 1); PG8_SCHED; PG8_LDA(At, 1, 0); PG8_STAGE(PG8_SA(0, 1), a2, vA2[1]);
;             PG8_WAIT_V(8); PG8_WAIT_L(0); PG8_BAR; PG8_MMA(0, 0, At, B0); PG8_MMA(0, 1, At, B1); PG8_BAR; PG8_SCHED;
;             PG8_LDA(At, 1, 1); PG8_STAGE(PG8_SB(1, 0), b3, voffB[0]); PG8_STAGE(PG8_SB(1, 1), b3, voffB[1]); PG8_STAGE(PG8_SA(1, 0), a3, vA2[0]);
;             PG8_WAIT_V(8); PG8_WAIT_L(0); PG8_BAR; PG8_MMA(1, 0, At, B0); PG8_MMA(1, 1, At, B1); PG8_BAR; PG8_SCHED;
	s_add_i32 s66, 0, 0x18000
	s_add_i32 s67, 0, 0x1c000
	v_add_u32_e32 v14, s66, v189
	v_add_u32_e32 v30, s67, v189
	ds_read_b128 v[2:5], v14
	ds_read_b128 v[6:9], v14 offset:1024
	ds_read_b128 v[10:13], v14 offset:2048
	ds_read_b128 v[14:17], v14 offset:3072
	ds_read_b128 v[18:21], v30
	ds_read_b128 v[22:25], v30 offset:1024
	ds_read_b128 v[26:29], v30 offset:2048
	ds_read_b128 v[30:33], v30 offset:3072
	s_mov_b32 m0, s50
	v_lshl_add_u64 v[228:229], s[42:43], 0, v[172:173]
	ds_read_b128 v[196:199], v193 offset:32768
	ds_read_b128 v[200:203], v193 offset:33792
	ds_read_b128 v[204:207], v193 offset:34816
	ds_read_b128 v[208:211], v193 offset:35840
	ds_read_b128 v[212:215], v193 offset:36864
	ds_read_b128 v[216:219], v193 offset:37888
	ds_read_b128 v[220:223], v193 offset:38912
	ds_read_b128 v[224:227], v193 offset:39936
	global_load_lds_dwordx4 v[228:229], off
	v_lshl_add_u64 v[228:229], s[42:43], 0, v[174:175]
	s_mov_b32 m0, s51
	s_nop 0
	global_load_lds_dwordx4 v[228:229], off
	s_waitcnt vmcnt(8)
	s_waitcnt lgkmcnt(0)
	v_mfma_scale_f32_16x16x128_f8f6f4 v[158:161], v[2:9], v[196:203], v[158:161], v194, v194 op_sel_hi:[0,0,0]
	v_mfma_scale_f32_16x16x128_f8f6f4 v[154:157], v[10:17], v[196:203], v[154:157], v194, v194 op_sel_hi:[0,0,0]
	v_mfma_scale_f32_16x16x128_f8f6f4 v[150:153], v[2:9], v[204:211], v[150:153], v194, v194 op_sel_hi:[0,0,0]
	v_mfma_scale_f32_16x16x128_f8f6f4 v[146:149], v[10:17], v[204:211], v[146:149], v194, v194 op_sel_hi:[0,0,0]
	v_mfma_scale_f32_16x16x128_f8f6f4 v[130:133], v[2:9], v[212:219], v[130:133], v194, v194 op_sel_hi:[0,0,0]
	v_mfma_scale_f32_16x16x128_f8f6f4 v[122:125], v[10:17], v[212:219], v[122:125], v194, v194 op_sel_hi:[0,0,0]
	v_mfma_scale_f32_16x16x128_f8f6f4 v[114:117], v[2:9], v[220:227], v[114:117], v194, v194 op_sel_hi:[0,0,0]
	v_mfma_scale_f32_16x16x128_f8f6f4 v[106:109], v[10:17], v[220:227], v[106:109], v194, v194 op_sel_hi:[0,0,0]
	s_nop 3
	v_mfma_scale_f32_16x16x128_f8f6f4 v[142:145], v[18:25], v[196:203], v[142:145], v194, v194 op_sel_hi:[0,0,0]
	v_mfma_scale_f32_16x16x128_f8f6f4 v[138:141], v[26:33], v[196:203], v[138:141], v194, v194 op_sel_hi:[0,0,0]
	v_mfma_scale_f32_16x16x128_f8f6f4 v[134:137], v[18:25], v[204:211], v[134:137], v194, v194 op_sel_hi:[0,0,0]
	v_mfma_scale_f32_16x16x128_f8f6f4 v[126:129], v[26:33], v[204:211], v[126:129], v194, v194 op_sel_hi:[0,0,0]
	v_mfma_scale_f32_16x16x128_f8f6f4 v[118:121], v[18:25], v[212:219], v[118:121], v194, v194 op_sel_hi:[0,0,0]
	v_mfma_scale_f32_16x16x128_f8f6f4 v[110:113], v[26:33], v[212:219], v[110:113], v194, v194 op_sel_hi:[0,0,0]
	v_mfma_scale_f32_16x16x128_f8f6f4 v[102:105], v[18:25], v[220:227], v[102:105], v194, v194 op_sel_hi:[0,0,0]
	v_mfma_scale_f32_16x16x128_f8f6f4 v[98:101], v[26:33], v[220:227], v[98:101], v194, v194 op_sel_hi:[0,0,0]
	s_barrier
	s_add_u32 s40, s40, 0x8000
	s_addc_u32 s41, s41, 0
	s_add_i32 s42, s66, s48
	v_lshl_add_u64 v[228:229], s[40:41], 0, v[162:163]
	s_mov_b32 m0, s42
	ds_read_b128 v[196:199], v193 offset:49152
	ds_read_b128 v[200:203], v193 offset:50176
	ds_read_b128 v[204:207], v193 offset:51200
	ds_read_b128 v[208:211], v193 offset:52224
	ds_read_b128 v[212:215], v193 offset:53248
	ds_read_b128 v[216:219], v193 offset:54272
	ds_read_b128 v[220:223], v193 offset:55296
	ds_read_b128 v[224:227], v193 offset:56320
	global_load_lds_dwordx4 v[228:229], off
	v_lshl_add_u64 v[228:229], s[40:41], 0, v[164:165]
	s_add_i32 m0, s42, 0x2000
	s_add_i32 s42, s67, s48
	global_load_lds_dwordx4 v[228:229], off
	v_lshl_add_u64 v[228:229], s[40:41], 0, v[176:177]
	s_mov_b32 m0, s42
	s_nop 0
	global_load_lds_dwordx4 v[228:229], off
	v_lshl_add_u64 v[228:229], s[40:41], 0, v[178:179]
	s_add_i32 m0, s42, 0x2000
	s_nop 0
	global_load_lds_dwordx4 v[228:229], off
	v_lshl_add_u64 v[228:229], s[30:31], 0, v[166:167]
	s_mov_b32 m0, s53
	s_nop 0
	global_load_lds_dwordx4 v[228:229], off
	v_lshl_add_u64 v[228:229], s[30:31], 0, v[168:169]
	s_mov_b32 m0, s58
	s_nop 0
	global_load_lds_dwordx4 v[228:229], off
	s_waitcnt vmcnt(8)
	s_waitcnt lgkmcnt(0)
	v_mfma_scale_f32_16x16x128_f8f6f4 v[94:97], v[2:9], v[196:203], v[94:97], v194, v194 op_sel_hi:[0,0,0]
	v_mfma_scale_f32_16x16x128_f8f6f4 v[90:93], v[10:17], v[196:203], v[90:93], v194, v194 op_sel_hi:[0,0,0]
	v_mfma_scale_f32_16x16x128_f8f6f4 v[82:85], v[2:9], v[204:211], v[82:85], v194, v194 op_sel_hi:[0,0,0]
	v_mfma_scale_f32_16x16x128_f8f6f4 v[74:77], v[10:17], v[204:211], v[74:77], v194, v194 op_sel_hi:[0,0,0]
	v_mfma_scale_f32_16x16x128_f8f6f4 v[66:69], v[2:9], v[212:219], v[66:69], v194, v194 op_sel_hi:[0,0,0]
	v_mfma_scale_f32_16x16x128_f8f6f4 v[58:61], v[10:17], v[212:219], v[58:61], v194, v194 op_sel_hi:[0,0,0]
	v_mfma_scale_f32_16x16x128_f8f6f4 v[50:53], v[2:9], v[220:227], v[50:53], v194, v194 op_sel_hi:[0,0,0]
	v_mfma_scale_f32_16x16x128_f8f6f4 v[42:45], v[10:17], v[220:227], v[42:45], v194, v194 op_sel_hi:[0,0,0]
	s_nop 3
	v_mfma_scale_f32_16x16x128_f8f6f4 v[86:89], v[18:25], v[196:203], v[86:89], v194, v194 op_sel_hi:[0,0,0]
	v_mfma_scale_f32_16x16x128_f8f6f4 v[78:81], v[26:33], v[196:203], v[78:81], v194, v194 op_sel_hi:[0,0,0]
	v_mfma_scale_f32_16x16x128_f8f6f4 v[70:73], v[18:25], v[204:211], v[70:73], v194, v194 op_sel_hi:[0,0,0]
	v_mfma_scale_f32_16x16x128_f8f6f4 v[62:65], v[26:33], v[204:211], v[62:65], v194, v194 op_sel_hi:[0,0,0]
	v_mfma_scale_f32_16x16x128_f8f6f4 v[54:57], v[18:25], v[212:219], v[54:57], v194, v194 op_sel_hi:[0,0,0]
	v_mfma_scale_f32_16x16x128_f8f6f4 v[46:49], v[26:33], v[212:219], v[46:49], v194, v194 op_sel_hi:[0,0,0]
	v_mfma_scale_f32_16x16x128_f8f6f4 v[38:41], v[18:25], v[220:227], v[38:41], v194, v194 op_sel_hi:[0,0,0]
	v_mfma_scale_f32_16x16x128_f8f6f4 v[34:37], v[26:33], v[220:227], v[34:37], v194, v194 op_sel_hi:[0,0,0]
	s_barrier
	s_add_i32 s65, s65, 2
	s_add_u32 s19, s19, 0x10000
	s_addc_u32 s21, s21, 0
	s_add_u32 s28, s28, 0x10000
	s_addc_u32 s29, s29, 0
	s_cmp_gt_u32 s65, 13
	s_cbranch_scc0 .LBB0_911
	s_branch .Lfx_26630

; #define PG8_STAGE(bufoff, gbase, voff) do { _Pragma("unroll") for (int _i = 0; _i < 2; ++_i) \
;         __builtin_amdgcn_global_load_lds((const unsigned*)((const char*)(gbase) + (voff)[_i]), (PG8_LAS unsigned*)(lds + (bufoff) + ldsw + _i * 8192), 16, 0, 0); } while (0)
; #define PG8_WAIT_V(n) asm volatile("s_waitcnt vmcnt(" #n ")" ::: "memory")
; #define PG8_WAIT_L(n) asm volatile("s_waitcnt lgkmcnt(" #n ")" ::: "memory")
; #define PG8_BAR __builtin_amdgcn_s_barrier()
; #define PG8_SCHED __builtin_amdgcn_sched_barrier(0)
; template <class Epi, class Sched, bool ALIGN_EPI = true, bool F8 = false>
; __device__ __forceinline__ void gemm_phase(PG8_LAS unsigned char* lds, const Sched& S, const Epi& E) {
;     ...
;             PG8_LDB(B0, 0, 0); PG8_LDB(B1, 0, 1); PG8_SCHED; PG8_LDA(At, 0, 0); PG8_STAGE(PG8_SA(1, 1), a1, voffA[1]);
;             PG8_WAIT_V(8); PG8_WAIT_L(0); PG8_BAR; PG8_MMA(0, 0, At, B0); PG8_MMA(0, 1, At, B1); PG8_BAR; PG8_SCHED;
;             PG8_LDA(At, 0, 1); PG8_STAGE(PG8_SB(0, 0), b2, voffB[0]); PG8_STAGE(PG8_SB(0, 1), b2, voffB[1]); PG8_STAGE(PG8_SA(0, 0), a2, vA2[0]);
;             PG8_WAIT_V(8); PG8_WAIT_L(0); PG8_BAR; PG8_MMA(1, 0, At, B0); PG8_MMA(1, 1, At, B1); PG8_BAR; PG8_SCHED;
;             PG8_LDB(B0, 1, 0); PG8_LDB(B1, 1, 1); PG8_SCHED; PG8_LDA(At, 1, 0); PG8_STAGE(PG8_SA(0, 1), a2, vA2[1]);
;             PG8_WAIT_V(8); PG8_WAIT_L(0); PG8_BAR; PG8_MMA(0, 0, At, B0); PG8_MMA(0, 1, At, B1); PG8_BAR; PG8_SCHED;
;             PG8_LDA(At, 1, 1); PG8_STAGE(PG8_SB(1, 0), b3, voffB[0]); PG8_STAGE(PG8_SB(1, 1), b3, voffB[1]); PG8_STAGE(PG8_SA(1, 0), a3, vA2[0]);
;             PG8_WAIT_V(8); PG8_WAIT_L(0); PG8_BAR; PG8_MMA(1, 0, At, B0); PG8_MMA(1, 1, At, B1); PG8_BAR; PG8_SCHED;
.Lpk1_911:
	ds_read_b128 v[18:21], v191
	ds_read_b128 v[22:25], v191 offset:1024
	ds_read_b128 v[26:29], v191 offset:2048
	ds_read_b128 v[30:33], v191 offset:3072
	ds_read_b128 v[2:5], v192
	ds_read_b128 v[6:9], v192 offset:1024
	ds_read_b128 v[10:13], v192 offset:2048
	ds_read_b128 v[14:17], v192 offset:3072
	s_add_u32 s30, s28, 0x8000
	s_addc_u32 s31, s29, 0
	s_cmp_eq_u32 s65, 12
	s_cselect_b32 s42, s22, s30
	s_cselect_b32 s43, s23, s31
	s_cselect_b32 s40, s24, s19
	s_cselect_b32 s41, s25, s21
	s_add_u32 s30, s42, 0x8000
	s_addc_u32 s31, s43, 0
	v_lshl_add_u64 v[228:229], s[28:29], 0, v[182:183]
	s_add_i32 m0, s27, 0xc000
	ds_read_b128 v[196:199], v193
	ds_read_b128 v[200:203], v193 offset:1024
	ds_read_b128 v[204:207], v193 offset:2048
	ds_read_b128 v[208:211], v193 offset:3072
	ds_read_b128 v[212:215], v193 offset:4096
	ds_read_b128 v[216:219], v193 offset:5120
	ds_read_b128 v[220:223], v193 offset:6144
	ds_read_b128 v[224:227], v193 offset:7168
	global_load_lds_dwordx4 v[228:229], off
	v_lshl_add_u64 v[228:229], s[28:29], 0, v[180:181]
	s_add_i32 m0, s27, 0xe000
	s_nop 0
	global_load_lds_dwordx4 v[228:229], off
	s_waitcnt vmcnt(8)
	s_waitcnt lgkmcnt(0)
	s_barrier
	v_mfma_scale_f32_16x16x128_f8f6f4 v[158:161], v[18:25], v[196:203], 0, v194, v194 op_sel_hi:[0,0,0]
	v_mfma_scale_f32_16x16x128_f8f6f4 v[154:157], v[26:33], v[196:203], 0, v194, v194 op_sel_hi:[0,0,0]
	v_mfma_scale_f32_16x16x128_f8f6f4 v[150:153], v[18:25], v[204:211], 0, v194, v194 op_sel_hi:[0,0,0]
	v_mfma_scale_f32_16x16x128_f8f6f4 v[146:149], v[26:33], v[204:211], 0, v194, v194 op_sel_hi:[0,0,0]
	v_mfma_scale_f32_16x16x128_f8f6f4 v[130:133], v[18:25], v[212:219], 0, v194, v194 op_sel_hi:[0,0,0]
	v_mfma_scale_f32_16x16x128_f8f6f4 v[122:125], v[26:33], v[212:219], 0, v194, v194 op_sel_hi:[0,0,0]
	v_mfma_scale_f32_16x16x128_f8f6f4 v[114:117], v[18:25], v[220:227], 0, v194, v194 op_sel_hi:[0,0,0]
	v_mfma_scale_f32_16x16x128_f8f6f4 v[106:109], v[26:33], v[220:227], 0, v194, v194 op_sel_hi:[0,0,0]
	s_nop 3
	v_mfma_scale_f32_16x16x128_f8f6f4 v[142:145], v[2:9], v[196:203], 0, v194, v194 op_sel_hi:[0,0,0]
	v_mfma_scale_f32_16x16x128_f8f6f4 v[138:141], v[10:17], v[196:203], 0, v194, v194 op_sel_hi:[0,0,0]
	v_mfma_scale_f32_16x16x128_f8f6f4 v[134:137], v[2:9], v[204:211], 0, v194, v194 op_sel_hi:[0,0,0]
	v_mfma_scale_f32_16x16x128_f8f6f4 v[126:129], v[10:17], v[204:211], 0, v194, v194 op_sel_hi:[0,0,0]
	v_mfma_scale_f32_16x16x128_f8f6f4 v[118:121], v[2:9], v[212:219], 0, v194, v194 op_sel_hi:[0,0,0]
	v_mfma_scale_f32_16x16x128_f8f6f4 v[110:113], v[10:17], v[212:219], 0, v194, v194 op_sel_hi:[0,0,0]
	v_mfma_scale_f32_16x16x128_f8f6f4 v[102:105], v[2:9], v[220:227], 0, v194, v194 op_sel_hi:[0,0,0]
	v_mfma_scale_f32_16x16x128_f8f6f4 v[98:101], v[10:17], v[220:227], 0, v194, v194 op_sel_hi:[0,0,0]
	s_add_i32 s66, s60, s48
	v_lshl_add_u64 v[228:229], s[40:41], 0, v[162:163]
	s_mov_b32 m0, s66
	ds_read_b128 v[196:199], v193 offset:16384
	ds_read_b128 v[200:203], v193 offset:17408
	ds_read_b128 v[204:207], v193 offset:18432
	ds_read_b128 v[208:211], v193 offset:19456
	ds_read_b128 v[212:215], v193 offset:20480
	ds_read_b128 v[216:219], v193 offset:21504
	ds_read_b128 v[220:223], v193 offset:22528
	ds_read_b128 v[224:227], v193 offset:23552
	global_load_lds_dwordx4 v[228:229], off
	v_lshl_add_u64 v[230:231], s[40:41], 0, v[164:165]
	s_add_i32 m0, s66, 0x2000
	s_add_i32 s66, s61, s48
	global_load_lds_dwordx4 v[230:231], off
	v_lshl_add_u64 v[228:229], v[228:229], 0, s[6:7]
	s_mov_b32 m0, s66
	s_nop 0
	global_load_lds_dwordx4 v[228:229], off
	v_lshl_add_u64 v[228:229], v[230:231], 0, s[6:7]
	s_add_i32 m0, s66, 0x2000
	s_nop 0
	global_load_lds_dwordx4 v[228:229], off
	v_lshl_add_u64 v[228:229], s[42:43], 0, v[166:167]
	s_mov_b32 m0, s27
	s_nop 0
	global_load_lds_dwordx4 v[228:229], off
	v_lshl_add_u64 v[228:229], s[42:43], 0, v[168:169]
	s_mov_b32 m0, s49
	s_nop 0
	global_load_lds_dwordx4 v[228:229], off
	s_waitcnt vmcnt(8)
	s_waitcnt lgkmcnt(0)
	s_barrier
	v_mfma_scale_f32_16x16x128_f8f6f4 v[94:97], v[18:25], v[196:203], 0, v194, v194 op_sel_hi:[0,0,0]
	v_mfma_scale_f32_16x16x128_f8f6f4 v[90:93], v[26:33], v[196:203], 0, v194, v194 op_sel_hi:[0,0,0]
	v_mfma_scale_f32_16x16x128_f8f6f4 v[82:85], v[18:25], v[204:211], 0, v194, v194 op_sel_hi:[0,0,0]
	v_mfma_scale_f32_16x16x128_f8f6f4 v[74:77], v[26:33], v[204:211], 0, v194, v194 op_sel_hi:[0,0,0]
	v_mfma_scale_f32_16x16x128_f8f6f4 v[66:69], v[18:25], v[212:219], 0, v194, v194 op_sel_hi:[0,0,0]
	v_mfma_scale_f32_16x16x128_f8f6f4 v[58:61], v[26:33], v[212:219], 0, v194, v194 op_sel_hi:[0,0,0]
	v_mfma_scale_f32_16x16x128_f8f6f4 v[50:53], v[18:25], v[220:227], 0, v194, v194 op_sel_hi:[0,0,0]
	v_mfma_scale_f32_16x16x128_f8f6f4 v[42:45], v[26:33], v[220:227], 0, v194, v194 op_sel_hi:[0,0,0]
	s_nop 3
	v_mfma_scale_f32_16x16x128_f8f6f4 v[86:89], v[2:9], v[196:203], 0, v194, v194 op_sel_hi:[0,0,0]
	v_mfma_scale_f32_16x16x128_f8f6f4 v[78:81], v[10:17], v[196:203], 0, v194, v194 op_sel_hi:[0,0,0]
	v_mfma_scale_f32_16x16x128_f8f6f4 v[70:73], v[2:9], v[204:211], 0, v194, v194 op_sel_hi:[0,0,0]
	v_mfma_scale_f32_16x16x128_f8f6f4 v[62:65], v[10:17], v[204:211], 0, v194, v194 op_sel_hi:[0,0,0]
	v_mfma_scale_f32_16x16x128_f8f6f4 v[54:57], v[2:9], v[212:219], 0, v194, v194 op_sel_hi:[0,0,0]
	v_mfma_scale_f32_16x16x128_f8f6f4 v[46:49], v[10:17], v[212:219], 0, v194, v194 op_sel_hi:[0,0,0]
	v_mfma_scale_f32_16x16x128_f8f6f4 v[38:41], v[2:9], v[220:227], 0, v194, v194 op_sel_hi:[0,0,0]
	v_mfma_scale_f32_16x16x128_f8f6f4 v[34:37], v[10:17], v[220:227], 0, v194, v194 op_sel_hi:[0,0,0]
	s_add_i32 s66, 0, 0x18000
	s_add_i32 s67, 0, 0x1c000
	v_add_u32_e32 v14, s66, v189
	v_add_u32_e32 v30, s67, v189
	ds_read_b128 v[2:5], v14
	ds_read_b128 v[6:9], v14 offset:1024
	ds_read_b128 v[10:13], v14 offset:2048
	ds_read_b128 v[14:17], v14 offset:3072
	ds_read_b128 v[18:21], v30
	ds_read_b128 v[22:25], v30 offset:1024
	ds_read_b128 v[26:29], v30 offset:2048
	ds_read_b128 v[30:33], v30 offset:3072
	s_mov_b32 m0, s50
	v_lshl_add_u64 v[228:229], s[42:43], 0, v[172:173]
	ds_read_b128 v[196:199], v193 offset:32768
	ds_read_b128 v[200:203], v193 offset:33792
	ds_read_b128 v[204:207], v193 offset:34816
	ds_read_b128 v[208:211], v193 offset:35840
	ds_read_b128 v[212:215], v193 offset:36864
	ds_read_b128 v[216:219], v193 offset:37888
	ds_read_b128 v[220:223], v193 offset:38912
	ds_read_b128 v[224:227], v193 offset:39936
	global_load_lds_dwordx4 v[228:229], off
	v_lshl_add_u64 v[228:229], s[42:43], 0, v[174:175]
	s_mov_b32 m0, s51
	s_nop 0
	global_load_lds_dwordx4 v[228:229], off
	s_waitcnt vmcnt(8)
	s_waitcnt lgkmcnt(0)
	s_barrier
; #define PG8_STAGE(bufoff, gbase, voff) do { _Pragma("unroll") for (int _i = 0; _i < 2; ++_i) \
;         __builtin_amdgcn_global_load_lds((const unsigned*)((const char*)(gbase) + (voff)[_i]), (PG8_LAS unsigned*)(lds + (bufoff) + ldsw + _i * 8192), 16, 0, 0); } while (0)
; #define PG8_WAIT_V(n) asm volatile("s_waitcnt vmcnt(" #n ")" ::: "memory")
; #define PG8_WAIT_L(n) asm volatile("s_waitcnt lgkmcnt(" #n ")" ::: "memory")
; #define PG8_BAR __builtin_amdgcn_s_barrier()
; #define PG8_SCHED __builtin_amdgcn_sched_barrier(0)
; template <class Epi, class Sched, bool ALIGN_EPI = true, bool F8 = false>
; __device__ __forceinline__ void gemm_phase(PG8_LAS unsigned char* lds, const Sched& S, const Epi& E) {
;     ...
;             PG8_LDB(B0, 0, 0); PG8_LDB(B1, 0, 1); PG8_SCHED; PG8_LDA(At, 0, 0); PG8_STAGE(PG8_SA(1, 1), a1, voffA[1]);
;             PG8_WAIT_V(8); PG8_WAIT_L(0); PG8_BAR; PG8_MMA(0, 0, At, B0); PG8_MMA(0, 1, At, B1); PG8_BAR; PG8_SCHED;
;             PG8_LDA(At, 0, 1); PG8_STAGE(PG8_SB(0, 0), b2, voffB[0]); PG8_STAGE(PG8_SB(0, 1), b2, voffB[1]); PG8_STAGE(PG8_SA(0, 0), a2, vA2[0]);
;             PG8_WAIT_V(8); PG8_WAIT_L(0); PG8_BAR; PG8_MMA(1, 0, At, B0); PG8_MMA(1, 1, At, B1); PG8_BAR; PG8_SCHED;
;             PG8_LDB(B0, 1, 0); PG8_LDB(B1, 1, 1); PG8_SCHED; PG8_LDA(At, 1, 0); PG8_STAGE(PG8_SA(0, 1), a2, vA2[1]);
;             PG8_WAIT_V(8); PG8_WAIT_L(0); PG8_BAR; PG8_MMA(0, 0, At, B0); PG8_MMA(0, 1, At, B1); PG8_BAR; PG8_SCHED;
;             PG8_LDA(At, 1, 1); PG8_STAGE(PG8_SB(1, 0), b3, voffB[0]); PG8_STAGE(PG8_SB(1, 1), b3, voffB[1]); PG8_STAGE(PG8_SA(1, 0), a3, vA2[0]);
;             PG8_WAIT_V(8); PG8_WAIT_L(0); PG8_BAR; PG8_MMA(1, 0, At, B0); PG8_MMA(1, 1, At, B1); PG8_BAR; PG8_SCHED;
	v_mfma_scale_f32_16x16x128_f8f6f4 v[158:161], v[2:9], v[196:203], v[158:161], v194, v194 op_sel_hi:[0,0,0]
	v_mfma_scale_f32_16x16x128_f8f6f4 v[154:157], v[10:17], v[196:203], v[154:157], v194, v194 op_sel_hi:[0,0,0]
	v_mfma_scale_f32_16x16x128_f8f6f4 v[150:153], v[2:9], v[204:211], v[150:153], v194, v194 op_sel_hi:[0,0,0]
	v_mfma_scale_f32_16x16x128_f8f6f4 v[146:149], v[10:17], v[204:211], v[146:149], v194, v194 op_sel_hi:[0,0,0]
	v_mfma_scale_f32_16x16x128_f8f6f4 v[130:133], v[2:9], v[212:219], v[130:133], v194, v194 op_sel_hi:[0,0,0]
	v_mfma_scale_f32_16x16x128_f8f6f4 v[122:125], v[10:17], v[212:219], v[122:125], v194, v194 op_sel_hi:[0,0,0]
	v_mfma_scale_f32_16x16x128_f8f6f4 v[114:117], v[2:9], v[220:227], v[114:117], v194, v194 op_sel_hi:[0,0,0]
	v_mfma_scale_f32_16x16x128_f8f6f4 v[106:109], v[10:17], v[220:227], v[106:109], v194, v194 op_sel_hi:[0,0,0]
	s_nop 3
	v_mfma_scale_f32_16x16x128_f8f6f4 v[142:145], v[18:25], v[196:203], v[142:145], v194, v194 op_sel_hi:[0,0,0]
	v_mfma_scale_f32_16x16x128_f8f6f4 v[138:141], v[26:33], v[196:203], v[138:141], v194, v194 op_sel_hi:[0,0,0]
	v_mfma_scale_f32_16x16x128_f8f6f4 v[134:137], v[18:25], v[204:211], v[134:137], v194, v194 op_sel_hi:[0,0,0]
	v_mfma_scale_f32_16x16x128_f8f6f4 v[126:129], v[26:33], v[204:211], v[126:129], v194, v194 op_sel_hi:[0,0,0]
	v_mfma_scale_f32_16x16x128_f8f6f4 v[118:121], v[18:25], v[212:219], v[118:121], v194, v194 op_sel_hi:[0,0,0]
	v_mfma_scale_f32_16x16x128_f8f6f4 v[110:113], v[26:33], v[212:219], v[110:113], v194, v194 op_sel_hi:[0,0,0]
	v_mfma_scale_f32_16x16x128_f8f6f4 v[102:105], v[18:25], v[220:227], v[102:105], v194, v194 op_sel_hi:[0,0,0]
	v_mfma_scale_f32_16x16x128_f8f6f4 v[98:101], v[26:33], v[220:227], v[98:101], v194, v194 op_sel_hi:[0,0,0]
	s_add_u32 s40, s40, 0x8000
	s_addc_u32 s41, s41, 0
	s_add_i32 s42, s66, s48
	v_lshl_add_u64 v[228:229], s[40:41], 0, v[162:163]
	s_mov_b32 m0, s42
	ds_read_b128 v[196:199], v193 offset:49152
	ds_read_b128 v[200:203], v193 offset:50176
	ds_read_b128 v[204:207], v193 offset:51200
	ds_read_b128 v[208:211], v193 offset:52224
	ds_read_b128 v[212:215], v193 offset:53248
	ds_read_b128 v[216:219], v193 offset:54272
	ds_read_b128 v[220:223], v193 offset:55296
	ds_read_b128 v[224:227], v193 offset:56320
	global_load_lds_dwordx4 v[228:229], off
	v_lshl_add_u64 v[228:229], s[40:41], 0, v[164:165]
	s_add_i32 m0, s42, 0x2000
	s_add_i32 s42, s67, s48
	global_load_lds_dwordx4 v[228:229], off
	v_lshl_add_u64 v[228:229], s[40:41], 0, v[176:177]
	s_mov_b32 m0, s42
	s_nop 0
	global_load_lds_dwordx4 v[228:229], off
	v_lshl_add_u64 v[228:229], s[40:41], 0, v[178:179]
	s_add_i32 m0, s42, 0x2000
	s_nop 0
	global_load_lds_dwordx4 v[228:229], off
	v_lshl_add_u64 v[228:229], s[30:31], 0, v[166:167]
	s_mov_b32 m0, s53
	s_nop 0
	global_load_lds_dwordx4 v[228:229], off
	v_lshl_add_u64 v[228:229], s[30:31], 0, v[168:169]
	s_mov_b32 m0, s58
	s_nop 0
	global_load_lds_dwordx4 v[228:229], off
	s_waitcnt vmcnt(8)
	s_waitcnt lgkmcnt(0)
	s_barrier
	v_mfma_scale_f32_16x16x128_f8f6f4 v[94:97], v[2:9], v[196:203], v[94:97], v194, v194 op_sel_hi:[0,0,0]
	v_mfma_scale_f32_16x16x128_f8f6f4 v[90:93], v[10:17], v[196:203], v[90:93], v194, v194 op_sel_hi:[0,0,0]
	v_mfma_scale_f32_16x16x128_f8f6f4 v[82:85], v[2:9], v[204:211], v[82:85], v194, v194 op_sel_hi:[0,0,0]
	v_mfma_scale_f32_16x16x128_f8f6f4 v[74:77], v[10:17], v[204:211], v[74:77], v194, v194 op_sel_hi:[0,0,0]
	v_mfma_scale_f32_16x16x128_f8f6f4 v[66:69], v[2:9], v[212:219], v[66:69], v194, v194 op_sel_hi:[0,0,0]
	v_mfma_scale_f32_16x16x128_f8f6f4 v[58:61], v[10:17], v[212:219], v[58:61], v194, v194 op_sel_hi:[0,0,0]
	v_mfma_scale_f32_16x16x128_f8f6f4 v[50:53], v[2:9], v[220:227], v[50:53], v194, v194 op_sel_hi:[0,0,0]
	v_mfma_scale_f32_16x16x128_f8f6f4 v[42:45], v[10:17], v[220:227], v[42:45], v194, v194 op_sel_hi:[0,0,0]
	s_nop 3
	v_mfma_scale_f32_16x16x128_f8f6f4 v[86:89], v[18:25], v[196:203], v[86:89], v194, v194 op_sel_hi:[0,0,0]
	v_mfma_scale_f32_16x16x128_f8f6f4 v[78:81], v[26:33], v[196:203], v[78:81], v194, v194 op_sel_hi:[0,0,0]
	v_mfma_scale_f32_16x16x128_f8f6f4 v[70:73], v[18:25], v[204:211], v[70:73], v194, v194 op_sel_hi:[0,0,0]
	v_mfma_scale_f32_16x16x128_f8f6f4 v[62:65], v[26:33], v[204:211], v[62:65], v194, v194 op_sel_hi:[0,0,0]
	v_mfma_scale_f32_16x16x128_f8f6f4 v[54:57], v[18:25], v[212:219], v[54:57], v194, v194 op_sel_hi:[0,0,0]
	v_mfma_scale_f32_16x16x128_f8f6f4 v[46:49], v[26:33], v[212:219], v[46:49], v194, v194 op_sel_hi:[0,0,0]
	v_mfma_scale_f32_16x16x128_f8f6f4 v[38:41], v[18:25], v[220:227], v[38:41], v194, v194 op_sel_hi:[0,0,0]
	v_mfma_scale_f32_16x16x128_f8f6f4 v[34:37], v[26:33], v[220:227], v[34:37], v194, v194 op_sel_hi:[0,0,0]
	s_add_i32 s65, s65, 2
	s_add_u32 s19, s19, 0x10000
	s_addc_u32 s21, s21, 0
	s_add_u32 s28, s28, 0x10000
	s_addc_u32 s29, s29, 0
	s_cmp_gt_u32 s65, 13
	s_cbranch_scc0 .Lh1_911
	s_branch .Lfx_26630
; #define PG8_STAGE(bufoff, gbase, voff) do { _Pragma("unroll") for (int _i = 0; _i < 2; ++_i) \
;         __builtin_amdgcn_global_load_lds((const unsigned*)((const char*)(gbase) + (voff)[_i]), (PG8_LAS unsigned*)(lds + (bufoff) + ldsw + _i * 8192), 16, 0, 0); } while (0)
; #define PG8_WAIT_V(n) asm volatile("s_waitcnt vmcnt(" #n ")" ::: "memory")
; #define PG8_WAIT_L(n) asm volatile("s_waitcnt lgkmcnt(" #n ")" ::: "memory")
; #define PG8_BAR __builtin_amdgcn_s_barrier()
; #define PG8_SCHED __builtin_amdgcn_sched_barrier(0)
; template <class Epi, class Sched, bool ALIGN_EPI = true, bool F8 = false>
; __device__ __forceinline__ void gemm_phase(PG8_LAS unsigned char* lds, const Sched& S, const Epi& E) {
;     ...
;             PG8_LDB(B0, 0, 0); PG8_LDB(B1, 0, 1); PG8_SCHED; PG8_LDA(At, 0, 0); PG8_STAGE(PG8_SA(1, 1), a1, voffA[1]);
;             PG8_WAIT_V(8); PG8_WAIT_L(0); PG8_BAR; PG8_MMA(0, 0, At, B0); PG8_MMA(0, 1, At, B1); PG8_BAR; PG8_SCHED;
;             PG8_LDA(At, 0, 1); PG8_STAGE(PG8_SB(0, 0), b2, voffB[0]); PG8_STAGE(PG8_SB(0, 1), b2, voffB[1]); PG8_STAGE(PG8_SA(0, 0), a2, vA2[0]);
;             PG8_WAIT_V(8); PG8_WAIT_L(0); PG8_BAR; PG8_MMA(1, 0, At, B0); PG8_MMA(1, 1, At, B1); PG8_BAR; PG8_SCHED;
;             PG8_LDB(B0, 1, 0); PG8_LDB(B1, 1, 1); PG8_SCHED; PG8_LDA(At, 1, 0); PG8_STAGE(PG8_SA(0, 1), a2, vA2[1]);
;             PG8_WAIT_V(8); PG8_WAIT_L(0); PG8_BAR; PG8_MMA(0, 0, At, B0); PG8_MMA(0, 1, At, B1); PG8_BAR; PG8_SCHED;
;             PG8_LDA(At, 1, 1); PG8_STAGE(PG8_SB(1, 0), b3, voffB[0]); PG8_STAGE(PG8_SB(1, 1), b3, voffB[1]); PG8_STAGE(PG8_SA(1, 0), a3, vA2[0]);
;             PG8_WAIT_V(8); PG8_WAIT_L(0); PG8_BAR; PG8_MMA(1, 0, At, B0); PG8_MMA(1, 1, At, B1); PG8_BAR; PG8_SCHED;
.Lh1_911:
	ds_read_b128 v[18:21], v191
	ds_read_b128 v[22:25], v191 offset:1024
	ds_read_b128 v[26:29], v191 offset:2048
	ds_read_b128 v[30:33], v191 offset:3072
	ds_read_b128 v[2:5], v192
	ds_read_b128 v[6:9], v192 offset:1024
	ds_read_b128 v[10:13], v192 offset:2048
	ds_read_b128 v[14:17], v192 offset:3072
	s_add_u32 s30, s28, 0x8000
	s_addc_u32 s31, s29, 0
	s_cmp_eq_u32 s65, 12
	s_cselect_b32 s42, s22, s30
	s_cselect_b32 s43, s23, s31
	s_cselect_b32 s40, s24, s19
	s_cselect_b32 s41, s25, s21
	s_add_u32 s30, s42, 0x8000
	s_addc_u32 s31, s43, 0
	v_lshl_add_u64 v[228:229], s[28:29], 0, v[182:183]
	s_add_i32 m0, s27, 0xc000
	ds_read_b128 v[196:199], v193
	ds_read_b128 v[200:203], v193 offset:1024
	ds_read_b128 v[204:207], v193 offset:2048
	ds_read_b128 v[208:211], v193 offset:3072
	ds_read_b128 v[212:215], v193 offset:4096
	ds_read_b128 v[216:219], v193 offset:5120
	ds_read_b128 v[220:223], v193 offset:6144
	ds_read_b128 v[224:227], v193 offset:7168
	global_load_lds_dwordx4 v[228:229], off
	v_lshl_add_u64 v[228:229], s[28:29], 0, v[180:181]
	s_add_i32 m0, s27, 0xe000
	s_nop 0
	global_load_lds_dwordx4 v[228:229], off
	s_waitcnt vmcnt(8)
	s_waitcnt lgkmcnt(0)
	s_barrier
	v_mfma_scale_f32_16x16x128_f8f6f4 v[158:161], v[18:25], v[196:203], v[158:161], v194, v194 op_sel_hi:[0,0,0]
	v_mfma_scale_f32_16x16x128_f8f6f4 v[154:157], v[26:33], v[196:203], v[154:157], v194, v194 op_sel_hi:[0,0,0]
	v_mfma_scale_f32_16x16x128_f8f6f4 v[150:153], v[18:25], v[204:211], v[150:153], v194, v194 op_sel_hi:[0,0,0]
	v_mfma_scale_f32_16x16x128_f8f6f4 v[146:149], v[26:33], v[204:211], v[146:149], v194, v194 op_sel_hi:[0,0,0]
	v_mfma_scale_f32_16x16x128_f8f6f4 v[130:133], v[18:25], v[212:219], v[130:133], v194, v194 op_sel_hi:[0,0,0]
	v_mfma_scale_f32_16x16x128_f8f6f4 v[122:125], v[26:33], v[212:219], v[122:125], v194, v194 op_sel_hi:[0,0,0]
	v_mfma_scale_f32_16x16x128_f8f6f4 v[114:117], v[18:25], v[220:227], v[114:117], v194, v194 op_sel_hi:[0,0,0]
	v_mfma_scale_f32_16x16x128_f8f6f4 v[106:109], v[26:33], v[220:227], v[106:109], v194, v194 op_sel_hi:[0,0,0]
	s_nop 3
	v_mfma_scale_f32_16x16x128_f8f6f4 v[142:145], v[2:9], v[196:203], v[142:145], v194, v194 op_sel_hi:[0,0,0]
	v_mfma_scale_f32_16x16x128_f8f6f4 v[138:141], v[10:17], v[196:203], v[138:141], v194, v194 op_sel_hi:[0,0,0]
	v_mfma_scale_f32_16x16x128_f8f6f4 v[134:137], v[2:9], v[204:211], v[134:137], v194, v194 op_sel_hi:[0,0,0]
	v_mfma_scale_f32_16x16x128_f8f6f4 v[126:129], v[10:17], v[204:211], v[126:129], v194, v194 op_sel_hi:[0,0,0]
	v_mfma_scale_f32_16x16x128_f8f6f4 v[118:121], v[2:9], v[212:219], v[118:121], v194, v194 op_sel_hi:[0,0,0]
	v_mfma_scale_f32_16x16x128_f8f6f4 v[110:113], v[10:17], v[212:219], v[110:113], v194, v194 op_sel_hi:[0,0,0]
	v_mfma_scale_f32_16x16x128_f8f6f4 v[102:105], v[2:9], v[220:227], v[102:105], v194, v194 op_sel_hi:[0,0,0]
	v_mfma_scale_f32_16x16x128_f8f6f4 v[98:101], v[10:17], v[220:227], v[98:101], v194, v194 op_sel_hi:[0,0,0]
	s_add_i32 s66, s60, s48
	v_lshl_add_u64 v[228:229], s[40:41], 0, v[162:163]
	s_mov_b32 m0, s66
	ds_read_b128 v[196:199], v193 offset:16384
	ds_read_b128 v[200:203], v193 offset:17408
	ds_read_b128 v[204:207], v193 offset:18432
	ds_read_b128 v[208:211], v193 offset:19456
	ds_read_b128 v[212:215], v193 offset:20480
	ds_read_b128 v[216:219], v193 offset:21504
	ds_read_b128 v[220:223], v193 offset:22528
	ds_read_b128 v[224:227], v193 offset:23552
	global_load_lds_dwordx4 v[228:229], off
	v_lshl_add_u64 v[230:231], s[40:41], 0, v[164:165]
	s_add_i32 m0, s66, 0x2000
	s_add_i32 s66, s61, s48
	global_load_lds_dwordx4 v[230:231], off
	v_lshl_add_u64 v[228:229], v[228:229], 0, s[6:7]
	s_mov_b32 m0, s66
	s_nop 0
	global_load_lds_dwordx4 v[228:229], off
	v_lshl_add_u64 v[228:229], v[230:231], 0, s[6:7]
	s_add_i32 m0, s66, 0x2000
	s_nop 0
	global_load_lds_dwordx4 v[228:229], off
	v_lshl_add_u64 v[228:229], s[42:43], 0, v[166:167]
	s_mov_b32 m0, s27
	s_nop 0
	global_load_lds_dwordx4 v[228:229], off
	v_lshl_add_u64 v[228:229], s[42:43], 0, v[168:169]
	s_mov_b32 m0, s49
	s_nop 0
	global_load_lds_dwordx4 v[228:229], off
	s_waitcnt vmcnt(8)
	s_waitcnt lgkmcnt(0)
	s_barrier
	v_mfma_scale_f32_16x16x128_f8f6f4 v[94:97], v[18:25], v[196:203], v[94:97], v194, v194 op_sel_hi:[0,0,0]
	v_mfma_scale_f32_16x16x128_f8f6f4 v[90:93], v[26:33], v[196:203], v[90:93], v194, v194 op_sel_hi:[0,0,0]
	v_mfma_scale_f32_16x16x128_f8f6f4 v[82:85], v[18:25], v[204:211], v[82:85], v194, v194 op_sel_hi:[0,0,0]
	v_mfma_scale_f32_16x16x128_f8f6f4 v[74:77], v[26:33], v[204:211], v[74:77], v194, v194 op_sel_hi:[0,0,0]
	v_mfma_scale_f32_16x16x128_f8f6f4 v[66:69], v[18:25], v[212:219], v[66:69], v194, v194 op_sel_hi:[0,0,0]
	v_mfma_scale_f32_16x16x128_f8f6f4 v[58:61], v[26:33], v[212:219], v[58:61], v194, v194 op_sel_hi:[0,0,0]
	v_mfma_scale_f32_16x16x128_f8f6f4 v[50:53], v[18:25], v[220:227], v[50:53], v194, v194 op_sel_hi:[0,0,0]
	v_mfma_scale_f32_16x16x128_f8f6f4 v[42:45], v[26:33], v[220:227], v[42:45], v194, v194 op_sel_hi:[0,0,0]
	s_nop 3
	v_mfma_scale_f32_16x16x128_f8f6f4 v[86:89], v[2:9], v[196:203], v[86:89], v194, v194 op_sel_hi:[0,0,0]
	v_mfma_scale_f32_16x16x128_f8f6f4 v[78:81], v[10:17], v[196:203], v[78:81], v194, v194 op_sel_hi:[0,0,0]
	v_mfma_scale_f32_16x16x128_f8f6f4 v[70:73], v[2:9], v[204:211], v[70:73], v194, v194 op_sel_hi:[0,0,0]
	v_mfma_scale_f32_16x16x128_f8f6f4 v[62:65], v[10:17], v[204:211], v[62:65], v194, v194 op_sel_hi:[0,0,0]
	v_mfma_scale_f32_16x16x128_f8f6f4 v[54:57], v[2:9], v[212:219], v[54:57], v194, v194 op_sel_hi:[0,0,0]
	v_mfma_scale_f32_16x16x128_f8f6f4 v[46:49], v[10:17], v[212:219], v[46:49], v194, v194 op_sel_hi:[0,0,0]
	v_mfma_scale_f32_16x16x128_f8f6f4 v[38:41], v[2:9], v[220:227], v[38:41], v194, v194 op_sel_hi:[0,0,0]
	v_mfma_scale_f32_16x16x128_f8f6f4 v[34:37], v[10:17], v[220:227], v[34:37], v194, v194 op_sel_hi:[0,0,0]
	s_add_i32 s66, 0, 0x18000
	s_add_i32 s67, 0, 0x1c000
	v_add_u32_e32 v14, s66, v189
	v_add_u32_e32 v30, s67, v189
	ds_read_b128 v[2:5], v14
	ds_read_b128 v[6:9], v14 offset:1024
	ds_read_b128 v[10:13], v14 offset:2048
	ds_read_b128 v[14:17], v14 offset:3072
	ds_read_b128 v[18:21], v30
	ds_read_b128 v[22:25], v30 offset:1024
	ds_read_b128 v[26:29], v30 offset:2048
	ds_read_b128 v[30:33], v30 offset:3072
	s_mov_b32 m0, s50
	v_lshl_add_u64 v[228:229], s[42:43], 0, v[172:173]
	ds_read_b128 v[196:199], v193 offset:32768
	ds_read_b128 v[200:203], v193 offset:33792
	ds_read_b128 v[204:207], v193 offset:34816
	ds_read_b128 v[208:211], v193 offset:35840
	ds_read_b128 v[212:215], v193 offset:36864
	ds_read_b128 v[216:219], v193 offset:37888
	ds_read_b128 v[220:223], v193 offset:38912
	ds_read_b128 v[224:227], v193 offset:39936
	global_load_lds_dwordx4 v[228:229], off
	v_lshl_add_u64 v[228:229], s[42:43], 0, v[174:175]
	s_mov_b32 m0, s51
	s_nop 0
	global_load_lds_dwordx4 v[228:229], off
	s_waitcnt vmcnt(8)
	s_waitcnt lgkmcnt(0)
	s_barrier
; #define PG8_STAGE(bufoff, gbase, voff) do { _Pragma("unroll") for (int _i = 0; _i < 2; ++_i) \
;         __builtin_amdgcn_global_load_lds((const unsigned*)((const char*)(gbase) + (voff)[_i]), (PG8_LAS unsigned*)(lds + (bufoff) + ldsw + _i * 8192), 16, 0, 0); } while (0)
; #define PG8_WAIT_V(n) asm volatile("s_waitcnt vmcnt(" #n ")" ::: "memory")
; #define PG8_WAIT_L(n) asm volatile("s_waitcnt lgkmcnt(" #n ")" ::: "memory")
; #define PG8_BAR __builtin_amdgcn_s_barrier()
; #define PG8_SCHED __builtin_amdgcn_sched_barrier(0)
; template <class Epi, class Sched, bool ALIGN_EPI = true, bool F8 = false>
; __device__ __forceinline__ void gemm_phase(PG8_LAS unsigned char* lds, const Sched& S, const Epi& E) {
;     ...
;             PG8_LDB(B0, 0, 0); PG8_LDB(B1, 0, 1); PG8_SCHED; PG8_LDA(At, 0, 0); PG8_STAGE(PG8_SA(1, 1), a1, voffA[1]);
;             PG8_WAIT_V(8); PG8_WAIT_L(0); PG8_BAR; PG8_MMA(0, 0, At, B0); PG8_MMA(0, 1, At, B1); PG8_BAR; PG8_SCHED;
;             PG8_LDA(At, 0, 1); PG8_STAGE(PG8_SB(0, 0), b2, voffB[0]); PG8_STAGE(PG8_SB(0, 1), b2, voffB[1]); PG8_STAGE(PG8_SA(0, 0), a2, vA2[0]);
;             PG8_WAIT_V(8); PG8_WAIT_L(0); PG8_BAR; PG8_MMA(1, 0, At, B0); PG8_MMA(1, 1, At, B1); PG8_BAR; PG8_SCHED;
;             PG8_LDB(B0, 1, 0); PG8_LDB(B1, 1, 1); PG8_SCHED; PG8_LDA(At, 1, 0); PG8_STAGE(PG8_SA(0, 1), a2, vA2[1]);
;             PG8_WAIT_V(8); PG8_WAIT_L(0); PG8_BAR; PG8_MMA(0, 0, At, B0); PG8_MMA(0, 1, At, B1); PG8_BAR; PG8_SCHED;
;             PG8_LDA(At, 1, 1); PG8_STAGE(PG8_SB(1, 0), b3, voffB[0]); PG8_STAGE(PG8_SB(1, 1), b3, voffB[1]); PG8_STAGE(PG8_SA(1, 0), a3, vA2[0]);
;             PG8_WAIT_V(8); PG8_WAIT_L(0); PG8_BAR; PG8_MMA(1, 0, At, B0); PG8_MMA(1, 1, At, B1); PG8_BAR; PG8_SCHED;
	v_mfma_scale_f32_16x16x128_f8f6f4 v[158:161], v[2:9], v[196:203], v[158:161], v194, v194 op_sel_hi:[0,0,0]
	v_mfma_scale_f32_16x16x128_f8f6f4 v[154:157], v[10:17], v[196:203], v[154:157], v194, v194 op_sel_hi:[0,0,0]
	v_mfma_scale_f32_16x16x128_f8f6f4 v[150:153], v[2:9], v[204:211], v[150:153], v194, v194 op_sel_hi:[0,0,0]
	v_mfma_scale_f32_16x16x128_f8f6f4 v[146:149], v[10:17], v[204:211], v[146:149], v194, v194 op_sel_hi:[0,0,0]
	v_mfma_scale_f32_16x16x128_f8f6f4 v[130:133], v[2:9], v[212:219], v[130:133], v194, v194 op_sel_hi:[0,0,0]
	v_mfma_scale_f32_16x16x128_f8f6f4 v[122:125], v[10:17], v[212:219], v[122:125], v194, v194 op_sel_hi:[0,0,0]
	v_mfma_scale_f32_16x16x128_f8f6f4 v[114:117], v[2:9], v[220:227], v[114:117], v194, v194 op_sel_hi:[0,0,0]
	v_mfma_scale_f32_16x16x128_f8f6f4 v[106:109], v[10:17], v[220:227], v[106:109], v194, v194 op_sel_hi:[0,0,0]
	s_nop 3
	v_mfma_scale_f32_16x16x128_f8f6f4 v[142:145], v[18:25], v[196:203], v[142:145], v194, v194 op_sel_hi:[0,0,0]
	v_mfma_scale_f32_16x16x128_f8f6f4 v[138:141], v[26:33], v[196:203], v[138:141], v194, v194 op_sel_hi:[0,0,0]
	v_mfma_scale_f32_16x16x128_f8f6f4 v[134:137], v[18:25], v[204:211], v[134:137], v194, v194 op_sel_hi:[0,0,0]
	v_mfma_scale_f32_16x16x128_f8f6f4 v[126:129], v[26:33], v[204:211], v[126:129], v194, v194 op_sel_hi:[0,0,0]
	v_mfma_scale_f32_16x16x128_f8f6f4 v[118:121], v[18:25], v[212:219], v[118:121], v194, v194 op_sel_hi:[0,0,0]
	v_mfma_scale_f32_16x16x128_f8f6f4 v[110:113], v[26:33], v[212:219], v[110:113], v194, v194 op_sel_hi:[0,0,0]
	v_mfma_scale_f32_16x16x128_f8f6f4 v[102:105], v[18:25], v[220:227], v[102:105], v194, v194 op_sel_hi:[0,0,0]
	v_mfma_scale_f32_16x16x128_f8f6f4 v[98:101], v[26:33], v[220:227], v[98:101], v194, v194 op_sel_hi:[0,0,0]
	s_add_u32 s40, s40, 0x8000
	s_addc_u32 s41, s41, 0
	s_add_i32 s42, s66, s48
	v_lshl_add_u64 v[228:229], s[40:41], 0, v[162:163]
	s_mov_b32 m0, s42
	ds_read_b128 v[196:199], v193 offset:49152
	ds_read_b128 v[200:203], v193 offset:50176
	ds_read_b128 v[204:207], v193 offset:51200
	ds_read_b128 v[208:211], v193 offset:52224
	ds_read_b128 v[212:215], v193 offset:53248
	ds_read_b128 v[216:219], v193 offset:54272
	ds_read_b128 v[220:223], v193 offset:55296
	ds_read_b128 v[224:227], v193 offset:56320
	global_load_lds_dwordx4 v[228:229], off
	v_lshl_add_u64 v[228:229], s[40:41], 0, v[164:165]
	s_add_i32 m0, s42, 0x2000
	s_add_i32 s42, s67, s48
	global_load_lds_dwordx4 v[228:229], off
	v_lshl_add_u64 v[228:229], s[40:41], 0, v[176:177]
	s_mov_b32 m0, s42
	s_nop 0
	global_load_lds_dwordx4 v[228:229], off
	v_lshl_add_u64 v[228:229], s[40:41], 0, v[178:179]
	s_add_i32 m0, s42, 0x2000
	s_nop 0
	global_load_lds_dwordx4 v[228:229], off
	v_lshl_add_u64 v[228:229], s[30:31], 0, v[166:167]
	s_mov_b32 m0, s53
	s_nop 0
	global_load_lds_dwordx4 v[228:229], off
	v_lshl_add_u64 v[228:229], s[30:31], 0, v[168:169]
	s_mov_b32 m0, s58
	s_nop 0
	global_load_lds_dwordx4 v[228:229], off
	s_waitcnt vmcnt(8)
	s_waitcnt lgkmcnt(0)
	s_barrier
	v_mfma_scale_f32_16x16x128_f8f6f4 v[94:97], v[2:9], v[196:203], v[94:97], v194, v194 op_sel_hi:[0,0,0]
	v_mfma_scale_f32_16x16x128_f8f6f4 v[90:93], v[10:17], v[196:203], v[90:93], v194, v194 op_sel_hi:[0,0,0]
	v_mfma_scale_f32_16x16x128_f8f6f4 v[82:85], v[2:9], v[204:211], v[82:85], v194, v194 op_sel_hi:[0,0,0]
	v_mfma_scale_f32_16x16x128_f8f6f4 v[74:77], v[10:17], v[204:211], v[74:77], v194, v194 op_sel_hi:[0,0,0]
	v_mfma_scale_f32_16x16x128_f8f6f4 v[66:69], v[2:9], v[212:219], v[66:69], v194, v194 op_sel_hi:[0,0,0]
	v_mfma_scale_f32_16x16x128_f8f6f4 v[58:61], v[10:17], v[212:219], v[58:61], v194, v194 op_sel_hi:[0,0,0]
	v_mfma_scale_f32_16x16x128_f8f6f4 v[50:53], v[2:9], v[220:227], v[50:53], v194, v194 op_sel_hi:[0,0,0]
	v_mfma_scale_f32_16x16x128_f8f6f4 v[42:45], v[10:17], v[220:227], v[42:45], v194, v194 op_sel_hi:[0,0,0]
	s_nop 3
	v_mfma_scale_f32_16x16x128_f8f6f4 v[86:89], v[18:25], v[196:203], v[86:89], v194, v194 op_sel_hi:[0,0,0]
	v_mfma_scale_f32_16x16x128_f8f6f4 v[78:81], v[26:33], v[196:203], v[78:81], v194, v194 op_sel_hi:[0,0,0]
	v_mfma_scale_f32_16x16x128_f8f6f4 v[70:73], v[18:25], v[204:211], v[70:73], v194, v194 op_sel_hi:[0,0,0]
	v_mfma_scale_f32_16x16x128_f8f6f4 v[62:65], v[26:33], v[204:211], v[62:65], v194, v194 op_sel_hi:[0,0,0]
	v_mfma_scale_f32_16x16x128_f8f6f4 v[54:57], v[18:25], v[212:219], v[54:57], v194, v194 op_sel_hi:[0,0,0]
	v_mfma_scale_f32_16x16x128_f8f6f4 v[46:49], v[26:33], v[212:219], v[46:49], v194, v194 op_sel_hi:[0,0,0]
	v_mfma_scale_f32_16x16x128_f8f6f4 v[38:41], v[18:25], v[220:227], v[38:41], v194, v194 op_sel_hi:[0,0,0]
	v_mfma_scale_f32_16x16x128_f8f6f4 v[34:37], v[26:33], v[220:227], v[34:37], v194, v194 op_sel_hi:[0,0,0]
	s_add_i32 s65, s65, 2
	s_add_u32 s19, s19, 0x10000
	s_addc_u32 s21, s21, 0
	s_add_u32 s28, s28, 0x10000
	s_addc_u32 s29, s29, 0
	s_cmp_gt_u32 s65, 13
	s_cbranch_scc0 .Lh1_911

; template <class Epi, class Sched, bool ALIGN_EPI = true, bool F8 = false>
; __device__ __forceinline__ void gemm_phase(PG8_LAS unsigned char* lds, const Sched& S, const Epi& E) {
;     ...
;         const bool has_next = S.next(ui + 1, nxt);
;         const char* nA = has_next ? nxt.A : cA; const char* nB = has_next ? nxt.B : cB;
;         const int nt = cur.nt;
; #pragma unroll 1
;         for (int t = 0; t < nt; t += 2) {
;             const bool last = (t == nt - 2);
;             if constexpr (Sched::GATHER) { if (last && has_next) S.a_off(nxt, Rs, Cs, voffAn); }
;             const char* a1 = cA + (size_t)(t + 1) * kstep;
;             const char* a2 = last ? nA : cA + (size_t)(t + 2) * kstep; const char* b2 = last ? nB : cB + (size_t)(t + 2) * kstepB;
;             const char* a3 = a2 + kstep; const char* b3 = b2 + kstepB;
;             unsigned vA2[2][2];
; #pragma unroll
;             for (int h = 0; h < 2; ++h)
; #pragma unroll
;                 for (int i = 0; i < 2; ++i) { if constexpr (Sched::GATHER) vA2[h][i] = (last && has_next) ? voffAn[h][i] : voffA[h][i]; else vA2[h][i] = voffA[h][i]; }
;     __device__ __forceinline__ void a_off(const GUnit& u, const int (&R)[2], const int (&C)[2], unsigned (&v)[2][2]) const {
;         const int* rl = rowlist + (size_t)u.x0 * ECAP; const int base = u.x1 * 256, cm = u.x3 - 1;
; #pragma unroll
;         for (int h = 0; h < 2; ++h)
; #pragma unroll
;             for (int i = 0; i < 2; ++i) { int p = base + h * 128 + R[i]; p = p < cm ? p : cm; const unsigned ent = (unsigned)rl[p]; v[h][i] = (ent >> SHIFT) * (unsigned)PA + (unsigned)C[i] * 2u; } }
.LBB0_1057:
	s_ashr_i32 s21, s20, 31
	s_lshl_b64 s[28:29], s[20:21], 17
	s_lshl_b32 s21, s66, 8
	s_add_i32 s30, s65, -1
	s_or_b32 s31, s21, 0x80
	v_or_b32_e32 v2, s21, v206
	v_or_b32_e32 v4, s21, v207
	v_or_b32_e32 v6, s31, v206
	v_or_b32_e32 v8, s31, v207
	s_add_u32 s28, s46, s28
	v_min_i32_e32 v2, s30, v2
	v_min_i32_e32 v4, s30, v4
	v_min_i32_e32 v6, s30, v6
	v_min_i32_e32 v8, s30, v8
	s_addc_u32 s29, s47, s29
	v_ashrrev_i32_e32 v3, 31, v2
	v_ashrrev_i32_e32 v5, 31, v4
	v_ashrrev_i32_e32 v7, 31, v6
	v_ashrrev_i32_e32 v9, 31, v8
	v_mov_b32_e32 v177, v171
	v_mov_b32_e32 v175, v171
	s_add_u32 s21, s8, 0x10000
	v_lshl_add_u64 v[186:187], v[2:3], 2, s[28:29]
	v_lshl_add_u64 v[188:189], v[4:5], 2, s[28:29]
	v_lshl_add_u64 v[190:191], v[6:7], 2, s[28:29]
	v_lshl_add_u64 v[192:193], v[8:9], 2, s[28:29]
	s_addc_u32 s68, s9, 0
	v_lshl_add_u64 v[194:195], s[14:15], 0, v[174:175]
	v_lshl_add_u64 v[196:197], s[14:15], 0, v[176:177]
	s_mov_b32 s69, -2
	s_mov_b64 s[30:31], 0
	s_bitcmp1_b32 s3, 2
	s_cbranch_scc1 .Lh1e_31412
	s_setprio 1

; #define PG8_STAGE(bufoff, gbase, voff) do { _Pragma("unroll") for (int _i = 0; _i < 2; ++_i) \
;         __builtin_amdgcn_global_load_lds((const unsigned*)((const char*)(gbase) + (voff)[_i]), (PG8_LAS unsigned*)(lds + (bufoff) + ldsw + _i * 8192), 16, 0, 0); } while (0)
; #define PG8_WAIT_V(n) asm volatile("s_waitcnt vmcnt(" #n ")" ::: "memory")
; #define PG8_WAIT_L(n) asm volatile("s_waitcnt lgkmcnt(" #n ")" ::: "memory")
; #define PG8_BAR __builtin_amdgcn_s_barrier()
; #define PG8_SCHED __builtin_amdgcn_sched_barrier(0)
; template <class Epi, class Sched, bool ALIGN_EPI = true, bool F8 = false>
; __device__ __forceinline__ void gemm_phase(PG8_LAS unsigned char* lds, const Sched& S, const Epi& E) {
;     ...
;             PG8_LDB(B0, 0, 0); PG8_LDB(B1, 0, 1); PG8_SCHED; PG8_LDA(At, 0, 0); PG8_STAGE(PG8_SA(1, 1), a1, voffA[1]);
;             PG8_WAIT_V(8); PG8_WAIT_L(0); PG8_BAR; PG8_MMA(0, 0, At, B0); PG8_MMA(0, 1, At, B1); PG8_BAR; PG8_SCHED;
;             PG8_LDA(At, 0, 1); PG8_STAGE(PG8_SB(0, 0), b2, voffB[0]); PG8_STAGE(PG8_SB(0, 1), b2, voffB[1]); PG8_STAGE(PG8_SA(0, 0), a2, vA2[0]);
;             PG8_WAIT_V(8); PG8_WAIT_L(0); PG8_BAR; PG8_MMA(1, 0, At, B0); PG8_MMA(1, 1, At, B1); PG8_BAR; PG8_SCHED;
;             PG8_LDB(B0, 1, 0); PG8_LDB(B1, 1, 1); PG8_SCHED; PG8_LDA(At, 1, 0); PG8_STAGE(PG8_SA(0, 1), a2, vA2[1]);
;             PG8_WAIT_V(8); PG8_WAIT_L(0); PG8_BAR; PG8_MMA(0, 0, At, B0); PG8_MMA(0, 1, At, B1); PG8_BAR; PG8_SCHED;
;             PG8_LDA(At, 1, 1); PG8_STAGE(PG8_SB(1, 0), b3, voffB[0]); PG8_STAGE(PG8_SB(1, 1), b3, voffB[1]); PG8_STAGE(PG8_SA(1, 0), a3, vA2[0]);
;             PG8_WAIT_V(8); PG8_WAIT_L(0); PG8_BAR; PG8_MMA(1, 0, At, B0); PG8_MMA(1, 1, At, B1); PG8_BAR; PG8_SCHED;
.Lpk0_1060:
	v_add_u32_e32 v2, s12, v210
	v_add_u32_e32 v14, s62, v210
	s_add_u32 s28, s30, 0x100
	ds_read_b128 v[18:21], v2
	ds_read_b128 v[22:25], v2 offset:1024
	ds_read_b128 v[26:29], v2 offset:2048
	ds_read_b128 v[30:33], v2 offset:3072
	ds_read_b128 v[2:5], v14
	ds_read_b128 v[6:9], v14 offset:1024
	ds_read_b128 v[10:13], v14 offset:2048
	ds_read_b128 v[14:17], v14 offset:3072
	s_addc_u32 s29, s31, 0
	s_and_b64 s[42:43], s[40:41], exec
	s_cselect_b32 s42, 0, s28
	s_cselect_b32 s43, 0, s29
	s_add_u32 s42, s6, s42
	s_addc_u32 s43, s7, s43
	s_and_b64 s[40:41], s[40:41], exec
	s_cselect_b32 s41, s25, s68
	s_cselect_b32 s40, s24, s21
	v_lshl_add_u64 v[204:205], v[196:197], 0, s[30:31]
	s_add_i32 m0, s52, 0xc000
	ds_read_b128 v[222:225], v213
	ds_read_b128 v[226:229], v213 offset:1024
	ds_read_b128 v[230:233], v213 offset:2048
	ds_read_b128 v[234:237], v213 offset:3072
	ds_read_b128 v[238:241], v213 offset:4096
	ds_read_b128 v[242:245], v213 offset:5120
	ds_read_b128 v[246:249], v213 offset:6144
	ds_read_b128 v[250:253], v213 offset:7168
	global_load_lds_dwordx4 v[204:205], off
	v_lshl_add_u64 v[204:205], v[194:195], 0, s[30:31]
	s_add_i32 m0, s52, 0xe000
	s_nop 0
	global_load_lds_dwordx4 v[204:205], off
	s_waitcnt vmcnt(8)
	s_waitcnt lgkmcnt(0)
	v_mfma_scale_f32_16x16x128_f8f6f4 v[142:145], v[18:25], v[222:229], 0, v214, v214 op_sel_hi:[0,0,0]
	v_mfma_scale_f32_16x16x128_f8f6f4 v[138:141], v[26:33], v[222:229], 0, v214, v214 op_sel_hi:[0,0,0]
	v_mfma_scale_f32_16x16x128_f8f6f4 v[134:137], v[18:25], v[230:237], 0, v214, v214 op_sel_hi:[0,0,0]
	v_mfma_scale_f32_16x16x128_f8f6f4 v[130:133], v[26:33], v[230:237], 0, v214, v214 op_sel_hi:[0,0,0]
	v_mfma_scale_f32_16x16x128_f8f6f4 v[126:129], v[18:25], v[238:245], 0, v214, v214 op_sel_hi:[0,0,0]
	v_mfma_scale_f32_16x16x128_f8f6f4 v[122:125], v[26:33], v[238:245], 0, v214, v214 op_sel_hi:[0,0,0]
	v_mfma_scale_f32_16x16x128_f8f6f4 v[118:121], v[18:25], v[246:253], 0, v214, v214 op_sel_hi:[0,0,0]
	v_mfma_scale_f32_16x16x128_f8f6f4 v[114:117], v[26:33], v[246:253], 0, v214, v214 op_sel_hi:[0,0,0]
	s_nop 3
	v_mfma_scale_f32_16x16x128_f8f6f4 v[110:113], v[2:9], v[222:229], 0, v214, v214 op_sel_hi:[0,0,0]
	v_mfma_scale_f32_16x16x128_f8f6f4 v[106:109], v[10:17], v[222:229], 0, v214, v214 op_sel_hi:[0,0,0]
	v_mfma_scale_f32_16x16x128_f8f6f4 v[102:105], v[2:9], v[230:237], 0, v214, v214 op_sel_hi:[0,0,0]
	v_mfma_scale_f32_16x16x128_f8f6f4 v[98:101], v[10:17], v[230:237], 0, v214, v214 op_sel_hi:[0,0,0]
	v_mfma_scale_f32_16x16x128_f8f6f4 v[94:97], v[2:9], v[238:245], 0, v214, v214 op_sel_hi:[0,0,0]
	v_mfma_scale_f32_16x16x128_f8f6f4 v[90:93], v[10:17], v[238:245], 0, v214, v214 op_sel_hi:[0,0,0]
	v_mfma_scale_f32_16x16x128_f8f6f4 v[86:89], v[2:9], v[246:253], 0, v214, v214 op_sel_hi:[0,0,0]
	v_mfma_scale_f32_16x16x128_f8f6f4 v[82:85], v[10:17], v[246:253], 0, v214, v214 op_sel_hi:[0,0,0]
	s_barrier
	s_add_i32 s30, s12, s48
	v_lshl_add_u64 v[204:205], s[40:41], 0, v[162:163]
	s_mov_b32 m0, s30
	ds_read_b128 v[222:225], v213 offset:16384
	ds_read_b128 v[226:229], v213 offset:17408
	ds_read_b128 v[230:233], v213 offset:18432
	ds_read_b128 v[234:237], v213 offset:19456
	ds_read_b128 v[238:241], v213 offset:20480
	ds_read_b128 v[242:245], v213 offset:21504
	ds_read_b128 v[246:249], v213 offset:22528
	ds_read_b128 v[250:253], v213 offset:23552
	global_load_lds_dwordx4 v[204:205], off
	v_lshl_add_u64 v[204:205], s[40:41], 0, v[164:165]
	s_add_i32 m0, s30, 0x2000
	s_add_i32 s30, s62, s48
	global_load_lds_dwordx4 v[204:205], off
	v_lshl_add_u64 v[204:205], s[40:41], 0, v[166:167]
	s_mov_b32 m0, s30
	v_mov_b32_e32 v203, v171
	global_load_lds_dwordx4 v[204:205], off
	v_lshl_add_u64 v[204:205], s[40:41], 0, v[168:169]
	s_add_i32 m0, s30, 0x2000
	s_nop 0
	global_load_lds_dwordx4 v[204:205], off
	s_mov_b32 m0, s52
	v_lshl_add_u64 v[204:205], s[42:43], 0, v[170:171]
	global_load_lds_dwordx4 v170, s[42:43]
	s_mov_b32 m0, s53
	s_nop 0
	global_load_lds_dwordx4 v202, s[42:43]
	s_waitcnt vmcnt(8)
	s_waitcnt lgkmcnt(0)
	v_lshl_add_u64 v[202:203], s[42:43], 0, v[202:203]
	v_mfma_scale_f32_16x16x128_f8f6f4 v[78:81], v[18:25], v[222:229], 0, v214, v214 op_sel_hi:[0,0,0]
	v_mfma_scale_f32_16x16x128_f8f6f4 v[74:77], v[26:33], v[222:229], 0, v214, v214 op_sel_hi:[0,0,0]
	v_mfma_scale_f32_16x16x128_f8f6f4 v[70:73], v[18:25], v[230:237], 0, v214, v214 op_sel_hi:[0,0,0]
	v_mfma_scale_f32_16x16x128_f8f6f4 v[66:69], v[26:33], v[230:237], 0, v214, v214 op_sel_hi:[0,0,0]
	v_mfma_scale_f32_16x16x128_f8f6f4 v[62:65], v[18:25], v[238:245], 0, v214, v214 op_sel_hi:[0,0,0]
	v_mfma_scale_f32_16x16x128_f8f6f4 v[58:61], v[26:33], v[238:245], 0, v214, v214 op_sel_hi:[0,0,0]
	v_mfma_scale_f32_16x16x128_f8f6f4 v[54:57], v[18:25], v[246:253], 0, v214, v214 op_sel_hi:[0,0,0]
	v_mfma_scale_f32_16x16x128_f8f6f4 v[50:53], v[26:33], v[246:253], 0, v214, v214 op_sel_hi:[0,0,0]
	s_nop 3
	v_mfma_scale_f32_16x16x128_f8f6f4 v[46:49], v[2:9], v[222:229], 0, v214, v214 op_sel_hi:[0,0,0]
	v_mfma_scale_f32_16x16x128_f8f6f4 v[42:45], v[10:17], v[222:229], 0, v214, v214 op_sel_hi:[0,0,0]
	v_mfma_scale_f32_16x16x128_f8f6f4 v[38:41], v[2:9], v[230:237], 0, v214, v214 op_sel_hi:[0,0,0]
	v_mfma_scale_f32_16x16x128_f8f6f4 v[34:37], v[10:17], v[230:237], 0, v214, v214 op_sel_hi:[0,0,0]
	v_mfma_scale_f32_16x16x128_f8f6f4 v[146:149], v[2:9], v[238:245], 0, v214, v214 op_sel_hi:[0,0,0]
	v_mfma_scale_f32_16x16x128_f8f6f4 v[150:153], v[10:17], v[238:245], 0, v214, v214 op_sel_hi:[0,0,0]
	v_mfma_scale_f32_16x16x128_f8f6f4 v[154:157], v[2:9], v[246:253], 0, v214, v214 op_sel_hi:[0,0,0]
	v_mfma_scale_f32_16x16x128_f8f6f4 v[158:161], v[10:17], v[246:253], 0, v214, v214 op_sel_hi:[0,0,0]
	s_barrier
; #define PG8_STAGE(bufoff, gbase, voff) do { _Pragma("unroll") for (int _i = 0; _i < 2; ++_i) \
;         __builtin_amdgcn_global_load_lds((const unsigned*)((const char*)(gbase) + (voff)[_i]), (PG8_LAS unsigned*)(lds + (bufoff) + ldsw + _i * 8192), 16, 0, 0); } while (0)
; #define PG8_WAIT_V(n) asm volatile("s_waitcnt vmcnt(" #n ")" ::: "memory")
; #define PG8_WAIT_L(n) asm volatile("s_waitcnt lgkmcnt(" #n ")" ::: "memory")
; #define PG8_BAR __builtin_amdgcn_s_barrier()
; #define PG8_SCHED __builtin_amdgcn_sched_barrier(0)
; template <class Epi, class Sched, bool ALIGN_EPI = true, bool F8 = false>
; __device__ __forceinline__ void gemm_phase(PG8_LAS unsigned char* lds, const Sched& S, const Epi& E) {
;     ...
;             PG8_LDB(B0, 1, 0); PG8_LDB(B1, 1, 1); PG8_SCHED; PG8_LDA(At, 1, 0); PG8_STAGE(PG8_SA(0, 1), a2, vA2[1]);
;             PG8_WAIT_V(8); PG8_WAIT_L(0); PG8_BAR; PG8_MMA(0, 0, At, B0); PG8_MMA(0, 1, At, B1); PG8_BAR; PG8_SCHED;
;             PG8_LDA(At, 1, 1); PG8_STAGE(PG8_SB(1, 0), b3, voffB[0]); PG8_STAGE(PG8_SB(1, 1), b3, voffB[1]); PG8_STAGE(PG8_SA(1, 0), a3, vA2[0]);
;             PG8_WAIT_V(8); PG8_WAIT_L(0); PG8_BAR; PG8_MMA(1, 0, At, B0); PG8_MMA(1, 1, At, B1); PG8_BAR; PG8_SCHED;
	s_add_i32 s70, 0, 0x18000
	s_add_i32 s71, 0, 0x1c000
	v_add_u32_e32 v14, s70, v210
	v_add_u32_e32 v30, s71, v210
	ds_read_b128 v[2:5], v14
	ds_read_b128 v[6:9], v14 offset:1024
	ds_read_b128 v[10:13], v14 offset:2048
	ds_read_b128 v[14:17], v14 offset:3072
	ds_read_b128 v[18:21], v30
	ds_read_b128 v[22:25], v30 offset:1024
	ds_read_b128 v[26:29], v30 offset:2048
	ds_read_b128 v[30:33], v30 offset:3072
	s_mov_b32 m0, s58
	v_lshl_add_u64 v[200:201], s[42:43], 0, v[200:201]
	ds_read_b128 v[222:225], v213 offset:32768
	ds_read_b128 v[226:229], v213 offset:33792
	ds_read_b128 v[230:233], v213 offset:34816
	ds_read_b128 v[234:237], v213 offset:35840
	ds_read_b128 v[238:241], v213 offset:36864
	ds_read_b128 v[242:245], v213 offset:37888
	ds_read_b128 v[246:249], v213 offset:38912
	ds_read_b128 v[250:253], v213 offset:39936
	global_load_lds_dwordx4 v[200:201], off
	v_lshl_add_u64 v[198:199], s[42:43], 0, v[198:199]
	s_mov_b32 m0, s59
	s_nop 0
	global_load_lds_dwordx4 v[198:199], off
	s_waitcnt vmcnt(8)
	s_waitcnt lgkmcnt(0)
	v_mfma_scale_f32_16x16x128_f8f6f4 v[142:145], v[2:9], v[222:229], v[142:145], v214, v214 op_sel_hi:[0,0,0]
	v_mfma_scale_f32_16x16x128_f8f6f4 v[138:141], v[10:17], v[222:229], v[138:141], v214, v214 op_sel_hi:[0,0,0]
	v_mfma_scale_f32_16x16x128_f8f6f4 v[134:137], v[2:9], v[230:237], v[134:137], v214, v214 op_sel_hi:[0,0,0]
	v_mfma_scale_f32_16x16x128_f8f6f4 v[130:133], v[10:17], v[230:237], v[130:133], v214, v214 op_sel_hi:[0,0,0]
	v_mfma_scale_f32_16x16x128_f8f6f4 v[126:129], v[2:9], v[238:245], v[126:129], v214, v214 op_sel_hi:[0,0,0]
	v_mfma_scale_f32_16x16x128_f8f6f4 v[122:125], v[10:17], v[238:245], v[122:125], v214, v214 op_sel_hi:[0,0,0]
	v_mfma_scale_f32_16x16x128_f8f6f4 v[118:121], v[2:9], v[246:253], v[118:121], v214, v214 op_sel_hi:[0,0,0]
	v_mfma_scale_f32_16x16x128_f8f6f4 v[114:117], v[10:17], v[246:253], v[114:117], v214, v214 op_sel_hi:[0,0,0]
	s_nop 3
	v_mfma_scale_f32_16x16x128_f8f6f4 v[110:113], v[18:25], v[222:229], v[110:113], v214, v214 op_sel_hi:[0,0,0]
	v_mfma_scale_f32_16x16x128_f8f6f4 v[106:109], v[26:33], v[222:229], v[106:109], v214, v214 op_sel_hi:[0,0,0]
	v_mfma_scale_f32_16x16x128_f8f6f4 v[102:105], v[18:25], v[230:237], v[102:105], v214, v214 op_sel_hi:[0,0,0]
	v_mfma_scale_f32_16x16x128_f8f6f4 v[98:101], v[26:33], v[230:237], v[98:101], v214, v214 op_sel_hi:[0,0,0]
	v_mfma_scale_f32_16x16x128_f8f6f4 v[94:97], v[18:25], v[238:245], v[94:97], v214, v214 op_sel_hi:[0,0,0]
	v_mfma_scale_f32_16x16x128_f8f6f4 v[90:93], v[26:33], v[238:245], v[90:93], v214, v214 op_sel_hi:[0,0,0]
	v_mfma_scale_f32_16x16x128_f8f6f4 v[86:89], v[18:25], v[246:253], v[86:89], v214, v214 op_sel_hi:[0,0,0]
	v_mfma_scale_f32_16x16x128_f8f6f4 v[82:85], v[26:33], v[246:253], v[82:85], v214, v214 op_sel_hi:[0,0,0]
	s_barrier
	s_add_u32 s30, s40, 0x8000
	s_addc_u32 s31, s41, 0
	s_add_i32 s40, s70, s48
	v_lshl_add_u64 v[198:199], s[30:31], 0, v[162:163]
	s_mov_b32 m0, s40
	ds_read_b128 v[222:225], v213 offset:49152
	ds_read_b128 v[226:229], v213 offset:50176
	ds_read_b128 v[230:233], v213 offset:51200
	ds_read_b128 v[234:237], v213 offset:52224
	ds_read_b128 v[238:241], v213 offset:53248
	ds_read_b128 v[242:245], v213 offset:54272
	ds_read_b128 v[246:249], v213 offset:55296
	ds_read_b128 v[250:253], v213 offset:56320
	global_load_lds_dwordx4 v[198:199], off
	v_lshl_add_u64 v[198:199], s[30:31], 0, v[164:165]
	s_add_i32 m0, s40, 0x2000
	s_add_i32 s40, s71, s48
	global_load_lds_dwordx4 v[198:199], off
	v_lshl_add_u64 v[198:199], s[30:31], 0, v[166:167]
	s_mov_b32 m0, s40
	s_nop 0
	global_load_lds_dwordx4 v[198:199], off
	v_lshl_add_u64 v[198:199], s[30:31], 0, v[168:169]
	s_add_i32 m0, s40, 0x2000
	s_nop 0
	global_load_lds_dwordx4 v[198:199], off
	v_lshl_add_u64 v[198:199], v[204:205], 0, s[18:19]
	s_mov_b32 m0, s60
	s_nop 0
	global_load_lds_dwordx4 v[198:199], off
	v_lshl_add_u64 v[198:199], v[202:203], 0, s[18:19]
	s_mov_b32 m0, s61
	s_nop 0
	global_load_lds_dwordx4 v[198:199], off
	s_waitcnt vmcnt(8)
	s_waitcnt lgkmcnt(0)
	v_mfma_scale_f32_16x16x128_f8f6f4 v[78:81], v[2:9], v[222:229], v[78:81], v214, v214 op_sel_hi:[0,0,0]
	v_mfma_scale_f32_16x16x128_f8f6f4 v[74:77], v[10:17], v[222:229], v[74:77], v214, v214 op_sel_hi:[0,0,0]
	v_mfma_scale_f32_16x16x128_f8f6f4 v[70:73], v[2:9], v[230:237], v[70:73], v214, v214 op_sel_hi:[0,0,0]
	v_mfma_scale_f32_16x16x128_f8f6f4 v[66:69], v[10:17], v[230:237], v[66:69], v214, v214 op_sel_hi:[0,0,0]
	v_mfma_scale_f32_16x16x128_f8f6f4 v[62:65], v[2:9], v[238:245], v[62:65], v214, v214 op_sel_hi:[0,0,0]
	v_mfma_scale_f32_16x16x128_f8f6f4 v[58:61], v[10:17], v[238:245], v[58:61], v214, v214 op_sel_hi:[0,0,0]
	v_mfma_scale_f32_16x16x128_f8f6f4 v[54:57], v[2:9], v[246:253], v[54:57], v214, v214 op_sel_hi:[0,0,0]
	v_mfma_scale_f32_16x16x128_f8f6f4 v[50:53], v[10:17], v[246:253], v[50:53], v214, v214 op_sel_hi:[0,0,0]
	s_nop 3
	v_mfma_scale_f32_16x16x128_f8f6f4 v[46:49], v[18:25], v[222:229], v[46:49], v214, v214 op_sel_hi:[0,0,0]
	v_mfma_scale_f32_16x16x128_f8f6f4 v[42:45], v[26:33], v[222:229], v[42:45], v214, v214 op_sel_hi:[0,0,0]
	v_mfma_scale_f32_16x16x128_f8f6f4 v[38:41], v[18:25], v[230:237], v[38:41], v214, v214 op_sel_hi:[0,0,0]
	v_mfma_scale_f32_16x16x128_f8f6f4 v[34:37], v[26:33], v[230:237], v[34:37], v214, v214 op_sel_hi:[0,0,0]
	v_mfma_scale_f32_16x16x128_f8f6f4 v[146:149], v[18:25], v[238:245], v[146:149], v214, v214 op_sel_hi:[0,0,0]
	v_mfma_scale_f32_16x16x128_f8f6f4 v[150:153], v[26:33], v[238:245], v[150:153], v214, v214 op_sel_hi:[0,0,0]
	v_mfma_scale_f32_16x16x128_f8f6f4 v[154:157], v[18:25], v[246:253], v[154:157], v214, v214 op_sel_hi:[0,0,0]
	v_mfma_scale_f32_16x16x128_f8f6f4 v[158:161], v[26:33], v[246:253], v[158:161], v214, v214 op_sel_hi:[0,0,0]
	s_barrier
	s_add_i32 s69, s69, 2
	s_add_u32 s21, s21, 0x10000
	s_addc_u32 s68, s68, 0
	s_cmp_gt_u32 s69, 13
	s_cbranch_scc1 .LBB0_1062
	s_mov_b64 s[30:31], s[28:29]
	s_branch .LBB0_1058

; #define PG8_STAGE(bufoff, gbase, voff) do { _Pragma("unroll") for (int _i = 0; _i < 2; ++_i) \
;         __builtin_amdgcn_global_load_lds((const unsigned*)((const char*)(gbase) + (voff)[_i]), (PG8_LAS unsigned*)(lds + (bufoff) + ldsw + _i * 8192), 16, 0, 0); } while (0)
; #define PG8_WAIT_V(n) asm volatile("s_waitcnt vmcnt(" #n ")" ::: "memory")
; #define PG8_WAIT_L(n) asm volatile("s_waitcnt lgkmcnt(" #n ")" ::: "memory")
; #define PG8_BAR __builtin_amdgcn_s_barrier()
; #define PG8_SCHED __builtin_amdgcn_sched_barrier(0)
; template <class Epi, class Sched, bool ALIGN_EPI = true, bool F8 = false>
; __device__ __forceinline__ void gemm_phase(PG8_LAS unsigned char* lds, const Sched& S, const Epi& E) {
;     ...
;             const char* a1 = cA + (size_t)(t + 1) * kstep;
;             const char* a2 = last ? nA : cA + (size_t)(t + 2) * kstep; const char* b2 = last ? nB : cB + (size_t)(t + 2) * kstepB;
;             const char* a3 = a2 + kstep; const char* b3 = b2 + kstepB;
;             unsigned vA2[2][2];
; #pragma unroll
;             for (int h = 0; h < 2; ++h)
; #pragma unroll
;                 for (int i = 0; i < 2; ++i) { if constexpr (Sched::GATHER) vA2[h][i] = (last && has_next) ? voffAn[h][i] : voffA[h][i]; else vA2[h][i] = voffA[h][i]; }
;             PG8_LDB(B0, 0, 0); PG8_LDB(B1, 0, 1); PG8_SCHED; PG8_LDA(At, 0, 0); PG8_STAGE(PG8_SA(1, 1), a1, voffA[1]);
;             PG8_WAIT_V(8); PG8_WAIT_L(0); PG8_BAR; PG8_MMA(0, 0, At, B0); PG8_MMA(0, 1, At, B1); PG8_BAR; PG8_SCHED;
;             PG8_LDA(At, 0, 1); PG8_STAGE(PG8_SB(0, 0), b2, voffB[0]); PG8_STAGE(PG8_SB(0, 1), b2, voffB[1]); PG8_STAGE(PG8_SA(0, 0), a2, vA2[0]);
;             PG8_WAIT_V(8); PG8_WAIT_L(0); PG8_BAR; PG8_MMA(1, 0, At, B0); PG8_MMA(1, 1, At, B1); PG8_BAR; PG8_SCHED;
.LBB0_1060:
	v_add_u32_e32 v2, s12, v210
	v_add_u32_e32 v14, s62, v210
	s_add_u32 s28, s30, 0x100
	ds_read_b128 v[18:21], v2
	ds_read_b128 v[22:25], v2 offset:1024
	ds_read_b128 v[26:29], v2 offset:2048
	ds_read_b128 v[30:33], v2 offset:3072
	ds_read_b128 v[2:5], v14
	ds_read_b128 v[6:9], v14 offset:1024
	ds_read_b128 v[10:13], v14 offset:2048
	ds_read_b128 v[14:17], v14 offset:3072
	s_addc_u32 s29, s31, 0
	s_and_b64 s[42:43], s[40:41], exec
	s_cselect_b32 s42, 0, s28
	s_cselect_b32 s43, 0, s29
	s_add_u32 s42, s6, s42
	s_addc_u32 s43, s7, s43
	s_and_b64 s[40:41], s[40:41], exec
	s_cselect_b32 s41, s25, s68
	s_cselect_b32 s40, s24, s21
	v_lshl_add_u64 v[204:205], v[196:197], 0, s[30:31]
	s_add_i32 m0, s52, 0xc000
	ds_read_b128 v[222:225], v213
	ds_read_b128 v[226:229], v213 offset:1024
	ds_read_b128 v[230:233], v213 offset:2048
	ds_read_b128 v[234:237], v213 offset:3072
	ds_read_b128 v[238:241], v213 offset:4096
	ds_read_b128 v[242:245], v213 offset:5120
	ds_read_b128 v[246:249], v213 offset:6144
	ds_read_b128 v[250:253], v213 offset:7168
	global_load_lds_dwordx4 v[204:205], off
	v_lshl_add_u64 v[204:205], v[194:195], 0, s[30:31]
	s_add_i32 m0, s52, 0xe000
	s_nop 0
	global_load_lds_dwordx4 v[204:205], off
	s_waitcnt vmcnt(8)
	s_waitcnt lgkmcnt(0)
	v_mfma_scale_f32_16x16x128_f8f6f4 v[142:145], v[18:25], v[222:229], v[142:145], v214, v214 op_sel_hi:[0,0,0]
	v_mfma_scale_f32_16x16x128_f8f6f4 v[138:141], v[26:33], v[222:229], v[138:141], v214, v214 op_sel_hi:[0,0,0]
	v_mfma_scale_f32_16x16x128_f8f6f4 v[134:137], v[18:25], v[230:237], v[134:137], v214, v214 op_sel_hi:[0,0,0]
	v_mfma_scale_f32_16x16x128_f8f6f4 v[130:133], v[26:33], v[230:237], v[130:133], v214, v214 op_sel_hi:[0,0,0]
	v_mfma_scale_f32_16x16x128_f8f6f4 v[126:129], v[18:25], v[238:245], v[126:129], v214, v214 op_sel_hi:[0,0,0]
	v_mfma_scale_f32_16x16x128_f8f6f4 v[122:125], v[26:33], v[238:245], v[122:125], v214, v214 op_sel_hi:[0,0,0]
	v_mfma_scale_f32_16x16x128_f8f6f4 v[118:121], v[18:25], v[246:253], v[118:121], v214, v214 op_sel_hi:[0,0,0]
	v_mfma_scale_f32_16x16x128_f8f6f4 v[114:117], v[26:33], v[246:253], v[114:117], v214, v214 op_sel_hi:[0,0,0]
	s_nop 3
	v_mfma_scale_f32_16x16x128_f8f6f4 v[110:113], v[2:9], v[222:229], v[110:113], v214, v214 op_sel_hi:[0,0,0]
	v_mfma_scale_f32_16x16x128_f8f6f4 v[106:109], v[10:17], v[222:229], v[106:109], v214, v214 op_sel_hi:[0,0,0]
	v_mfma_scale_f32_16x16x128_f8f6f4 v[102:105], v[2:9], v[230:237], v[102:105], v214, v214 op_sel_hi:[0,0,0]
	v_mfma_scale_f32_16x16x128_f8f6f4 v[98:101], v[10:17], v[230:237], v[98:101], v214, v214 op_sel_hi:[0,0,0]
	v_mfma_scale_f32_16x16x128_f8f6f4 v[94:97], v[2:9], v[238:245], v[94:97], v214, v214 op_sel_hi:[0,0,0]
	v_mfma_scale_f32_16x16x128_f8f6f4 v[90:93], v[10:17], v[238:245], v[90:93], v214, v214 op_sel_hi:[0,0,0]
	v_mfma_scale_f32_16x16x128_f8f6f4 v[86:89], v[2:9], v[246:253], v[86:89], v214, v214 op_sel_hi:[0,0,0]
	v_mfma_scale_f32_16x16x128_f8f6f4 v[82:85], v[10:17], v[246:253], v[82:85], v214, v214 op_sel_hi:[0,0,0]
	s_barrier
	s_add_i32 s30, s12, s48
	v_lshl_add_u64 v[204:205], s[40:41], 0, v[162:163]
	s_mov_b32 m0, s30
	ds_read_b128 v[222:225], v213 offset:16384
	ds_read_b128 v[226:229], v213 offset:17408
	ds_read_b128 v[230:233], v213 offset:18432
	ds_read_b128 v[234:237], v213 offset:19456
	ds_read_b128 v[238:241], v213 offset:20480
	ds_read_b128 v[242:245], v213 offset:21504
	ds_read_b128 v[246:249], v213 offset:22528
	ds_read_b128 v[250:253], v213 offset:23552
	global_load_lds_dwordx4 v[204:205], off
	v_lshl_add_u64 v[204:205], s[40:41], 0, v[164:165]
	s_add_i32 m0, s30, 0x2000
	s_add_i32 s30, s62, s48
	global_load_lds_dwordx4 v[204:205], off
	v_lshl_add_u64 v[204:205], s[40:41], 0, v[166:167]
	s_mov_b32 m0, s30
	v_mov_b32_e32 v203, v171
	global_load_lds_dwordx4 v[204:205], off
	v_lshl_add_u64 v[204:205], s[40:41], 0, v[168:169]
	s_add_i32 m0, s30, 0x2000
	s_nop 0
	global_load_lds_dwordx4 v[204:205], off
	s_mov_b32 m0, s52
	v_lshl_add_u64 v[204:205], s[42:43], 0, v[170:171]
	global_load_lds_dwordx4 v170, s[42:43]
	s_mov_b32 m0, s53
	s_nop 0
	global_load_lds_dwordx4 v202, s[42:43]
	s_waitcnt vmcnt(8)
	s_waitcnt lgkmcnt(0)
	v_lshl_add_u64 v[202:203], s[42:43], 0, v[202:203]
	v_mfma_scale_f32_16x16x128_f8f6f4 v[78:81], v[18:25], v[222:229], v[78:81], v214, v214 op_sel_hi:[0,0,0]
	v_mfma_scale_f32_16x16x128_f8f6f4 v[74:77], v[26:33], v[222:229], v[74:77], v214, v214 op_sel_hi:[0,0,0]
	v_mfma_scale_f32_16x16x128_f8f6f4 v[70:73], v[18:25], v[230:237], v[70:73], v214, v214 op_sel_hi:[0,0,0]
	v_mfma_scale_f32_16x16x128_f8f6f4 v[66:69], v[26:33], v[230:237], v[66:69], v214, v214 op_sel_hi:[0,0,0]
	v_mfma_scale_f32_16x16x128_f8f6f4 v[62:65], v[18:25], v[238:245], v[62:65], v214, v214 op_sel_hi:[0,0,0]
	v_mfma_scale_f32_16x16x128_f8f6f4 v[58:61], v[26:33], v[238:245], v[58:61], v214, v214 op_sel_hi:[0,0,0]
	v_mfma_scale_f32_16x16x128_f8f6f4 v[54:57], v[18:25], v[246:253], v[54:57], v214, v214 op_sel_hi:[0,0,0]
	v_mfma_scale_f32_16x16x128_f8f6f4 v[50:53], v[26:33], v[246:253], v[50:53], v214, v214 op_sel_hi:[0,0,0]
	s_nop 3
	v_mfma_scale_f32_16x16x128_f8f6f4 v[46:49], v[2:9], v[222:229], v[46:49], v214, v214 op_sel_hi:[0,0,0]
	v_mfma_scale_f32_16x16x128_f8f6f4 v[42:45], v[10:17], v[222:229], v[42:45], v214, v214 op_sel_hi:[0,0,0]
	v_mfma_scale_f32_16x16x128_f8f6f4 v[38:41], v[2:9], v[230:237], v[38:41], v214, v214 op_sel_hi:[0,0,0]
	v_mfma_scale_f32_16x16x128_f8f6f4 v[34:37], v[10:17], v[230:237], v[34:37], v214, v214 op_sel_hi:[0,0,0]
	v_mfma_scale_f32_16x16x128_f8f6f4 v[146:149], v[2:9], v[238:245], v[146:149], v214, v214 op_sel_hi:[0,0,0]
	v_mfma_scale_f32_16x16x128_f8f6f4 v[150:153], v[10:17], v[238:245], v[150:153], v214, v214 op_sel_hi:[0,0,0]
	v_mfma_scale_f32_16x16x128_f8f6f4 v[154:157], v[2:9], v[246:253], v[154:157], v214, v214 op_sel_hi:[0,0,0]
	v_mfma_scale_f32_16x16x128_f8f6f4 v[158:161], v[10:17], v[246:253], v[158:161], v214, v214 op_sel_hi:[0,0,0]
	s_barrier
; #define PG8_STAGE(bufoff, gbase, voff) do { _Pragma("unroll") for (int _i = 0; _i < 2; ++_i) \
;         __builtin_amdgcn_global_load_lds((const unsigned*)((const char*)(gbase) + (voff)[_i]), (PG8_LAS unsigned*)(lds + (bufoff) + ldsw + _i * 8192), 16, 0, 0); } while (0)
; #define PG8_WAIT_V(n) asm volatile("s_waitcnt vmcnt(" #n ")" ::: "memory")
; #define PG8_WAIT_L(n) asm volatile("s_waitcnt lgkmcnt(" #n ")" ::: "memory")
; #define PG8_BAR __builtin_amdgcn_s_barrier()
; #define PG8_SCHED __builtin_amdgcn_sched_barrier(0)
; template <class Epi, class Sched, bool ALIGN_EPI = true, bool F8 = false>
; __device__ __forceinline__ void gemm_phase(PG8_LAS unsigned char* lds, const Sched& S, const Epi& E) {
;     ...
;             PG8_LDB(B0, 1, 0); PG8_LDB(B1, 1, 1); PG8_SCHED; PG8_LDA(At, 1, 0); PG8_STAGE(PG8_SA(0, 1), a2, vA2[1]);
;             PG8_WAIT_V(8); PG8_WAIT_L(0); PG8_BAR; PG8_MMA(0, 0, At, B0); PG8_MMA(0, 1, At, B1); PG8_BAR; PG8_SCHED;
;             PG8_LDA(At, 1, 1); PG8_STAGE(PG8_SB(1, 0), b3, voffB[0]); PG8_STAGE(PG8_SB(1, 1), b3, voffB[1]); PG8_STAGE(PG8_SA(1, 0), a3, vA2[0]);
;             PG8_WAIT_V(8); PG8_WAIT_L(0); PG8_BAR; PG8_MMA(1, 0, At, B0); PG8_MMA(1, 1, At, B1); PG8_BAR; PG8_SCHED;
	s_add_i32 s70, 0, 0x18000
	s_add_i32 s71, 0, 0x1c000
	v_add_u32_e32 v14, s70, v210
	v_add_u32_e32 v30, s71, v210
	ds_read_b128 v[2:5], v14
	ds_read_b128 v[6:9], v14 offset:1024
	ds_read_b128 v[10:13], v14 offset:2048
	ds_read_b128 v[14:17], v14 offset:3072
	ds_read_b128 v[18:21], v30
	ds_read_b128 v[22:25], v30 offset:1024
	ds_read_b128 v[26:29], v30 offset:2048
	ds_read_b128 v[30:33], v30 offset:3072
	s_mov_b32 m0, s58
	v_lshl_add_u64 v[200:201], s[42:43], 0, v[200:201]
	ds_read_b128 v[222:225], v213 offset:32768
	ds_read_b128 v[226:229], v213 offset:33792
	ds_read_b128 v[230:233], v213 offset:34816
	ds_read_b128 v[234:237], v213 offset:35840
	ds_read_b128 v[238:241], v213 offset:36864
	ds_read_b128 v[242:245], v213 offset:37888
	ds_read_b128 v[246:249], v213 offset:38912
	ds_read_b128 v[250:253], v213 offset:39936
	global_load_lds_dwordx4 v[200:201], off
	v_lshl_add_u64 v[198:199], s[42:43], 0, v[198:199]
	s_mov_b32 m0, s59
	s_nop 0
	global_load_lds_dwordx4 v[198:199], off
	s_waitcnt vmcnt(8)
	s_waitcnt lgkmcnt(0)
	v_mfma_scale_f32_16x16x128_f8f6f4 v[142:145], v[2:9], v[222:229], v[142:145], v214, v214 op_sel_hi:[0,0,0]
	v_mfma_scale_f32_16x16x128_f8f6f4 v[138:141], v[10:17], v[222:229], v[138:141], v214, v214 op_sel_hi:[0,0,0]
	v_mfma_scale_f32_16x16x128_f8f6f4 v[134:137], v[2:9], v[230:237], v[134:137], v214, v214 op_sel_hi:[0,0,0]
	v_mfma_scale_f32_16x16x128_f8f6f4 v[130:133], v[10:17], v[230:237], v[130:133], v214, v214 op_sel_hi:[0,0,0]
	v_mfma_scale_f32_16x16x128_f8f6f4 v[126:129], v[2:9], v[238:245], v[126:129], v214, v214 op_sel_hi:[0,0,0]
	v_mfma_scale_f32_16x16x128_f8f6f4 v[122:125], v[10:17], v[238:245], v[122:125], v214, v214 op_sel_hi:[0,0,0]
	v_mfma_scale_f32_16x16x128_f8f6f4 v[118:121], v[2:9], v[246:253], v[118:121], v214, v214 op_sel_hi:[0,0,0]
	v_mfma_scale_f32_16x16x128_f8f6f4 v[114:117], v[10:17], v[246:253], v[114:117], v214, v214 op_sel_hi:[0,0,0]
	s_nop 3
	v_mfma_scale_f32_16x16x128_f8f6f4 v[110:113], v[18:25], v[222:229], v[110:113], v214, v214 op_sel_hi:[0,0,0]
	v_mfma_scale_f32_16x16x128_f8f6f4 v[106:109], v[26:33], v[222:229], v[106:109], v214, v214 op_sel_hi:[0,0,0]
	v_mfma_scale_f32_16x16x128_f8f6f4 v[102:105], v[18:25], v[230:237], v[102:105], v214, v214 op_sel_hi:[0,0,0]
	v_mfma_scale_f32_16x16x128_f8f6f4 v[98:101], v[26:33], v[230:237], v[98:101], v214, v214 op_sel_hi:[0,0,0]
	v_mfma_scale_f32_16x16x128_f8f6f4 v[94:97], v[18:25], v[238:245], v[94:97], v214, v214 op_sel_hi:[0,0,0]
	v_mfma_scale_f32_16x16x128_f8f6f4 v[90:93], v[26:33], v[238:245], v[90:93], v214, v214 op_sel_hi:[0,0,0]
	v_mfma_scale_f32_16x16x128_f8f6f4 v[86:89], v[18:25], v[246:253], v[86:89], v214, v214 op_sel_hi:[0,0,0]
	v_mfma_scale_f32_16x16x128_f8f6f4 v[82:85], v[26:33], v[246:253], v[82:85], v214, v214 op_sel_hi:[0,0,0]
	s_barrier
	s_add_u32 s30, s40, 0x8000
	s_addc_u32 s31, s41, 0
	s_add_i32 s40, s70, s48
	v_lshl_add_u64 v[198:199], s[30:31], 0, v[162:163]
	s_mov_b32 m0, s40
	ds_read_b128 v[222:225], v213 offset:49152
	ds_read_b128 v[226:229], v213 offset:50176
	ds_read_b128 v[230:233], v213 offset:51200
	ds_read_b128 v[234:237], v213 offset:52224
	ds_read_b128 v[238:241], v213 offset:53248
	ds_read_b128 v[242:245], v213 offset:54272
	ds_read_b128 v[246:249], v213 offset:55296
	ds_read_b128 v[250:253], v213 offset:56320
	global_load_lds_dwordx4 v[198:199], off
	v_lshl_add_u64 v[198:199], s[30:31], 0, v[164:165]
	s_add_i32 m0, s40, 0x2000
	s_add_i32 s40, s71, s48
	global_load_lds_dwordx4 v[198:199], off
	v_lshl_add_u64 v[198:199], s[30:31], 0, v[166:167]
	s_mov_b32 m0, s40
	s_nop 0
	global_load_lds_dwordx4 v[198:199], off
	v_lshl_add_u64 v[198:199], s[30:31], 0, v[168:169]
	s_add_i32 m0, s40, 0x2000
	s_nop 0
	global_load_lds_dwordx4 v[198:199], off
	v_lshl_add_u64 v[198:199], v[204:205], 0, s[18:19]
	s_mov_b32 m0, s60
	s_nop 0
	global_load_lds_dwordx4 v[198:199], off
	v_lshl_add_u64 v[198:199], v[202:203], 0, s[18:19]
	s_mov_b32 m0, s61
	s_nop 0
	global_load_lds_dwordx4 v[198:199], off
	s_waitcnt vmcnt(8)
	s_waitcnt lgkmcnt(0)
	v_mfma_scale_f32_16x16x128_f8f6f4 v[78:81], v[2:9], v[222:229], v[78:81], v214, v214 op_sel_hi:[0,0,0]
	v_mfma_scale_f32_16x16x128_f8f6f4 v[74:77], v[10:17], v[222:229], v[74:77], v214, v214 op_sel_hi:[0,0,0]
	v_mfma_scale_f32_16x16x128_f8f6f4 v[70:73], v[2:9], v[230:237], v[70:73], v214, v214 op_sel_hi:[0,0,0]
	v_mfma_scale_f32_16x16x128_f8f6f4 v[66:69], v[10:17], v[230:237], v[66:69], v214, v214 op_sel_hi:[0,0,0]
	v_mfma_scale_f32_16x16x128_f8f6f4 v[62:65], v[2:9], v[238:245], v[62:65], v214, v214 op_sel_hi:[0,0,0]
	v_mfma_scale_f32_16x16x128_f8f6f4 v[58:61], v[10:17], v[238:245], v[58:61], v214, v214 op_sel_hi:[0,0,0]
	v_mfma_scale_f32_16x16x128_f8f6f4 v[54:57], v[2:9], v[246:253], v[54:57], v214, v214 op_sel_hi:[0,0,0]
	v_mfma_scale_f32_16x16x128_f8f6f4 v[50:53], v[10:17], v[246:253], v[50:53], v214, v214 op_sel_hi:[0,0,0]
	s_nop 3
	v_mfma_scale_f32_16x16x128_f8f6f4 v[46:49], v[18:25], v[222:229], v[46:49], v214, v214 op_sel_hi:[0,0,0]
	v_mfma_scale_f32_16x16x128_f8f6f4 v[42:45], v[26:33], v[222:229], v[42:45], v214, v214 op_sel_hi:[0,0,0]
	v_mfma_scale_f32_16x16x128_f8f6f4 v[38:41], v[18:25], v[230:237], v[38:41], v214, v214 op_sel_hi:[0,0,0]
	v_mfma_scale_f32_16x16x128_f8f6f4 v[34:37], v[26:33], v[230:237], v[34:37], v214, v214 op_sel_hi:[0,0,0]
	v_mfma_scale_f32_16x16x128_f8f6f4 v[146:149], v[18:25], v[238:245], v[146:149], v214, v214 op_sel_hi:[0,0,0]
	v_mfma_scale_f32_16x16x128_f8f6f4 v[150:153], v[26:33], v[238:245], v[150:153], v214, v214 op_sel_hi:[0,0,0]
	v_mfma_scale_f32_16x16x128_f8f6f4 v[154:157], v[18:25], v[246:253], v[154:157], v214, v214 op_sel_hi:[0,0,0]
	v_mfma_scale_f32_16x16x128_f8f6f4 v[158:161], v[26:33], v[246:253], v[158:161], v214, v214 op_sel_hi:[0,0,0]
	s_barrier
	s_add_i32 s69, s69, 2
	s_add_u32 s21, s21, 0x10000
	s_addc_u32 s68, s68, 0
	s_cmp_gt_u32 s69, 13
	s_cbranch_scc1 .LBB0_1062
	s_mov_b64 s[30:31], s[28:29]
	s_branch .LBB0_1058

; #define PG8_STAGE(bufoff, gbase, voff) do { _Pragma("unroll") for (int _i = 0; _i < 2; ++_i) \
;         __builtin_amdgcn_global_load_lds((const unsigned*)((const char*)(gbase) + (voff)[_i]), (PG8_LAS unsigned*)(lds + (bufoff) + ldsw + _i * 8192), 16, 0, 0); } while (0)
; #define PG8_WAIT_V(n) asm volatile("s_waitcnt vmcnt(" #n ")" ::: "memory")
; #define PG8_WAIT_L(n) asm volatile("s_waitcnt lgkmcnt(" #n ")" ::: "memory")
; #define PG8_BAR __builtin_amdgcn_s_barrier()
; #define PG8_SCHED __builtin_amdgcn_sched_barrier(0)
; template <class Epi, class Sched, bool ALIGN_EPI = true, bool F8 = false>
; __device__ __forceinline__ void gemm_phase(PG8_LAS unsigned char* lds, const Sched& S, const Epi& E) {
;     ...
;             const char* a1 = cA + (size_t)(t + 1) * kstep;
;             const char* a2 = last ? nA : cA + (size_t)(t + 2) * kstep; const char* b2 = last ? nB : cB + (size_t)(t + 2) * kstepB;
;             const char* a3 = a2 + kstep; const char* b3 = b2 + kstepB;
;             unsigned vA2[2][2];
; #pragma unroll
;             for (int h = 0; h < 2; ++h)
; #pragma unroll
;                 for (int i = 0; i < 2; ++i) { if constexpr (Sched::GATHER) vA2[h][i] = (last && has_next) ? voffAn[h][i] : voffA[h][i]; else vA2[h][i] = voffA[h][i]; }
;             PG8_LDB(B0, 0, 0); PG8_LDB(B1, 0, 1); PG8_SCHED; PG8_LDA(At, 0, 0); PG8_STAGE(PG8_SA(1, 1), a1, voffA[1]);
;             PG8_WAIT_V(8); PG8_WAIT_L(0); PG8_BAR; PG8_MMA(0, 0, At, B0); PG8_MMA(0, 1, At, B1); PG8_BAR; PG8_SCHED;
;             PG8_LDA(At, 0, 1); PG8_STAGE(PG8_SB(0, 0), b2, voffB[0]); PG8_STAGE(PG8_SB(0, 1), b2, voffB[1]); PG8_STAGE(PG8_SA(0, 0), a2, vA2[0]);
;             PG8_WAIT_V(8); PG8_WAIT_L(0); PG8_BAR; PG8_MMA(1, 0, At, B0); PG8_MMA(1, 1, At, B1); PG8_BAR; PG8_SCHED;
;             PG8_LDB(B0, 1, 0); PG8_LDB(B1, 1, 1); PG8_SCHED; PG8_LDA(At, 1, 0); PG8_STAGE(PG8_SA(0, 1), a2, vA2[1]);
;             PG8_WAIT_V(8); PG8_WAIT_L(0); PG8_BAR; PG8_MMA(0, 0, At, B0); PG8_MMA(0, 1, At, B1); PG8_BAR; PG8_SCHED;
.Lpk1_1060:
	v_add_u32_e32 v2, s12, v210
	v_add_u32_e32 v14, s62, v210
	s_add_u32 s28, s30, 0x100
	ds_read_b128 v[18:21], v2
	ds_read_b128 v[22:25], v2 offset:1024
	ds_read_b128 v[26:29], v2 offset:2048
	ds_read_b128 v[30:33], v2 offset:3072
	ds_read_b128 v[2:5], v14
	ds_read_b128 v[6:9], v14 offset:1024
	ds_read_b128 v[10:13], v14 offset:2048
	ds_read_b128 v[14:17], v14 offset:3072
	s_addc_u32 s29, s31, 0
	s_and_b64 s[42:43], s[40:41], exec
	s_cselect_b32 s42, 0, s28
	s_cselect_b32 s43, 0, s29
	s_add_u32 s42, s6, s42
	s_addc_u32 s43, s7, s43
	s_and_b64 s[40:41], s[40:41], exec
	s_cselect_b32 s41, s25, s68
	s_cselect_b32 s40, s24, s21
	v_lshl_add_u64 v[204:205], v[196:197], 0, s[30:31]
	s_add_i32 m0, s52, 0xc000
	ds_read_b128 v[222:225], v213
	ds_read_b128 v[226:229], v213 offset:1024
	ds_read_b128 v[230:233], v213 offset:2048
	ds_read_b128 v[234:237], v213 offset:3072
	ds_read_b128 v[238:241], v213 offset:4096
	ds_read_b128 v[242:245], v213 offset:5120
	ds_read_b128 v[246:249], v213 offset:6144
	ds_read_b128 v[250:253], v213 offset:7168
	global_load_lds_dwordx4 v[204:205], off
	v_lshl_add_u64 v[204:205], v[194:195], 0, s[30:31]
	s_add_i32 m0, s52, 0xe000
	s_nop 0
	global_load_lds_dwordx4 v[204:205], off
	s_waitcnt vmcnt(8)
	s_waitcnt lgkmcnt(0)
	s_barrier
	v_mfma_scale_f32_16x16x128_f8f6f4 v[142:145], v[18:25], v[222:229], 0, v214, v214 op_sel_hi:[0,0,0]
	v_mfma_scale_f32_16x16x128_f8f6f4 v[138:141], v[26:33], v[222:229], 0, v214, v214 op_sel_hi:[0,0,0]
	v_mfma_scale_f32_16x16x128_f8f6f4 v[134:137], v[18:25], v[230:237], 0, v214, v214 op_sel_hi:[0,0,0]
	v_mfma_scale_f32_16x16x128_f8f6f4 v[130:133], v[26:33], v[230:237], 0, v214, v214 op_sel_hi:[0,0,0]
	v_mfma_scale_f32_16x16x128_f8f6f4 v[126:129], v[18:25], v[238:245], 0, v214, v214 op_sel_hi:[0,0,0]
	v_mfma_scale_f32_16x16x128_f8f6f4 v[122:125], v[26:33], v[238:245], 0, v214, v214 op_sel_hi:[0,0,0]
	v_mfma_scale_f32_16x16x128_f8f6f4 v[118:121], v[18:25], v[246:253], 0, v214, v214 op_sel_hi:[0,0,0]
	v_mfma_scale_f32_16x16x128_f8f6f4 v[114:117], v[26:33], v[246:253], 0, v214, v214 op_sel_hi:[0,0,0]
	s_nop 3
	v_mfma_scale_f32_16x16x128_f8f6f4 v[110:113], v[2:9], v[222:229], 0, v214, v214 op_sel_hi:[0,0,0]
	v_mfma_scale_f32_16x16x128_f8f6f4 v[106:109], v[10:17], v[222:229], 0, v214, v214 op_sel_hi:[0,0,0]
	v_mfma_scale_f32_16x16x128_f8f6f4 v[102:105], v[2:9], v[230:237], 0, v214, v214 op_sel_hi:[0,0,0]
	v_mfma_scale_f32_16x16x128_f8f6f4 v[98:101], v[10:17], v[230:237], 0, v214, v214 op_sel_hi:[0,0,0]
	v_mfma_scale_f32_16x16x128_f8f6f4 v[94:97], v[2:9], v[238:245], 0, v214, v214 op_sel_hi:[0,0,0]
	v_mfma_scale_f32_16x16x128_f8f6f4 v[90:93], v[10:17], v[238:245], 0, v214, v214 op_sel_hi:[0,0,0]
	v_mfma_scale_f32_16x16x128_f8f6f4 v[86:89], v[2:9], v[246:253], 0, v214, v214 op_sel_hi:[0,0,0]
	v_mfma_scale_f32_16x16x128_f8f6f4 v[82:85], v[10:17], v[246:253], 0, v214, v214 op_sel_hi:[0,0,0]
	s_add_i32 s30, s12, s48
	v_lshl_add_u64 v[204:205], s[40:41], 0, v[162:163]
	s_mov_b32 m0, s30
	ds_read_b128 v[222:225], v213 offset:16384
	ds_read_b128 v[226:229], v213 offset:17408
	ds_read_b128 v[230:233], v213 offset:18432
	ds_read_b128 v[234:237], v213 offset:19456
	ds_read_b128 v[238:241], v213 offset:20480
	ds_read_b128 v[242:245], v213 offset:21504
	ds_read_b128 v[246:249], v213 offset:22528
	ds_read_b128 v[250:253], v213 offset:23552
	global_load_lds_dwordx4 v[204:205], off
	v_lshl_add_u64 v[204:205], s[40:41], 0, v[164:165]
	s_add_i32 m0, s30, 0x2000
	s_add_i32 s30, s62, s48
	global_load_lds_dwordx4 v[204:205], off
	v_lshl_add_u64 v[204:205], s[40:41], 0, v[166:167]
	s_mov_b32 m0, s30
	v_mov_b32_e32 v203, v171
	global_load_lds_dwordx4 v[204:205], off
	v_lshl_add_u64 v[204:205], s[40:41], 0, v[168:169]
	s_add_i32 m0, s30, 0x2000
	s_nop 0
	global_load_lds_dwordx4 v[204:205], off
	s_mov_b32 m0, s52
	v_lshl_add_u64 v[204:205], s[42:43], 0, v[170:171]
	global_load_lds_dwordx4 v170, s[42:43]
	s_mov_b32 m0, s53
	s_nop 0
	global_load_lds_dwordx4 v202, s[42:43]
	s_waitcnt vmcnt(8)
	s_waitcnt lgkmcnt(0)
	v_lshl_add_u64 v[202:203], s[42:43], 0, v[202:203]
	s_barrier
	v_mfma_scale_f32_16x16x128_f8f6f4 v[78:81], v[18:25], v[222:229], 0, v214, v214 op_sel_hi:[0,0,0]
	v_mfma_scale_f32_16x16x128_f8f6f4 v[74:77], v[26:33], v[222:229], 0, v214, v214 op_sel_hi:[0,0,0]
	v_mfma_scale_f32_16x16x128_f8f6f4 v[70:73], v[18:25], v[230:237], 0, v214, v214 op_sel_hi:[0,0,0]
	v_mfma_scale_f32_16x16x128_f8f6f4 v[66:69], v[26:33], v[230:237], 0, v214, v214 op_sel_hi:[0,0,0]
	v_mfma_scale_f32_16x16x128_f8f6f4 v[62:65], v[18:25], v[238:245], 0, v214, v214 op_sel_hi:[0,0,0]
	v_mfma_scale_f32_16x16x128_f8f6f4 v[58:61], v[26:33], v[238:245], 0, v214, v214 op_sel_hi:[0,0,0]
	v_mfma_scale_f32_16x16x128_f8f6f4 v[54:57], v[18:25], v[246:253], 0, v214, v214 op_sel_hi:[0,0,0]
	v_mfma_scale_f32_16x16x128_f8f6f4 v[50:53], v[26:33], v[246:253], 0, v214, v214 op_sel_hi:[0,0,0]
	s_nop 3
	v_mfma_scale_f32_16x16x128_f8f6f4 v[46:49], v[2:9], v[222:229], 0, v214, v214 op_sel_hi:[0,0,0]
	v_mfma_scale_f32_16x16x128_f8f6f4 v[42:45], v[10:17], v[222:229], 0, v214, v214 op_sel_hi:[0,0,0]
	v_mfma_scale_f32_16x16x128_f8f6f4 v[38:41], v[2:9], v[230:237], 0, v214, v214 op_sel_hi:[0,0,0]
	v_mfma_scale_f32_16x16x128_f8f6f4 v[34:37], v[10:17], v[230:237], 0, v214, v214 op_sel_hi:[0,0,0]
	v_mfma_scale_f32_16x16x128_f8f6f4 v[146:149], v[2:9], v[238:245], 0, v214, v214 op_sel_hi:[0,0,0]
	v_mfma_scale_f32_16x16x128_f8f6f4 v[150:153], v[10:17], v[238:245], 0, v214, v214 op_sel_hi:[0,0,0]
	v_mfma_scale_f32_16x16x128_f8f6f4 v[154:157], v[2:9], v[246:253], 0, v214, v214 op_sel_hi:[0,0,0]
	v_mfma_scale_f32_16x16x128_f8f6f4 v[158:161], v[10:17], v[246:253], 0, v214, v214 op_sel_hi:[0,0,0]
	s_add_i32 s70, 0, 0x18000
	s_add_i32 s71, 0, 0x1c000
	v_add_u32_e32 v14, s70, v210
	v_add_u32_e32 v30, s71, v210
	ds_read_b128 v[2:5], v14
	ds_read_b128 v[6:9], v14 offset:1024
	ds_read_b128 v[10:13], v14 offset:2048
	ds_read_b128 v[14:17], v14 offset:3072
	ds_read_b128 v[18:21], v30
	ds_read_b128 v[22:25], v30 offset:1024
	ds_read_b128 v[26:29], v30 offset:2048
	ds_read_b128 v[30:33], v30 offset:3072
	s_mov_b32 m0, s58
	v_lshl_add_u64 v[200:201], s[42:43], 0, v[200:201]
	ds_read_b128 v[222:225], v213 offset:32768
	ds_read_b128 v[226:229], v213 offset:33792
	ds_read_b128 v[230:233], v213 offset:34816
	ds_read_b128 v[234:237], v213 offset:35840
	ds_read_b128 v[238:241], v213 offset:36864
	ds_read_b128 v[242:245], v213 offset:37888
	ds_read_b128 v[246:249], v213 offset:38912
	ds_read_b128 v[250:253], v213 offset:39936
	global_load_lds_dwordx4 v[200:201], off
	v_lshl_add_u64 v[198:199], s[42:43], 0, v[198:199]
	s_mov_b32 m0, s59
	s_nop 0
	global_load_lds_dwordx4 v[198:199], off
	s_waitcnt vmcnt(8)
	s_waitcnt lgkmcnt(0)
	s_barrier
; #define PG8_STAGE(bufoff, gbase, voff) do { _Pragma("unroll") for (int _i = 0; _i < 2; ++_i) \
;         __builtin_amdgcn_global_load_lds((const unsigned*)((const char*)(gbase) + (voff)[_i]), (PG8_LAS unsigned*)(lds + (bufoff) + ldsw + _i * 8192), 16, 0, 0); } while (0)
; #define PG8_WAIT_V(n) asm volatile("s_waitcnt vmcnt(" #n ")" ::: "memory")
; #define PG8_WAIT_L(n) asm volatile("s_waitcnt lgkmcnt(" #n ")" ::: "memory")
; #define PG8_BAR __builtin_amdgcn_s_barrier()
; #define PG8_SCHED __builtin_amdgcn_sched_barrier(0)
; template <class Epi, class Sched, bool ALIGN_EPI = true, bool F8 = false>
; __device__ __forceinline__ void gemm_phase(PG8_LAS unsigned char* lds, const Sched& S, const Epi& E) {
;     ...
;             PG8_WAIT_V(8); PG8_WAIT_L(0); PG8_BAR; PG8_MMA(0, 0, At, B0); PG8_MMA(0, 1, At, B1); PG8_BAR; PG8_SCHED;
;             PG8_LDA(At, 1, 1); PG8_STAGE(PG8_SB(1, 0), b3, voffB[0]); PG8_STAGE(PG8_SB(1, 1), b3, voffB[1]); PG8_STAGE(PG8_SA(1, 0), a3, vA2[0]);
;             PG8_WAIT_V(8); PG8_WAIT_L(0); PG8_BAR; PG8_MMA(1, 0, At, B0); PG8_MMA(1, 1, At, B1); PG8_BAR; PG8_SCHED;
	v_mfma_scale_f32_16x16x128_f8f6f4 v[142:145], v[2:9], v[222:229], v[142:145], v214, v214 op_sel_hi:[0,0,0]
	v_mfma_scale_f32_16x16x128_f8f6f4 v[138:141], v[10:17], v[222:229], v[138:141], v214, v214 op_sel_hi:[0,0,0]
	v_mfma_scale_f32_16x16x128_f8f6f4 v[134:137], v[2:9], v[230:237], v[134:137], v214, v214 op_sel_hi:[0,0,0]
	v_mfma_scale_f32_16x16x128_f8f6f4 v[130:133], v[10:17], v[230:237], v[130:133], v214, v214 op_sel_hi:[0,0,0]
	v_mfma_scale_f32_16x16x128_f8f6f4 v[126:129], v[2:9], v[238:245], v[126:129], v214, v214 op_sel_hi:[0,0,0]
	v_mfma_scale_f32_16x16x128_f8f6f4 v[122:125], v[10:17], v[238:245], v[122:125], v214, v214 op_sel_hi:[0,0,0]
	v_mfma_scale_f32_16x16x128_f8f6f4 v[118:121], v[2:9], v[246:253], v[118:121], v214, v214 op_sel_hi:[0,0,0]
	v_mfma_scale_f32_16x16x128_f8f6f4 v[114:117], v[10:17], v[246:253], v[114:117], v214, v214 op_sel_hi:[0,0,0]
	s_nop 3
	v_mfma_scale_f32_16x16x128_f8f6f4 v[110:113], v[18:25], v[222:229], v[110:113], v214, v214 op_sel_hi:[0,0,0]
	v_mfma_scale_f32_16x16x128_f8f6f4 v[106:109], v[26:33], v[222:229], v[106:109], v214, v214 op_sel_hi:[0,0,0]
	v_mfma_scale_f32_16x16x128_f8f6f4 v[102:105], v[18:25], v[230:237], v[102:105], v214, v214 op_sel_hi:[0,0,0]
	v_mfma_scale_f32_16x16x128_f8f6f4 v[98:101], v[26:33], v[230:237], v[98:101], v214, v214 op_sel_hi:[0,0,0]
	v_mfma_scale_f32_16x16x128_f8f6f4 v[94:97], v[18:25], v[238:245], v[94:97], v214, v214 op_sel_hi:[0,0,0]
	v_mfma_scale_f32_16x16x128_f8f6f4 v[90:93], v[26:33], v[238:245], v[90:93], v214, v214 op_sel_hi:[0,0,0]
	v_mfma_scale_f32_16x16x128_f8f6f4 v[86:89], v[18:25], v[246:253], v[86:89], v214, v214 op_sel_hi:[0,0,0]
	v_mfma_scale_f32_16x16x128_f8f6f4 v[82:85], v[26:33], v[246:253], v[82:85], v214, v214 op_sel_hi:[0,0,0]
	s_add_u32 s30, s40, 0x8000
	s_addc_u32 s31, s41, 0
	s_add_i32 s40, s70, s48
	v_lshl_add_u64 v[198:199], s[30:31], 0, v[162:163]
	s_mov_b32 m0, s40
	ds_read_b128 v[222:225], v213 offset:49152
	ds_read_b128 v[226:229], v213 offset:50176
	ds_read_b128 v[230:233], v213 offset:51200
	ds_read_b128 v[234:237], v213 offset:52224
	ds_read_b128 v[238:241], v213 offset:53248
	ds_read_b128 v[242:245], v213 offset:54272
	ds_read_b128 v[246:249], v213 offset:55296
	ds_read_b128 v[250:253], v213 offset:56320
	global_load_lds_dwordx4 v[198:199], off
	v_lshl_add_u64 v[198:199], s[30:31], 0, v[164:165]
	s_add_i32 m0, s40, 0x2000
	s_add_i32 s40, s71, s48
	global_load_lds_dwordx4 v[198:199], off
	v_lshl_add_u64 v[198:199], s[30:31], 0, v[166:167]
	s_mov_b32 m0, s40
	s_nop 0
	global_load_lds_dwordx4 v[198:199], off
	v_lshl_add_u64 v[198:199], s[30:31], 0, v[168:169]
	s_add_i32 m0, s40, 0x2000
	s_nop 0
	global_load_lds_dwordx4 v[198:199], off
	v_lshl_add_u64 v[198:199], v[204:205], 0, s[18:19]
	s_mov_b32 m0, s60
	s_nop 0
	global_load_lds_dwordx4 v[198:199], off
	v_lshl_add_u64 v[198:199], v[202:203], 0, s[18:19]
	s_mov_b32 m0, s61
	s_nop 0
	global_load_lds_dwordx4 v[198:199], off
	s_waitcnt vmcnt(8)
	s_waitcnt lgkmcnt(0)
	s_barrier
	v_mfma_scale_f32_16x16x128_f8f6f4 v[78:81], v[2:9], v[222:229], v[78:81], v214, v214 op_sel_hi:[0,0,0]
	v_mfma_scale_f32_16x16x128_f8f6f4 v[74:77], v[10:17], v[222:229], v[74:77], v214, v214 op_sel_hi:[0,0,0]
	v_mfma_scale_f32_16x16x128_f8f6f4 v[70:73], v[2:9], v[230:237], v[70:73], v214, v214 op_sel_hi:[0,0,0]
	v_mfma_scale_f32_16x16x128_f8f6f4 v[66:69], v[10:17], v[230:237], v[66:69], v214, v214 op_sel_hi:[0,0,0]
	v_mfma_scale_f32_16x16x128_f8f6f4 v[62:65], v[2:9], v[238:245], v[62:65], v214, v214 op_sel_hi:[0,0,0]
	v_mfma_scale_f32_16x16x128_f8f6f4 v[58:61], v[10:17], v[238:245], v[58:61], v214, v214 op_sel_hi:[0,0,0]
	v_mfma_scale_f32_16x16x128_f8f6f4 v[54:57], v[2:9], v[246:253], v[54:57], v214, v214 op_sel_hi:[0,0,0]
	v_mfma_scale_f32_16x16x128_f8f6f4 v[50:53], v[10:17], v[246:253], v[50:53], v214, v214 op_sel_hi:[0,0,0]
	s_nop 3
	v_mfma_scale_f32_16x16x128_f8f6f4 v[46:49], v[18:25], v[222:229], v[46:49], v214, v214 op_sel_hi:[0,0,0]
	v_mfma_scale_f32_16x16x128_f8f6f4 v[42:45], v[26:33], v[222:229], v[42:45], v214, v214 op_sel_hi:[0,0,0]
	v_mfma_scale_f32_16x16x128_f8f6f4 v[38:41], v[18:25], v[230:237], v[38:41], v214, v214 op_sel_hi:[0,0,0]
	v_mfma_scale_f32_16x16x128_f8f6f4 v[34:37], v[26:33], v[230:237], v[34:37], v214, v214 op_sel_hi:[0,0,0]
	v_mfma_scale_f32_16x16x128_f8f6f4 v[146:149], v[18:25], v[238:245], v[146:149], v214, v214 op_sel_hi:[0,0,0]
	v_mfma_scale_f32_16x16x128_f8f6f4 v[150:153], v[26:33], v[238:245], v[150:153], v214, v214 op_sel_hi:[0,0,0]
	v_mfma_scale_f32_16x16x128_f8f6f4 v[154:157], v[18:25], v[246:253], v[154:157], v214, v214 op_sel_hi:[0,0,0]
	v_mfma_scale_f32_16x16x128_f8f6f4 v[158:161], v[26:33], v[246:253], v[158:161], v214, v214 op_sel_hi:[0,0,0]
	s_add_i32 s69, s69, 2
	s_add_u32 s21, s21, 0x10000
	s_addc_u32 s68, s68, 0
	s_cmp_gt_u32 s69, 13
	s_cbranch_scc1 .LBB0_1062
	s_mov_b64 s[30:31], s[28:29]
	s_branch .Lh1_1058

; #define PG8_STAGE(bufoff, gbase, voff) do { _Pragma("unroll") for (int _i = 0; _i < 2; ++_i) \
;         __builtin_amdgcn_global_load_lds((const unsigned*)((const char*)(gbase) + (voff)[_i]), (PG8_LAS unsigned*)(lds + (bufoff) + ldsw + _i * 8192), 16, 0, 0); } while (0)
; #define PG8_WAIT_V(n) asm volatile("s_waitcnt vmcnt(" #n ")" ::: "memory")
; #define PG8_WAIT_L(n) asm volatile("s_waitcnt lgkmcnt(" #n ")" ::: "memory")
; #define PG8_BAR __builtin_amdgcn_s_barrier()
; #define PG8_SCHED __builtin_amdgcn_sched_barrier(0)
; template <class Epi, class Sched, bool ALIGN_EPI = true, bool F8 = false>
; __device__ __forceinline__ void gemm_phase(PG8_LAS unsigned char* lds, const Sched& S, const Epi& E) {
;     ...
;             const char* a1 = cA + (size_t)(t + 1) * kstep;
;             const char* a2 = last ? nA : cA + (size_t)(t + 2) * kstep; const char* b2 = last ? nB : cB + (size_t)(t + 2) * kstepB;
;             const char* a3 = a2 + kstep; const char* b3 = b2 + kstepB;
;             unsigned vA2[2][2];
; #pragma unroll
;             for (int h = 0; h < 2; ++h)
; #pragma unroll
;                 for (int i = 0; i < 2; ++i) { if constexpr (Sched::GATHER) vA2[h][i] = (last && has_next) ? voffAn[h][i] : voffA[h][i]; else vA2[h][i] = voffA[h][i]; }
;             PG8_LDB(B0, 0, 0); PG8_LDB(B1, 0, 1); PG8_SCHED; PG8_LDA(At, 0, 0); PG8_STAGE(PG8_SA(1, 1), a1, voffA[1]);
;             PG8_WAIT_V(8); PG8_WAIT_L(0); PG8_BAR; PG8_MMA(0, 0, At, B0); PG8_MMA(0, 1, At, B1); PG8_BAR; PG8_SCHED;
;             PG8_LDA(At, 0, 1); PG8_STAGE(PG8_SB(0, 0), b2, voffB[0]); PG8_STAGE(PG8_SB(0, 1), b2, voffB[1]); PG8_STAGE(PG8_SA(0, 0), a2, vA2[0]);
;             PG8_WAIT_V(8); PG8_WAIT_L(0); PG8_BAR; PG8_MMA(1, 0, At, B0); PG8_MMA(1, 1, At, B1); PG8_BAR; PG8_SCHED;
;             PG8_LDB(B0, 1, 0); PG8_LDB(B1, 1, 1); PG8_SCHED; PG8_LDA(At, 1, 0); PG8_STAGE(PG8_SA(0, 1), a2, vA2[1]);
;             PG8_WAIT_V(8); PG8_WAIT_L(0); PG8_BAR; PG8_MMA(0, 0, At, B0); PG8_MMA(0, 1, At, B1); PG8_BAR; PG8_SCHED;
.Lh1_1060:
	v_add_u32_e32 v2, s12, v210
	v_add_u32_e32 v14, s62, v210
	s_add_u32 s28, s30, 0x100
	ds_read_b128 v[18:21], v2
	ds_read_b128 v[22:25], v2 offset:1024
	ds_read_b128 v[26:29], v2 offset:2048
	ds_read_b128 v[30:33], v2 offset:3072
	ds_read_b128 v[2:5], v14
	ds_read_b128 v[6:9], v14 offset:1024
	ds_read_b128 v[10:13], v14 offset:2048
	ds_read_b128 v[14:17], v14 offset:3072
	s_addc_u32 s29, s31, 0
	s_and_b64 s[42:43], s[40:41], exec
	s_cselect_b32 s42, 0, s28
	s_cselect_b32 s43, 0, s29
	s_add_u32 s42, s6, s42
	s_addc_u32 s43, s7, s43
	s_and_b64 s[40:41], s[40:41], exec
	s_cselect_b32 s41, s25, s68
	s_cselect_b32 s40, s24, s21
	v_lshl_add_u64 v[204:205], v[196:197], 0, s[30:31]
	s_add_i32 m0, s52, 0xc000
	ds_read_b128 v[222:225], v213
	ds_read_b128 v[226:229], v213 offset:1024
	ds_read_b128 v[230:233], v213 offset:2048
	ds_read_b128 v[234:237], v213 offset:3072
	ds_read_b128 v[238:241], v213 offset:4096
	ds_read_b128 v[242:245], v213 offset:5120
	ds_read_b128 v[246:249], v213 offset:6144
	ds_read_b128 v[250:253], v213 offset:7168
	global_load_lds_dwordx4 v[204:205], off
	v_lshl_add_u64 v[204:205], v[194:195], 0, s[30:31]
	s_add_i32 m0, s52, 0xe000
	s_nop 0
	global_load_lds_dwordx4 v[204:205], off
	s_waitcnt vmcnt(8)
	s_waitcnt lgkmcnt(0)
	s_barrier
	v_mfma_scale_f32_16x16x128_f8f6f4 v[142:145], v[18:25], v[222:229], v[142:145], v214, v214 op_sel_hi:[0,0,0]
	v_mfma_scale_f32_16x16x128_f8f6f4 v[138:141], v[26:33], v[222:229], v[138:141], v214, v214 op_sel_hi:[0,0,0]
	v_mfma_scale_f32_16x16x128_f8f6f4 v[134:137], v[18:25], v[230:237], v[134:137], v214, v214 op_sel_hi:[0,0,0]
	v_mfma_scale_f32_16x16x128_f8f6f4 v[130:133], v[26:33], v[230:237], v[130:133], v214, v214 op_sel_hi:[0,0,0]
	v_mfma_scale_f32_16x16x128_f8f6f4 v[126:129], v[18:25], v[238:245], v[126:129], v214, v214 op_sel_hi:[0,0,0]
	v_mfma_scale_f32_16x16x128_f8f6f4 v[122:125], v[26:33], v[238:245], v[122:125], v214, v214 op_sel_hi:[0,0,0]
	v_mfma_scale_f32_16x16x128_f8f6f4 v[118:121], v[18:25], v[246:253], v[118:121], v214, v214 op_sel_hi:[0,0,0]
	v_mfma_scale_f32_16x16x128_f8f6f4 v[114:117], v[26:33], v[246:253], v[114:117], v214, v214 op_sel_hi:[0,0,0]
	s_nop 3
	v_mfma_scale_f32_16x16x128_f8f6f4 v[110:113], v[2:9], v[222:229], v[110:113], v214, v214 op_sel_hi:[0,0,0]
	v_mfma_scale_f32_16x16x128_f8f6f4 v[106:109], v[10:17], v[222:229], v[106:109], v214, v214 op_sel_hi:[0,0,0]
	v_mfma_scale_f32_16x16x128_f8f6f4 v[102:105], v[2:9], v[230:237], v[102:105], v214, v214 op_sel_hi:[0,0,0]
	v_mfma_scale_f32_16x16x128_f8f6f4 v[98:101], v[10:17], v[230:237], v[98:101], v214, v214 op_sel_hi:[0,0,0]
	v_mfma_scale_f32_16x16x128_f8f6f4 v[94:97], v[2:9], v[238:245], v[94:97], v214, v214 op_sel_hi:[0,0,0]
	v_mfma_scale_f32_16x16x128_f8f6f4 v[90:93], v[10:17], v[238:245], v[90:93], v214, v214 op_sel_hi:[0,0,0]
	v_mfma_scale_f32_16x16x128_f8f6f4 v[86:89], v[2:9], v[246:253], v[86:89], v214, v214 op_sel_hi:[0,0,0]
	v_mfma_scale_f32_16x16x128_f8f6f4 v[82:85], v[10:17], v[246:253], v[82:85], v214, v214 op_sel_hi:[0,0,0]
	s_add_i32 s30, s12, s48
	v_lshl_add_u64 v[204:205], s[40:41], 0, v[162:163]
	s_mov_b32 m0, s30
	ds_read_b128 v[222:225], v213 offset:16384
	ds_read_b128 v[226:229], v213 offset:17408
	ds_read_b128 v[230:233], v213 offset:18432
	ds_read_b128 v[234:237], v213 offset:19456
	ds_read_b128 v[238:241], v213 offset:20480
	ds_read_b128 v[242:245], v213 offset:21504
	ds_read_b128 v[246:249], v213 offset:22528
	ds_read_b128 v[250:253], v213 offset:23552
	global_load_lds_dwordx4 v[204:205], off
	v_lshl_add_u64 v[204:205], s[40:41], 0, v[164:165]
	s_add_i32 m0, s30, 0x2000
	s_add_i32 s30, s62, s48
	global_load_lds_dwordx4 v[204:205], off
	v_lshl_add_u64 v[204:205], s[40:41], 0, v[166:167]
	s_mov_b32 m0, s30
	v_mov_b32_e32 v203, v171
	global_load_lds_dwordx4 v[204:205], off
	v_lshl_add_u64 v[204:205], s[40:41], 0, v[168:169]
	s_add_i32 m0, s30, 0x2000
	s_nop 0
	global_load_lds_dwordx4 v[204:205], off
	s_mov_b32 m0, s52
	v_lshl_add_u64 v[204:205], s[42:43], 0, v[170:171]
	global_load_lds_dwordx4 v170, s[42:43]
	s_mov_b32 m0, s53
	s_nop 0
	global_load_lds_dwordx4 v202, s[42:43]
	s_waitcnt vmcnt(8)
	s_waitcnt lgkmcnt(0)
	v_lshl_add_u64 v[202:203], s[42:43], 0, v[202:203]
	s_barrier
	v_mfma_scale_f32_16x16x128_f8f6f4 v[78:81], v[18:25], v[222:229], v[78:81], v214, v214 op_sel_hi:[0,0,0]
	v_mfma_scale_f32_16x16x128_f8f6f4 v[74:77], v[26:33], v[222:229], v[74:77], v214, v214 op_sel_hi:[0,0,0]
	v_mfma_scale_f32_16x16x128_f8f6f4 v[70:73], v[18:25], v[230:237], v[70:73], v214, v214 op_sel_hi:[0,0,0]
	v_mfma_scale_f32_16x16x128_f8f6f4 v[66:69], v[26:33], v[230:237], v[66:69], v214, v214 op_sel_hi:[0,0,0]
	v_mfma_scale_f32_16x16x128_f8f6f4 v[62:65], v[18:25], v[238:245], v[62:65], v214, v214 op_sel_hi:[0,0,0]
	v_mfma_scale_f32_16x16x128_f8f6f4 v[58:61], v[26:33], v[238:245], v[58:61], v214, v214 op_sel_hi:[0,0,0]
	v_mfma_scale_f32_16x16x128_f8f6f4 v[54:57], v[18:25], v[246:253], v[54:57], v214, v214 op_sel_hi:[0,0,0]
	v_mfma_scale_f32_16x16x128_f8f6f4 v[50:53], v[26:33], v[246:253], v[50:53], v214, v214 op_sel_hi:[0,0,0]
	s_nop 3
	v_mfma_scale_f32_16x16x128_f8f6f4 v[46:49], v[2:9], v[222:229], v[46:49], v214, v214 op_sel_hi:[0,0,0]
	v_mfma_scale_f32_16x16x128_f8f6f4 v[42:45], v[10:17], v[222:229], v[42:45], v214, v214 op_sel_hi:[0,0,0]
	v_mfma_scale_f32_16x16x128_f8f6f4 v[38:41], v[2:9], v[230:237], v[38:41], v214, v214 op_sel_hi:[0,0,0]
	v_mfma_scale_f32_16x16x128_f8f6f4 v[34:37], v[10:17], v[230:237], v[34:37], v214, v214 op_sel_hi:[0,0,0]
	v_mfma_scale_f32_16x16x128_f8f6f4 v[146:149], v[2:9], v[238:245], v[146:149], v214, v214 op_sel_hi:[0,0,0]
	v_mfma_scale_f32_16x16x128_f8f6f4 v[150:153], v[10:17], v[238:245], v[150:153], v214, v214 op_sel_hi:[0,0,0]
	v_mfma_scale_f32_16x16x128_f8f6f4 v[154:157], v[2:9], v[246:253], v[154:157], v214, v214 op_sel_hi:[0,0,0]
	v_mfma_scale_f32_16x16x128_f8f6f4 v[158:161], v[10:17], v[246:253], v[158:161], v214, v214 op_sel_hi:[0,0,0]
	s_add_i32 s70, 0, 0x18000
	s_add_i32 s71, 0, 0x1c000
	v_add_u32_e32 v14, s70, v210
	v_add_u32_e32 v30, s71, v210
	ds_read_b128 v[2:5], v14
	ds_read_b128 v[6:9], v14 offset:1024
	ds_read_b128 v[10:13], v14 offset:2048
	ds_read_b128 v[14:17], v14 offset:3072
	ds_read_b128 v[18:21], v30
	ds_read_b128 v[22:25], v30 offset:1024
	ds_read_b128 v[26:29], v30 offset:2048
	ds_read_b128 v[30:33], v30 offset:3072
	s_mov_b32 m0, s58
	v_lshl_add_u64 v[200:201], s[42:43], 0, v[200:201]
	ds_read_b128 v[222:225], v213 offset:32768
	ds_read_b128 v[226:229], v213 offset:33792
	ds_read_b128 v[230:233], v213 offset:34816
	ds_read_b128 v[234:237], v213 offset:35840
	ds_read_b128 v[238:241], v213 offset:36864
	ds_read_b128 v[242:245], v213 offset:37888
	ds_read_b128 v[246:249], v213 offset:38912
	ds_read_b128 v[250:253], v213 offset:39936
	global_load_lds_dwordx4 v[200:201], off
	v_lshl_add_u64 v[198:199], s[42:43], 0, v[198:199]
	s_mov_b32 m0, s59
	s_nop 0
	global_load_lds_dwordx4 v[198:199], off
	s_waitcnt vmcnt(8)
	s_waitcnt lgkmcnt(0)
	s_barrier
; #define PG8_STAGE(bufoff, gbase, voff) do { _Pragma("unroll") for (int _i = 0; _i < 2; ++_i) \
;         __builtin_amdgcn_global_load_lds((const unsigned*)((const char*)(gbase) + (voff)[_i]), (PG8_LAS unsigned*)(lds + (bufoff) + ldsw + _i * 8192), 16, 0, 0); } while (0)
; #define PG8_WAIT_V(n) asm volatile("s_waitcnt vmcnt(" #n ")" ::: "memory")
; #define PG8_WAIT_L(n) asm volatile("s_waitcnt lgkmcnt(" #n ")" ::: "memory")
; #define PG8_BAR __builtin_amdgcn_s_barrier()
; #define PG8_SCHED __builtin_amdgcn_sched_barrier(0)
; template <class Epi, class Sched, bool ALIGN_EPI = true, bool F8 = false>
; __device__ __forceinline__ void gemm_phase(PG8_LAS unsigned char* lds, const Sched& S, const Epi& E) {
;     ...
;             PG8_WAIT_V(8); PG8_WAIT_L(0); PG8_BAR; PG8_MMA(0, 0, At, B0); PG8_MMA(0, 1, At, B1); PG8_BAR; PG8_SCHED;
;             PG8_LDA(At, 1, 1); PG8_STAGE(PG8_SB(1, 0), b3, voffB[0]); PG8_STAGE(PG8_SB(1, 1), b3, voffB[1]); PG8_STAGE(PG8_SA(1, 0), a3, vA2[0]);
;             PG8_WAIT_V(8); PG8_WAIT_L(0); PG8_BAR; PG8_MMA(1, 0, At, B0); PG8_MMA(1, 1, At, B1); PG8_BAR; PG8_SCHED;
	v_mfma_scale_f32_16x16x128_f8f6f4 v[142:145], v[2:9], v[222:229], v[142:145], v214, v214 op_sel_hi:[0,0,0]
	v_mfma_scale_f32_16x16x128_f8f6f4 v[138:141], v[10:17], v[222:229], v[138:141], v214, v214 op_sel_hi:[0,0,0]
	v_mfma_scale_f32_16x16x128_f8f6f4 v[134:137], v[2:9], v[230:237], v[134:137], v214, v214 op_sel_hi:[0,0,0]
	v_mfma_scale_f32_16x16x128_f8f6f4 v[130:133], v[10:17], v[230:237], v[130:133], v214, v214 op_sel_hi:[0,0,0]
	v_mfma_scale_f32_16x16x128_f8f6f4 v[126:129], v[2:9], v[238:245], v[126:129], v214, v214 op_sel_hi:[0,0,0]
	v_mfma_scale_f32_16x16x128_f8f6f4 v[122:125], v[10:17], v[238:245], v[122:125], v214, v214 op_sel_hi:[0,0,0]
	v_mfma_scale_f32_16x16x128_f8f6f4 v[118:121], v[2:9], v[246:253], v[118:121], v214, v214 op_sel_hi:[0,0,0]
	v_mfma_scale_f32_16x16x128_f8f6f4 v[114:117], v[10:17], v[246:253], v[114:117], v214, v214 op_sel_hi:[0,0,0]
	s_nop 3
	v_mfma_scale_f32_16x16x128_f8f6f4 v[110:113], v[18:25], v[222:229], v[110:113], v214, v214 op_sel_hi:[0,0,0]
	v_mfma_scale_f32_16x16x128_f8f6f4 v[106:109], v[26:33], v[222:229], v[106:109], v214, v214 op_sel_hi:[0,0,0]
	v_mfma_scale_f32_16x16x128_f8f6f4 v[102:105], v[18:25], v[230:237], v[102:105], v214, v214 op_sel_hi:[0,0,0]
	v_mfma_scale_f32_16x16x128_f8f6f4 v[98:101], v[26:33], v[230:237], v[98:101], v214, v214 op_sel_hi:[0,0,0]
	v_mfma_scale_f32_16x16x128_f8f6f4 v[94:97], v[18:25], v[238:245], v[94:97], v214, v214 op_sel_hi:[0,0,0]
	v_mfma_scale_f32_16x16x128_f8f6f4 v[90:93], v[26:33], v[238:245], v[90:93], v214, v214 op_sel_hi:[0,0,0]
	v_mfma_scale_f32_16x16x128_f8f6f4 v[86:89], v[18:25], v[246:253], v[86:89], v214, v214 op_sel_hi:[0,0,0]
	v_mfma_scale_f32_16x16x128_f8f6f4 v[82:85], v[26:33], v[246:253], v[82:85], v214, v214 op_sel_hi:[0,0,0]
	s_add_u32 s30, s40, 0x8000
	s_addc_u32 s31, s41, 0
	s_add_i32 s40, s70, s48
	v_lshl_add_u64 v[198:199], s[30:31], 0, v[162:163]
	s_mov_b32 m0, s40
	ds_read_b128 v[222:225], v213 offset:49152
	ds_read_b128 v[226:229], v213 offset:50176
	ds_read_b128 v[230:233], v213 offset:51200
	ds_read_b128 v[234:237], v213 offset:52224
	ds_read_b128 v[238:241], v213 offset:53248
	ds_read_b128 v[242:245], v213 offset:54272
	ds_read_b128 v[246:249], v213 offset:55296
	ds_read_b128 v[250:253], v213 offset:56320
	global_load_lds_dwordx4 v[198:199], off
	v_lshl_add_u64 v[198:199], s[30:31], 0, v[164:165]
	s_add_i32 m0, s40, 0x2000
	s_add_i32 s40, s71, s48
	global_load_lds_dwordx4 v[198:199], off
	v_lshl_add_u64 v[198:199], s[30:31], 0, v[166:167]
	s_mov_b32 m0, s40
	s_nop 0
	global_load_lds_dwordx4 v[198:199], off
	v_lshl_add_u64 v[198:199], s[30:31], 0, v[168:169]
	s_add_i32 m0, s40, 0x2000
	s_nop 0
	global_load_lds_dwordx4 v[198:199], off
	v_lshl_add_u64 v[198:199], v[204:205], 0, s[18:19]
	s_mov_b32 m0, s60
	s_nop 0
	global_load_lds_dwordx4 v[198:199], off
	v_lshl_add_u64 v[198:199], v[202:203], 0, s[18:19]
	s_mov_b32 m0, s61
	s_nop 0
	global_load_lds_dwordx4 v[198:199], off
	s_waitcnt vmcnt(8)
	s_waitcnt lgkmcnt(0)
	s_barrier
	v_mfma_scale_f32_16x16x128_f8f6f4 v[78:81], v[2:9], v[222:229], v[78:81], v214, v214 op_sel_hi:[0,0,0]
	v_mfma_scale_f32_16x16x128_f8f6f4 v[74:77], v[10:17], v[222:229], v[74:77], v214, v214 op_sel_hi:[0,0,0]
	v_mfma_scale_f32_16x16x128_f8f6f4 v[70:73], v[2:9], v[230:237], v[70:73], v214, v214 op_sel_hi:[0,0,0]
	v_mfma_scale_f32_16x16x128_f8f6f4 v[66:69], v[10:17], v[230:237], v[66:69], v214, v214 op_sel_hi:[0,0,0]
	v_mfma_scale_f32_16x16x128_f8f6f4 v[62:65], v[2:9], v[238:245], v[62:65], v214, v214 op_sel_hi:[0,0,0]
	v_mfma_scale_f32_16x16x128_f8f6f4 v[58:61], v[10:17], v[238:245], v[58:61], v214, v214 op_sel_hi:[0,0,0]
	v_mfma_scale_f32_16x16x128_f8f6f4 v[54:57], v[2:9], v[246:253], v[54:57], v214, v214 op_sel_hi:[0,0,0]
	v_mfma_scale_f32_16x16x128_f8f6f4 v[50:53], v[10:17], v[246:253], v[50:53], v214, v214 op_sel_hi:[0,0,0]
	s_nop 3
	v_mfma_scale_f32_16x16x128_f8f6f4 v[46:49], v[18:25], v[222:229], v[46:49], v214, v214 op_sel_hi:[0,0,0]
	v_mfma_scale_f32_16x16x128_f8f6f4 v[42:45], v[26:33], v[222:229], v[42:45], v214, v214 op_sel_hi:[0,0,0]
	v_mfma_scale_f32_16x16x128_f8f6f4 v[38:41], v[18:25], v[230:237], v[38:41], v214, v214 op_sel_hi:[0,0,0]
	v_mfma_scale_f32_16x16x128_f8f6f4 v[34:37], v[26:33], v[230:237], v[34:37], v214, v214 op_sel_hi:[0,0,0]
	v_mfma_scale_f32_16x16x128_f8f6f4 v[146:149], v[18:25], v[238:245], v[146:149], v214, v214 op_sel_hi:[0,0,0]
	v_mfma_scale_f32_16x16x128_f8f6f4 v[150:153], v[26:33], v[238:245], v[150:153], v214, v214 op_sel_hi:[0,0,0]
	v_mfma_scale_f32_16x16x128_f8f6f4 v[154:157], v[18:25], v[246:253], v[154:157], v214, v214 op_sel_hi:[0,0,0]
	v_mfma_scale_f32_16x16x128_f8f6f4 v[158:161], v[26:33], v[246:253], v[158:161], v214, v214 op_sel_hi:[0,0,0]
	s_add_i32 s69, s69, 2
	s_add_u32 s21, s21, 0x10000
	s_addc_u32 s68, s68, 0
	s_cmp_gt_u32 s69, 13
	s_cbranch_scc1 .LBB0_1062
	s_mov_b64 s[30:31], s[28:29]
	s_branch .Lh1_1058

; #define PG8_STAGE(bufoff, gbase, voff) do { _Pragma("unroll") for (int _i = 0; _i < 2; ++_i) \
;         __builtin_amdgcn_global_load_lds((const unsigned*)((const char*)(gbase) + (voff)[_i]), (PG8_LAS unsigned*)(lds + (bufoff) + ldsw + _i * 8192), 16, 0, 0); } while (0)
; #define PG8_WAIT_V(n) asm volatile("s_waitcnt vmcnt(" #n ")" ::: "memory")
; #define PG8_WAIT_L(n) asm volatile("s_waitcnt lgkmcnt(" #n ")" ::: "memory")
; #define PG8_BAR __builtin_amdgcn_s_barrier()
; #define PG8_SCHED __builtin_amdgcn_sched_barrier(0)
; template <class Epi, class Sched, bool ALIGN_EPI = true, bool F8 = false>
; __device__ __forceinline__ void gemm_phase(PG8_LAS unsigned char* lds, const Sched& S, const Epi& E) {
;     ...
;         const bool has_next = S.next(ui + 1, nxt);
;         const char* nA = has_next ? nxt.A : cA; const char* nB = has_next ? nxt.B : cB;
;         const int nt = cur.nt;
; #pragma unroll 1
;         for (int t = 0; t < nt; t += 2) {
;             const bool last = (t == nt - 2);
;             if constexpr (Sched::GATHER) { if (last && has_next) S.a_off(nxt, Rs, Cs, voffAn); }
;             const char* a1 = cA + (size_t)(t + 1) * kstep;
;             const char* a2 = last ? nA : cA + (size_t)(t + 2) * kstep; const char* b2 = last ? nB : cB + (size_t)(t + 2) * kstepB;
;             const char* a3 = a2 + kstep; const char* b3 = b2 + kstepB;
;             unsigned vA2[2][2];
; #pragma unroll
;             for (int h = 0; h < 2; ++h)
; #pragma unroll
;                 for (int i = 0; i < 2; ++i) { if constexpr (Sched::GATHER) vA2[h][i] = (last && has_next) ? voffAn[h][i] : voffA[h][i]; else vA2[h][i] = voffA[h][i]; }
;             PG8_LDB(B0, 0, 0); PG8_LDB(B1, 0, 1); PG8_SCHED; PG8_LDA(At, 0, 0); PG8_STAGE(PG8_SA(1, 1), a1, voffA[1]);
;             PG8_WAIT_V(8); PG8_WAIT_L(0); PG8_BAR; PG8_MMA(0, 0, At, B0); PG8_MMA(0, 1, At, B1); PG8_BAR; PG8_SCHED;
;             PG8_LDA(At, 0, 1); PG8_STAGE(PG8_SB(0, 0), b2, voffB[0]); PG8_STAGE(PG8_SB(0, 1), b2, voffB[1]); PG8_STAGE(PG8_SA(0, 0), a2, vA2[0]);
;             PG8_WAIT_V(8); PG8_WAIT_L(0); PG8_BAR; PG8_MMA(1, 0, At, B0); PG8_MMA(1, 1, At, B1); PG8_BAR; PG8_SCHED;
.LBB0_1137:
	s_add_u32 s23, s26, 0x10000
	s_addc_u32 s67, s27, 0
	s_add_u32 s24, s24, 0x8000
	s_addc_u32 s25, s25, 0
	s_mov_b32 s68, -2
	s_bitcmp1_b32 s3, 2
	s_cbranch_scc1 .Lh1e_33571
	s_setprio 1
.Lpk0_1138:
	ds_read_b128 v[18:21], v189
	ds_read_b128 v[22:25], v189 offset:1024
	ds_read_b128 v[26:29], v189 offset:2048
	ds_read_b128 v[30:33], v189 offset:3072
	ds_read_b128 v[2:5], v190
	ds_read_b128 v[6:9], v190 offset:1024
	ds_read_b128 v[10:13], v190 offset:2048
	ds_read_b128 v[14:17], v190 offset:3072
	s_add_u32 s26, s24, 0x8000
	s_addc_u32 s27, s25, 0
	s_cmp_eq_u32 s68, 4
	s_cselect_b32 s30, s16, s26
	s_cselect_b32 s31, s17, s27
	s_cselect_b32 s28, s18, s23
	s_cselect_b32 s29, s19, s67
	s_add_u32 s26, s30, 0x8000
	s_addc_u32 s27, s31, 0
	v_lshl_add_u64 v[226:227], s[24:25], 0, v[184:185]
	s_add_i32 m0, s44, 0xc000
	ds_read_b128 v[194:197], v191
	ds_read_b128 v[198:201], v191 offset:1024
	ds_read_b128 v[202:205], v191 offset:2048
	ds_read_b128 v[206:209], v191 offset:3072
	ds_read_b128 v[210:213], v191 offset:4096
	ds_read_b128 v[214:217], v191 offset:5120
	ds_read_b128 v[218:221], v191 offset:6144
	ds_read_b128 v[222:225], v191 offset:7168
	global_load_lds_dwordx4 v[226:227], off
	v_lshl_add_u64 v[226:227], s[24:25], 0, v[182:183]
	s_add_i32 m0, s44, 0xe000
	s_nop 0
	global_load_lds_dwordx4 v[226:227], off
	s_waitcnt vmcnt(8)
	s_waitcnt lgkmcnt(0)
	v_mfma_scale_f32_16x16x128_f8f6f4 v[158:161], v[18:25], v[194:201], 0, v192, v192 op_sel_hi:[0,0,0]
	v_mfma_scale_f32_16x16x128_f8f6f4 v[154:157], v[26:33], v[194:201], 0, v192, v192 op_sel_hi:[0,0,0]
	v_mfma_scale_f32_16x16x128_f8f6f4 v[142:145], v[18:25], v[202:209], 0, v192, v192 op_sel_hi:[0,0,0]
	v_mfma_scale_f32_16x16x128_f8f6f4 v[138:141], v[26:33], v[202:209], 0, v192, v192 op_sel_hi:[0,0,0]
	v_mfma_scale_f32_16x16x128_f8f6f4 v[126:129], v[18:25], v[210:217], 0, v192, v192 op_sel_hi:[0,0,0]
	v_mfma_scale_f32_16x16x128_f8f6f4 v[122:125], v[26:33], v[210:217], 0, v192, v192 op_sel_hi:[0,0,0]
	v_mfma_scale_f32_16x16x128_f8f6f4 v[110:113], v[18:25], v[218:225], 0, v192, v192 op_sel_hi:[0,0,0]
	v_mfma_scale_f32_16x16x128_f8f6f4 v[106:109], v[26:33], v[218:225], 0, v192, v192 op_sel_hi:[0,0,0]
	s_nop 3
	v_mfma_scale_f32_16x16x128_f8f6f4 v[150:153], v[2:9], v[194:201], 0, v192, v192 op_sel_hi:[0,0,0]
	v_mfma_scale_f32_16x16x128_f8f6f4 v[146:149], v[10:17], v[194:201], 0, v192, v192 op_sel_hi:[0,0,0]
	v_mfma_scale_f32_16x16x128_f8f6f4 v[134:137], v[2:9], v[202:209], 0, v192, v192 op_sel_hi:[0,0,0]
	v_mfma_scale_f32_16x16x128_f8f6f4 v[130:133], v[10:17], v[202:209], 0, v192, v192 op_sel_hi:[0,0,0]
	v_mfma_scale_f32_16x16x128_f8f6f4 v[118:121], v[2:9], v[210:217], 0, v192, v192 op_sel_hi:[0,0,0]
	v_mfma_scale_f32_16x16x128_f8f6f4 v[114:117], v[10:17], v[210:217], 0, v192, v192 op_sel_hi:[0,0,0]
	v_mfma_scale_f32_16x16x128_f8f6f4 v[102:105], v[2:9], v[218:225], 0, v192, v192 op_sel_hi:[0,0,0]
	v_mfma_scale_f32_16x16x128_f8f6f4 v[98:101], v[10:17], v[218:225], 0, v192, v192 op_sel_hi:[0,0,0]
	s_barrier
	s_add_i32 s69, s53, s43
	v_lshl_add_u64 v[226:227], s[28:29], 0, v[164:165]
	s_mov_b32 m0, s69
	ds_read_b128 v[194:197], v191 offset:16384
	ds_read_b128 v[198:201], v191 offset:17408
	ds_read_b128 v[202:205], v191 offset:18432
	ds_read_b128 v[206:209], v191 offset:19456
	ds_read_b128 v[210:213], v191 offset:20480
	ds_read_b128 v[214:217], v191 offset:21504
	ds_read_b128 v[218:221], v191 offset:22528
	ds_read_b128 v[222:225], v191 offset:23552
	global_load_lds_dwordx4 v[226:227], off
	v_lshl_add_u64 v[228:229], s[28:29], 0, v[166:167]
	s_add_i32 m0, s69, 0x2000
	s_add_i32 s69, s58, s43
	global_load_lds_dwordx4 v[228:229], off
	v_lshl_add_u64 v[226:227], v[226:227], 0, s[4:5]
	s_mov_b32 m0, s69
	s_nop 0
	global_load_lds_dwordx4 v[226:227], off
	v_lshl_add_u64 v[226:227], v[228:229], 0, s[4:5]
	s_add_i32 m0, s69, 0x2000
	s_nop 0
	global_load_lds_dwordx4 v[226:227], off
	v_lshl_add_u64 v[226:227], s[30:31], 0, v[168:169]
	s_mov_b32 m0, s44
	s_nop 0
	global_load_lds_dwordx4 v[226:227], off
	v_lshl_add_u64 v[226:227], s[30:31], 0, v[170:171]
	s_mov_b32 m0, s45
	s_nop 0
	global_load_lds_dwordx4 v[226:227], off
	s_waitcnt vmcnt(8)
	s_waitcnt lgkmcnt(0)
	v_mfma_scale_f32_16x16x128_f8f6f4 v[94:97], v[18:25], v[194:201], 0, v192, v192 op_sel_hi:[0,0,0]
	v_mfma_scale_f32_16x16x128_f8f6f4 v[90:93], v[26:33], v[194:201], 0, v192, v192 op_sel_hi:[0,0,0]
	v_mfma_scale_f32_16x16x128_f8f6f4 v[78:81], v[18:25], v[202:209], 0, v192, v192 op_sel_hi:[0,0,0]
	v_mfma_scale_f32_16x16x128_f8f6f4 v[74:77], v[26:33], v[202:209], 0, v192, v192 op_sel_hi:[0,0,0]
	v_mfma_scale_f32_16x16x128_f8f6f4 v[62:65], v[18:25], v[210:217], 0, v192, v192 op_sel_hi:[0,0,0]
	v_mfma_scale_f32_16x16x128_f8f6f4 v[58:61], v[26:33], v[210:217], 0, v192, v192 op_sel_hi:[0,0,0]
	v_mfma_scale_f32_16x16x128_f8f6f4 v[46:49], v[18:25], v[218:225], 0, v192, v192 op_sel_hi:[0,0,0]
	v_mfma_scale_f32_16x16x128_f8f6f4 v[42:45], v[26:33], v[218:225], 0, v192, v192 op_sel_hi:[0,0,0]
	s_nop 3
	v_mfma_scale_f32_16x16x128_f8f6f4 v[86:89], v[2:9], v[194:201], 0, v192, v192 op_sel_hi:[0,0,0]
	v_mfma_scale_f32_16x16x128_f8f6f4 v[82:85], v[10:17], v[194:201], 0, v192, v192 op_sel_hi:[0,0,0]
	v_mfma_scale_f32_16x16x128_f8f6f4 v[70:73], v[2:9], v[202:209], 0, v192, v192 op_sel_hi:[0,0,0]
	v_mfma_scale_f32_16x16x128_f8f6f4 v[66:69], v[10:17], v[202:209], 0, v192, v192 op_sel_hi:[0,0,0]
	v_mfma_scale_f32_16x16x128_f8f6f4 v[54:57], v[2:9], v[210:217], 0, v192, v192 op_sel_hi:[0,0,0]
	v_mfma_scale_f32_16x16x128_f8f6f4 v[50:53], v[10:17], v[210:217], 0, v192, v192 op_sel_hi:[0,0,0]
	v_mfma_scale_f32_16x16x128_f8f6f4 v[38:41], v[2:9], v[218:225], 0, v192, v192 op_sel_hi:[0,0,0]
	v_mfma_scale_f32_16x16x128_f8f6f4 v[34:37], v[10:17], v[218:225], 0, v192, v192 op_sel_hi:[0,0,0]
	s_barrier
; #define PG8_STAGE(bufoff, gbase, voff) do { _Pragma("unroll") for (int _i = 0; _i < 2; ++_i) \
;         __builtin_amdgcn_global_load_lds((const unsigned*)((const char*)(gbase) + (voff)[_i]), (PG8_LAS unsigned*)(lds + (bufoff) + ldsw + _i * 8192), 16, 0, 0); } while (0)
; #define PG8_WAIT_V(n) asm volatile("s_waitcnt vmcnt(" #n ")" ::: "memory")
; #define PG8_WAIT_L(n) asm volatile("s_waitcnt lgkmcnt(" #n ")" ::: "memory")
; #define PG8_BAR __builtin_amdgcn_s_barrier()
; #define PG8_SCHED __builtin_amdgcn_sched_barrier(0)
; template <class Epi, class Sched, bool ALIGN_EPI = true, bool F8 = false>
; __device__ __forceinline__ void gemm_phase(PG8_LAS unsigned char* lds, const Sched& S, const Epi& E) {
;     ...
;             PG8_LDB(B0, 1, 0); PG8_LDB(B1, 1, 1); PG8_SCHED; PG8_LDA(At, 1, 0); PG8_STAGE(PG8_SA(0, 1), a2, vA2[1]);
;             PG8_WAIT_V(8); PG8_WAIT_L(0); PG8_BAR; PG8_MMA(0, 0, At, B0); PG8_MMA(0, 1, At, B1); PG8_BAR; PG8_SCHED;
;             PG8_LDA(At, 1, 1); PG8_STAGE(PG8_SB(1, 0), b3, voffB[0]); PG8_STAGE(PG8_SB(1, 1), b3, voffB[1]); PG8_STAGE(PG8_SA(1, 0), a3, vA2[0]);
;             PG8_WAIT_V(8); PG8_WAIT_L(0); PG8_BAR; PG8_MMA(1, 0, At, B0); PG8_MMA(1, 1, At, B1); PG8_BAR; PG8_SCHED;
	s_add_i32 s69, 0, 0x18000
	s_add_i32 s70, 0, 0x1c000
	v_add_u32_e32 v14, s69, v187
	v_add_u32_e32 v30, s70, v187
	ds_read_b128 v[2:5], v14
	ds_read_b128 v[6:9], v14 offset:1024
	ds_read_b128 v[10:13], v14 offset:2048
	ds_read_b128 v[14:17], v14 offset:3072
	ds_read_b128 v[18:21], v30
	ds_read_b128 v[22:25], v30 offset:1024
	ds_read_b128 v[26:29], v30 offset:2048
	ds_read_b128 v[30:33], v30 offset:3072
	s_mov_b32 m0, s46
	v_lshl_add_u64 v[226:227], s[30:31], 0, v[172:173]
	ds_read_b128 v[194:197], v191 offset:32768
	ds_read_b128 v[198:201], v191 offset:33792
	ds_read_b128 v[202:205], v191 offset:34816
	ds_read_b128 v[206:209], v191 offset:35840
	ds_read_b128 v[210:213], v191 offset:36864
	ds_read_b128 v[214:217], v191 offset:37888
	ds_read_b128 v[218:221], v191 offset:38912
	ds_read_b128 v[222:225], v191 offset:39936
	global_load_lds_dwordx4 v[226:227], off
	v_lshl_add_u64 v[226:227], s[30:31], 0, v[174:175]
	s_mov_b32 m0, s47
	s_nop 0
	global_load_lds_dwordx4 v[226:227], off
	s_waitcnt vmcnt(8)
	s_waitcnt lgkmcnt(0)
	v_mfma_scale_f32_16x16x128_f8f6f4 v[158:161], v[2:9], v[194:201], v[158:161], v192, v192 op_sel_hi:[0,0,0]
	v_mfma_scale_f32_16x16x128_f8f6f4 v[154:157], v[10:17], v[194:201], v[154:157], v192, v192 op_sel_hi:[0,0,0]
	v_mfma_scale_f32_16x16x128_f8f6f4 v[142:145], v[2:9], v[202:209], v[142:145], v192, v192 op_sel_hi:[0,0,0]
	v_mfma_scale_f32_16x16x128_f8f6f4 v[138:141], v[10:17], v[202:209], v[138:141], v192, v192 op_sel_hi:[0,0,0]
	v_mfma_scale_f32_16x16x128_f8f6f4 v[126:129], v[2:9], v[210:217], v[126:129], v192, v192 op_sel_hi:[0,0,0]
	v_mfma_scale_f32_16x16x128_f8f6f4 v[122:125], v[10:17], v[210:217], v[122:125], v192, v192 op_sel_hi:[0,0,0]
	v_mfma_scale_f32_16x16x128_f8f6f4 v[110:113], v[2:9], v[218:225], v[110:113], v192, v192 op_sel_hi:[0,0,0]
	v_mfma_scale_f32_16x16x128_f8f6f4 v[106:109], v[10:17], v[218:225], v[106:109], v192, v192 op_sel_hi:[0,0,0]
	s_nop 3
	v_mfma_scale_f32_16x16x128_f8f6f4 v[150:153], v[18:25], v[194:201], v[150:153], v192, v192 op_sel_hi:[0,0,0]
	v_mfma_scale_f32_16x16x128_f8f6f4 v[146:149], v[26:33], v[194:201], v[146:149], v192, v192 op_sel_hi:[0,0,0]
	v_mfma_scale_f32_16x16x128_f8f6f4 v[134:137], v[18:25], v[202:209], v[134:137], v192, v192 op_sel_hi:[0,0,0]
	v_mfma_scale_f32_16x16x128_f8f6f4 v[130:133], v[26:33], v[202:209], v[130:133], v192, v192 op_sel_hi:[0,0,0]
	v_mfma_scale_f32_16x16x128_f8f6f4 v[118:121], v[18:25], v[210:217], v[118:121], v192, v192 op_sel_hi:[0,0,0]
	v_mfma_scale_f32_16x16x128_f8f6f4 v[114:117], v[26:33], v[210:217], v[114:117], v192, v192 op_sel_hi:[0,0,0]
	v_mfma_scale_f32_16x16x128_f8f6f4 v[102:105], v[18:25], v[218:225], v[102:105], v192, v192 op_sel_hi:[0,0,0]
	v_mfma_scale_f32_16x16x128_f8f6f4 v[98:101], v[26:33], v[218:225], v[98:101], v192, v192 op_sel_hi:[0,0,0]
	s_barrier
	s_add_u32 s28, s28, 0x8000
	s_addc_u32 s29, s29, 0
	s_add_i32 s30, s69, s43
	v_lshl_add_u64 v[226:227], s[28:29], 0, v[164:165]
	s_mov_b32 m0, s30
	ds_read_b128 v[194:197], v191 offset:49152
	ds_read_b128 v[198:201], v191 offset:50176
	ds_read_b128 v[202:205], v191 offset:51200
	ds_read_b128 v[206:209], v191 offset:52224
	ds_read_b128 v[210:213], v191 offset:53248
	ds_read_b128 v[214:217], v191 offset:54272
	ds_read_b128 v[218:221], v191 offset:55296
	ds_read_b128 v[222:225], v191 offset:56320
	global_load_lds_dwordx4 v[226:227], off
	v_lshl_add_u64 v[226:227], s[28:29], 0, v[166:167]
	s_add_i32 m0, s30, 0x2000
	s_add_i32 s30, s70, s43
	global_load_lds_dwordx4 v[226:227], off
	v_lshl_add_u64 v[226:227], s[28:29], 0, v[178:179]
	s_mov_b32 m0, s30
	s_nop 0
	global_load_lds_dwordx4 v[226:227], off
	v_lshl_add_u64 v[226:227], s[28:29], 0, v[180:181]
	s_add_i32 m0, s30, 0x2000
	s_nop 0
	global_load_lds_dwordx4 v[226:227], off
	v_lshl_add_u64 v[226:227], s[26:27], 0, v[168:169]
	s_mov_b32 m0, s51
	s_nop 0
	global_load_lds_dwordx4 v[226:227], off
	v_lshl_add_u64 v[226:227], s[26:27], 0, v[170:171]
	s_mov_b32 m0, s52
	s_nop 0
	global_load_lds_dwordx4 v[226:227], off
	s_waitcnt vmcnt(8)
	s_waitcnt lgkmcnt(0)
	v_mfma_scale_f32_16x16x128_f8f6f4 v[94:97], v[2:9], v[194:201], v[94:97], v192, v192 op_sel_hi:[0,0,0]
	v_mfma_scale_f32_16x16x128_f8f6f4 v[90:93], v[10:17], v[194:201], v[90:93], v192, v192 op_sel_hi:[0,0,0]
	v_mfma_scale_f32_16x16x128_f8f6f4 v[78:81], v[2:9], v[202:209], v[78:81], v192, v192 op_sel_hi:[0,0,0]
	v_mfma_scale_f32_16x16x128_f8f6f4 v[74:77], v[10:17], v[202:209], v[74:77], v192, v192 op_sel_hi:[0,0,0]
	v_mfma_scale_f32_16x16x128_f8f6f4 v[62:65], v[2:9], v[210:217], v[62:65], v192, v192 op_sel_hi:[0,0,0]
	v_mfma_scale_f32_16x16x128_f8f6f4 v[58:61], v[10:17], v[210:217], v[58:61], v192, v192 op_sel_hi:[0,0,0]
	v_mfma_scale_f32_16x16x128_f8f6f4 v[46:49], v[2:9], v[218:225], v[46:49], v192, v192 op_sel_hi:[0,0,0]
	v_mfma_scale_f32_16x16x128_f8f6f4 v[42:45], v[10:17], v[218:225], v[42:45], v192, v192 op_sel_hi:[0,0,0]
	s_nop 3
	v_mfma_scale_f32_16x16x128_f8f6f4 v[86:89], v[18:25], v[194:201], v[86:89], v192, v192 op_sel_hi:[0,0,0]
	v_mfma_scale_f32_16x16x128_f8f6f4 v[82:85], v[26:33], v[194:201], v[82:85], v192, v192 op_sel_hi:[0,0,0]
	v_mfma_scale_f32_16x16x128_f8f6f4 v[70:73], v[18:25], v[202:209], v[70:73], v192, v192 op_sel_hi:[0,0,0]
	v_mfma_scale_f32_16x16x128_f8f6f4 v[66:69], v[26:33], v[202:209], v[66:69], v192, v192 op_sel_hi:[0,0,0]
	v_mfma_scale_f32_16x16x128_f8f6f4 v[54:57], v[18:25], v[210:217], v[54:57], v192, v192 op_sel_hi:[0,0,0]
	v_mfma_scale_f32_16x16x128_f8f6f4 v[50:53], v[26:33], v[210:217], v[50:53], v192, v192 op_sel_hi:[0,0,0]
	v_mfma_scale_f32_16x16x128_f8f6f4 v[38:41], v[18:25], v[218:225], v[38:41], v192, v192 op_sel_hi:[0,0,0]
	v_mfma_scale_f32_16x16x128_f8f6f4 v[34:37], v[26:33], v[218:225], v[34:37], v192, v192 op_sel_hi:[0,0,0]
	s_barrier
	s_add_i32 s68, s68, 2
	s_add_u32 s23, s23, 0x10000
	s_addc_u32 s67, s67, 0
	s_add_u32 s24, s24, 0x10000
	s_addc_u32 s25, s25, 0
	s_cmp_gt_u32 s68, 5
	s_cbranch_scc0 .LBB0_1138
	s_branch .Lfx_33571
; #define PG8_STAGE(bufoff, gbase, voff) do { _Pragma("unroll") for (int _i = 0; _i < 2; ++_i) \
;         __builtin_amdgcn_global_load_lds((const unsigned*)((const char*)(gbase) + (voff)[_i]), (PG8_LAS unsigned*)(lds + (bufoff) + ldsw + _i * 8192), 16, 0, 0); } while (0)
; #define PG8_WAIT_V(n) asm volatile("s_waitcnt vmcnt(" #n ")" ::: "memory")
; #define PG8_WAIT_L(n) asm volatile("s_waitcnt lgkmcnt(" #n ")" ::: "memory")
; #define PG8_BAR __builtin_amdgcn_s_barrier()
; #define PG8_SCHED __builtin_amdgcn_sched_barrier(0)
; template <class Epi, class Sched, bool ALIGN_EPI = true, bool F8 = false>
; __device__ __forceinline__ void gemm_phase(PG8_LAS unsigned char* lds, const Sched& S, const Epi& E) {
;     ...
;             PG8_LDB(B0, 0, 0); PG8_LDB(B1, 0, 1); PG8_SCHED; PG8_LDA(At, 0, 0); PG8_STAGE(PG8_SA(1, 1), a1, voffA[1]);
;             PG8_WAIT_V(8); PG8_WAIT_L(0); PG8_BAR; PG8_MMA(0, 0, At, B0); PG8_MMA(0, 1, At, B1); PG8_BAR; PG8_SCHED;
;             PG8_LDA(At, 0, 1); PG8_STAGE(PG8_SB(0, 0), b2, voffB[0]); PG8_STAGE(PG8_SB(0, 1), b2, voffB[1]); PG8_STAGE(PG8_SA(0, 0), a2, vA2[0]);
;             PG8_WAIT_V(8); PG8_WAIT_L(0); PG8_BAR; PG8_MMA(1, 0, At, B0); PG8_MMA(1, 1, At, B1); PG8_BAR; PG8_SCHED;
.LBB0_1138:
	ds_read_b128 v[18:21], v189
	ds_read_b128 v[22:25], v189 offset:1024
	ds_read_b128 v[26:29], v189 offset:2048
	ds_read_b128 v[30:33], v189 offset:3072
	ds_read_b128 v[2:5], v190
	ds_read_b128 v[6:9], v190 offset:1024
	ds_read_b128 v[10:13], v190 offset:2048
	ds_read_b128 v[14:17], v190 offset:3072
	s_add_u32 s26, s24, 0x8000
	s_addc_u32 s27, s25, 0
	s_cmp_eq_u32 s68, 4
	s_cselect_b32 s30, s16, s26
	s_cselect_b32 s31, s17, s27
	s_cselect_b32 s28, s18, s23
	s_cselect_b32 s29, s19, s67
	s_add_u32 s26, s30, 0x8000
	s_addc_u32 s27, s31, 0
	v_lshl_add_u64 v[226:227], s[24:25], 0, v[184:185]
	s_add_i32 m0, s44, 0xc000
	ds_read_b128 v[194:197], v191
	ds_read_b128 v[198:201], v191 offset:1024
	ds_read_b128 v[202:205], v191 offset:2048
	ds_read_b128 v[206:209], v191 offset:3072
	ds_read_b128 v[210:213], v191 offset:4096
	ds_read_b128 v[214:217], v191 offset:5120
	ds_read_b128 v[218:221], v191 offset:6144
	ds_read_b128 v[222:225], v191 offset:7168
	global_load_lds_dwordx4 v[226:227], off
	v_lshl_add_u64 v[226:227], s[24:25], 0, v[182:183]
	s_add_i32 m0, s44, 0xe000
	s_nop 0
	global_load_lds_dwordx4 v[226:227], off
	s_waitcnt vmcnt(8)
	s_waitcnt lgkmcnt(0)
	v_mfma_scale_f32_16x16x128_f8f6f4 v[158:161], v[18:25], v[194:201], v[158:161], v192, v192 op_sel_hi:[0,0,0]
	v_mfma_scale_f32_16x16x128_f8f6f4 v[154:157], v[26:33], v[194:201], v[154:157], v192, v192 op_sel_hi:[0,0,0]
	v_mfma_scale_f32_16x16x128_f8f6f4 v[142:145], v[18:25], v[202:209], v[142:145], v192, v192 op_sel_hi:[0,0,0]
	v_mfma_scale_f32_16x16x128_f8f6f4 v[138:141], v[26:33], v[202:209], v[138:141], v192, v192 op_sel_hi:[0,0,0]
	v_mfma_scale_f32_16x16x128_f8f6f4 v[126:129], v[18:25], v[210:217], v[126:129], v192, v192 op_sel_hi:[0,0,0]
	v_mfma_scale_f32_16x16x128_f8f6f4 v[122:125], v[26:33], v[210:217], v[122:125], v192, v192 op_sel_hi:[0,0,0]
	v_mfma_scale_f32_16x16x128_f8f6f4 v[110:113], v[18:25], v[218:225], v[110:113], v192, v192 op_sel_hi:[0,0,0]
	v_mfma_scale_f32_16x16x128_f8f6f4 v[106:109], v[26:33], v[218:225], v[106:109], v192, v192 op_sel_hi:[0,0,0]
	s_nop 3
	v_mfma_scale_f32_16x16x128_f8f6f4 v[150:153], v[2:9], v[194:201], v[150:153], v192, v192 op_sel_hi:[0,0,0]
	v_mfma_scale_f32_16x16x128_f8f6f4 v[146:149], v[10:17], v[194:201], v[146:149], v192, v192 op_sel_hi:[0,0,0]
	v_mfma_scale_f32_16x16x128_f8f6f4 v[134:137], v[2:9], v[202:209], v[134:137], v192, v192 op_sel_hi:[0,0,0]
	v_mfma_scale_f32_16x16x128_f8f6f4 v[130:133], v[10:17], v[202:209], v[130:133], v192, v192 op_sel_hi:[0,0,0]
	v_mfma_scale_f32_16x16x128_f8f6f4 v[118:121], v[2:9], v[210:217], v[118:121], v192, v192 op_sel_hi:[0,0,0]
	v_mfma_scale_f32_16x16x128_f8f6f4 v[114:117], v[10:17], v[210:217], v[114:117], v192, v192 op_sel_hi:[0,0,0]
	v_mfma_scale_f32_16x16x128_f8f6f4 v[102:105], v[2:9], v[218:225], v[102:105], v192, v192 op_sel_hi:[0,0,0]
	v_mfma_scale_f32_16x16x128_f8f6f4 v[98:101], v[10:17], v[218:225], v[98:101], v192, v192 op_sel_hi:[0,0,0]
	s_barrier
	s_add_i32 s69, s53, s43
	v_lshl_add_u64 v[226:227], s[28:29], 0, v[164:165]
	s_mov_b32 m0, s69
	ds_read_b128 v[194:197], v191 offset:16384
	ds_read_b128 v[198:201], v191 offset:17408
	ds_read_b128 v[202:205], v191 offset:18432
	ds_read_b128 v[206:209], v191 offset:19456
	ds_read_b128 v[210:213], v191 offset:20480
	ds_read_b128 v[214:217], v191 offset:21504
	ds_read_b128 v[218:221], v191 offset:22528
	ds_read_b128 v[222:225], v191 offset:23552
	global_load_lds_dwordx4 v[226:227], off
	v_lshl_add_u64 v[228:229], s[28:29], 0, v[166:167]
	s_add_i32 m0, s69, 0x2000
	s_add_i32 s69, s58, s43
	global_load_lds_dwordx4 v[228:229], off
	v_lshl_add_u64 v[226:227], v[226:227], 0, s[4:5]
	s_mov_b32 m0, s69
	s_nop 0
	global_load_lds_dwordx4 v[226:227], off
	v_lshl_add_u64 v[226:227], v[228:229], 0, s[4:5]
	s_add_i32 m0, s69, 0x2000
	s_nop 0
	global_load_lds_dwordx4 v[226:227], off
	v_lshl_add_u64 v[226:227], s[30:31], 0, v[168:169]
	s_mov_b32 m0, s44
	s_nop 0
	global_load_lds_dwordx4 v[226:227], off
	v_lshl_add_u64 v[226:227], s[30:31], 0, v[170:171]
	s_mov_b32 m0, s45
	s_nop 0
	global_load_lds_dwordx4 v[226:227], off
	s_waitcnt vmcnt(8)
	s_waitcnt lgkmcnt(0)
	v_mfma_scale_f32_16x16x128_f8f6f4 v[94:97], v[18:25], v[194:201], v[94:97], v192, v192 op_sel_hi:[0,0,0]
	v_mfma_scale_f32_16x16x128_f8f6f4 v[90:93], v[26:33], v[194:201], v[90:93], v192, v192 op_sel_hi:[0,0,0]
	v_mfma_scale_f32_16x16x128_f8f6f4 v[78:81], v[18:25], v[202:209], v[78:81], v192, v192 op_sel_hi:[0,0,0]
	v_mfma_scale_f32_16x16x128_f8f6f4 v[74:77], v[26:33], v[202:209], v[74:77], v192, v192 op_sel_hi:[0,0,0]
	v_mfma_scale_f32_16x16x128_f8f6f4 v[62:65], v[18:25], v[210:217], v[62:65], v192, v192 op_sel_hi:[0,0,0]
	v_mfma_scale_f32_16x16x128_f8f6f4 v[58:61], v[26:33], v[210:217], v[58:61], v192, v192 op_sel_hi:[0,0,0]
	v_mfma_scale_f32_16x16x128_f8f6f4 v[46:49], v[18:25], v[218:225], v[46:49], v192, v192 op_sel_hi:[0,0,0]
	v_mfma_scale_f32_16x16x128_f8f6f4 v[42:45], v[26:33], v[218:225], v[42:45], v192, v192 op_sel_hi:[0,0,0]
	s_nop 3
	v_mfma_scale_f32_16x16x128_f8f6f4 v[86:89], v[2:9], v[194:201], v[86:89], v192, v192 op_sel_hi:[0,0,0]
	v_mfma_scale_f32_16x16x128_f8f6f4 v[82:85], v[10:17], v[194:201], v[82:85], v192, v192 op_sel_hi:[0,0,0]
	v_mfma_scale_f32_16x16x128_f8f6f4 v[70:73], v[2:9], v[202:209], v[70:73], v192, v192 op_sel_hi:[0,0,0]
	v_mfma_scale_f32_16x16x128_f8f6f4 v[66:69], v[10:17], v[202:209], v[66:69], v192, v192 op_sel_hi:[0,0,0]
	v_mfma_scale_f32_16x16x128_f8f6f4 v[54:57], v[2:9], v[210:217], v[54:57], v192, v192 op_sel_hi:[0,0,0]
	v_mfma_scale_f32_16x16x128_f8f6f4 v[50:53], v[10:17], v[210:217], v[50:53], v192, v192 op_sel_hi:[0,0,0]
	v_mfma_scale_f32_16x16x128_f8f6f4 v[38:41], v[2:9], v[218:225], v[38:41], v192, v192 op_sel_hi:[0,0,0]
	v_mfma_scale_f32_16x16x128_f8f6f4 v[34:37], v[10:17], v[218:225], v[34:37], v192, v192 op_sel_hi:[0,0,0]
	s_barrier
; #define PG8_STAGE(bufoff, gbase, voff) do { _Pragma("unroll") for (int _i = 0; _i < 2; ++_i) \
;         __builtin_amdgcn_global_load_lds((const unsigned*)((const char*)(gbase) + (voff)[_i]), (PG8_LAS unsigned*)(lds + (bufoff) + ldsw + _i * 8192), 16, 0, 0); } while (0)
; #define PG8_WAIT_V(n) asm volatile("s_waitcnt vmcnt(" #n ")" ::: "memory")
; #define PG8_WAIT_L(n) asm volatile("s_waitcnt lgkmcnt(" #n ")" ::: "memory")
; #define PG8_BAR __builtin_amdgcn_s_barrier()
; #define PG8_SCHED __builtin_amdgcn_sched_barrier(0)
; template <class Epi, class Sched, bool ALIGN_EPI = true, bool F8 = false>
; __device__ __forceinline__ void gemm_phase(PG8_LAS unsigned char* lds, const Sched& S, const Epi& E) {
;     ...
;             PG8_LDB(B0, 1, 0); PG8_LDB(B1, 1, 1); PG8_SCHED; PG8_LDA(At, 1, 0); PG8_STAGE(PG8_SA(0, 1), a2, vA2[1]);
;             PG8_WAIT_V(8); PG8_WAIT_L(0); PG8_BAR; PG8_MMA(0, 0, At, B0); PG8_MMA(0, 1, At, B1); PG8_BAR; PG8_SCHED;
;             PG8_LDA(At, 1, 1); PG8_STAGE(PG8_SB(1, 0), b3, voffB[0]); PG8_STAGE(PG8_SB(1, 1), b3, voffB[1]); PG8_STAGE(PG8_SA(1, 0), a3, vA2[0]);
;             PG8_WAIT_V(8); PG8_WAIT_L(0); PG8_BAR; PG8_MMA(1, 0, At, B0); PG8_MMA(1, 1, At, B1); PG8_BAR; PG8_SCHED;
	s_add_i32 s69, 0, 0x18000
	s_add_i32 s70, 0, 0x1c000
	v_add_u32_e32 v14, s69, v187
	v_add_u32_e32 v30, s70, v187
	ds_read_b128 v[2:5], v14
	ds_read_b128 v[6:9], v14 offset:1024
	ds_read_b128 v[10:13], v14 offset:2048
	ds_read_b128 v[14:17], v14 offset:3072
	ds_read_b128 v[18:21], v30
	ds_read_b128 v[22:25], v30 offset:1024
	ds_read_b128 v[26:29], v30 offset:2048
	ds_read_b128 v[30:33], v30 offset:3072
	s_mov_b32 m0, s46
	v_lshl_add_u64 v[226:227], s[30:31], 0, v[172:173]
	ds_read_b128 v[194:197], v191 offset:32768
	ds_read_b128 v[198:201], v191 offset:33792
	ds_read_b128 v[202:205], v191 offset:34816
	ds_read_b128 v[206:209], v191 offset:35840
	ds_read_b128 v[210:213], v191 offset:36864
	ds_read_b128 v[214:217], v191 offset:37888
	ds_read_b128 v[218:221], v191 offset:38912
	ds_read_b128 v[222:225], v191 offset:39936
	global_load_lds_dwordx4 v[226:227], off
	v_lshl_add_u64 v[226:227], s[30:31], 0, v[174:175]
	s_mov_b32 m0, s47
	s_nop 0
	global_load_lds_dwordx4 v[226:227], off
	s_waitcnt vmcnt(8)
	s_waitcnt lgkmcnt(0)
	v_mfma_scale_f32_16x16x128_f8f6f4 v[158:161], v[2:9], v[194:201], v[158:161], v192, v192 op_sel_hi:[0,0,0]
	v_mfma_scale_f32_16x16x128_f8f6f4 v[154:157], v[10:17], v[194:201], v[154:157], v192, v192 op_sel_hi:[0,0,0]
	v_mfma_scale_f32_16x16x128_f8f6f4 v[142:145], v[2:9], v[202:209], v[142:145], v192, v192 op_sel_hi:[0,0,0]
	v_mfma_scale_f32_16x16x128_f8f6f4 v[138:141], v[10:17], v[202:209], v[138:141], v192, v192 op_sel_hi:[0,0,0]
	v_mfma_scale_f32_16x16x128_f8f6f4 v[126:129], v[2:9], v[210:217], v[126:129], v192, v192 op_sel_hi:[0,0,0]
	v_mfma_scale_f32_16x16x128_f8f6f4 v[122:125], v[10:17], v[210:217], v[122:125], v192, v192 op_sel_hi:[0,0,0]
	v_mfma_scale_f32_16x16x128_f8f6f4 v[110:113], v[2:9], v[218:225], v[110:113], v192, v192 op_sel_hi:[0,0,0]
	v_mfma_scale_f32_16x16x128_f8f6f4 v[106:109], v[10:17], v[218:225], v[106:109], v192, v192 op_sel_hi:[0,0,0]
	s_nop 3
	v_mfma_scale_f32_16x16x128_f8f6f4 v[150:153], v[18:25], v[194:201], v[150:153], v192, v192 op_sel_hi:[0,0,0]
	v_mfma_scale_f32_16x16x128_f8f6f4 v[146:149], v[26:33], v[194:201], v[146:149], v192, v192 op_sel_hi:[0,0,0]
	v_mfma_scale_f32_16x16x128_f8f6f4 v[134:137], v[18:25], v[202:209], v[134:137], v192, v192 op_sel_hi:[0,0,0]
	v_mfma_scale_f32_16x16x128_f8f6f4 v[130:133], v[26:33], v[202:209], v[130:133], v192, v192 op_sel_hi:[0,0,0]
	v_mfma_scale_f32_16x16x128_f8f6f4 v[118:121], v[18:25], v[210:217], v[118:121], v192, v192 op_sel_hi:[0,0,0]
	v_mfma_scale_f32_16x16x128_f8f6f4 v[114:117], v[26:33], v[210:217], v[114:117], v192, v192 op_sel_hi:[0,0,0]
	v_mfma_scale_f32_16x16x128_f8f6f4 v[102:105], v[18:25], v[218:225], v[102:105], v192, v192 op_sel_hi:[0,0,0]
	v_mfma_scale_f32_16x16x128_f8f6f4 v[98:101], v[26:33], v[218:225], v[98:101], v192, v192 op_sel_hi:[0,0,0]
	s_barrier
	s_add_u32 s28, s28, 0x8000
	s_addc_u32 s29, s29, 0
	s_add_i32 s30, s69, s43
	v_lshl_add_u64 v[226:227], s[28:29], 0, v[164:165]
	s_mov_b32 m0, s30
	ds_read_b128 v[194:197], v191 offset:49152
	ds_read_b128 v[198:201], v191 offset:50176
	ds_read_b128 v[202:205], v191 offset:51200
	ds_read_b128 v[206:209], v191 offset:52224
	ds_read_b128 v[210:213], v191 offset:53248
	ds_read_b128 v[214:217], v191 offset:54272
	ds_read_b128 v[218:221], v191 offset:55296
	ds_read_b128 v[222:225], v191 offset:56320
	global_load_lds_dwordx4 v[226:227], off
	v_lshl_add_u64 v[226:227], s[28:29], 0, v[166:167]
	s_add_i32 m0, s30, 0x2000
	s_add_i32 s30, s70, s43
	global_load_lds_dwordx4 v[226:227], off
	v_lshl_add_u64 v[226:227], s[28:29], 0, v[178:179]
	s_mov_b32 m0, s30
	s_nop 0
	global_load_lds_dwordx4 v[226:227], off
	v_lshl_add_u64 v[226:227], s[28:29], 0, v[180:181]
	s_add_i32 m0, s30, 0x2000
	s_nop 0
	global_load_lds_dwordx4 v[226:227], off
	v_lshl_add_u64 v[226:227], s[26:27], 0, v[168:169]
	s_mov_b32 m0, s51
	s_nop 0
	global_load_lds_dwordx4 v[226:227], off
	v_lshl_add_u64 v[226:227], s[26:27], 0, v[170:171]
	s_mov_b32 m0, s52
	s_nop 0
	global_load_lds_dwordx4 v[226:227], off
	s_waitcnt vmcnt(8)
	s_waitcnt lgkmcnt(0)
	v_mfma_scale_f32_16x16x128_f8f6f4 v[94:97], v[2:9], v[194:201], v[94:97], v192, v192 op_sel_hi:[0,0,0]
	v_mfma_scale_f32_16x16x128_f8f6f4 v[90:93], v[10:17], v[194:201], v[90:93], v192, v192 op_sel_hi:[0,0,0]
	v_mfma_scale_f32_16x16x128_f8f6f4 v[78:81], v[2:9], v[202:209], v[78:81], v192, v192 op_sel_hi:[0,0,0]
	v_mfma_scale_f32_16x16x128_f8f6f4 v[74:77], v[10:17], v[202:209], v[74:77], v192, v192 op_sel_hi:[0,0,0]
	v_mfma_scale_f32_16x16x128_f8f6f4 v[62:65], v[2:9], v[210:217], v[62:65], v192, v192 op_sel_hi:[0,0,0]
	v_mfma_scale_f32_16x16x128_f8f6f4 v[58:61], v[10:17], v[210:217], v[58:61], v192, v192 op_sel_hi:[0,0,0]
	v_mfma_scale_f32_16x16x128_f8f6f4 v[46:49], v[2:9], v[218:225], v[46:49], v192, v192 op_sel_hi:[0,0,0]
	v_mfma_scale_f32_16x16x128_f8f6f4 v[42:45], v[10:17], v[218:225], v[42:45], v192, v192 op_sel_hi:[0,0,0]
	s_nop 3
	v_mfma_scale_f32_16x16x128_f8f6f4 v[86:89], v[18:25], v[194:201], v[86:89], v192, v192 op_sel_hi:[0,0,0]
	v_mfma_scale_f32_16x16x128_f8f6f4 v[82:85], v[26:33], v[194:201], v[82:85], v192, v192 op_sel_hi:[0,0,0]
	v_mfma_scale_f32_16x16x128_f8f6f4 v[70:73], v[18:25], v[202:209], v[70:73], v192, v192 op_sel_hi:[0,0,0]
	v_mfma_scale_f32_16x16x128_f8f6f4 v[66:69], v[26:33], v[202:209], v[66:69], v192, v192 op_sel_hi:[0,0,0]
	v_mfma_scale_f32_16x16x128_f8f6f4 v[54:57], v[18:25], v[210:217], v[54:57], v192, v192 op_sel_hi:[0,0,0]
	v_mfma_scale_f32_16x16x128_f8f6f4 v[50:53], v[26:33], v[210:217], v[50:53], v192, v192 op_sel_hi:[0,0,0]
	v_mfma_scale_f32_16x16x128_f8f6f4 v[38:41], v[18:25], v[218:225], v[38:41], v192, v192 op_sel_hi:[0,0,0]
	v_mfma_scale_f32_16x16x128_f8f6f4 v[34:37], v[26:33], v[218:225], v[34:37], v192, v192 op_sel_hi:[0,0,0]
	s_barrier
	s_add_i32 s68, s68, 2
	s_add_u32 s23, s23, 0x10000
	s_addc_u32 s67, s67, 0
	s_add_u32 s24, s24, 0x10000
	s_addc_u32 s25, s25, 0
	s_cmp_gt_u32 s68, 5
	s_cbranch_scc0 .LBB0_1138
	s_branch .Lfx_33571

; #define PG8_STAGE(bufoff, gbase, voff) do { _Pragma("unroll") for (int _i = 0; _i < 2; ++_i) \
;         __builtin_amdgcn_global_load_lds((const unsigned*)((const char*)(gbase) + (voff)[_i]), (PG8_LAS unsigned*)(lds + (bufoff) + ldsw + _i * 8192), 16, 0, 0); } while (0)
; #define PG8_WAIT_V(n) asm volatile("s_waitcnt vmcnt(" #n ")" ::: "memory")
; #define PG8_WAIT_L(n) asm volatile("s_waitcnt lgkmcnt(" #n ")" ::: "memory")
; #define PG8_BAR __builtin_amdgcn_s_barrier()
; #define PG8_SCHED __builtin_amdgcn_sched_barrier(0)
; template <class Epi, class Sched, bool ALIGN_EPI = true, bool F8 = false>
; __device__ __forceinline__ void gemm_phase(PG8_LAS unsigned char* lds, const Sched& S, const Epi& E) {
;     ...
;             const char* a1 = cA + (size_t)(t + 1) * kstep;
;             const char* a2 = last ? nA : cA + (size_t)(t + 2) * kstep; const char* b2 = last ? nB : cB + (size_t)(t + 2) * kstepB;
;             const char* a3 = a2 + kstep; const char* b3 = b2 + kstepB;
;             unsigned vA2[2][2];
; #pragma unroll
;             for (int h = 0; h < 2; ++h)
; #pragma unroll
;                 for (int i = 0; i < 2; ++i) { if constexpr (Sched::GATHER) vA2[h][i] = (last && has_next) ? voffAn[h][i] : voffA[h][i]; else vA2[h][i] = voffA[h][i]; }
;             PG8_LDB(B0, 0, 0); PG8_LDB(B1, 0, 1); PG8_SCHED; PG8_LDA(At, 0, 0); PG8_STAGE(PG8_SA(1, 1), a1, voffA[1]);
;             PG8_WAIT_V(8); PG8_WAIT_L(0); PG8_BAR; PG8_MMA(0, 0, At, B0); PG8_MMA(0, 1, At, B1); PG8_BAR; PG8_SCHED;
;             PG8_LDA(At, 0, 1); PG8_STAGE(PG8_SB(0, 0), b2, voffB[0]); PG8_STAGE(PG8_SB(0, 1), b2, voffB[1]); PG8_STAGE(PG8_SA(0, 0), a2, vA2[0]);
;             PG8_WAIT_V(8); PG8_WAIT_L(0); PG8_BAR; PG8_MMA(1, 0, At, B0); PG8_MMA(1, 1, At, B1); PG8_BAR; PG8_SCHED;
;             PG8_LDB(B0, 1, 0); PG8_LDB(B1, 1, 1); PG8_SCHED; PG8_LDA(At, 1, 0); PG8_STAGE(PG8_SA(0, 1), a2, vA2[1]);
;             PG8_WAIT_V(8); PG8_WAIT_L(0); PG8_BAR; PG8_MMA(0, 0, At, B0); PG8_MMA(0, 1, At, B1); PG8_BAR; PG8_SCHED;
.Lpk1_1138:
	ds_read_b128 v[18:21], v189
	ds_read_b128 v[22:25], v189 offset:1024
	ds_read_b128 v[26:29], v189 offset:2048
	ds_read_b128 v[30:33], v189 offset:3072
	ds_read_b128 v[2:5], v190
	ds_read_b128 v[6:9], v190 offset:1024
	ds_read_b128 v[10:13], v190 offset:2048
	ds_read_b128 v[14:17], v190 offset:3072
	s_add_u32 s26, s24, 0x8000
	s_addc_u32 s27, s25, 0
	s_cmp_eq_u32 s68, 4
	s_cselect_b32 s30, s16, s26
	s_cselect_b32 s31, s17, s27
	s_cselect_b32 s28, s18, s23
	s_cselect_b32 s29, s19, s67
	s_add_u32 s26, s30, 0x8000
	s_addc_u32 s27, s31, 0
	v_lshl_add_u64 v[226:227], s[24:25], 0, v[184:185]
	s_add_i32 m0, s44, 0xc000
	ds_read_b128 v[194:197], v191
	ds_read_b128 v[198:201], v191 offset:1024
	ds_read_b128 v[202:205], v191 offset:2048
	ds_read_b128 v[206:209], v191 offset:3072
	ds_read_b128 v[210:213], v191 offset:4096
	ds_read_b128 v[214:217], v191 offset:5120
	ds_read_b128 v[218:221], v191 offset:6144
	ds_read_b128 v[222:225], v191 offset:7168
	global_load_lds_dwordx4 v[226:227], off
	v_lshl_add_u64 v[226:227], s[24:25], 0, v[182:183]
	s_add_i32 m0, s44, 0xe000
	s_nop 0
	global_load_lds_dwordx4 v[226:227], off
	s_waitcnt vmcnt(8)
	s_waitcnt lgkmcnt(0)
	s_barrier
	v_mfma_scale_f32_16x16x128_f8f6f4 v[158:161], v[18:25], v[194:201], 0, v192, v192 op_sel_hi:[0,0,0]
	v_mfma_scale_f32_16x16x128_f8f6f4 v[154:157], v[26:33], v[194:201], 0, v192, v192 op_sel_hi:[0,0,0]
	v_mfma_scale_f32_16x16x128_f8f6f4 v[142:145], v[18:25], v[202:209], 0, v192, v192 op_sel_hi:[0,0,0]
	v_mfma_scale_f32_16x16x128_f8f6f4 v[138:141], v[26:33], v[202:209], 0, v192, v192 op_sel_hi:[0,0,0]
	v_mfma_scale_f32_16x16x128_f8f6f4 v[126:129], v[18:25], v[210:217], 0, v192, v192 op_sel_hi:[0,0,0]
	v_mfma_scale_f32_16x16x128_f8f6f4 v[122:125], v[26:33], v[210:217], 0, v192, v192 op_sel_hi:[0,0,0]
	v_mfma_scale_f32_16x16x128_f8f6f4 v[110:113], v[18:25], v[218:225], 0, v192, v192 op_sel_hi:[0,0,0]
	v_mfma_scale_f32_16x16x128_f8f6f4 v[106:109], v[26:33], v[218:225], 0, v192, v192 op_sel_hi:[0,0,0]
	s_nop 3
	v_mfma_scale_f32_16x16x128_f8f6f4 v[150:153], v[2:9], v[194:201], 0, v192, v192 op_sel_hi:[0,0,0]
	v_mfma_scale_f32_16x16x128_f8f6f4 v[146:149], v[10:17], v[194:201], 0, v192, v192 op_sel_hi:[0,0,0]
	v_mfma_scale_f32_16x16x128_f8f6f4 v[134:137], v[2:9], v[202:209], 0, v192, v192 op_sel_hi:[0,0,0]
	v_mfma_scale_f32_16x16x128_f8f6f4 v[130:133], v[10:17], v[202:209], 0, v192, v192 op_sel_hi:[0,0,0]
	v_mfma_scale_f32_16x16x128_f8f6f4 v[118:121], v[2:9], v[210:217], 0, v192, v192 op_sel_hi:[0,0,0]
	v_mfma_scale_f32_16x16x128_f8f6f4 v[114:117], v[10:17], v[210:217], 0, v192, v192 op_sel_hi:[0,0,0]
	v_mfma_scale_f32_16x16x128_f8f6f4 v[102:105], v[2:9], v[218:225], 0, v192, v192 op_sel_hi:[0,0,0]
	v_mfma_scale_f32_16x16x128_f8f6f4 v[98:101], v[10:17], v[218:225], 0, v192, v192 op_sel_hi:[0,0,0]
	s_add_i32 s69, s53, s43
	v_lshl_add_u64 v[226:227], s[28:29], 0, v[164:165]
	s_mov_b32 m0, s69
	ds_read_b128 v[194:197], v191 offset:16384
	ds_read_b128 v[198:201], v191 offset:17408
	ds_read_b128 v[202:205], v191 offset:18432
	ds_read_b128 v[206:209], v191 offset:19456
	ds_read_b128 v[210:213], v191 offset:20480
	ds_read_b128 v[214:217], v191 offset:21504
	ds_read_b128 v[218:221], v191 offset:22528
	ds_read_b128 v[222:225], v191 offset:23552
	global_load_lds_dwordx4 v[226:227], off
	v_lshl_add_u64 v[228:229], s[28:29], 0, v[166:167]
	s_add_i32 m0, s69, 0x2000
	s_add_i32 s69, s58, s43
	global_load_lds_dwordx4 v[228:229], off
	v_lshl_add_u64 v[226:227], v[226:227], 0, s[4:5]
	s_mov_b32 m0, s69
	s_nop 0
	global_load_lds_dwordx4 v[226:227], off
	v_lshl_add_u64 v[226:227], v[228:229], 0, s[4:5]
	s_add_i32 m0, s69, 0x2000
	s_nop 0
	global_load_lds_dwordx4 v[226:227], off
	v_lshl_add_u64 v[226:227], s[30:31], 0, v[168:169]
	s_mov_b32 m0, s44
	s_nop 0
	global_load_lds_dwordx4 v[226:227], off
	v_lshl_add_u64 v[226:227], s[30:31], 0, v[170:171]
	s_mov_b32 m0, s45
	s_nop 0
	global_load_lds_dwordx4 v[226:227], off
	s_waitcnt vmcnt(8)
	s_waitcnt lgkmcnt(0)
	s_barrier
	v_mfma_scale_f32_16x16x128_f8f6f4 v[94:97], v[18:25], v[194:201], 0, v192, v192 op_sel_hi:[0,0,0]
	v_mfma_scale_f32_16x16x128_f8f6f4 v[90:93], v[26:33], v[194:201], 0, v192, v192 op_sel_hi:[0,0,0]
	v_mfma_scale_f32_16x16x128_f8f6f4 v[78:81], v[18:25], v[202:209], 0, v192, v192 op_sel_hi:[0,0,0]
	v_mfma_scale_f32_16x16x128_f8f6f4 v[74:77], v[26:33], v[202:209], 0, v192, v192 op_sel_hi:[0,0,0]
	v_mfma_scale_f32_16x16x128_f8f6f4 v[62:65], v[18:25], v[210:217], 0, v192, v192 op_sel_hi:[0,0,0]
	v_mfma_scale_f32_16x16x128_f8f6f4 v[58:61], v[26:33], v[210:217], 0, v192, v192 op_sel_hi:[0,0,0]
	v_mfma_scale_f32_16x16x128_f8f6f4 v[46:49], v[18:25], v[218:225], 0, v192, v192 op_sel_hi:[0,0,0]
	v_mfma_scale_f32_16x16x128_f8f6f4 v[42:45], v[26:33], v[218:225], 0, v192, v192 op_sel_hi:[0,0,0]
	s_nop 3
	v_mfma_scale_f32_16x16x128_f8f6f4 v[86:89], v[2:9], v[194:201], 0, v192, v192 op_sel_hi:[0,0,0]
	v_mfma_scale_f32_16x16x128_f8f6f4 v[82:85], v[10:17], v[194:201], 0, v192, v192 op_sel_hi:[0,0,0]
	v_mfma_scale_f32_16x16x128_f8f6f4 v[70:73], v[2:9], v[202:209], 0, v192, v192 op_sel_hi:[0,0,0]
	v_mfma_scale_f32_16x16x128_f8f6f4 v[66:69], v[10:17], v[202:209], 0, v192, v192 op_sel_hi:[0,0,0]
	v_mfma_scale_f32_16x16x128_f8f6f4 v[54:57], v[2:9], v[210:217], 0, v192, v192 op_sel_hi:[0,0,0]
	v_mfma_scale_f32_16x16x128_f8f6f4 v[50:53], v[10:17], v[210:217], 0, v192, v192 op_sel_hi:[0,0,0]
	v_mfma_scale_f32_16x16x128_f8f6f4 v[38:41], v[2:9], v[218:225], 0, v192, v192 op_sel_hi:[0,0,0]
	v_mfma_scale_f32_16x16x128_f8f6f4 v[34:37], v[10:17], v[218:225], 0, v192, v192 op_sel_hi:[0,0,0]
	s_add_i32 s69, 0, 0x18000
	s_add_i32 s70, 0, 0x1c000
	v_add_u32_e32 v14, s69, v187
	v_add_u32_e32 v30, s70, v187
	ds_read_b128 v[2:5], v14
	ds_read_b128 v[6:9], v14 offset:1024
	ds_read_b128 v[10:13], v14 offset:2048
	ds_read_b128 v[14:17], v14 offset:3072
	ds_read_b128 v[18:21], v30
	ds_read_b128 v[22:25], v30 offset:1024
	ds_read_b128 v[26:29], v30 offset:2048
	ds_read_b128 v[30:33], v30 offset:3072
	s_mov_b32 m0, s46
	v_lshl_add_u64 v[226:227], s[30:31], 0, v[172:173]
	ds_read_b128 v[194:197], v191 offset:32768
	ds_read_b128 v[198:201], v191 offset:33792
	ds_read_b128 v[202:205], v191 offset:34816
	ds_read_b128 v[206:209], v191 offset:35840
	ds_read_b128 v[210:213], v191 offset:36864
	ds_read_b128 v[214:217], v191 offset:37888
	ds_read_b128 v[218:221], v191 offset:38912
	ds_read_b128 v[222:225], v191 offset:39936
	global_load_lds_dwordx4 v[226:227], off
	v_lshl_add_u64 v[226:227], s[30:31], 0, v[174:175]
	s_mov_b32 m0, s47
	s_nop 0
	global_load_lds_dwordx4 v[226:227], off
	s_waitcnt vmcnt(8)
	s_waitcnt lgkmcnt(0)
	s_barrier
; #define PG8_STAGE(bufoff, gbase, voff) do { _Pragma("unroll") for (int _i = 0; _i < 2; ++_i) \
;         __builtin_amdgcn_global_load_lds((const unsigned*)((const char*)(gbase) + (voff)[_i]), (PG8_LAS unsigned*)(lds + (bufoff) + ldsw + _i * 8192), 16, 0, 0); } while (0)
; #define PG8_WAIT_V(n) asm volatile("s_waitcnt vmcnt(" #n ")" ::: "memory")
; #define PG8_WAIT_L(n) asm volatile("s_waitcnt lgkmcnt(" #n ")" ::: "memory")
; #define PG8_BAR __builtin_amdgcn_s_barrier()
; #define PG8_SCHED __builtin_amdgcn_sched_barrier(0)
; template <class Epi, class Sched, bool ALIGN_EPI = true, bool F8 = false>
; __device__ __forceinline__ void gemm_phase(PG8_LAS unsigned char* lds, const Sched& S, const Epi& E) {
;     ...
;             PG8_WAIT_V(8); PG8_WAIT_L(0); PG8_BAR; PG8_MMA(0, 0, At, B0); PG8_MMA(0, 1, At, B1); PG8_BAR; PG8_SCHED;
;             PG8_LDA(At, 1, 1); PG8_STAGE(PG8_SB(1, 0), b3, voffB[0]); PG8_STAGE(PG8_SB(1, 1), b3, voffB[1]); PG8_STAGE(PG8_SA(1, 0), a3, vA2[0]);
;             PG8_WAIT_V(8); PG8_WAIT_L(0); PG8_BAR; PG8_MMA(1, 0, At, B0); PG8_MMA(1, 1, At, B1); PG8_BAR; PG8_SCHED;
	v_mfma_scale_f32_16x16x128_f8f6f4 v[158:161], v[2:9], v[194:201], v[158:161], v192, v192 op_sel_hi:[0,0,0]
	v_mfma_scale_f32_16x16x128_f8f6f4 v[154:157], v[10:17], v[194:201], v[154:157], v192, v192 op_sel_hi:[0,0,0]
	v_mfma_scale_f32_16x16x128_f8f6f4 v[142:145], v[2:9], v[202:209], v[142:145], v192, v192 op_sel_hi:[0,0,0]
	v_mfma_scale_f32_16x16x128_f8f6f4 v[138:141], v[10:17], v[202:209], v[138:141], v192, v192 op_sel_hi:[0,0,0]
	v_mfma_scale_f32_16x16x128_f8f6f4 v[126:129], v[2:9], v[210:217], v[126:129], v192, v192 op_sel_hi:[0,0,0]
	v_mfma_scale_f32_16x16x128_f8f6f4 v[122:125], v[10:17], v[210:217], v[122:125], v192, v192 op_sel_hi:[0,0,0]
	v_mfma_scale_f32_16x16x128_f8f6f4 v[110:113], v[2:9], v[218:225], v[110:113], v192, v192 op_sel_hi:[0,0,0]
	v_mfma_scale_f32_16x16x128_f8f6f4 v[106:109], v[10:17], v[218:225], v[106:109], v192, v192 op_sel_hi:[0,0,0]
	s_nop 3
	v_mfma_scale_f32_16x16x128_f8f6f4 v[150:153], v[18:25], v[194:201], v[150:153], v192, v192 op_sel_hi:[0,0,0]
	v_mfma_scale_f32_16x16x128_f8f6f4 v[146:149], v[26:33], v[194:201], v[146:149], v192, v192 op_sel_hi:[0,0,0]
	v_mfma_scale_f32_16x16x128_f8f6f4 v[134:137], v[18:25], v[202:209], v[134:137], v192, v192 op_sel_hi:[0,0,0]
	v_mfma_scale_f32_16x16x128_f8f6f4 v[130:133], v[26:33], v[202:209], v[130:133], v192, v192 op_sel_hi:[0,0,0]
	v_mfma_scale_f32_16x16x128_f8f6f4 v[118:121], v[18:25], v[210:217], v[118:121], v192, v192 op_sel_hi:[0,0,0]
	v_mfma_scale_f32_16x16x128_f8f6f4 v[114:117], v[26:33], v[210:217], v[114:117], v192, v192 op_sel_hi:[0,0,0]
	v_mfma_scale_f32_16x16x128_f8f6f4 v[102:105], v[18:25], v[218:225], v[102:105], v192, v192 op_sel_hi:[0,0,0]
	v_mfma_scale_f32_16x16x128_f8f6f4 v[98:101], v[26:33], v[218:225], v[98:101], v192, v192 op_sel_hi:[0,0,0]
	s_add_u32 s28, s28, 0x8000
	s_addc_u32 s29, s29, 0
	s_add_i32 s30, s69, s43
	v_lshl_add_u64 v[226:227], s[28:29], 0, v[164:165]
	s_mov_b32 m0, s30
	ds_read_b128 v[194:197], v191 offset:49152
	ds_read_b128 v[198:201], v191 offset:50176
	ds_read_b128 v[202:205], v191 offset:51200
	ds_read_b128 v[206:209], v191 offset:52224
	ds_read_b128 v[210:213], v191 offset:53248
	ds_read_b128 v[214:217], v191 offset:54272
	ds_read_b128 v[218:221], v191 offset:55296
	ds_read_b128 v[222:225], v191 offset:56320
	global_load_lds_dwordx4 v[226:227], off
	v_lshl_add_u64 v[226:227], s[28:29], 0, v[166:167]
	s_add_i32 m0, s30, 0x2000
	s_add_i32 s30, s70, s43
	global_load_lds_dwordx4 v[226:227], off
	v_lshl_add_u64 v[226:227], s[28:29], 0, v[178:179]
	s_mov_b32 m0, s30
	s_nop 0
	global_load_lds_dwordx4 v[226:227], off
	v_lshl_add_u64 v[226:227], s[28:29], 0, v[180:181]
	s_add_i32 m0, s30, 0x2000
	s_nop 0
	global_load_lds_dwordx4 v[226:227], off
	v_lshl_add_u64 v[226:227], s[26:27], 0, v[168:169]
	s_mov_b32 m0, s51
	s_nop 0
	global_load_lds_dwordx4 v[226:227], off
	v_lshl_add_u64 v[226:227], s[26:27], 0, v[170:171]
	s_mov_b32 m0, s52
	s_nop 0
	global_load_lds_dwordx4 v[226:227], off
	s_waitcnt vmcnt(8)
	s_waitcnt lgkmcnt(0)
	s_barrier
	v_mfma_scale_f32_16x16x128_f8f6f4 v[94:97], v[2:9], v[194:201], v[94:97], v192, v192 op_sel_hi:[0,0,0]
	v_mfma_scale_f32_16x16x128_f8f6f4 v[90:93], v[10:17], v[194:201], v[90:93], v192, v192 op_sel_hi:[0,0,0]
	v_mfma_scale_f32_16x16x128_f8f6f4 v[78:81], v[2:9], v[202:209], v[78:81], v192, v192 op_sel_hi:[0,0,0]
	v_mfma_scale_f32_16x16x128_f8f6f4 v[74:77], v[10:17], v[202:209], v[74:77], v192, v192 op_sel_hi:[0,0,0]
	v_mfma_scale_f32_16x16x128_f8f6f4 v[62:65], v[2:9], v[210:217], v[62:65], v192, v192 op_sel_hi:[0,0,0]
	v_mfma_scale_f32_16x16x128_f8f6f4 v[58:61], v[10:17], v[210:217], v[58:61], v192, v192 op_sel_hi:[0,0,0]
	v_mfma_scale_f32_16x16x128_f8f6f4 v[46:49], v[2:9], v[218:225], v[46:49], v192, v192 op_sel_hi:[0,0,0]
	v_mfma_scale_f32_16x16x128_f8f6f4 v[42:45], v[10:17], v[218:225], v[42:45], v192, v192 op_sel_hi:[0,0,0]
	s_nop 3
	v_mfma_scale_f32_16x16x128_f8f6f4 v[86:89], v[18:25], v[194:201], v[86:89], v192, v192 op_sel_hi:[0,0,0]
	v_mfma_scale_f32_16x16x128_f8f6f4 v[82:85], v[26:33], v[194:201], v[82:85], v192, v192 op_sel_hi:[0,0,0]
	v_mfma_scale_f32_16x16x128_f8f6f4 v[70:73], v[18:25], v[202:209], v[70:73], v192, v192 op_sel_hi:[0,0,0]
	v_mfma_scale_f32_16x16x128_f8f6f4 v[66:69], v[26:33], v[202:209], v[66:69], v192, v192 op_sel_hi:[0,0,0]
	v_mfma_scale_f32_16x16x128_f8f6f4 v[54:57], v[18:25], v[210:217], v[54:57], v192, v192 op_sel_hi:[0,0,0]
	v_mfma_scale_f32_16x16x128_f8f6f4 v[50:53], v[26:33], v[210:217], v[50:53], v192, v192 op_sel_hi:[0,0,0]
	v_mfma_scale_f32_16x16x128_f8f6f4 v[38:41], v[18:25], v[218:225], v[38:41], v192, v192 op_sel_hi:[0,0,0]
	v_mfma_scale_f32_16x16x128_f8f6f4 v[34:37], v[26:33], v[218:225], v[34:37], v192, v192 op_sel_hi:[0,0,0]
	s_add_i32 s68, s68, 2
	s_add_u32 s23, s23, 0x10000
	s_addc_u32 s67, s67, 0
	s_add_u32 s24, s24, 0x10000
	s_addc_u32 s25, s25, 0
	s_cmp_gt_u32 s68, 5
	s_cbranch_scc0 .Lh1_1138
	s_branch .Lfx_33571
; #define PG8_STAGE(bufoff, gbase, voff) do { _Pragma("unroll") for (int _i = 0; _i < 2; ++_i) \
;         __builtin_amdgcn_global_load_lds((const unsigned*)((const char*)(gbase) + (voff)[_i]), (PG8_LAS unsigned*)(lds + (bufoff) + ldsw + _i * 8192), 16, 0, 0); } while (0)
; #define PG8_WAIT_V(n) asm volatile("s_waitcnt vmcnt(" #n ")" ::: "memory")
; #define PG8_WAIT_L(n) asm volatile("s_waitcnt lgkmcnt(" #n ")" ::: "memory")
; #define PG8_BAR __builtin_amdgcn_s_barrier()
; #define PG8_SCHED __builtin_amdgcn_sched_barrier(0)
; template <class Epi, class Sched, bool ALIGN_EPI = true, bool F8 = false>
; __device__ __forceinline__ void gemm_phase(PG8_LAS unsigned char* lds, const Sched& S, const Epi& E) {
;     ...
;             const char* a1 = cA + (size_t)(t + 1) * kstep;
;             const char* a2 = last ? nA : cA + (size_t)(t + 2) * kstep; const char* b2 = last ? nB : cB + (size_t)(t + 2) * kstepB;
;             const char* a3 = a2 + kstep; const char* b3 = b2 + kstepB;
;             unsigned vA2[2][2];
; #pragma unroll
;             for (int h = 0; h < 2; ++h)
; #pragma unroll
;                 for (int i = 0; i < 2; ++i) { if constexpr (Sched::GATHER) vA2[h][i] = (last && has_next) ? voffAn[h][i] : voffA[h][i]; else vA2[h][i] = voffA[h][i]; }
;             PG8_LDB(B0, 0, 0); PG8_LDB(B1, 0, 1); PG8_SCHED; PG8_LDA(At, 0, 0); PG8_STAGE(PG8_SA(1, 1), a1, voffA[1]);
;             PG8_WAIT_V(8); PG8_WAIT_L(0); PG8_BAR; PG8_MMA(0, 0, At, B0); PG8_MMA(0, 1, At, B1); PG8_BAR; PG8_SCHED;
;             PG8_LDA(At, 0, 1); PG8_STAGE(PG8_SB(0, 0), b2, voffB[0]); PG8_STAGE(PG8_SB(0, 1), b2, voffB[1]); PG8_STAGE(PG8_SA(0, 0), a2, vA2[0]);
;             PG8_WAIT_V(8); PG8_WAIT_L(0); PG8_BAR; PG8_MMA(1, 0, At, B0); PG8_MMA(1, 1, At, B1); PG8_BAR; PG8_SCHED;
;             PG8_LDB(B0, 1, 0); PG8_LDB(B1, 1, 1); PG8_SCHED; PG8_LDA(At, 1, 0); PG8_STAGE(PG8_SA(0, 1), a2, vA2[1]);
;             PG8_WAIT_V(8); PG8_WAIT_L(0); PG8_BAR; PG8_MMA(0, 0, At, B0); PG8_MMA(0, 1, At, B1); PG8_BAR; PG8_SCHED;
.Lh1_1138:
	ds_read_b128 v[18:21], v189
	ds_read_b128 v[22:25], v189 offset:1024
	ds_read_b128 v[26:29], v189 offset:2048
	ds_read_b128 v[30:33], v189 offset:3072
	ds_read_b128 v[2:5], v190
	ds_read_b128 v[6:9], v190 offset:1024
	ds_read_b128 v[10:13], v190 offset:2048
	ds_read_b128 v[14:17], v190 offset:3072
	s_add_u32 s26, s24, 0x8000
	s_addc_u32 s27, s25, 0
	s_cmp_eq_u32 s68, 4
	s_cselect_b32 s30, s16, s26
	s_cselect_b32 s31, s17, s27
	s_cselect_b32 s28, s18, s23
	s_cselect_b32 s29, s19, s67
	s_add_u32 s26, s30, 0x8000
	s_addc_u32 s27, s31, 0
	v_lshl_add_u64 v[226:227], s[24:25], 0, v[184:185]
	s_add_i32 m0, s44, 0xc000
	ds_read_b128 v[194:197], v191
	ds_read_b128 v[198:201], v191 offset:1024
	ds_read_b128 v[202:205], v191 offset:2048
	ds_read_b128 v[206:209], v191 offset:3072
	ds_read_b128 v[210:213], v191 offset:4096
	ds_read_b128 v[214:217], v191 offset:5120
	ds_read_b128 v[218:221], v191 offset:6144
	ds_read_b128 v[222:225], v191 offset:7168
	global_load_lds_dwordx4 v[226:227], off
	v_lshl_add_u64 v[226:227], s[24:25], 0, v[182:183]
	s_add_i32 m0, s44, 0xe000
	s_nop 0
	global_load_lds_dwordx4 v[226:227], off
	s_waitcnt vmcnt(8)
	s_waitcnt lgkmcnt(0)
	s_barrier
	v_mfma_scale_f32_16x16x128_f8f6f4 v[158:161], v[18:25], v[194:201], v[158:161], v192, v192 op_sel_hi:[0,0,0]
	v_mfma_scale_f32_16x16x128_f8f6f4 v[154:157], v[26:33], v[194:201], v[154:157], v192, v192 op_sel_hi:[0,0,0]
	v_mfma_scale_f32_16x16x128_f8f6f4 v[142:145], v[18:25], v[202:209], v[142:145], v192, v192 op_sel_hi:[0,0,0]
	v_mfma_scale_f32_16x16x128_f8f6f4 v[138:141], v[26:33], v[202:209], v[138:141], v192, v192 op_sel_hi:[0,0,0]
	v_mfma_scale_f32_16x16x128_f8f6f4 v[126:129], v[18:25], v[210:217], v[126:129], v192, v192 op_sel_hi:[0,0,0]
	v_mfma_scale_f32_16x16x128_f8f6f4 v[122:125], v[26:33], v[210:217], v[122:125], v192, v192 op_sel_hi:[0,0,0]
	v_mfma_scale_f32_16x16x128_f8f6f4 v[110:113], v[18:25], v[218:225], v[110:113], v192, v192 op_sel_hi:[0,0,0]
	v_mfma_scale_f32_16x16x128_f8f6f4 v[106:109], v[26:33], v[218:225], v[106:109], v192, v192 op_sel_hi:[0,0,0]
	s_nop 3
	v_mfma_scale_f32_16x16x128_f8f6f4 v[150:153], v[2:9], v[194:201], v[150:153], v192, v192 op_sel_hi:[0,0,0]
	v_mfma_scale_f32_16x16x128_f8f6f4 v[146:149], v[10:17], v[194:201], v[146:149], v192, v192 op_sel_hi:[0,0,0]
	v_mfma_scale_f32_16x16x128_f8f6f4 v[134:137], v[2:9], v[202:209], v[134:137], v192, v192 op_sel_hi:[0,0,0]
	v_mfma_scale_f32_16x16x128_f8f6f4 v[130:133], v[10:17], v[202:209], v[130:133], v192, v192 op_sel_hi:[0,0,0]
	v_mfma_scale_f32_16x16x128_f8f6f4 v[118:121], v[2:9], v[210:217], v[118:121], v192, v192 op_sel_hi:[0,0,0]
	v_mfma_scale_f32_16x16x128_f8f6f4 v[114:117], v[10:17], v[210:217], v[114:117], v192, v192 op_sel_hi:[0,0,0]
	v_mfma_scale_f32_16x16x128_f8f6f4 v[102:105], v[2:9], v[218:225], v[102:105], v192, v192 op_sel_hi:[0,0,0]
	v_mfma_scale_f32_16x16x128_f8f6f4 v[98:101], v[10:17], v[218:225], v[98:101], v192, v192 op_sel_hi:[0,0,0]
	s_add_i32 s69, s53, s43
	v_lshl_add_u64 v[226:227], s[28:29], 0, v[164:165]
	s_mov_b32 m0, s69
	ds_read_b128 v[194:197], v191 offset:16384
	ds_read_b128 v[198:201], v191 offset:17408
	ds_read_b128 v[202:205], v191 offset:18432
	ds_read_b128 v[206:209], v191 offset:19456
	ds_read_b128 v[210:213], v191 offset:20480
	ds_read_b128 v[214:217], v191 offset:21504
	ds_read_b128 v[218:221], v191 offset:22528
	ds_read_b128 v[222:225], v191 offset:23552
	global_load_lds_dwordx4 v[226:227], off
	v_lshl_add_u64 v[228:229], s[28:29], 0, v[166:167]
	s_add_i32 m0, s69, 0x2000
	s_add_i32 s69, s58, s43
	global_load_lds_dwordx4 v[228:229], off
	v_lshl_add_u64 v[226:227], v[226:227], 0, s[4:5]
	s_mov_b32 m0, s69
	s_nop 0
	global_load_lds_dwordx4 v[226:227], off
	v_lshl_add_u64 v[226:227], v[228:229], 0, s[4:5]
	s_add_i32 m0, s69, 0x2000
	s_nop 0
	global_load_lds_dwordx4 v[226:227], off
	v_lshl_add_u64 v[226:227], s[30:31], 0, v[168:169]
	s_mov_b32 m0, s44
	s_nop 0
	global_load_lds_dwordx4 v[226:227], off
	v_lshl_add_u64 v[226:227], s[30:31], 0, v[170:171]
	s_mov_b32 m0, s45
	s_nop 0
	global_load_lds_dwordx4 v[226:227], off
	s_waitcnt vmcnt(8)
	s_waitcnt lgkmcnt(0)
	s_barrier
	v_mfma_scale_f32_16x16x128_f8f6f4 v[94:97], v[18:25], v[194:201], v[94:97], v192, v192 op_sel_hi:[0,0,0]
	v_mfma_scale_f32_16x16x128_f8f6f4 v[90:93], v[26:33], v[194:201], v[90:93], v192, v192 op_sel_hi:[0,0,0]
	v_mfma_scale_f32_16x16x128_f8f6f4 v[78:81], v[18:25], v[202:209], v[78:81], v192, v192 op_sel_hi:[0,0,0]
	v_mfma_scale_f32_16x16x128_f8f6f4 v[74:77], v[26:33], v[202:209], v[74:77], v192, v192 op_sel_hi:[0,0,0]
	v_mfma_scale_f32_16x16x128_f8f6f4 v[62:65], v[18:25], v[210:217], v[62:65], v192, v192 op_sel_hi:[0,0,0]
	v_mfma_scale_f32_16x16x128_f8f6f4 v[58:61], v[26:33], v[210:217], v[58:61], v192, v192 op_sel_hi:[0,0,0]
	v_mfma_scale_f32_16x16x128_f8f6f4 v[46:49], v[18:25], v[218:225], v[46:49], v192, v192 op_sel_hi:[0,0,0]
	v_mfma_scale_f32_16x16x128_f8f6f4 v[42:45], v[26:33], v[218:225], v[42:45], v192, v192 op_sel_hi:[0,0,0]
	s_nop 3
	v_mfma_scale_f32_16x16x128_f8f6f4 v[86:89], v[2:9], v[194:201], v[86:89], v192, v192 op_sel_hi:[0,0,0]
	v_mfma_scale_f32_16x16x128_f8f6f4 v[82:85], v[10:17], v[194:201], v[82:85], v192, v192 op_sel_hi:[0,0,0]
	v_mfma_scale_f32_16x16x128_f8f6f4 v[70:73], v[2:9], v[202:209], v[70:73], v192, v192 op_sel_hi:[0,0,0]
	v_mfma_scale_f32_16x16x128_f8f6f4 v[66:69], v[10:17], v[202:209], v[66:69], v192, v192 op_sel_hi:[0,0,0]
	v_mfma_scale_f32_16x16x128_f8f6f4 v[54:57], v[2:9], v[210:217], v[54:57], v192, v192 op_sel_hi:[0,0,0]
	v_mfma_scale_f32_16x16x128_f8f6f4 v[50:53], v[10:17], v[210:217], v[50:53], v192, v192 op_sel_hi:[0,0,0]
	v_mfma_scale_f32_16x16x128_f8f6f4 v[38:41], v[2:9], v[218:225], v[38:41], v192, v192 op_sel_hi:[0,0,0]
	v_mfma_scale_f32_16x16x128_f8f6f4 v[34:37], v[10:17], v[218:225], v[34:37], v192, v192 op_sel_hi:[0,0,0]
	s_add_i32 s69, 0, 0x18000
	s_add_i32 s70, 0, 0x1c000
	v_add_u32_e32 v14, s69, v187
	v_add_u32_e32 v30, s70, v187
	ds_read_b128 v[2:5], v14
	ds_read_b128 v[6:9], v14 offset:1024
	ds_read_b128 v[10:13], v14 offset:2048
	ds_read_b128 v[14:17], v14 offset:3072
	ds_read_b128 v[18:21], v30
	ds_read_b128 v[22:25], v30 offset:1024
	ds_read_b128 v[26:29], v30 offset:2048
	ds_read_b128 v[30:33], v30 offset:3072
	s_mov_b32 m0, s46
	v_lshl_add_u64 v[226:227], s[30:31], 0, v[172:173]
	ds_read_b128 v[194:197], v191 offset:32768
	ds_read_b128 v[198:201], v191 offset:33792
	ds_read_b128 v[202:205], v191 offset:34816
	ds_read_b128 v[206:209], v191 offset:35840
	ds_read_b128 v[210:213], v191 offset:36864
	ds_read_b128 v[214:217], v191 offset:37888
	ds_read_b128 v[218:221], v191 offset:38912
	ds_read_b128 v[222:225], v191 offset:39936
	global_load_lds_dwordx4 v[226:227], off
	v_lshl_add_u64 v[226:227], s[30:31], 0, v[174:175]
	s_mov_b32 m0, s47
	s_nop 0
	global_load_lds_dwordx4 v[226:227], off
	s_waitcnt vmcnt(8)
	s_waitcnt lgkmcnt(0)
	s_barrier
; #define PG8_STAGE(bufoff, gbase, voff) do { _Pragma("unroll") for (int _i = 0; _i < 2; ++_i) \
;         __builtin_amdgcn_global_load_lds((const unsigned*)((const char*)(gbase) + (voff)[_i]), (PG8_LAS unsigned*)(lds + (bufoff) + ldsw + _i * 8192), 16, 0, 0); } while (0)
; #define PG8_WAIT_V(n) asm volatile("s_waitcnt vmcnt(" #n ")" ::: "memory")
; #define PG8_WAIT_L(n) asm volatile("s_waitcnt lgkmcnt(" #n ")" ::: "memory")
; #define PG8_BAR __builtin_amdgcn_s_barrier()
; #define PG8_SCHED __builtin_amdgcn_sched_barrier(0)
; template <class Epi, class Sched, bool ALIGN_EPI = true, bool F8 = false>
; __device__ __forceinline__ void gemm_phase(PG8_LAS unsigned char* lds, const Sched& S, const Epi& E) {
;     ...
;             PG8_WAIT_V(8); PG8_WAIT_L(0); PG8_BAR; PG8_MMA(0, 0, At, B0); PG8_MMA(0, 1, At, B1); PG8_BAR; PG8_SCHED;
;             PG8_LDA(At, 1, 1); PG8_STAGE(PG8_SB(1, 0), b3, voffB[0]); PG8_STAGE(PG8_SB(1, 1), b3, voffB[1]); PG8_STAGE(PG8_SA(1, 0), a3, vA2[0]);
;             PG8_WAIT_V(8); PG8_WAIT_L(0); PG8_BAR; PG8_MMA(1, 0, At, B0); PG8_MMA(1, 1, At, B1); PG8_BAR; PG8_SCHED;
	v_mfma_scale_f32_16x16x128_f8f6f4 v[158:161], v[2:9], v[194:201], v[158:161], v192, v192 op_sel_hi:[0,0,0]
	v_mfma_scale_f32_16x16x128_f8f6f4 v[154:157], v[10:17], v[194:201], v[154:157], v192, v192 op_sel_hi:[0,0,0]
	v_mfma_scale_f32_16x16x128_f8f6f4 v[142:145], v[2:9], v[202:209], v[142:145], v192, v192 op_sel_hi:[0,0,0]
	v_mfma_scale_f32_16x16x128_f8f6f4 v[138:141], v[10:17], v[202:209], v[138:141], v192, v192 op_sel_hi:[0,0,0]
	v_mfma_scale_f32_16x16x128_f8f6f4 v[126:129], v[2:9], v[210:217], v[126:129], v192, v192 op_sel_hi:[0,0,0]
	v_mfma_scale_f32_16x16x128_f8f6f4 v[122:125], v[10:17], v[210:217], v[122:125], v192, v192 op_sel_hi:[0,0,0]
	v_mfma_scale_f32_16x16x128_f8f6f4 v[110:113], v[2:9], v[218:225], v[110:113], v192, v192 op_sel_hi:[0,0,0]
	v_mfma_scale_f32_16x16x128_f8f6f4 v[106:109], v[10:17], v[218:225], v[106:109], v192, v192 op_sel_hi:[0,0,0]
	s_nop 3
	v_mfma_scale_f32_16x16x128_f8f6f4 v[150:153], v[18:25], v[194:201], v[150:153], v192, v192 op_sel_hi:[0,0,0]
	v_mfma_scale_f32_16x16x128_f8f6f4 v[146:149], v[26:33], v[194:201], v[146:149], v192, v192 op_sel_hi:[0,0,0]
	v_mfma_scale_f32_16x16x128_f8f6f4 v[134:137], v[18:25], v[202:209], v[134:137], v192, v192 op_sel_hi:[0,0,0]
	v_mfma_scale_f32_16x16x128_f8f6f4 v[130:133], v[26:33], v[202:209], v[130:133], v192, v192 op_sel_hi:[0,0,0]
	v_mfma_scale_f32_16x16x128_f8f6f4 v[118:121], v[18:25], v[210:217], v[118:121], v192, v192 op_sel_hi:[0,0,0]
	v_mfma_scale_f32_16x16x128_f8f6f4 v[114:117], v[26:33], v[210:217], v[114:117], v192, v192 op_sel_hi:[0,0,0]
	v_mfma_scale_f32_16x16x128_f8f6f4 v[102:105], v[18:25], v[218:225], v[102:105], v192, v192 op_sel_hi:[0,0,0]
	v_mfma_scale_f32_16x16x128_f8f6f4 v[98:101], v[26:33], v[218:225], v[98:101], v192, v192 op_sel_hi:[0,0,0]
	s_add_u32 s28, s28, 0x8000
	s_addc_u32 s29, s29, 0
	s_add_i32 s30, s69, s43
	v_lshl_add_u64 v[226:227], s[28:29], 0, v[164:165]
	s_mov_b32 m0, s30
	ds_read_b128 v[194:197], v191 offset:49152
	ds_read_b128 v[198:201], v191 offset:50176
	ds_read_b128 v[202:205], v191 offset:51200
	ds_read_b128 v[206:209], v191 offset:52224
	ds_read_b128 v[210:213], v191 offset:53248
	ds_read_b128 v[214:217], v191 offset:54272
	ds_read_b128 v[218:221], v191 offset:55296
	ds_read_b128 v[222:225], v191 offset:56320
	global_load_lds_dwordx4 v[226:227], off
	v_lshl_add_u64 v[226:227], s[28:29], 0, v[166:167]
	s_add_i32 m0, s30, 0x2000
	s_add_i32 s30, s70, s43
	global_load_lds_dwordx4 v[226:227], off
	v_lshl_add_u64 v[226:227], s[28:29], 0, v[178:179]
	s_mov_b32 m0, s30
	s_nop 0
	global_load_lds_dwordx4 v[226:227], off
	v_lshl_add_u64 v[226:227], s[28:29], 0, v[180:181]
	s_add_i32 m0, s30, 0x2000
	s_nop 0
	global_load_lds_dwordx4 v[226:227], off
	v_lshl_add_u64 v[226:227], s[26:27], 0, v[168:169]
	s_mov_b32 m0, s51
	s_nop 0
	global_load_lds_dwordx4 v[226:227], off
	v_lshl_add_u64 v[226:227], s[26:27], 0, v[170:171]
	s_mov_b32 m0, s52
	s_nop 0
	global_load_lds_dwordx4 v[226:227], off
	s_waitcnt vmcnt(8)
	s_waitcnt lgkmcnt(0)
	s_barrier
	v_mfma_scale_f32_16x16x128_f8f6f4 v[94:97], v[2:9], v[194:201], v[94:97], v192, v192 op_sel_hi:[0,0,0]
	v_mfma_scale_f32_16x16x128_f8f6f4 v[90:93], v[10:17], v[194:201], v[90:93], v192, v192 op_sel_hi:[0,0,0]
	v_mfma_scale_f32_16x16x128_f8f6f4 v[78:81], v[2:9], v[202:209], v[78:81], v192, v192 op_sel_hi:[0,0,0]
	v_mfma_scale_f32_16x16x128_f8f6f4 v[74:77], v[10:17], v[202:209], v[74:77], v192, v192 op_sel_hi:[0,0,0]
	v_mfma_scale_f32_16x16x128_f8f6f4 v[62:65], v[2:9], v[210:217], v[62:65], v192, v192 op_sel_hi:[0,0,0]
	v_mfma_scale_f32_16x16x128_f8f6f4 v[58:61], v[10:17], v[210:217], v[58:61], v192, v192 op_sel_hi:[0,0,0]
	v_mfma_scale_f32_16x16x128_f8f6f4 v[46:49], v[2:9], v[218:225], v[46:49], v192, v192 op_sel_hi:[0,0,0]
	v_mfma_scale_f32_16x16x128_f8f6f4 v[42:45], v[10:17], v[218:225], v[42:45], v192, v192 op_sel_hi:[0,0,0]
	s_nop 3
	v_mfma_scale_f32_16x16x128_f8f6f4 v[86:89], v[18:25], v[194:201], v[86:89], v192, v192 op_sel_hi:[0,0,0]
	v_mfma_scale_f32_16x16x128_f8f6f4 v[82:85], v[26:33], v[194:201], v[82:85], v192, v192 op_sel_hi:[0,0,0]
	v_mfma_scale_f32_16x16x128_f8f6f4 v[70:73], v[18:25], v[202:209], v[70:73], v192, v192 op_sel_hi:[0,0,0]
	v_mfma_scale_f32_16x16x128_f8f6f4 v[66:69], v[26:33], v[202:209], v[66:69], v192, v192 op_sel_hi:[0,0,0]
	v_mfma_scale_f32_16x16x128_f8f6f4 v[54:57], v[18:25], v[210:217], v[54:57], v192, v192 op_sel_hi:[0,0,0]
	v_mfma_scale_f32_16x16x128_f8f6f4 v[50:53], v[26:33], v[210:217], v[50:53], v192, v192 op_sel_hi:[0,0,0]
	v_mfma_scale_f32_16x16x128_f8f6f4 v[38:41], v[18:25], v[218:225], v[38:41], v192, v192 op_sel_hi:[0,0,0]
	v_mfma_scale_f32_16x16x128_f8f6f4 v[34:37], v[26:33], v[218:225], v[34:37], v192, v192 op_sel_hi:[0,0,0]
	s_add_i32 s68, s68, 2
	s_add_u32 s23, s23, 0x10000
	s_addc_u32 s67, s67, 0
	s_add_u32 s24, s24, 0x10000
	s_addc_u32 s25, s25, 0
	s_cmp_gt_u32 s68, 5
	s_cbranch_scc0 .Lh1_1138
